# b3 + converter bf16 weight stores marked nt (streaming) so they do not displace GEMM operands in L2
# speedup vs baseline: 1.0099x; 1.0099x over previous
.LBB0_51:
	v_add_u32_e32 v2, s4, v74
	v_ashrrev_i32_e32 v3, 31, v2
	v_mul_lo_u32 v4, s34, v3
	v_mul_lo_u32 v5, s35, v2
	v_mad_u64_u32 v[2:3], s[54:55], s34, v2, 0
	v_add3_u32 v3, v3, v4, v5
	v_add_u32_e32 v4, s4, v73
	v_ashrrev_i32_e32 v5, 31, v4
	s_ashr_i32 s31, s30, 31
	v_mul_lo_u32 v6, s34, v5
	v_mul_lo_u32 v7, s35, v4
	v_mad_u64_u32 v[4:5], s[54:55], s34, v4, 0
	v_lshl_add_u64 v[2:3], v[2:3], 2, s[0:1]
	s_lshl_b64 s[30:31], s[30:31], 2
	v_add3_u32 v5, v5, v6, v7
	v_lshl_add_u64 v[2:3], v[2:3], 0, s[30:31]
	v_lshl_add_u64 v[4:5], v[4:5], 2, s[0:1]
	v_lshl_add_u64 v[2:3], v[2:3], 0, v[68:69]
	v_lshl_add_u64 v[4:5], v[4:5], 0, s[30:31]
	v_lshl_add_u64 v[4:5], v[4:5], 0, v[68:69]
	global_load_dwordx4 v[30:33], v[2:3], off nt
	global_load_dwordx4 v[18:21], v[4:5], off nt
	v_add_u32_e32 v2, s4, v72
	v_ashrrev_i32_e32 v3, 31, v2
	v_mul_lo_u32 v4, s34, v3
	v_mul_lo_u32 v5, s35, v2
	v_mad_u64_u32 v[2:3], s[54:55], s34, v2, 0
	v_add3_u32 v3, v3, v4, v5
	v_add_u32_e32 v4, s4, v71
	v_ashrrev_i32_e32 v5, 31, v4
	v_mul_lo_u32 v6, s34, v5
	v_mul_lo_u32 v7, s35, v4
	v_mad_u64_u32 v[4:5], s[54:55], s34, v4, 0
	v_lshl_add_u64 v[2:3], v[2:3], 2, s[0:1]
	v_add3_u32 v5, v5, v6, v7
	v_lshl_add_u64 v[2:3], v[2:3], 0, s[30:31]
	v_lshl_add_u64 v[4:5], v[4:5], 2, s[0:1]
	v_lshl_add_u64 v[2:3], v[2:3], 0, v[68:69]
	v_lshl_add_u64 v[4:5], v[4:5], 0, s[30:31]
	v_lshl_add_u64 v[4:5], v[4:5], 0, v[68:69]
	global_load_dwordx4 v[26:29], v[2:3], off nt
	global_load_dwordx4 v[10:13], v[4:5], off nt
	v_add_u32_e32 v2, s4, v75
	v_ashrrev_i32_e32 v3, 31, v2
	v_mul_lo_u32 v4, s34, v3
	v_mul_lo_u32 v5, s35, v2
	v_mad_u64_u32 v[2:3], s[54:55], s34, v2, 0
	v_add3_u32 v3, v3, v4, v5
	v_add_u32_e32 v4, s4, v79
	v_ashrrev_i32_e32 v5, 31, v4
	v_mul_lo_u32 v6, s34, v5
	v_mul_lo_u32 v7, s35, v4
	v_mad_u64_u32 v[4:5], s[54:55], s34, v4, 0
	v_lshl_add_u64 v[2:3], v[2:3], 2, s[0:1]
	v_add3_u32 v5, v5, v6, v7
	v_lshl_add_u64 v[2:3], v[2:3], 0, s[30:31]
	v_lshl_add_u64 v[4:5], v[4:5], 2, s[0:1]
	v_lshl_add_u64 v[2:3], v[2:3], 0, v[68:69]
	v_lshl_add_u64 v[4:5], v[4:5], 0, s[30:31]
	v_lshl_add_u64 v[4:5], v[4:5], 0, v[68:69]
	global_load_dwordx4 v[22:25], v[2:3], off nt
	global_load_dwordx4 v[6:9], v[4:5], off nt
	v_add_u32_e32 v2, s4, v80
	v_ashrrev_i32_e32 v3, 31, v2
	v_mul_lo_u32 v4, s34, v3
	v_mul_lo_u32 v5, s35, v2
	v_mad_u64_u32 v[2:3], s[54:55], s34, v2, 0
	v_add3_u32 v3, v3, v4, v5
	v_add_u32_e32 v4, s4, v81
	v_ashrrev_i32_e32 v5, 31, v4
	v_mul_lo_u32 v14, s34, v5
	v_mul_lo_u32 v15, s35, v4
	v_mad_u64_u32 v[4:5], s[34:35], s34, v4, 0
	v_add3_u32 v5, v5, v14, v15
	v_lshl_add_u64 v[2:3], v[2:3], 2, s[0:1]
	v_lshl_add_u64 v[4:5], v[4:5], 2, s[0:1]
	v_lshl_add_u64 v[2:3], v[2:3], 0, s[30:31]
	v_lshl_add_u64 v[4:5], v[4:5], 0, s[30:31]
	v_lshl_add_u64 v[2:3], v[2:3], 0, v[68:69]
	v_lshl_add_u64 v[4:5], v[4:5], 0, v[68:69]
	global_load_dwordx4 v[14:17], v[2:3], off nt
	s_nop 0
	global_load_dwordx4 v[2:5], v[4:5], off nt
	s_waitcnt vmcnt(15)
	ds_write2_b32 v87, v34, v35 offset1:1
	ds_write2_b32 v87, v36, v37 offset0:2 offset1:3
	v_add_u32_e32 v34, 0x420, v87
	s_waitcnt vmcnt(14)
	ds_write2_b32 v34, v38, v39 offset1:1
	v_add_u32_e32 v34, 0x428, v87
	ds_write2_b32 v34, v40, v41 offset1:1
	v_add_u32_e32 v34, 0x840, v87
	s_waitcnt vmcnt(13)
	ds_write2_b32 v34, v42, v43 offset1:1
	v_add_u32_e32 v34, 0x848, v87
	ds_write2_b32 v34, v44, v45 offset1:1
	v_add_u32_e32 v34, 0xc60, v87
	s_waitcnt vmcnt(12)
	ds_write2_b32 v34, v46, v47 offset1:1
	v_add_u32_e32 v34, 0xc68, v87
	ds_write2_b32 v34, v48, v49 offset1:1
	v_add_u32_e32 v34, 0x1080, v87
	s_waitcnt vmcnt(11)
	ds_write2_b32 v34, v50, v51 offset1:1
	v_add_u32_e32 v34, 0x1088, v87
	ds_write2_b32 v34, v52, v53 offset1:1
	v_add_u32_e32 v34, 0x14a0, v87
	s_waitcnt vmcnt(10)
	ds_write2_b32 v34, v54, v55 offset1:1
	v_add_u32_e32 v34, 0x14a8, v87
	ds_write2_b32 v34, v56, v57 offset1:1
	v_add_u32_e32 v34, 0x18c0, v87
	s_waitcnt vmcnt(9)
	ds_write2_b32 v34, v58, v59 offset1:1
	v_add_u32_e32 v34, 0x18c8, v87
	ds_write2_b32 v34, v60, v61 offset1:1
	v_add_u32_e32 v34, 0x1ce0, v87
	s_waitcnt vmcnt(8)
	ds_write2_b32 v34, v62, v63 offset1:1
	v_add_u32_e32 v34, 0x1ce8, v87
	ds_write2_b32 v34, v64, v65 offset1:1
	s_waitcnt lgkmcnt(0)
	ds_read2_b32 v[46:47], v86 offset1:33
	ds_read2_b32 v[44:45], v86 offset0:66 offset1:99
	ds_read2_b32 v[40:41], v86 offset0:132 offset1:165
	ds_read2_b32 v[38:39], v86 offset0:198 offset1:231
	s_cmp_lg_u64 s[10:11], 0
	s_cselect_b64 s[30:31], -1, 0
	v_add_u32_e32 v42, s6, v66
	s_and_b64 vcc, exec, s[30:31]
	v_add_u32_e32 v48, s42, v74
	v_ashrrev_i32_e32 v56, 5, v42
	v_lshlrev_b32_e32 v57, 1, v42
	v_ashrrev_i32_e32 v43, 31, v42
	s_waitcnt lgkmcnt(3)
	v_cvt_pk_bf16_f32 v34, v46, v47
	s_waitcnt lgkmcnt(2)
	v_cvt_pk_bf16_f32 v35, v44, v45
	s_waitcnt lgkmcnt(1)
	v_cvt_pk_bf16_f32 v36, v40, v41
	s_waitcnt lgkmcnt(0)
	v_cvt_pk_bf16_f32 v37, v38, v39
	s_cbranch_vccz .LBB0_65
	v_readlane_b32 s56, v243, 40
	v_readlane_b32 s58, v243, 42
	v_readlane_b32 s59, v243, 43
	v_lshlrev_b32_e32 v49, 2, v48
	v_and_b32_e32 v49, 0xffffffc0, v49
	v_lshl_add_u64 v[54:55], v[42:43], 2, s[58:59]
	global_load_dwordx4 v[50:53], v[54:55], off
	global_load_dwordx4 v[58:61], v[54:55], off offset:16
	v_add_u32_e32 v54, v49, v56
	v_ashrrev_i32_e32 v55, 31, v54
	v_and_b32_e32 v62, 48, v57
	v_and_b32_e32 v63, 15, v48
	v_lshlrev_b64 v[54:55], 6, v[54:55]
	v_or3_b32 v54, v54, v62, v63
	v_lshlrev_b64 v[54:55], 4, v[54:55]
	v_lshl_add_u64 v[88:89], s[2:3], 0, v[54:55]
	v_readlane_b32 s57, v243, 41
	v_readlane_b32 s60, v243, 44
	v_readlane_b32 s61, v243, 45
	v_readlane_b32 s62, v243, 46
	v_readlane_b32 s63, v243, 47
	v_readlane_b32 s64, v243, 48
	v_readlane_b32 s65, v243, 49
	v_readlane_b32 s66, v243, 50
	v_readlane_b32 s67, v243, 51
	v_readlane_b32 s68, v243, 52
	v_readlane_b32 s69, v243, 53
	v_readlane_b32 s70, v243, 54
	v_readlane_b32 s71, v243, 55
	v_lshl_add_u64 v[54:55], s[10:11], 0, v[54:55]
	s_waitcnt vmcnt(1)
	v_mul_f32_e32 v62, v47, v51
	v_mul_f32_e32 v63, v44, v52
	v_mul_f32_e32 v64, v45, v53
	v_mul_f32_e32 v49, v46, v50
	s_waitcnt vmcnt(0)
	v_mul_f32_e32 v65, v40, v58
	v_mul_f32_e32 v90, v41, v59
	v_mul_f32_e32 v91, v38, v60
	v_mul_f32_e32 v92, v39, v61
	v_cvt_pk_bf16_f32 v62, v49, v62
	v_cvt_pk_bf16_f32 v63, v63, v64
	v_cvt_pk_bf16_f32 v64, v65, v90
	v_cvt_pk_bf16_f32 v65, v91, v92
	s_nop 0
	v_lshlrev_b32_e32 v93, 16, v64
	v_and_b32_e32 v94, 0xffff0000, v64
	v_lshlrev_b32_e32 v49, 16, v62
	v_and_b32_e32 v90, 0xffff0000, v62
	v_lshlrev_b32_e32 v91, 16, v63
	v_and_b32_e32 v92, 0xffff0000, v63
	v_lshlrev_b32_e32 v95, 16, v65
	v_and_b32_e32 v96, 0xffff0000, v65
	v_fma_f32 v40, v40, v58, -v93
	v_fma_f32 v41, v41, v59, -v94
	v_fma_f32 v46, v46, v50, -v49
	v_fma_f32 v47, v47, v51, -v90
	v_fma_f32 v44, v44, v52, -v91
	v_fma_f32 v45, v45, v53, -v92
	v_fma_f32 v49, v38, v60, -v95
	v_fma_f32 v50, v39, v61, -v96
	v_cvt_pk_bf16_f32 v38, v46, v47
	v_cvt_pk_bf16_f32 v39, v44, v45
	v_cvt_pk_bf16_f32 v40, v40, v41
	v_cvt_pk_bf16_f32 v41, v49, v50
	global_store_dwordx4 v[88:89], v[62:65], off nt
	v_lshlrev_b32_e32 v44, 1, v66
	s_cbranch_execnz .LBB0_54

.LBB0_54:
	ds_read2_b32 v[52:53], v86 offset0:8 offset1:41
	ds_read2_b32 v[50:51], v86 offset0:74 offset1:107
	ds_read2_b32 v[48:49], v86 offset0:140 offset1:173
	ds_read2_b32 v[46:47], v86 offset0:206 offset1:239
	global_store_dwordx4 v[54:55], v[38:41], off nt
	s_andn2_b64 vcc, exec, s[30:31]
	v_add_u32_e32 v45, s42, v73
	v_cndmask_b32_e64 v38, 0, 1, s[30:31]
	v_cmp_ne_u32_e64 s[0:1], 1, v38
	s_waitcnt lgkmcnt(3)
	v_cvt_pk_bf16_f32 v34, v52, v53
	s_waitcnt lgkmcnt(2)
	v_cvt_pk_bf16_f32 v35, v50, v51
	s_waitcnt lgkmcnt(1)
	v_cvt_pk_bf16_f32 v36, v48, v49
	s_waitcnt lgkmcnt(0)
	v_cvt_pk_bf16_f32 v37, v46, v47
	s_cbranch_vccnz .LBB0_66
	v_readlane_b32 s56, v243, 40
	v_readlane_b32 s58, v243, 42
	v_readlane_b32 s59, v243, 43
	v_and_b32_e32 v62, 48, v57
	v_and_b32_e32 v63, 15, v45
	v_lshl_add_u64 v[54:55], v[42:43], 2, s[58:59]
	global_load_dwordx4 v[38:41], v[54:55], off
	global_load_dwordx4 v[58:61], v[54:55], off offset:16
	v_lshlrev_b32_e32 v54, 2, v45
	v_and_b32_e32 v54, 0xffffffc0, v54
	v_add_u32_e32 v54, v54, v56
	v_ashrrev_i32_e32 v55, 31, v54
	v_lshlrev_b64 v[54:55], 6, v[54:55]
	v_or3_b32 v54, v54, v62, v63
	v_lshlrev_b64 v[54:55], 4, v[54:55]
	v_lshl_add_u64 v[88:89], s[2:3], 0, v[54:55]
	v_lshl_add_u64 v[54:55], s[10:11], 0, v[54:55]
	v_readlane_b32 s57, v243, 41
	v_readlane_b32 s60, v243, 44
	v_readlane_b32 s61, v243, 45
	v_readlane_b32 s62, v243, 46
	v_readlane_b32 s63, v243, 47
	v_readlane_b32 s64, v243, 48
	v_readlane_b32 s65, v243, 49
	v_readlane_b32 s66, v243, 50
	v_readlane_b32 s67, v243, 51
	v_readlane_b32 s68, v243, 52
	v_readlane_b32 s69, v243, 53
	v_readlane_b32 s70, v243, 54
	v_readlane_b32 s71, v243, 55
	s_waitcnt vmcnt(1)
	v_mul_f32_e32 v62, v52, v38
	v_mul_f32_e32 v63, v53, v39
	v_mul_f32_e32 v64, v50, v40
	v_mul_f32_e32 v65, v51, v41
	s_waitcnt vmcnt(0)
	v_mul_f32_e32 v90, v48, v58
	v_mul_f32_e32 v91, v49, v59
	v_mul_f32_e32 v92, v46, v60
	v_mul_f32_e32 v93, v47, v61
	v_cvt_pk_bf16_f32 v62, v62, v63
	v_cvt_pk_bf16_f32 v63, v64, v65
	v_cvt_pk_bf16_f32 v64, v90, v91
	v_cvt_pk_bf16_f32 v65, v92, v93
	s_nop 0
	v_lshlrev_b32_e32 v90, 16, v62
	v_and_b32_e32 v91, 0xffff0000, v62
	v_lshlrev_b32_e32 v92, 16, v63
	v_and_b32_e32 v93, 0xffff0000, v63
	v_lshlrev_b32_e32 v94, 16, v64
	v_and_b32_e32 v95, 0xffff0000, v64
	v_lshlrev_b32_e32 v96, 16, v65
	v_and_b32_e32 v97, 0xffff0000, v65
	v_fma_f32 v38, v52, v38, -v90
	v_fma_f32 v39, v53, v39, -v91
	v_fma_f32 v40, v50, v40, -v92
	v_fma_f32 v41, v51, v41, -v93
	v_fma_f32 v48, v48, v58, -v94
	v_fma_f32 v49, v49, v59, -v95
	v_fma_f32 v46, v46, v60, -v96
	v_fma_f32 v47, v47, v61, -v97
	v_cvt_pk_bf16_f32 v38, v38, v39
	v_cvt_pk_bf16_f32 v39, v40, v41
	v_cvt_pk_bf16_f32 v40, v48, v49
	v_cvt_pk_bf16_f32 v41, v46, v47
	global_store_dwordx4 v[88:89], v[62:65], off nt
	s_cbranch_execnz .LBB0_57

.LBB0_57:
	ds_read2_b32 v[52:53], v86 offset0:16 offset1:49
	ds_read2_b32 v[50:51], v86 offset0:82 offset1:115
	ds_read2_b32 v[48:49], v86 offset0:148 offset1:181
	ds_read2_b32 v[46:47], v86 offset0:214 offset1:247
	s_and_b64 vcc, exec, s[0:1]
	v_add_u32_e32 v45, s42, v72
	global_store_dwordx4 v[54:55], v[38:41], off nt
	s_waitcnt lgkmcnt(3)
	v_cvt_pk_bf16_f32 v34, v52, v53
	s_waitcnt lgkmcnt(2)
	v_cvt_pk_bf16_f32 v35, v50, v51
	s_waitcnt lgkmcnt(1)
	v_cvt_pk_bf16_f32 v36, v48, v49
	s_waitcnt lgkmcnt(0)
	v_cvt_pk_bf16_f32 v37, v46, v47
	s_cbranch_vccnz .LBB0_67
	v_readlane_b32 s56, v243, 40
	v_readlane_b32 s58, v243, 42
	v_readlane_b32 s59, v243, 43
	v_and_b32_e32 v62, 48, v57
	v_and_b32_e32 v63, 15, v45
	v_lshl_add_u64 v[54:55], v[42:43], 2, s[58:59]
	global_load_dwordx4 v[38:41], v[54:55], off
	global_load_dwordx4 v[58:61], v[54:55], off offset:16
	v_lshlrev_b32_e32 v54, 2, v45
	v_and_b32_e32 v54, 0xffffffc0, v54
	v_add_u32_e32 v54, v54, v56
	v_ashrrev_i32_e32 v55, 31, v54
	v_lshlrev_b64 v[54:55], 6, v[54:55]
	v_or3_b32 v54, v54, v62, v63
	v_lshlrev_b64 v[54:55], 4, v[54:55]
	v_lshl_add_u64 v[88:89], s[2:3], 0, v[54:55]
	v_lshl_add_u64 v[54:55], s[10:11], 0, v[54:55]
	v_readlane_b32 s57, v243, 41
	v_readlane_b32 s60, v243, 44
	v_readlane_b32 s61, v243, 45
	v_readlane_b32 s62, v243, 46
	v_readlane_b32 s63, v243, 47
	v_readlane_b32 s64, v243, 48
	v_readlane_b32 s65, v243, 49
	v_readlane_b32 s66, v243, 50
	v_readlane_b32 s67, v243, 51
	v_readlane_b32 s68, v243, 52
	v_readlane_b32 s69, v243, 53
	v_readlane_b32 s70, v243, 54
	v_readlane_b32 s71, v243, 55
	s_waitcnt vmcnt(1)
	v_mul_f32_e32 v62, v52, v38
	v_mul_f32_e32 v63, v53, v39
	v_mul_f32_e32 v64, v50, v40
	v_mul_f32_e32 v65, v51, v41
	s_waitcnt vmcnt(0)
	v_mul_f32_e32 v90, v48, v58
	v_mul_f32_e32 v91, v49, v59
	v_mul_f32_e32 v92, v46, v60
	v_mul_f32_e32 v93, v47, v61
	v_cvt_pk_bf16_f32 v62, v62, v63
	v_cvt_pk_bf16_f32 v63, v64, v65
	v_cvt_pk_bf16_f32 v64, v90, v91
	v_cvt_pk_bf16_f32 v65, v92, v93
	s_nop 0
	v_lshlrev_b32_e32 v90, 16, v62
	v_and_b32_e32 v91, 0xffff0000, v62
	v_lshlrev_b32_e32 v92, 16, v63
	v_and_b32_e32 v93, 0xffff0000, v63
	v_lshlrev_b32_e32 v94, 16, v64
	v_and_b32_e32 v95, 0xffff0000, v64
	v_lshlrev_b32_e32 v96, 16, v65
	v_and_b32_e32 v97, 0xffff0000, v65
	v_fma_f32 v38, v52, v38, -v90
	v_fma_f32 v39, v53, v39, -v91
	v_fma_f32 v40, v50, v40, -v92
	v_fma_f32 v41, v51, v41, -v93
	v_fma_f32 v48, v48, v58, -v94
	v_fma_f32 v49, v49, v59, -v95
	v_fma_f32 v46, v46, v60, -v96
	v_fma_f32 v47, v47, v61, -v97
	v_cvt_pk_bf16_f32 v38, v38, v39
	v_cvt_pk_bf16_f32 v39, v40, v41
	v_cvt_pk_bf16_f32 v40, v48, v49
	v_cvt_pk_bf16_f32 v41, v46, v47
	global_store_dwordx4 v[88:89], v[62:65], off nt
	s_cbranch_execnz .LBB0_60

.LBB0_60:
	ds_read2_b32 v[52:53], v86 offset0:24 offset1:57
	ds_read2_b32 v[50:51], v86 offset0:90 offset1:123
	ds_read2_b32 v[48:49], v86 offset0:156 offset1:189
	ds_read2_b32 v[46:47], v86 offset0:222 offset1:255
	s_and_b64 vcc, exec, s[0:1]
	v_add_u32_e32 v45, s42, v71
	global_store_dwordx4 v[54:55], v[38:41], off nt
	s_waitcnt lgkmcnt(3)
	v_cvt_pk_bf16_f32 v34, v52, v53
	s_waitcnt lgkmcnt(2)
	v_cvt_pk_bf16_f32 v35, v50, v51
	s_waitcnt lgkmcnt(1)
	v_cvt_pk_bf16_f32 v36, v48, v49
	s_waitcnt lgkmcnt(0)
	v_cvt_pk_bf16_f32 v37, v46, v47
	s_cbranch_vccnz .LBB0_68
	v_readlane_b32 s56, v243, 40
	v_readlane_b32 s58, v243, 42
	v_readlane_b32 s59, v243, 43
	v_and_b32_e32 v54, 48, v57
	v_and_b32_e32 v55, 15, v45
	v_lshl_add_u64 v[42:43], v[42:43], 2, s[58:59]
	global_load_dwordx4 v[38:41], v[42:43], off
	global_load_dwordx4 v[58:61], v[42:43], off offset:16
	v_lshlrev_b32_e32 v42, 2, v45
	v_and_b32_e32 v42, 0xffffffc0, v42
	v_add_u32_e32 v42, v42, v56
	v_ashrrev_i32_e32 v43, 31, v42
	v_lshlrev_b64 v[42:43], 6, v[42:43]
	v_or3_b32 v42, v42, v54, v55
	v_lshlrev_b64 v[42:43], 4, v[42:43]
	v_lshl_add_u64 v[62:63], s[2:3], 0, v[42:43]
	v_lshl_add_u64 v[42:43], s[10:11], 0, v[42:43]
	v_readlane_b32 s57, v243, 41
	v_readlane_b32 s60, v243, 44
	v_readlane_b32 s61, v243, 45
	v_readlane_b32 s62, v243, 46
	v_readlane_b32 s63, v243, 47
	v_readlane_b32 s64, v243, 48
	v_readlane_b32 s65, v243, 49
	v_readlane_b32 s66, v243, 50
	v_readlane_b32 s67, v243, 51
	v_readlane_b32 s68, v243, 52
	v_readlane_b32 s69, v243, 53
	v_readlane_b32 s70, v243, 54
	v_readlane_b32 s71, v243, 55
	s_waitcnt vmcnt(1)
	v_mul_f32_e32 v54, v52, v38
	v_mul_f32_e32 v55, v53, v39
	v_mul_f32_e32 v56, v50, v40
	v_mul_f32_e32 v57, v51, v41
	s_waitcnt vmcnt(0)
	v_mul_f32_e32 v64, v48, v58
	v_mul_f32_e32 v65, v49, v59
	v_mul_f32_e32 v88, v46, v60
	v_mul_f32_e32 v89, v47, v61
	v_cvt_pk_bf16_f32 v54, v54, v55
	v_cvt_pk_bf16_f32 v55, v56, v57
	v_cvt_pk_bf16_f32 v56, v64, v65
	v_cvt_pk_bf16_f32 v57, v88, v89
	s_nop 0
	v_lshlrev_b32_e32 v64, 16, v54
	v_and_b32_e32 v65, 0xffff0000, v54
	v_lshlrev_b32_e32 v88, 16, v55
	v_and_b32_e32 v89, 0xffff0000, v55
	v_lshlrev_b32_e32 v90, 16, v56
	v_and_b32_e32 v91, 0xffff0000, v56
	v_lshlrev_b32_e32 v92, 16, v57
	v_and_b32_e32 v93, 0xffff0000, v57
	v_fma_f32 v38, v52, v38, -v64
	v_fma_f32 v39, v53, v39, -v65
	v_fma_f32 v40, v50, v40, -v88
	v_fma_f32 v41, v51, v41, -v89
	v_fma_f32 v48, v48, v58, -v90
	v_fma_f32 v49, v49, v59, -v91
	v_fma_f32 v46, v46, v60, -v92
	v_fma_f32 v47, v47, v61, -v93
	v_cvt_pk_bf16_f32 v38, v38, v39
	v_cvt_pk_bf16_f32 v39, v40, v41
	v_cvt_pk_bf16_f32 v40, v48, v49
	v_cvt_pk_bf16_f32 v41, v46, v47
	global_store_dwordx4 v[62:63], v[54:57], off nt
	s_cbranch_execnz .LBB0_63

.LBB0_71:
	s_waitcnt vmcnt(7)
	v_add_u32_e32 v34, v85, v83
	ds_write2_b32 v34, v30, v31 offset1:1
	ds_write2_b32 v34, v32, v33 offset0:2 offset1:3
	v_add_u32_e32 v30, v85, v76
	ds_write2_b32 v30, v18, v19 offset1:1
	ds_write2_b32 v30, v20, v21 offset0:2 offset1:3
	v_add_u32_e32 v18, v85, v77
	ds_write2_b32 v18, v26, v27 offset1:1
	ds_write2_b32 v18, v28, v29 offset0:2 offset1:3
	v_add_u32_e32 v18, v85, v78
	ds_write2_b32 v18, v10, v11 offset1:1
	ds_write2_b32 v18, v12, v13 offset0:2 offset1:3
	v_add_u32_e32 v10, 0x1080, v34
	ds_write2_b32 v10, v22, v23 offset1:1
	v_add_u32_e32 v10, 0x1088, v34
	ds_write2_b32 v10, v24, v25 offset1:1
	v_add_u32_e32 v10, 0x14a0, v34
	s_waitcnt vmcnt(6)
	ds_write2_b32 v10, v6, v7 offset1:1
	v_add_u32_e32 v6, 0x14a8, v34
	ds_write2_b32 v6, v8, v9 offset1:1
	v_add_u32_e32 v6, 0x18c0, v34
	s_waitcnt vmcnt(5)
	ds_write2_b32 v6, v14, v15 offset1:1
	v_add_u32_e32 v6, 0x18c8, v34
	ds_write2_b32 v6, v16, v17 offset1:1
	v_add_u32_e32 v6, 0x1ce0, v34
	s_waitcnt vmcnt(4)
	ds_write2_b32 v6, v2, v3 offset1:1
	v_add_u32_e32 v2, 0x1ce8, v34
	ds_write2_b32 v2, v4, v5 offset1:1
	s_waitcnt lgkmcnt(0)
	v_add3_u32 v24, s43, v82, v84
	ds_read2_b32 v[14:15], v24 offset1:33
	ds_read2_b32 v[12:13], v24 offset0:66 offset1:99
	ds_read2_b32 v[8:9], v24 offset0:132 offset1:165
	ds_read2_b32 v[6:7], v24 offset0:198 offset1:231
	s_cmp_lg_u64 s[12:13], 0
	s_cselect_b64 s[2:3], -1, 0
	v_add_u32_e32 v10, s4, v66
	s_mov_b64 s[0:1], 0
	s_and_b64 vcc, exec, s[2:3]
	v_add_u32_e32 v16, s36, v74
	v_ashrrev_i32_e32 v22, 5, v10
	v_lshlrev_b32_e32 v23, 1, v10
	v_ashrrev_i32_e32 v11, 31, v10
	s_waitcnt lgkmcnt(3)
	v_cvt_pk_bf16_f32 v2, v14, v15
	s_waitcnt lgkmcnt(2)
	v_cvt_pk_bf16_f32 v3, v12, v13
	s_waitcnt lgkmcnt(1)
	v_cvt_pk_bf16_f32 v4, v8, v9
	s_waitcnt lgkmcnt(0)
	v_cvt_pk_bf16_f32 v5, v6, v7
	s_cbranch_vccz .LBB0_122
	v_readlane_b32 s44, v243, 40
	v_readlane_b32 s46, v243, 42
	v_readlane_b32 s47, v243, 43
	v_lshlrev_b32_e32 v17, 2, v16
	v_and_b32_e32 v17, 0xffffffc0, v17
	v_lshl_add_u64 v[26:27], v[10:11], 2, s[46:47]
	global_load_dwordx4 v[18:21], v[26:27], off
	s_nop 0
	global_load_dwordx4 v[26:29], v[26:27], off offset:16
	v_add_u32_e32 v30, v17, v22
	v_ashrrev_i32_e32 v31, 31, v30
	v_and_b32_e32 v25, 48, v23
	v_and_b32_e32 v32, 15, v16
	v_lshlrev_b64 v[30:31], 6, v[30:31]
	v_or3_b32 v30, v30, v25, v32
	v_lshlrev_b64 v[34:35], 4, v[30:31]
	v_lshl_add_u64 v[36:37], s[8:9], 0, v[34:35]
	v_readlane_b32 s45, v243, 41
	v_readlane_b32 s48, v243, 44
	v_readlane_b32 s49, v243, 45
	v_readlane_b32 s50, v243, 46
	v_readlane_b32 s51, v243, 47
	v_readlane_b32 s52, v243, 48
	v_readlane_b32 s53, v243, 49
	v_readlane_b32 s54, v243, 50
	v_readlane_b32 s55, v243, 51
	v_readlane_b32 s56, v243, 52
	v_readlane_b32 s57, v243, 53
	v_readlane_b32 s58, v243, 54
	v_readlane_b32 s59, v243, 55
	s_waitcnt vmcnt(1)
	v_mul_f32_e32 v31, v12, v20
	v_mul_f32_e32 v32, v13, v21
	s_waitcnt vmcnt(0)
	v_mul_f32_e32 v33, v8, v26
	v_mul_f32_e32 v40, v7, v29
	v_mul_f32_e32 v17, v14, v18
	v_mul_f32_e32 v25, v15, v19
	v_mul_f32_e32 v38, v9, v27
	v_mul_f32_e32 v39, v6, v28
	v_cvt_pk_bf16_f32 v30, v17, v25
	v_cvt_pk_bf16_f32 v31, v31, v32
	v_cvt_pk_bf16_f32 v32, v33, v38
	v_cvt_pk_bf16_f32 v33, v39, v40
	s_nop 0
	v_lshlrev_b32_e32 v40, 16, v32
	v_and_b32_e32 v41, 0xffff0000, v32
	v_lshlrev_b32_e32 v17, 16, v30
	v_and_b32_e32 v25, 0xffff0000, v30
	v_lshlrev_b32_e32 v38, 16, v31
	v_and_b32_e32 v39, 0xffff0000, v31
	v_lshlrev_b32_e32 v42, 16, v33
	v_and_b32_e32 v43, 0xffff0000, v33
	v_fma_f32 v8, v8, v26, -v40
	v_fma_f32 v9, v9, v27, -v41
	v_fma_f32 v14, v14, v18, -v17
	v_fma_f32 v15, v15, v19, -v25
	v_fma_f32 v12, v12, v20, -v38
	v_fma_f32 v13, v13, v21, -v39
	v_fma_f32 v17, v6, v28, -v42
	v_fma_f32 v18, v7, v29, -v43
	v_cvt_pk_bf16_f32 v6, v14, v15
	v_cvt_pk_bf16_f32 v7, v12, v13
	v_cvt_pk_bf16_f32 v8, v8, v9
	v_cvt_pk_bf16_f32 v9, v17, v18
	global_store_dwordx4 v[36:37], v[30:33], off nt
	v_lshl_add_u64 v[20:21], s[12:13], 0, v[34:35]
	s_andn2_b64 vcc, exec, s[0:1]
	s_cbranch_vccnz .LBB0_74

.LBB0_74:
	ds_read2_b32 v[18:19], v24 offset0:8 offset1:41
	ds_read2_b32 v[16:17], v24 offset0:74 offset1:107
	ds_read2_b32 v[14:15], v24 offset0:140 offset1:173
	ds_read2_b32 v[12:13], v24 offset0:206 offset1:239
	global_store_dwordx4 v[20:21], v[6:9], off nt
	s_andn2_b64 vcc, exec, s[2:3]
	v_add_u32_e32 v25, s36, v73
	v_cndmask_b32_e64 v6, 0, 1, s[2:3]
	v_cmp_ne_u32_e64 s[0:1], 1, v6
	s_waitcnt lgkmcnt(3)
	v_cvt_pk_bf16_f32 v2, v18, v19
	s_waitcnt lgkmcnt(2)
	v_cvt_pk_bf16_f32 v3, v16, v17
	s_waitcnt lgkmcnt(1)
	v_cvt_pk_bf16_f32 v4, v14, v15
	s_waitcnt lgkmcnt(0)
	v_cvt_pk_bf16_f32 v5, v12, v13
	s_cbranch_vccnz .LBB0_123
	v_readlane_b32 s44, v243, 40
	v_readlane_b32 s46, v243, 42
	v_readlane_b32 s47, v243, 43
	v_and_b32_e32 v30, 48, v23
	v_and_b32_e32 v31, 15, v25
	v_lshl_add_u64 v[20:21], v[10:11], 2, s[46:47]
	global_load_dwordx4 v[6:9], v[20:21], off
	global_load_dwordx4 v[26:29], v[20:21], off offset:16
	v_lshlrev_b32_e32 v20, 2, v25
	v_and_b32_e32 v20, 0xffffffc0, v20
	v_add_u32_e32 v20, v20, v22
	v_ashrrev_i32_e32 v21, 31, v20
	v_lshlrev_b64 v[20:21], 6, v[20:21]
	v_or3_b32 v20, v20, v30, v31
	v_lshlrev_b64 v[20:21], 4, v[20:21]
	v_lshl_add_u64 v[34:35], s[8:9], 0, v[20:21]
	v_lshl_add_u64 v[20:21], s[12:13], 0, v[20:21]
	v_readlane_b32 s45, v243, 41
	v_readlane_b32 s48, v243, 44
	v_readlane_b32 s49, v243, 45
	v_readlane_b32 s50, v243, 46
	v_readlane_b32 s51, v243, 47
	v_readlane_b32 s52, v243, 48
	v_readlane_b32 s53, v243, 49
	v_readlane_b32 s54, v243, 50
	v_readlane_b32 s55, v243, 51
	v_readlane_b32 s56, v243, 52
	v_readlane_b32 s57, v243, 53
	v_readlane_b32 s58, v243, 54
	v_readlane_b32 s59, v243, 55
	s_waitcnt vmcnt(1)
	v_mul_f32_e32 v30, v18, v6
	v_mul_f32_e32 v31, v19, v7
	v_mul_f32_e32 v32, v16, v8
	v_mul_f32_e32 v33, v17, v9
	s_waitcnt vmcnt(0)
	v_mul_f32_e32 v36, v14, v26
	v_mul_f32_e32 v37, v15, v27
	v_mul_f32_e32 v38, v12, v28
	v_mul_f32_e32 v39, v13, v29
	v_cvt_pk_bf16_f32 v30, v30, v31
	v_cvt_pk_bf16_f32 v31, v32, v33
	v_cvt_pk_bf16_f32 v32, v36, v37
	v_cvt_pk_bf16_f32 v33, v38, v39
	s_nop 0
	v_lshlrev_b32_e32 v36, 16, v30
	v_and_b32_e32 v37, 0xffff0000, v30
	v_lshlrev_b32_e32 v38, 16, v31
	v_and_b32_e32 v39, 0xffff0000, v31
	v_lshlrev_b32_e32 v40, 16, v32
	v_and_b32_e32 v41, 0xffff0000, v32
	v_lshlrev_b32_e32 v42, 16, v33
	v_and_b32_e32 v43, 0xffff0000, v33
	v_fma_f32 v6, v18, v6, -v36
	v_fma_f32 v7, v19, v7, -v37
	v_fma_f32 v8, v16, v8, -v38
	v_fma_f32 v9, v17, v9, -v39
	v_fma_f32 v14, v14, v26, -v40
	v_fma_f32 v15, v15, v27, -v41
	v_fma_f32 v12, v12, v28, -v42
	v_fma_f32 v13, v13, v29, -v43
	v_cvt_pk_bf16_f32 v6, v6, v7
	v_cvt_pk_bf16_f32 v7, v8, v9
	v_cvt_pk_bf16_f32 v8, v14, v15
	v_cvt_pk_bf16_f32 v9, v12, v13
	global_store_dwordx4 v[34:35], v[30:33], off nt
	s_cbranch_execnz .LBB0_77

.LBB0_77:
	ds_read2_b32 v[18:19], v24 offset0:16 offset1:49
	ds_read2_b32 v[16:17], v24 offset0:82 offset1:115
	ds_read2_b32 v[14:15], v24 offset0:148 offset1:181
	ds_read2_b32 v[12:13], v24 offset0:214 offset1:247
	s_and_b64 vcc, exec, s[0:1]
	v_add_u32_e32 v25, s36, v72
	global_store_dwordx4 v[20:21], v[6:9], off nt
	s_waitcnt lgkmcnt(3)
	v_cvt_pk_bf16_f32 v2, v18, v19
	s_waitcnt lgkmcnt(2)
	v_cvt_pk_bf16_f32 v3, v16, v17
	s_waitcnt lgkmcnt(1)
	v_cvt_pk_bf16_f32 v4, v14, v15
	s_waitcnt lgkmcnt(0)
	v_cvt_pk_bf16_f32 v5, v12, v13
	s_cbranch_vccnz .LBB0_124
	v_readlane_b32 s44, v243, 40
	v_readlane_b32 s46, v243, 42
	v_readlane_b32 s47, v243, 43
	v_and_b32_e32 v30, 48, v23
	v_and_b32_e32 v31, 15, v25
	v_lshl_add_u64 v[20:21], v[10:11], 2, s[46:47]
	global_load_dwordx4 v[6:9], v[20:21], off
	global_load_dwordx4 v[26:29], v[20:21], off offset:16
	v_lshlrev_b32_e32 v20, 2, v25
	v_and_b32_e32 v20, 0xffffffc0, v20
	v_add_u32_e32 v20, v20, v22
	v_ashrrev_i32_e32 v21, 31, v20
	v_lshlrev_b64 v[20:21], 6, v[20:21]
	v_or3_b32 v20, v20, v30, v31
	v_lshlrev_b64 v[20:21], 4, v[20:21]
	v_lshl_add_u64 v[34:35], s[8:9], 0, v[20:21]
	v_lshl_add_u64 v[20:21], s[12:13], 0, v[20:21]
	v_readlane_b32 s45, v243, 41
	v_readlane_b32 s48, v243, 44
	v_readlane_b32 s49, v243, 45
	v_readlane_b32 s50, v243, 46
	v_readlane_b32 s51, v243, 47
	v_readlane_b32 s52, v243, 48
	v_readlane_b32 s53, v243, 49
	v_readlane_b32 s54, v243, 50
	v_readlane_b32 s55, v243, 51
	v_readlane_b32 s56, v243, 52
	v_readlane_b32 s57, v243, 53
	v_readlane_b32 s58, v243, 54
	v_readlane_b32 s59, v243, 55
	s_waitcnt vmcnt(1)
	v_mul_f32_e32 v30, v18, v6
	v_mul_f32_e32 v31, v19, v7
	v_mul_f32_e32 v32, v16, v8
	v_mul_f32_e32 v33, v17, v9
	s_waitcnt vmcnt(0)
	v_mul_f32_e32 v36, v14, v26
	v_mul_f32_e32 v37, v15, v27
	v_mul_f32_e32 v38, v12, v28
	v_mul_f32_e32 v39, v13, v29
	v_cvt_pk_bf16_f32 v30, v30, v31
	v_cvt_pk_bf16_f32 v31, v32, v33
	v_cvt_pk_bf16_f32 v32, v36, v37
	v_cvt_pk_bf16_f32 v33, v38, v39
	s_nop 0
	v_lshlrev_b32_e32 v36, 16, v30
	v_and_b32_e32 v37, 0xffff0000, v30
	v_lshlrev_b32_e32 v38, 16, v31
	v_and_b32_e32 v39, 0xffff0000, v31
	v_lshlrev_b32_e32 v40, 16, v32
	v_and_b32_e32 v41, 0xffff0000, v32
	v_lshlrev_b32_e32 v42, 16, v33
	v_and_b32_e32 v43, 0xffff0000, v33
	v_fma_f32 v6, v18, v6, -v36
	v_fma_f32 v7, v19, v7, -v37
	v_fma_f32 v8, v16, v8, -v38
	v_fma_f32 v9, v17, v9, -v39
	v_fma_f32 v14, v14, v26, -v40
	v_fma_f32 v15, v15, v27, -v41
	v_fma_f32 v12, v12, v28, -v42
	v_fma_f32 v13, v13, v29, -v43
	v_cvt_pk_bf16_f32 v6, v6, v7
	v_cvt_pk_bf16_f32 v7, v8, v9
	v_cvt_pk_bf16_f32 v8, v14, v15
	v_cvt_pk_bf16_f32 v9, v12, v13
	global_store_dwordx4 v[34:35], v[30:33], off nt
	s_cbranch_execnz .LBB0_80

.LBB0_80:
	ds_read2_b32 v[18:19], v24 offset0:24 offset1:57
	ds_read2_b32 v[16:17], v24 offset0:90 offset1:123
	ds_read2_b32 v[14:15], v24 offset0:156 offset1:189
	ds_read2_b32 v[12:13], v24 offset0:222 offset1:255
	global_store_dwordx4 v[20:21], v[6:9], off nt
	s_and_b64 vcc, exec, s[0:1]
	v_add_u32_e32 v20, s36, v71
	s_waitcnt lgkmcnt(3)
	v_cvt_pk_bf16_f32 v2, v18, v19
	s_waitcnt lgkmcnt(2)
	v_cvt_pk_bf16_f32 v3, v16, v17
	s_waitcnt lgkmcnt(1)
	v_cvt_pk_bf16_f32 v4, v14, v15
	s_waitcnt lgkmcnt(0)
	v_cvt_pk_bf16_f32 v5, v12, v13
	s_cbranch_vccnz .LBB0_125
	v_readlane_b32 s44, v243, 40
	v_readlane_b32 s46, v243, 42
	v_readlane_b32 s47, v243, 43
	v_and_b32_e32 v21, 48, v23
	v_and_b32_e32 v23, 15, v20
	v_lshl_add_u64 v[10:11], v[10:11], 2, s[46:47]
	global_load_dwordx4 v[6:9], v[10:11], off
	global_load_dwordx4 v[24:27], v[10:11], off offset:16
	v_lshlrev_b32_e32 v10, 2, v20
	v_and_b32_e32 v10, 0xffffffc0, v10
	v_add_u32_e32 v10, v10, v22
	v_ashrrev_i32_e32 v11, 31, v10
	v_lshlrev_b64 v[10:11], 6, v[10:11]
	v_or3_b32 v10, v10, v21, v23
	v_lshlrev_b64 v[10:11], 4, v[10:11]
	v_lshl_add_u64 v[22:23], s[8:9], 0, v[10:11]
	v_lshl_add_u64 v[10:11], s[12:13], 0, v[10:11]
	v_readlane_b32 s45, v243, 41
	v_readlane_b32 s48, v243, 44
	v_readlane_b32 s49, v243, 45
	v_readlane_b32 s50, v243, 46
	v_readlane_b32 s51, v243, 47
	v_readlane_b32 s52, v243, 48
	v_readlane_b32 s53, v243, 49
	v_readlane_b32 s54, v243, 50
	v_readlane_b32 s55, v243, 51
	v_readlane_b32 s56, v243, 52
	v_readlane_b32 s57, v243, 53
	v_readlane_b32 s58, v243, 54
	v_readlane_b32 s59, v243, 55
	s_waitcnt vmcnt(1)
	v_mul_f32_e32 v21, v18, v6
	v_mul_f32_e32 v28, v19, v7
	v_mul_f32_e32 v29, v16, v8
	v_mul_f32_e32 v30, v17, v9
	s_waitcnt vmcnt(0)
	v_mul_f32_e32 v31, v14, v24
	v_mul_f32_e32 v32, v15, v25
	v_mul_f32_e32 v33, v12, v26
	v_mul_f32_e32 v34, v13, v27
	v_cvt_pk_bf16_f32 v28, v21, v28
	v_cvt_pk_bf16_f32 v29, v29, v30
	v_cvt_pk_bf16_f32 v30, v31, v32
	v_cvt_pk_bf16_f32 v31, v33, v34
	s_nop 0
	v_lshlrev_b32_e32 v21, 16, v28
	v_and_b32_e32 v32, 0xffff0000, v28
	v_lshlrev_b32_e32 v33, 16, v29
	v_and_b32_e32 v34, 0xffff0000, v29
	v_lshlrev_b32_e32 v35, 16, v30
	v_and_b32_e32 v36, 0xffff0000, v30
	v_lshlrev_b32_e32 v37, 16, v31
	v_and_b32_e32 v38, 0xffff0000, v31
	v_fma_f32 v6, v18, v6, -v21
	v_fma_f32 v7, v19, v7, -v32
	v_fma_f32 v8, v16, v8, -v33
	v_fma_f32 v9, v17, v9, -v34
	v_fma_f32 v14, v14, v24, -v35
	v_fma_f32 v15, v15, v25, -v36
	v_fma_f32 v12, v12, v26, -v37
	v_fma_f32 v13, v13, v27, -v38
	v_cvt_pk_bf16_f32 v6, v6, v7
	v_cvt_pk_bf16_f32 v7, v8, v9
	v_cvt_pk_bf16_f32 v8, v14, v15
	v_cvt_pk_bf16_f32 v9, v12, v13
	global_store_dwordx4 v[22:23], v[28:31], off nt
	s_cbranch_execnz .LBB0_83

.LBB0_457:
	v_add_u32_e32 v161, 0x420, v160
	v_add_u32_e32 v162, 0x428, v160
	v_add_u32_e32 v163, 0x840, v160
	v_add_u32_e32 v164, 0x848, v160
	v_add_u32_e32 v165, 0xc60, v160
	v_add_u32_e32 v166, 0xc68, v160
	v_add_u32_e32 v167, 0x1080, v160
	v_add_u32_e32 v168, 0x1088, v160
	v_add_u32_e32 v169, 0x14a0, v160
	v_add_u32_e32 v170, 0x14a8, v160
	v_add_u32_e32 v171, 0x18c0, v160
	v_add_u32_e32 v172, 0x18c8, v160
	v_add_u32_e32 v173, 0x1ce0, v160
	v_add_u32_e32 v174, 0x1ce8, v160
	s_waitcnt vmcnt(0)
	ds_write2_b32 v160, v8, v9 offset1:1
	ds_write2_b32 v160, v10, v11 offset0:2 offset1:3
	ds_write2_b32 v161, v4, v5 offset1:1
	ds_write2_b32 v162, v6, v7 offset1:1
	ds_write2_b32 v163, v16, v17 offset1:1
	ds_write2_b32 v164, v18, v19 offset1:1
	ds_write2_b32 v165, v12, v13 offset1:1
	ds_write2_b32 v166, v14, v15 offset1:1
	ds_write2_b32 v167, v24, v25 offset1:1
	ds_write2_b32 v168, v26, v27 offset1:1
	ds_write2_b32 v169, v20, v21 offset1:1
	ds_write2_b32 v170, v22, v23 offset1:1
	ds_write2_b32 v171, v32, v33 offset1:1
	ds_write2_b32 v172, v34, v35 offset1:1
	ds_write2_b32 v173, v28, v29 offset1:1
	ds_write2_b32 v174, v30, v31 offset1:1
	s_waitcnt lgkmcnt(0)
	ds_read2_b32 v[136:137], v155 offset1:33
	ds_read2_b32 v[150:151], v155 offset0:66 offset1:99
	ds_read2_b32 v[138:139], v155 offset0:132 offset1:165
	ds_read2_b32 v[148:149], v155 offset0:198 offset1:231
	s_cmp_lg_u64 s[10:11], 0
	s_cselect_b64 s[40:41], -1, 0
	s_and_b64 vcc, exec, s[40:41]
	v_add_u32_e32 v2, s4, v1
	v_add_u32_e32 v146, s6, v142
	s_waitcnt lgkmcnt(0)
	v_cvt_pk_bf16_f32 v132, v136, v137
	v_cvt_pk_bf16_f32 v133, v150, v151
	v_cvt_pk_bf16_f32 v134, v138, v139
	v_cvt_pk_bf16_f32 v135, v148, v149
	s_cbranch_vccz .LBB0_506
	v_lshlrev_b32_e32 v144, 2, v2
	v_and_b32_e32 v144, 0xffffffc0, v144
	v_ashrrev_i32_e32 v145, 5, v146
	v_add_u32_e32 v144, v145, v144
	v_ashrrev_i32_e32 v145, 31, v144
	v_lshlrev_b32_e32 v147, 1, v146
	v_lshlrev_b64 v[144:145], 6, v[144:145]
	v_and_b32_e32 v147, 48, v147
	v_and_b32_e32 v152, 15, v2
	v_or3_b32 v144, v144, v147, v152
	v_ashrrev_i32_e32 v147, 31, v146
	v_lshl_add_u64 v[152:153], v[146:147], 2, s[12:13]
	global_load_dwordx4 v[176:179], v[152:153], off offset:16
	global_load_dwordx4 v[180:183], v[152:153], off
	v_lshlrev_b64 v[144:145], 4, v[144:145]
	s_waitcnt vmcnt(1)
	v_mul_f32_e32 v186, v138, v176
	s_waitcnt vmcnt(0)
	v_mul_f32_e32 v147, v136, v180
	v_mul_f32_e32 v152, v137, v181
	v_cvt_pk_bf16_f32 v184, v147, v152
	v_mul_f32_e32 v187, v139, v177
	v_lshlrev_b32_e32 v147, 16, v184
	v_fma_f32 v136, v136, v180, -v147
	v_and_b32_e32 v147, 0xffff0000, v184
	v_fma_f32 v137, v137, v181, -v147
	v_mul_f32_e32 v153, v150, v182
	v_mul_f32_e32 v175, v151, v183
	v_mul_f32_e32 v188, v148, v178
	v_mul_f32_e32 v189, v149, v179
	v_cvt_pk_bf16_f32 v185, v153, v175
	v_cvt_pk_bf16_f32 v186, v186, v187
	v_cvt_pk_bf16_f32 v187, v188, v189
	v_cvt_pk_bf16_f32 v136, v136, v137
	s_nop 0
	v_lshlrev_b32_e32 v137, 16, v185
	v_and_b32_e32 v147, 0xffff0000, v185
	v_fma_f32 v137, v150, v182, -v137
	v_fma_f32 v147, v151, v183, -v147
	v_cvt_pk_bf16_f32 v137, v137, v147
	v_lshlrev_b32_e32 v147, 16, v186
	v_fma_f32 v138, v138, v176, -v147
	v_and_b32_e32 v147, 0xffff0000, v186
	v_fma_f32 v139, v139, v177, -v147
	v_cvt_pk_bf16_f32 v138, v138, v139
	v_lshlrev_b32_e32 v139, 16, v187
	v_and_b32_e32 v147, 0xffff0000, v187
	v_fma_f32 v139, v148, v178, -v139
	v_fma_f32 v147, v149, v179, -v147
	v_lshl_add_u64 v[148:149], s[8:9], 0, v[144:145]
	v_cvt_pk_bf16_f32 v139, v139, v147
	global_store_dwordx4 v[148:149], v[184:187], off nt
	v_lshl_add_u64 v[148:149], s[10:11], 0, v[144:145]
	v_lshlrev_b32_e32 v144, 1, v142
	s_cbranch_execnz .LBB0_460

.LBB0_460:
	global_store_dwordx4 v[148:149], v[136:139], off nt
	ds_read2_b32 v[136:137], v155 offset0:8 offset1:41
	ds_read2_b32 v[152:153], v155 offset0:74 offset1:107
	ds_read2_b32 v[138:139], v155 offset0:140 offset1:173
	ds_read2_b32 v[150:151], v155 offset0:206 offset1:239
	v_cndmask_b32_e64 v2, 0, 1, s[40:41]
	v_cmp_ne_u32_e64 s[2:3], 1, v2
	s_andn2_b64 vcc, exec, s[40:41]
	v_add_u32_e32 v2, s4, v141
	s_waitcnt lgkmcnt(3)
	v_cvt_pk_bf16_f32 v132, v136, v137
	s_waitcnt lgkmcnt(2)
	v_cvt_pk_bf16_f32 v133, v152, v153
	s_waitcnt lgkmcnt(1)
	v_cvt_pk_bf16_f32 v134, v138, v139
	s_waitcnt lgkmcnt(0)
	v_cvt_pk_bf16_f32 v135, v150, v151
	s_cbranch_vccnz .LBB0_507
	v_lshlrev_b32_e32 v145, 2, v2
	v_and_b32_e32 v145, 0xffffffc0, v145
	v_ashrrev_i32_e32 v147, 5, v146
	v_add_u32_e32 v148, v147, v145
	v_ashrrev_i32_e32 v149, 31, v148
	v_lshlrev_b32_e32 v145, 1, v146
	v_lshlrev_b64 v[148:149], 6, v[148:149]
	v_and_b32_e32 v145, 48, v145
	v_and_b32_e32 v147, 15, v2
	v_or3_b32 v148, v148, v145, v147
	v_ashrrev_i32_e32 v147, 31, v146
	v_lshl_add_u64 v[180:181], v[146:147], 2, s[12:13]
	global_load_dwordx4 v[176:179], v[180:181], off offset:16
	s_nop 0
	global_load_dwordx4 v[180:183], v[180:181], off
	v_lshlrev_b64 v[148:149], 4, v[148:149]
	s_waitcnt vmcnt(1)
	v_mul_f32_e32 v186, v138, v176
	s_waitcnt vmcnt(0)
	v_mul_f32_e32 v145, v136, v180
	v_mul_f32_e32 v147, v137, v181
	v_cvt_pk_bf16_f32 v184, v145, v147
	v_mul_f32_e32 v185, v153, v183
	v_lshlrev_b32_e32 v145, 16, v184
	v_fma_f32 v136, v136, v180, -v145
	v_and_b32_e32 v145, 0xffff0000, v184
	v_mul_f32_e32 v187, v139, v177
	v_fma_f32 v137, v137, v181, -v145
	v_mul_f32_e32 v175, v152, v182
	v_mul_f32_e32 v188, v150, v178
	v_mul_f32_e32 v189, v151, v179
	v_cvt_pk_bf16_f32 v185, v175, v185
	v_cvt_pk_bf16_f32 v186, v186, v187
	v_cvt_pk_bf16_f32 v187, v188, v189
	v_cvt_pk_bf16_f32 v136, v136, v137
	s_nop 0
	v_lshlrev_b32_e32 v137, 16, v185
	v_and_b32_e32 v145, 0xffff0000, v185
	v_fma_f32 v137, v152, v182, -v137
	v_fma_f32 v145, v153, v183, -v145
	v_cvt_pk_bf16_f32 v137, v137, v145
	v_lshlrev_b32_e32 v145, 16, v186
	v_fma_f32 v138, v138, v176, -v145
	v_and_b32_e32 v145, 0xffff0000, v186
	v_fma_f32 v139, v139, v177, -v145
	v_cvt_pk_bf16_f32 v138, v138, v139
	v_lshlrev_b32_e32 v139, 16, v187
	v_and_b32_e32 v145, 0xffff0000, v187
	v_fma_f32 v139, v150, v178, -v139
	v_fma_f32 v145, v151, v179, -v145
	v_lshl_add_u64 v[150:151], s[8:9], 0, v[148:149]
	v_lshl_add_u64 v[148:149], s[10:11], 0, v[148:149]
	v_cvt_pk_bf16_f32 v139, v139, v145
	global_store_dwordx4 v[150:151], v[184:187], off nt
	s_cbranch_execnz .LBB0_463

.LBB0_463:
	global_store_dwordx4 v[148:149], v[136:139], off nt
	ds_read2_b32 v[136:137], v155 offset0:16 offset1:49
	ds_read2_b32 v[152:153], v155 offset0:82 offset1:115
	ds_read2_b32 v[138:139], v155 offset0:148 offset1:181
	ds_read2_b32 v[150:151], v155 offset0:214 offset1:247
	s_and_b64 vcc, exec, s[2:3]
	v_add_u32_e32 v2, s4, v143
	s_waitcnt lgkmcnt(3)
	v_cvt_pk_bf16_f32 v132, v136, v137
	s_waitcnt lgkmcnt(2)
	v_cvt_pk_bf16_f32 v133, v152, v153
	s_waitcnt lgkmcnt(1)
	v_cvt_pk_bf16_f32 v134, v138, v139
	s_waitcnt lgkmcnt(0)
	v_cvt_pk_bf16_f32 v135, v150, v151
	s_cbranch_vccnz .LBB0_508
	v_lshlrev_b32_e32 v145, 2, v2
	v_and_b32_e32 v145, 0xffffffc0, v145
	v_ashrrev_i32_e32 v147, 5, v146
	v_add_u32_e32 v148, v147, v145
	v_ashrrev_i32_e32 v149, 31, v148
	v_lshlrev_b32_e32 v145, 1, v146
	v_lshlrev_b64 v[148:149], 6, v[148:149]
	v_and_b32_e32 v145, 48, v145
	v_and_b32_e32 v147, 15, v2
	v_or3_b32 v148, v148, v145, v147
	v_ashrrev_i32_e32 v147, 31, v146
	v_lshl_add_u64 v[180:181], v[146:147], 2, s[12:13]
	global_load_dwordx4 v[176:179], v[180:181], off offset:16
	s_nop 0
	global_load_dwordx4 v[180:183], v[180:181], off
	v_lshlrev_b64 v[148:149], 4, v[148:149]
	s_waitcnt vmcnt(1)
	v_mul_f32_e32 v186, v138, v176
	s_waitcnt vmcnt(0)
	v_mul_f32_e32 v145, v136, v180
	v_mul_f32_e32 v147, v137, v181
	v_cvt_pk_bf16_f32 v184, v145, v147
	v_mul_f32_e32 v185, v153, v183
	v_lshlrev_b32_e32 v145, 16, v184
	v_fma_f32 v136, v136, v180, -v145
	v_and_b32_e32 v145, 0xffff0000, v184
	v_mul_f32_e32 v187, v139, v177
	v_fma_f32 v137, v137, v181, -v145
	v_mul_f32_e32 v175, v152, v182
	v_mul_f32_e32 v188, v150, v178
	v_mul_f32_e32 v189, v151, v179
	v_cvt_pk_bf16_f32 v185, v175, v185
	v_cvt_pk_bf16_f32 v186, v186, v187
	v_cvt_pk_bf16_f32 v187, v188, v189
	v_cvt_pk_bf16_f32 v136, v136, v137
	s_nop 0
	v_lshlrev_b32_e32 v137, 16, v185
	v_and_b32_e32 v145, 0xffff0000, v185
	v_fma_f32 v137, v152, v182, -v137
	v_fma_f32 v145, v153, v183, -v145
	v_cvt_pk_bf16_f32 v137, v137, v145
	v_lshlrev_b32_e32 v145, 16, v186
	v_fma_f32 v138, v138, v176, -v145
	v_and_b32_e32 v145, 0xffff0000, v186
	v_fma_f32 v139, v139, v177, -v145
	v_cvt_pk_bf16_f32 v138, v138, v139
	v_lshlrev_b32_e32 v139, 16, v187
	v_and_b32_e32 v145, 0xffff0000, v187
	v_fma_f32 v139, v150, v178, -v139
	v_fma_f32 v145, v151, v179, -v145
	v_lshl_add_u64 v[150:151], s[8:9], 0, v[148:149]
	v_lshl_add_u64 v[148:149], s[10:11], 0, v[148:149]
	v_cvt_pk_bf16_f32 v139, v139, v145
	global_store_dwordx4 v[150:151], v[184:187], off nt
	s_cbranch_execnz .LBB0_466

.LBB0_466:
	global_store_dwordx4 v[148:149], v[136:139], off nt
	ds_read2_b32 v[136:137], v155 offset0:24 offset1:57
	ds_read2_b32 v[152:153], v155 offset0:90 offset1:123
	ds_read2_b32 v[138:139], v155 offset0:156 offset1:189
	ds_read2_b32 v[150:151], v155 offset0:222 offset1:255
	s_and_b64 vcc, exec, s[2:3]
	v_add_u32_e32 v2, s4, v154
	s_waitcnt lgkmcnt(3)
	v_cvt_pk_bf16_f32 v132, v136, v137
	s_waitcnt lgkmcnt(2)
	v_cvt_pk_bf16_f32 v133, v152, v153
	s_waitcnt lgkmcnt(1)
	v_cvt_pk_bf16_f32 v134, v138, v139
	s_waitcnt lgkmcnt(0)
	v_cvt_pk_bf16_f32 v135, v150, v151
	s_cbranch_vccnz .LBB0_509
	v_lshlrev_b32_e32 v145, 2, v2
	v_and_b32_e32 v145, 0xffffffc0, v145
	v_ashrrev_i32_e32 v147, 5, v146
	v_add_u32_e32 v148, v147, v145
	v_ashrrev_i32_e32 v149, 31, v148
	v_lshlrev_b32_e32 v145, 1, v146
	v_lshlrev_b64 v[148:149], 6, v[148:149]
	v_and_b32_e32 v145, 48, v145
	v_and_b32_e32 v147, 15, v2
	v_or3_b32 v148, v148, v145, v147
	v_ashrrev_i32_e32 v147, 31, v146
	v_lshl_add_u64 v[146:147], v[146:147], 2, s[12:13]
	global_load_dwordx4 v[176:179], v[146:147], off offset:16
	global_load_dwordx4 v[180:183], v[146:147], off
	s_waitcnt vmcnt(1)
	v_mul_f32_e32 v186, v138, v176
	s_waitcnt vmcnt(0)
	v_mul_f32_e32 v145, v136, v180
	v_mul_f32_e32 v146, v137, v181
	v_cvt_pk_bf16_f32 v184, v145, v146
	v_mul_f32_e32 v187, v139, v177
	v_lshlrev_b32_e32 v145, 16, v184
	v_fma_f32 v136, v136, v180, -v145
	v_and_b32_e32 v145, 0xffff0000, v184
	v_fma_f32 v137, v137, v181, -v145
	v_mul_f32_e32 v147, v152, v182
	v_mul_f32_e32 v175, v153, v183
	v_mul_f32_e32 v188, v150, v178
	v_mul_f32_e32 v189, v151, v179
	v_cvt_pk_bf16_f32 v185, v147, v175
	v_cvt_pk_bf16_f32 v186, v186, v187
	v_cvt_pk_bf16_f32 v187, v188, v189
	v_cvt_pk_bf16_f32 v136, v136, v137
	v_lshlrev_b64 v[146:147], 4, v[148:149]
	v_lshlrev_b32_e32 v137, 16, v185
	v_and_b32_e32 v145, 0xffff0000, v185
	v_fma_f32 v137, v152, v182, -v137
	v_fma_f32 v145, v153, v183, -v145
	v_cvt_pk_bf16_f32 v137, v137, v145
	v_lshlrev_b32_e32 v145, 16, v186
	v_fma_f32 v138, v138, v176, -v145
	v_and_b32_e32 v145, 0xffff0000, v186
	v_fma_f32 v139, v139, v177, -v145
	v_cvt_pk_bf16_f32 v138, v138, v139
	v_lshlrev_b32_e32 v139, 16, v187
	v_fma_f32 v139, v150, v178, -v139
	v_and_b32_e32 v145, 0xffff0000, v187
	v_lshl_add_u64 v[148:149], s[8:9], 0, v[146:147]
	v_lshl_add_u64 v[146:147], s[10:11], 0, v[146:147]
	v_fma_f32 v145, v151, v179, -v145
	v_cvt_pk_bf16_f32 v139, v139, v145
	global_store_dwordx4 v[148:149], v[184:187], off nt
	s_cbranch_execnz .LBB0_469

.LBB0_469:
	s_lshr_b32 s2, s93, 3
	s_mul_i32 s2, s2, s86
	s_add_i32 s2, s2, s68
	s_and_b32 s73, s93, 4
	global_store_dwordx4 v[146:147], v[136:139], off nt
	s_lshl_b32 s72, s2, 6
	s_add_i32 s2, s87, s73
	s_waitcnt lgkmcnt(0)
	s_add_i32 s2, s2, s72
	s_cmp_lt_i32 s2, s50
	s_cselect_b32 s7, s2, -1
	s_cmp_lt_i32 s7, 0
	s_cbranch_scc1 .LBB0_519
	s_mul_hi_u32 s2, s7, 0x9824d8ed
	s_lshr_b32 s2, s2, 15
	s_mul_i32 s3, s2, 0xd760
	s_sub_i32 s85, s7, s3
	s_cmpk_gt_u32 s85, 0xc2ff
	s_mov_b64 s[44:45], -1
	s_cbranch_scc0 .LBB0_499
	s_add_i32 s44, s2, 1
	s_add_i32 s3, s85, 0xffff3d00
	s_cmpk_lt_u32 s3, 0x1400
	s_cselect_b32 s3, s3, s85
	s_cmpk_gt_u32 s3, 0xbff
	s_mov_b64 s[48:49], -1
	s_cbranch_scc0 .LBB0_496
	s_cmpk_gt_u32 s3, 0x13ff
	s_cbranch_scc0 .LBB0_493
	s_cmpk_gt_u32 s3, 0x93ff
	s_cbranch_scc0 .LBB0_490
	s_cmpk_gt_u32 s3, 0xd3ff
	s_cbranch_scc0 .LBB0_487
	s_cmpk_gt_u32 s3, 0xd5ff
	s_cbranch_scc0 .LBB0_484
	s_cmpk_gt_u32 s3, 0xd6ff
	s_cbranch_scc0 .LBB0_481
	s_cmpk_gt_u32 s3, 0xd71f
	s_mov_b64 s[42:43], -1
	s_cbranch_scc0 .LBB0_479
	s_mov_b32 s45, s47
	v_readlane_b32 s48, v243, 40
	s_lshl_b64 s[8:9], s[44:45], 19
	v_readlane_b32 s54, v243, 46
	v_readlane_b32 s55, v243, 47
	s_add_u32 s40, s54, s8
	s_addc_u32 s41, s55, s9
	s_lshl_b64 s[10:11], s[44:45], 18
	v_readlane_b32 s4, v242, 42
	s_add_u32 s8, s4, s10
	v_readlane_b32 s4, v242, 43
	s_addc_u32 s9, s4, s11
	v_readlane_b32 s4, v242, 44
	s_add_u32 s10, s4, s10
	v_readlane_b32 s4, v242, 45
	v_readlane_b32 s50, v243, 42
	s_addc_u32 s11, s4, s11
	s_lshl_b32 s6, s44, 13
	v_readlane_b32 s51, v243, 43
	s_add_u32 s12, s50, s6
	s_addc_u32 s13, s51, 0
	s_lshl_b32 s42, s3, 5
	s_and_b32 s6, s42, 0x7fffffc0
	v_readlane_b32 s49, v243, 41
	v_readlane_b32 s52, v243, 44
	v_readlane_b32 s53, v243, 45
	v_readlane_b32 s56, v243, 48
	v_readlane_b32 s57, v243, 49
	v_readlane_b32 s58, v243, 50
	v_readlane_b32 s59, v243, 51
	v_readlane_b32 s60, v243, 52
	v_readlane_b32 s61, v243, 53
	v_readlane_b32 s62, v243, 54
	v_readlane_b32 s63, v243, 55
	s_mov_b32 s50, s79
	v_readlane_b32 s51, v242, 29
	s_add_i32 s6, s6, 0xffe51c00
	s_and_b32 s4, s42, 32
	s_mov_b64 s[42:43], 0

.LBB0_519:
	s_cmp_lt_i32 s15, 0
	s_mov_b64 s[2:3], -1
	s_cbranch_scc1 .LBB0_456
	ds_write2_b32 v160, v36, v37 offset1:1
	ds_write2_b32 v160, v38, v39 offset0:2 offset1:3
	ds_write2_b32 v161, v40, v41 offset1:1
	ds_write2_b32 v162, v42, v43 offset1:1
	ds_write2_b32 v163, v44, v45 offset1:1
	ds_write2_b32 v164, v46, v47 offset1:1
	ds_write2_b32 v165, v48, v49 offset1:1
	ds_write2_b32 v166, v50, v51 offset1:1
	ds_write2_b32 v167, v52, v53 offset1:1
	ds_write2_b32 v168, v54, v55 offset1:1
	ds_write2_b32 v169, v56, v57 offset1:1
	ds_write2_b32 v170, v58, v59 offset1:1
	ds_write2_b32 v171, v60, v61 offset1:1
	ds_write2_b32 v172, v62, v63 offset1:1
	ds_write2_b32 v173, v64, v65 offset1:1
	ds_write2_b32 v174, v66, v67 offset1:1
	s_waitcnt lgkmcnt(0)
	ds_read2_b32 v[136:137], v155 offset1:33
	ds_read2_b32 v[152:153], v155 offset0:66 offset1:99
	ds_read2_b32 v[138:139], v155 offset0:132 offset1:165
	ds_read2_b32 v[150:151], v155 offset0:198 offset1:231
	s_cmp_lg_u64 s[18:19], 0
	s_cselect_b64 s[40:41], -1, 0
	s_and_b64 vcc, exec, s[40:41]
	v_add_u32_e32 v2, s0, v1
	v_add_u32_e32 v146, s14, v142
	s_waitcnt lgkmcnt(3)
	v_cvt_pk_bf16_f32 v132, v136, v137
	s_waitcnt lgkmcnt(2)
	v_cvt_pk_bf16_f32 v133, v152, v153
	s_waitcnt lgkmcnt(1)
	v_cvt_pk_bf16_f32 v134, v138, v139
	s_waitcnt lgkmcnt(0)
	v_cvt_pk_bf16_f32 v135, v150, v151
	s_cbranch_vccz .LBB0_569
	v_lshlrev_b32_e32 v145, 2, v2
	v_and_b32_e32 v145, 0xffffffc0, v145
	v_ashrrev_i32_e32 v147, 5, v146
	v_add_u32_e32 v148, v145, v147
	v_ashrrev_i32_e32 v149, 31, v148
	v_lshlrev_b32_e32 v145, 1, v146
	v_lshlrev_b64 v[148:149], 6, v[148:149]
	v_and_b32_e32 v145, 48, v145
	v_and_b32_e32 v147, 15, v2
	v_or3_b32 v148, v148, v145, v147
	v_ashrrev_i32_e32 v147, 31, v146
	v_lshl_add_u64 v[180:181], v[146:147], 2, s[20:21]
	global_load_dwordx4 v[176:179], v[180:181], off offset:16
	s_nop 0
	global_load_dwordx4 v[180:183], v[180:181], off
	v_lshlrev_b64 v[148:149], 4, v[148:149]
	s_waitcnt vmcnt(1)
	v_mul_f32_e32 v186, v138, v176
	s_waitcnt vmcnt(0)
	v_mul_f32_e32 v145, v136, v180
	v_mul_f32_e32 v147, v137, v181
	v_cvt_pk_bf16_f32 v184, v145, v147
	v_mul_f32_e32 v185, v153, v183
	v_lshlrev_b32_e32 v145, 16, v184
	v_fma_f32 v136, v136, v180, -v145
	v_and_b32_e32 v145, 0xffff0000, v184
	v_mul_f32_e32 v187, v139, v177
	v_fma_f32 v137, v137, v181, -v145
	v_mul_f32_e32 v175, v152, v182
	v_mul_f32_e32 v188, v150, v178
	v_mul_f32_e32 v189, v151, v179
	v_cvt_pk_bf16_f32 v185, v175, v185
	v_cvt_pk_bf16_f32 v186, v186, v187
	v_cvt_pk_bf16_f32 v187, v188, v189
	v_cvt_pk_bf16_f32 v136, v136, v137
	s_nop 0
	v_lshlrev_b32_e32 v137, 16, v185
	v_and_b32_e32 v145, 0xffff0000, v185
	v_fma_f32 v137, v152, v182, -v137
	v_fma_f32 v145, v153, v183, -v145
	v_cvt_pk_bf16_f32 v137, v137, v145
	v_lshlrev_b32_e32 v145, 16, v186
	v_fma_f32 v138, v138, v176, -v145
	v_and_b32_e32 v145, 0xffff0000, v186
	v_fma_f32 v139, v139, v177, -v145
	v_cvt_pk_bf16_f32 v138, v138, v139
	v_lshlrev_b32_e32 v139, 16, v187
	v_and_b32_e32 v145, 0xffff0000, v187
	v_fma_f32 v139, v150, v178, -v139
	v_fma_f32 v145, v151, v179, -v145
	v_lshl_add_u64 v[150:151], s[16:17], 0, v[148:149]
	v_cvt_pk_bf16_f32 v139, v139, v145
	global_store_dwordx4 v[150:151], v[184:187], off nt
	v_lshl_add_u64 v[148:149], s[18:19], 0, v[148:149]
	s_cbranch_execnz .LBB0_523

.LBB0_523:
	global_store_dwordx4 v[148:149], v[136:139], off nt
	ds_read2_b32 v[136:137], v155 offset0:8 offset1:41
	ds_read2_b32 v[152:153], v155 offset0:74 offset1:107
	ds_read2_b32 v[138:139], v155 offset0:140 offset1:173
	ds_read2_b32 v[150:151], v155 offset0:206 offset1:239
	v_cndmask_b32_e64 v2, 0, 1, s[40:41]
	v_cmp_ne_u32_e64 s[2:3], 1, v2
	s_andn2_b64 vcc, exec, s[40:41]
	v_add_u32_e32 v2, s0, v141
	s_waitcnt lgkmcnt(3)
	v_cvt_pk_bf16_f32 v132, v136, v137
	s_waitcnt lgkmcnt(2)
	v_cvt_pk_bf16_f32 v133, v152, v153
	s_waitcnt lgkmcnt(1)
	v_cvt_pk_bf16_f32 v134, v138, v139
	s_waitcnt lgkmcnt(0)
	v_cvt_pk_bf16_f32 v135, v150, v151
	s_cbranch_vccnz .LBB0_570
	v_lshlrev_b32_e32 v145, 2, v2
	v_and_b32_e32 v145, 0xffffffc0, v145
	v_ashrrev_i32_e32 v147, 5, v146
	v_add_u32_e32 v148, v145, v147
	v_ashrrev_i32_e32 v149, 31, v148
	v_lshlrev_b32_e32 v145, 1, v146
	v_lshlrev_b64 v[148:149], 6, v[148:149]
	v_and_b32_e32 v145, 48, v145
	v_and_b32_e32 v147, 15, v2
	v_or3_b32 v148, v148, v145, v147
	v_ashrrev_i32_e32 v147, 31, v146
	v_lshl_add_u64 v[180:181], v[146:147], 2, s[20:21]
	global_load_dwordx4 v[176:179], v[180:181], off offset:16
	s_nop 0
	global_load_dwordx4 v[180:183], v[180:181], off
	v_lshlrev_b64 v[148:149], 4, v[148:149]
	s_waitcnt vmcnt(1)
	v_mul_f32_e32 v186, v138, v176
	s_waitcnt vmcnt(0)
	v_mul_f32_e32 v145, v136, v180
	v_mul_f32_e32 v147, v137, v181
	v_cvt_pk_bf16_f32 v184, v145, v147
	v_mul_f32_e32 v185, v153, v183
	v_lshlrev_b32_e32 v145, 16, v184
	v_fma_f32 v136, v136, v180, -v145
	v_and_b32_e32 v145, 0xffff0000, v184
	v_mul_f32_e32 v187, v139, v177
	v_fma_f32 v137, v137, v181, -v145
	v_mul_f32_e32 v175, v152, v182
	v_mul_f32_e32 v188, v150, v178
	v_mul_f32_e32 v189, v151, v179
	v_cvt_pk_bf16_f32 v185, v175, v185
	v_cvt_pk_bf16_f32 v186, v186, v187
	v_cvt_pk_bf16_f32 v187, v188, v189
	v_cvt_pk_bf16_f32 v136, v136, v137
	s_nop 0
	v_lshlrev_b32_e32 v137, 16, v185
	v_and_b32_e32 v145, 0xffff0000, v185
	v_fma_f32 v137, v152, v182, -v137
	v_fma_f32 v145, v153, v183, -v145
	v_cvt_pk_bf16_f32 v137, v137, v145
	v_lshlrev_b32_e32 v145, 16, v186
	v_fma_f32 v138, v138, v176, -v145
	v_and_b32_e32 v145, 0xffff0000, v186
	v_fma_f32 v139, v139, v177, -v145
	v_cvt_pk_bf16_f32 v138, v138, v139
	v_lshlrev_b32_e32 v139, 16, v187
	v_and_b32_e32 v145, 0xffff0000, v187
	v_fma_f32 v139, v150, v178, -v139
	v_fma_f32 v145, v151, v179, -v145
	v_lshl_add_u64 v[150:151], s[16:17], 0, v[148:149]
	v_lshl_add_u64 v[148:149], s[18:19], 0, v[148:149]
	v_cvt_pk_bf16_f32 v139, v139, v145
	global_store_dwordx4 v[150:151], v[184:187], off nt
	s_cbranch_execnz .LBB0_526

.LBB0_526:
	global_store_dwordx4 v[148:149], v[136:139], off nt
	ds_read2_b32 v[136:137], v155 offset0:16 offset1:49
	ds_read2_b32 v[152:153], v155 offset0:82 offset1:115
	ds_read2_b32 v[138:139], v155 offset0:148 offset1:181
	ds_read2_b32 v[150:151], v155 offset0:214 offset1:247
	s_and_b64 vcc, exec, s[2:3]
	v_add_u32_e32 v2, s0, v143
	s_waitcnt lgkmcnt(3)
	v_cvt_pk_bf16_f32 v132, v136, v137
	s_waitcnt lgkmcnt(2)
	v_cvt_pk_bf16_f32 v133, v152, v153
	s_waitcnt lgkmcnt(1)
	v_cvt_pk_bf16_f32 v134, v138, v139
	s_waitcnt lgkmcnt(0)
	v_cvt_pk_bf16_f32 v135, v150, v151
	s_cbranch_vccnz .LBB0_571
	v_lshlrev_b32_e32 v145, 2, v2
	v_and_b32_e32 v145, 0xffffffc0, v145
	v_ashrrev_i32_e32 v147, 5, v146
	v_add_u32_e32 v148, v145, v147
	v_ashrrev_i32_e32 v149, 31, v148
	v_lshlrev_b32_e32 v145, 1, v146
	v_lshlrev_b64 v[148:149], 6, v[148:149]
	v_and_b32_e32 v145, 48, v145
	v_and_b32_e32 v147, 15, v2
	v_or3_b32 v148, v148, v145, v147
	v_ashrrev_i32_e32 v147, 31, v146
	v_lshl_add_u64 v[180:181], v[146:147], 2, s[20:21]
	global_load_dwordx4 v[176:179], v[180:181], off offset:16
	s_nop 0
	global_load_dwordx4 v[180:183], v[180:181], off
	v_lshlrev_b64 v[148:149], 4, v[148:149]
	s_waitcnt vmcnt(1)
	v_mul_f32_e32 v186, v138, v176
	s_waitcnt vmcnt(0)
	v_mul_f32_e32 v145, v136, v180
	v_mul_f32_e32 v147, v137, v181
	v_cvt_pk_bf16_f32 v184, v145, v147
	v_mul_f32_e32 v185, v153, v183
	v_lshlrev_b32_e32 v145, 16, v184
	v_fma_f32 v136, v136, v180, -v145
	v_and_b32_e32 v145, 0xffff0000, v184
	v_mul_f32_e32 v187, v139, v177
	v_fma_f32 v137, v137, v181, -v145
	v_mul_f32_e32 v175, v152, v182
	v_mul_f32_e32 v188, v150, v178
	v_mul_f32_e32 v189, v151, v179
	v_cvt_pk_bf16_f32 v185, v175, v185
	v_cvt_pk_bf16_f32 v186, v186, v187
	v_cvt_pk_bf16_f32 v187, v188, v189
	v_cvt_pk_bf16_f32 v136, v136, v137
	s_nop 0
	v_lshlrev_b32_e32 v137, 16, v185
	v_and_b32_e32 v145, 0xffff0000, v185
	v_fma_f32 v137, v152, v182, -v137
	v_fma_f32 v145, v153, v183, -v145
	v_cvt_pk_bf16_f32 v137, v137, v145
	v_lshlrev_b32_e32 v145, 16, v186
	v_fma_f32 v138, v138, v176, -v145
	v_and_b32_e32 v145, 0xffff0000, v186
	v_fma_f32 v139, v139, v177, -v145
	v_cvt_pk_bf16_f32 v138, v138, v139
	v_lshlrev_b32_e32 v139, 16, v187
	v_and_b32_e32 v145, 0xffff0000, v187
	v_fma_f32 v139, v150, v178, -v139
	v_fma_f32 v145, v151, v179, -v145
	v_lshl_add_u64 v[150:151], s[16:17], 0, v[148:149]
	v_lshl_add_u64 v[148:149], s[18:19], 0, v[148:149]
	v_cvt_pk_bf16_f32 v139, v139, v145
	global_store_dwordx4 v[150:151], v[184:187], off nt
	s_cbranch_execnz .LBB0_529

.LBB0_529:
	global_store_dwordx4 v[148:149], v[136:139], off nt
	ds_read2_b32 v[136:137], v155 offset0:24 offset1:57
	ds_read2_b32 v[152:153], v155 offset0:90 offset1:123
	ds_read2_b32 v[138:139], v155 offset0:156 offset1:189
	ds_read2_b32 v[150:151], v155 offset0:222 offset1:255
	s_and_b64 vcc, exec, s[2:3]
	v_add_u32_e32 v2, s0, v154
	s_waitcnt lgkmcnt(3)
	v_cvt_pk_bf16_f32 v132, v136, v137
	s_waitcnt lgkmcnt(2)
	v_cvt_pk_bf16_f32 v133, v152, v153
	s_waitcnt lgkmcnt(1)
	v_cvt_pk_bf16_f32 v134, v138, v139
	s_waitcnt lgkmcnt(0)
	v_cvt_pk_bf16_f32 v135, v150, v151
	s_cbranch_vccnz .LBB0_572
	v_lshlrev_b32_e32 v145, 2, v2
	v_and_b32_e32 v145, 0xffffffc0, v145
	v_ashrrev_i32_e32 v147, 5, v146
	v_add_u32_e32 v148, v145, v147
	v_ashrrev_i32_e32 v149, 31, v148
	v_lshlrev_b32_e32 v145, 1, v146
	v_lshlrev_b64 v[148:149], 6, v[148:149]
	v_and_b32_e32 v145, 48, v145
	v_and_b32_e32 v147, 15, v2
	v_or3_b32 v148, v148, v145, v147
	v_ashrrev_i32_e32 v147, 31, v146
	v_lshl_add_u64 v[146:147], v[146:147], 2, s[20:21]
	global_load_dwordx4 v[176:179], v[146:147], off offset:16
	global_load_dwordx4 v[180:183], v[146:147], off
	s_waitcnt vmcnt(1)
	v_mul_f32_e32 v186, v138, v176
	s_waitcnt vmcnt(0)
	v_mul_f32_e32 v145, v136, v180
	v_mul_f32_e32 v146, v137, v181
	v_cvt_pk_bf16_f32 v184, v145, v146
	v_mul_f32_e32 v187, v139, v177
	v_lshlrev_b32_e32 v145, 16, v184
	v_fma_f32 v136, v136, v180, -v145
	v_and_b32_e32 v145, 0xffff0000, v184
	v_fma_f32 v137, v137, v181, -v145
	v_mul_f32_e32 v147, v152, v182
	v_mul_f32_e32 v175, v153, v183
	v_mul_f32_e32 v188, v150, v178
	v_mul_f32_e32 v189, v151, v179
	v_cvt_pk_bf16_f32 v185, v147, v175
	v_cvt_pk_bf16_f32 v186, v186, v187
	v_cvt_pk_bf16_f32 v187, v188, v189
	v_cvt_pk_bf16_f32 v136, v136, v137
	v_lshlrev_b64 v[146:147], 4, v[148:149]
	v_lshlrev_b32_e32 v137, 16, v185
	v_and_b32_e32 v145, 0xffff0000, v185
	v_fma_f32 v137, v152, v182, -v137
	v_fma_f32 v145, v153, v183, -v145
	v_cvt_pk_bf16_f32 v137, v137, v145
	v_lshlrev_b32_e32 v145, 16, v186
	v_fma_f32 v138, v138, v176, -v145
	v_and_b32_e32 v145, 0xffff0000, v186
	v_fma_f32 v139, v139, v177, -v145
	v_cvt_pk_bf16_f32 v138, v138, v139
	v_lshlrev_b32_e32 v139, 16, v187
	v_fma_f32 v139, v150, v178, -v139
	v_and_b32_e32 v145, 0xffff0000, v187
	v_lshl_add_u64 v[148:149], s[16:17], 0, v[146:147]
	v_lshl_add_u64 v[146:147], s[18:19], 0, v[146:147]
	v_fma_f32 v145, v151, v179, -v145
	v_cvt_pk_bf16_f32 v139, v139, v145
	global_store_dwordx4 v[148:149], v[184:187], off nt
	s_cbranch_execnz .LBB0_532

.LBB0_532:
	global_store_dwordx4 v[146:147], v[136:139], off nt
	s_add_i32 s2, s74, s73
	s_waitcnt lgkmcnt(0)
	s_add_i32 s2, s2, s72
	s_cmp_lt_i32 s2, s50
	s_cselect_b32 s15, s2, -1
	s_cmp_lt_i32 s15, 0
	s_cbranch_scc1 .LBB0_582
	s_mul_hi_u32 s2, s15, 0x9824d8ed
	s_lshr_b32 s2, s2, 15
	s_mul_i32 s3, s2, 0xd760
	s_sub_i32 s85, s15, s3
	s_cmpk_gt_u32 s85, 0xc2ff
	s_mov_b64 s[44:45], -1
	s_cbranch_scc0 .LBB0_562
	s_add_i32 s44, s2, 1
	s_add_i32 s3, s85, 0xffff3d00
	s_cmpk_lt_u32 s3, 0x1400
	s_cselect_b32 s3, s3, s85
	s_cmpk_gt_u32 s3, 0xbff
	s_mov_b64 s[48:49], -1
	s_cbranch_scc0 .LBB0_559
	s_cmpk_gt_u32 s3, 0x13ff
	s_cbranch_scc0 .LBB0_556
	s_cmpk_gt_u32 s3, 0x93ff
	s_cbranch_scc0 .LBB0_553
	s_cmpk_gt_u32 s3, 0xd3ff
	s_cbranch_scc0 .LBB0_550
	s_cmpk_gt_u32 s3, 0xd5ff
	s_cbranch_scc0 .LBB0_547
	s_cmpk_gt_u32 s3, 0xd6ff
	s_cbranch_scc0 .LBB0_544
	s_cmpk_gt_u32 s3, 0xd71f
	s_mov_b64 s[42:43], -1
	s_cbranch_scc0 .LBB0_542
	s_mov_b32 s45, s47
	v_readlane_b32 s48, v243, 40
	s_lshl_b64 s[16:17], s[44:45], 19
	v_readlane_b32 s54, v243, 46
	v_readlane_b32 s55, v243, 47
	s_add_u32 s40, s54, s16
	s_addc_u32 s41, s55, s17
	s_lshl_b64 s[18:19], s[44:45], 18
	v_readlane_b32 s0, v242, 42
	s_add_u32 s16, s0, s18
	v_readlane_b32 s0, v242, 43
	s_addc_u32 s17, s0, s19
	v_readlane_b32 s0, v242, 44
	s_add_u32 s18, s0, s18
	v_readlane_b32 s0, v242, 45
	v_readlane_b32 s50, v243, 42
	s_addc_u32 s19, s0, s19
	s_lshl_b32 s14, s44, 13
	v_readlane_b32 s51, v243, 43
	s_add_u32 s20, s50, s14
	s_addc_u32 s21, s51, 0
	s_lshl_b32 s42, s3, 5
	s_and_b32 s14, s42, 0x7fffffc0
	v_readlane_b32 s49, v243, 41
	v_readlane_b32 s52, v243, 44
	v_readlane_b32 s53, v243, 45
	v_readlane_b32 s56, v243, 48
	v_readlane_b32 s57, v243, 49
	v_readlane_b32 s58, v243, 50
	v_readlane_b32 s59, v243, 51
	v_readlane_b32 s60, v243, 52
	v_readlane_b32 s61, v243, 53
	v_readlane_b32 s62, v243, 54
	v_readlane_b32 s63, v243, 55
	s_mov_b32 s50, s79
	v_readlane_b32 s51, v242, 29
	s_add_i32 s14, s14, 0xffe51c00
	s_and_b32 s0, s42, 32
	s_mov_b64 s[42:43], 0

.LBB0_582:
	s_cmp_lt_i32 s23, 0
	s_mov_b64 s[2:3], -1
	s_cbranch_scc1 .LBB0_456
	ds_write2_b32 v160, v68, v69 offset1:1
	ds_write2_b32 v160, v70, v71 offset0:2 offset1:3
	ds_write2_b32 v161, v72, v73 offset1:1
	ds_write2_b32 v162, v74, v75 offset1:1
	ds_write2_b32 v163, v76, v77 offset1:1
	ds_write2_b32 v164, v78, v79 offset1:1
	ds_write2_b32 v165, v80, v81 offset1:1
	ds_write2_b32 v166, v82, v83 offset1:1
	ds_write2_b32 v167, v84, v85 offset1:1
	ds_write2_b32 v168, v86, v87 offset1:1
	ds_write2_b32 v169, v88, v89 offset1:1
	ds_write2_b32 v170, v90, v91 offset1:1
	ds_write2_b32 v171, v92, v93 offset1:1
	ds_write2_b32 v172, v94, v95 offset1:1
	ds_write2_b32 v173, v96, v97 offset1:1
	ds_write2_b32 v174, v98, v99 offset1:1
	s_waitcnt lgkmcnt(0)
	ds_read2_b32 v[136:137], v155 offset1:33
	ds_read2_b32 v[152:153], v155 offset0:66 offset1:99
	ds_read2_b32 v[138:139], v155 offset0:132 offset1:165
	ds_read2_b32 v[150:151], v155 offset0:198 offset1:231
	s_cmp_lg_u64 s[76:77], 0
	s_cselect_b64 s[40:41], -1, 0
	s_and_b64 vcc, exec, s[40:41]
	v_add_u32_e32 v2, s80, v1
	v_add_u32_e32 v146, s22, v142
	s_waitcnt lgkmcnt(3)
	v_cvt_pk_bf16_f32 v132, v136, v137
	s_waitcnt lgkmcnt(2)
	v_cvt_pk_bf16_f32 v133, v152, v153
	s_waitcnt lgkmcnt(1)
	v_cvt_pk_bf16_f32 v134, v138, v139
	s_waitcnt lgkmcnt(0)
	v_cvt_pk_bf16_f32 v135, v150, v151
	s_cbranch_vccz .LBB0_632
	v_lshlrev_b32_e32 v145, 2, v2
	v_and_b32_e32 v145, 0xffffffc0, v145
	v_ashrrev_i32_e32 v147, 5, v146
	v_add_u32_e32 v148, v145, v147
	v_ashrrev_i32_e32 v149, 31, v148
	v_lshlrev_b32_e32 v145, 1, v146
	v_lshlrev_b64 v[148:149], 6, v[148:149]
	v_and_b32_e32 v145, 48, v145
	v_and_b32_e32 v147, 15, v2
	v_or3_b32 v148, v148, v145, v147
	v_ashrrev_i32_e32 v147, 31, v146
	v_lshl_add_u64 v[180:181], v[146:147], 2, s[26:27]
	global_load_dwordx4 v[176:179], v[180:181], off offset:16
	s_nop 0
	global_load_dwordx4 v[180:183], v[180:181], off
	v_lshlrev_b64 v[148:149], 4, v[148:149]
	s_waitcnt vmcnt(1)
	v_mul_f32_e32 v186, v138, v176
	s_waitcnt vmcnt(0)
	v_mul_f32_e32 v145, v136, v180
	v_mul_f32_e32 v147, v137, v181
	v_cvt_pk_bf16_f32 v184, v145, v147
	v_mul_f32_e32 v185, v153, v183
	v_lshlrev_b32_e32 v145, 16, v184
	v_fma_f32 v136, v136, v180, -v145
	v_and_b32_e32 v145, 0xffff0000, v184
	v_mul_f32_e32 v187, v139, v177
	v_fma_f32 v137, v137, v181, -v145
	v_mul_f32_e32 v175, v152, v182
	v_mul_f32_e32 v188, v150, v178
	v_mul_f32_e32 v189, v151, v179
	v_cvt_pk_bf16_f32 v185, v175, v185
	v_cvt_pk_bf16_f32 v186, v186, v187
	v_cvt_pk_bf16_f32 v187, v188, v189
	v_cvt_pk_bf16_f32 v136, v136, v137
	s_nop 0
	v_lshlrev_b32_e32 v137, 16, v185
	v_and_b32_e32 v145, 0xffff0000, v185
	v_fma_f32 v137, v152, v182, -v137
	v_fma_f32 v145, v153, v183, -v145
	v_cvt_pk_bf16_f32 v137, v137, v145
	v_lshlrev_b32_e32 v145, 16, v186
	v_fma_f32 v138, v138, v176, -v145
	v_and_b32_e32 v145, 0xffff0000, v186
	v_fma_f32 v139, v139, v177, -v145
	v_cvt_pk_bf16_f32 v138, v138, v139
	v_lshlrev_b32_e32 v139, 16, v187
	v_and_b32_e32 v145, 0xffff0000, v187
	v_fma_f32 v139, v150, v178, -v139
	v_fma_f32 v145, v151, v179, -v145
	v_lshl_add_u64 v[150:151], s[82:83], 0, v[148:149]
	v_cvt_pk_bf16_f32 v139, v139, v145
	global_store_dwordx4 v[150:151], v[184:187], off nt
	v_lshl_add_u64 v[148:149], s[76:77], 0, v[148:149]
	s_cbranch_execnz .LBB0_586

.LBB0_586:
	global_store_dwordx4 v[148:149], v[136:139], off nt
	ds_read2_b32 v[136:137], v155 offset0:8 offset1:41
	ds_read2_b32 v[152:153], v155 offset0:74 offset1:107
	ds_read2_b32 v[138:139], v155 offset0:140 offset1:173
	ds_read2_b32 v[150:151], v155 offset0:206 offset1:239
	v_cndmask_b32_e64 v2, 0, 1, s[40:41]
	v_cmp_ne_u32_e64 s[2:3], 1, v2
	s_andn2_b64 vcc, exec, s[40:41]
	v_add_u32_e32 v2, s80, v141
	s_waitcnt lgkmcnt(3)
	v_cvt_pk_bf16_f32 v132, v136, v137
	s_waitcnt lgkmcnt(2)
	v_cvt_pk_bf16_f32 v133, v152, v153
	s_waitcnt lgkmcnt(1)
	v_cvt_pk_bf16_f32 v134, v138, v139
	s_waitcnt lgkmcnt(0)
	v_cvt_pk_bf16_f32 v135, v150, v151
	s_cbranch_vccnz .LBB0_633
	v_lshlrev_b32_e32 v145, 2, v2
	v_and_b32_e32 v145, 0xffffffc0, v145
	v_ashrrev_i32_e32 v147, 5, v146
	v_add_u32_e32 v148, v145, v147
	v_ashrrev_i32_e32 v149, 31, v148
	v_lshlrev_b32_e32 v145, 1, v146
	v_lshlrev_b64 v[148:149], 6, v[148:149]
	v_and_b32_e32 v145, 48, v145
	v_and_b32_e32 v147, 15, v2
	v_or3_b32 v148, v148, v145, v147
	v_ashrrev_i32_e32 v147, 31, v146
	v_lshl_add_u64 v[180:181], v[146:147], 2, s[26:27]
	global_load_dwordx4 v[176:179], v[180:181], off offset:16
	s_nop 0
	global_load_dwordx4 v[180:183], v[180:181], off
	v_lshlrev_b64 v[148:149], 4, v[148:149]
	s_waitcnt vmcnt(1)
	v_mul_f32_e32 v186, v138, v176
	s_waitcnt vmcnt(0)
	v_mul_f32_e32 v145, v136, v180
	v_mul_f32_e32 v147, v137, v181
	v_cvt_pk_bf16_f32 v184, v145, v147
	v_mul_f32_e32 v185, v153, v183
	v_lshlrev_b32_e32 v145, 16, v184
	v_fma_f32 v136, v136, v180, -v145
	v_and_b32_e32 v145, 0xffff0000, v184
	v_mul_f32_e32 v187, v139, v177
	v_fma_f32 v137, v137, v181, -v145
	v_mul_f32_e32 v175, v152, v182
	v_mul_f32_e32 v188, v150, v178
	v_mul_f32_e32 v189, v151, v179
	v_cvt_pk_bf16_f32 v185, v175, v185
	v_cvt_pk_bf16_f32 v186, v186, v187
	v_cvt_pk_bf16_f32 v187, v188, v189
	v_cvt_pk_bf16_f32 v136, v136, v137
	s_nop 0
	v_lshlrev_b32_e32 v137, 16, v185
	v_and_b32_e32 v145, 0xffff0000, v185
	v_fma_f32 v137, v152, v182, -v137
	v_fma_f32 v145, v153, v183, -v145
	v_cvt_pk_bf16_f32 v137, v137, v145
	v_lshlrev_b32_e32 v145, 16, v186
	v_fma_f32 v138, v138, v176, -v145
	v_and_b32_e32 v145, 0xffff0000, v186
	v_fma_f32 v139, v139, v177, -v145
	v_cvt_pk_bf16_f32 v138, v138, v139
	v_lshlrev_b32_e32 v139, 16, v187
	v_and_b32_e32 v145, 0xffff0000, v187
	v_fma_f32 v139, v150, v178, -v139
	v_fma_f32 v145, v151, v179, -v145
	v_lshl_add_u64 v[150:151], s[82:83], 0, v[148:149]
	v_lshl_add_u64 v[148:149], s[76:77], 0, v[148:149]
	v_cvt_pk_bf16_f32 v139, v139, v145
	global_store_dwordx4 v[150:151], v[184:187], off nt
	s_cbranch_execnz .LBB0_589

.LBB0_589:
	global_store_dwordx4 v[148:149], v[136:139], off nt
	ds_read2_b32 v[136:137], v155 offset0:16 offset1:49
	ds_read2_b32 v[152:153], v155 offset0:82 offset1:115
	ds_read2_b32 v[138:139], v155 offset0:148 offset1:181
	ds_read2_b32 v[150:151], v155 offset0:214 offset1:247
	s_and_b64 vcc, exec, s[2:3]
	v_add_u32_e32 v2, s80, v143
	s_waitcnt lgkmcnt(3)
	v_cvt_pk_bf16_f32 v132, v136, v137
	s_waitcnt lgkmcnt(2)
	v_cvt_pk_bf16_f32 v133, v152, v153
	s_waitcnt lgkmcnt(1)
	v_cvt_pk_bf16_f32 v134, v138, v139
	s_waitcnt lgkmcnt(0)
	v_cvt_pk_bf16_f32 v135, v150, v151
	s_cbranch_vccnz .LBB0_634
	v_lshlrev_b32_e32 v145, 2, v2
	v_and_b32_e32 v145, 0xffffffc0, v145
	v_ashrrev_i32_e32 v147, 5, v146
	v_add_u32_e32 v148, v145, v147
	v_ashrrev_i32_e32 v149, 31, v148
	v_lshlrev_b32_e32 v145, 1, v146
	v_lshlrev_b64 v[148:149], 6, v[148:149]
	v_and_b32_e32 v145, 48, v145
	v_and_b32_e32 v147, 15, v2
	v_or3_b32 v148, v148, v145, v147
	v_ashrrev_i32_e32 v147, 31, v146
	v_lshl_add_u64 v[180:181], v[146:147], 2, s[26:27]
	global_load_dwordx4 v[176:179], v[180:181], off offset:16
	s_nop 0
	global_load_dwordx4 v[180:183], v[180:181], off
	v_lshlrev_b64 v[148:149], 4, v[148:149]
	s_waitcnt vmcnt(1)
	v_mul_f32_e32 v186, v138, v176
	s_waitcnt vmcnt(0)
	v_mul_f32_e32 v145, v136, v180
	v_mul_f32_e32 v147, v137, v181
	v_cvt_pk_bf16_f32 v184, v145, v147
	v_mul_f32_e32 v185, v153, v183
	v_lshlrev_b32_e32 v145, 16, v184
	v_fma_f32 v136, v136, v180, -v145
	v_and_b32_e32 v145, 0xffff0000, v184
	v_mul_f32_e32 v187, v139, v177
	v_fma_f32 v137, v137, v181, -v145
	v_mul_f32_e32 v175, v152, v182
	v_mul_f32_e32 v188, v150, v178
	v_mul_f32_e32 v189, v151, v179
	v_cvt_pk_bf16_f32 v185, v175, v185
	v_cvt_pk_bf16_f32 v186, v186, v187
	v_cvt_pk_bf16_f32 v187, v188, v189
	v_cvt_pk_bf16_f32 v136, v136, v137
	s_nop 0
	v_lshlrev_b32_e32 v137, 16, v185
	v_and_b32_e32 v145, 0xffff0000, v185
	v_fma_f32 v137, v152, v182, -v137
	v_fma_f32 v145, v153, v183, -v145
	v_cvt_pk_bf16_f32 v137, v137, v145
	v_lshlrev_b32_e32 v145, 16, v186
	v_fma_f32 v138, v138, v176, -v145
	v_and_b32_e32 v145, 0xffff0000, v186
	v_fma_f32 v139, v139, v177, -v145
	v_cvt_pk_bf16_f32 v138, v138, v139
	v_lshlrev_b32_e32 v139, 16, v187
	v_and_b32_e32 v145, 0xffff0000, v187
	v_fma_f32 v139, v150, v178, -v139
	v_fma_f32 v145, v151, v179, -v145
	v_lshl_add_u64 v[150:151], s[82:83], 0, v[148:149]
	v_lshl_add_u64 v[148:149], s[76:77], 0, v[148:149]
	v_cvt_pk_bf16_f32 v139, v139, v145
	global_store_dwordx4 v[150:151], v[184:187], off nt
	s_cbranch_execnz .LBB0_592

.LBB0_592:
	global_store_dwordx4 v[148:149], v[136:139], off nt
	ds_read2_b32 v[136:137], v155 offset0:24 offset1:57
	ds_read2_b32 v[152:153], v155 offset0:90 offset1:123
	ds_read2_b32 v[138:139], v155 offset0:156 offset1:189
	ds_read2_b32 v[150:151], v155 offset0:222 offset1:255
	s_and_b64 vcc, exec, s[2:3]
	v_add_u32_e32 v2, s80, v154
	s_waitcnt lgkmcnt(3)
	v_cvt_pk_bf16_f32 v132, v136, v137
	s_waitcnt lgkmcnt(2)
	v_cvt_pk_bf16_f32 v133, v152, v153
	s_waitcnt lgkmcnt(1)
	v_cvt_pk_bf16_f32 v134, v138, v139
	s_waitcnt lgkmcnt(0)
	v_cvt_pk_bf16_f32 v135, v150, v151
	s_cbranch_vccnz .LBB0_635
	v_lshlrev_b32_e32 v145, 2, v2
	v_and_b32_e32 v145, 0xffffffc0, v145
	v_ashrrev_i32_e32 v147, 5, v146
	v_add_u32_e32 v148, v145, v147
	v_ashrrev_i32_e32 v149, 31, v148
	v_lshlrev_b32_e32 v145, 1, v146
	v_lshlrev_b64 v[148:149], 6, v[148:149]
	v_and_b32_e32 v145, 48, v145
	v_and_b32_e32 v147, 15, v2
	v_or3_b32 v148, v148, v145, v147
	v_ashrrev_i32_e32 v147, 31, v146
	v_lshl_add_u64 v[146:147], v[146:147], 2, s[26:27]
	global_load_dwordx4 v[176:179], v[146:147], off offset:16
	global_load_dwordx4 v[180:183], v[146:147], off
	s_waitcnt vmcnt(1)
	v_mul_f32_e32 v186, v138, v176
	s_waitcnt vmcnt(0)
	v_mul_f32_e32 v145, v136, v180
	v_mul_f32_e32 v146, v137, v181
	v_cvt_pk_bf16_f32 v184, v145, v146
	v_mul_f32_e32 v187, v139, v177
	v_lshlrev_b32_e32 v145, 16, v184
	v_fma_f32 v136, v136, v180, -v145
	v_and_b32_e32 v145, 0xffff0000, v184
	v_fma_f32 v137, v137, v181, -v145
	v_mul_f32_e32 v147, v152, v182
	v_mul_f32_e32 v175, v153, v183
	v_mul_f32_e32 v188, v150, v178
	v_mul_f32_e32 v189, v151, v179
	v_cvt_pk_bf16_f32 v185, v147, v175
	v_cvt_pk_bf16_f32 v186, v186, v187
	v_cvt_pk_bf16_f32 v187, v188, v189
	v_cvt_pk_bf16_f32 v136, v136, v137
	v_lshlrev_b64 v[146:147], 4, v[148:149]
	v_lshlrev_b32_e32 v137, 16, v185
	v_and_b32_e32 v145, 0xffff0000, v185
	v_fma_f32 v137, v152, v182, -v137
	v_fma_f32 v145, v153, v183, -v145
	v_cvt_pk_bf16_f32 v137, v137, v145
	v_lshlrev_b32_e32 v145, 16, v186
	v_fma_f32 v138, v138, v176, -v145
	v_and_b32_e32 v145, 0xffff0000, v186
	v_fma_f32 v139, v139, v177, -v145
	v_cvt_pk_bf16_f32 v138, v138, v139
	v_lshlrev_b32_e32 v139, 16, v187
	v_fma_f32 v139, v150, v178, -v139
	v_and_b32_e32 v145, 0xffff0000, v187
	v_lshl_add_u64 v[148:149], s[82:83], 0, v[146:147]
	v_lshl_add_u64 v[146:147], s[76:77], 0, v[146:147]
	v_fma_f32 v145, v151, v179, -v145
	v_cvt_pk_bf16_f32 v139, v139, v145
	global_store_dwordx4 v[148:149], v[184:187], off nt
	s_cbranch_execnz .LBB0_595

.LBB0_595:
	v_readlane_b32 s2, v242, 50
	global_store_dwordx4 v[146:147], v[136:139], off nt
	s_add_i32 s2, s2, s73
	s_waitcnt lgkmcnt(0)
	s_add_i32 s2, s2, s72
	s_cmp_lt_i32 s2, s50
	s_cselect_b32 s23, s2, -1
	s_cmp_lt_i32 s23, 0
	s_cbranch_scc1 .LBB0_645
	s_mul_hi_u32 s2, s23, 0x9824d8ed
	s_lshr_b32 s2, s2, 15
	s_mul_i32 s3, s2, 0xd760
	s_sub_i32 s85, s23, s3
	s_cmpk_gt_u32 s85, 0xc2ff
	s_mov_b64 s[44:45], -1
	s_cbranch_scc0 .LBB0_625
	s_add_i32 s44, s2, 1
	s_add_i32 s3, s85, 0xffff3d00
	s_cmpk_lt_u32 s3, 0x1400
	s_cselect_b32 s3, s3, s85
	s_cmpk_gt_u32 s3, 0xbff
	s_mov_b64 s[48:49], -1
	s_cbranch_scc0 .LBB0_622
	s_cmpk_gt_u32 s3, 0x13ff
	s_cbranch_scc0 .LBB0_619
	s_cmpk_gt_u32 s3, 0x93ff
	s_cbranch_scc0 .LBB0_616
	s_cmpk_gt_u32 s3, 0xd3ff
	s_cbranch_scc0 .LBB0_613
	s_cmpk_gt_u32 s3, 0xd5ff
	s_cbranch_scc0 .LBB0_610
	s_cmpk_gt_u32 s3, 0xd6ff
	s_cbranch_scc0 .LBB0_607
	s_cmpk_gt_u32 s3, 0xd71f
	s_mov_b64 s[42:43], -1
	s_cbranch_scc0 .LBB0_605
	s_mov_b32 s45, s47
	v_readlane_b32 s48, v243, 40
	s_lshl_b64 s[24:25], s[44:45], 19
	v_readlane_b32 s54, v243, 46
	v_readlane_b32 s55, v243, 47
	s_add_u32 s40, s54, s24
	s_addc_u32 s41, s55, s25
	s_lshl_b64 s[26:27], s[44:45], 18
	v_readlane_b32 s22, v242, 42
	s_add_u32 s82, s22, s26
	v_readlane_b32 s22, v242, 43
	s_addc_u32 s83, s22, s27
	v_readlane_b32 s22, v242, 44
	s_add_u32 s76, s22, s26
	v_readlane_b32 s22, v242, 45
	v_readlane_b32 s50, v243, 42
	s_addc_u32 s77, s22, s27
	s_lshl_b32 s22, s44, 13
	v_readlane_b32 s51, v243, 43
	s_add_u32 s26, s50, s22
	s_addc_u32 s27, s51, 0
	s_lshl_b32 s42, s3, 5
	s_and_b32 s22, s42, 0x7fffffc0
	v_readlane_b32 s49, v243, 41
	v_readlane_b32 s52, v243, 44
	v_readlane_b32 s53, v243, 45
	v_readlane_b32 s56, v243, 48
	v_readlane_b32 s57, v243, 49
	v_readlane_b32 s58, v243, 50
	v_readlane_b32 s59, v243, 51
	v_readlane_b32 s60, v243, 52
	v_readlane_b32 s61, v243, 53
	v_readlane_b32 s62, v243, 54
	v_readlane_b32 s63, v243, 55
	s_mov_b32 s50, s79
	v_readlane_b32 s51, v242, 29
	s_add_i32 s22, s22, 0xffe51c00
	s_and_b32 s80, s42, 32
	s_mov_b64 s[42:43], 0

.LBB0_645:
	s_cmp_lt_i32 s81, 0
	s_mov_b64 s[2:3], -1
	s_cbranch_scc1 .LBB0_456
	ds_write2_b32 v160, v100, v101 offset1:1
	ds_write2_b32 v160, v102, v103 offset0:2 offset1:3
	ds_write2_b32 v161, v104, v105 offset1:1
	ds_write2_b32 v162, v106, v107 offset1:1
	ds_write2_b32 v163, v108, v109 offset1:1
	ds_write2_b32 v164, v110, v111 offset1:1
	ds_write2_b32 v165, v112, v113 offset1:1
	ds_write2_b32 v166, v114, v115 offset1:1
	ds_write2_b32 v167, v116, v117 offset1:1
	ds_write2_b32 v168, v118, v119 offset1:1
	ds_write2_b32 v169, v120, v121 offset1:1
	ds_write2_b32 v170, v122, v123 offset1:1
	ds_write2_b32 v171, v124, v125 offset1:1
	ds_write2_b32 v172, v126, v127 offset1:1
	ds_write2_b32 v173, v128, v129 offset1:1
	ds_write2_b32 v174, v130, v131 offset1:1
	s_waitcnt lgkmcnt(0)
	ds_read2_b32 v[136:137], v155 offset1:33
	ds_read2_b32 v[152:153], v155 offset0:66 offset1:99
	ds_read2_b32 v[138:139], v155 offset0:132 offset1:165
	ds_read2_b32 v[150:151], v155 offset0:198 offset1:231
	s_cmp_lg_u64 s[36:37], 0
	s_cselect_b64 s[40:41], -1, 0
	s_and_b64 vcc, exec, s[40:41]
	v_add_u32_e32 v2, s75, v1
	v_add_u32_e32 v146, s30, v142
	s_waitcnt lgkmcnt(3)
	v_cvt_pk_bf16_f32 v132, v136, v137
	s_waitcnt lgkmcnt(2)
	v_cvt_pk_bf16_f32 v133, v152, v153
	s_waitcnt lgkmcnt(1)
	v_cvt_pk_bf16_f32 v134, v138, v139
	s_waitcnt lgkmcnt(0)
	v_cvt_pk_bf16_f32 v135, v150, v151
	s_cbranch_vccz .LBB0_670
	v_lshlrev_b32_e32 v145, 2, v2
	v_and_b32_e32 v145, 0xffffffc0, v145
	v_ashrrev_i32_e32 v147, 5, v146
	v_add_u32_e32 v148, v145, v147
	v_ashrrev_i32_e32 v149, 31, v148
	v_lshlrev_b32_e32 v145, 1, v146
	v_lshlrev_b64 v[148:149], 6, v[148:149]
	v_and_b32_e32 v145, 48, v145
	v_and_b32_e32 v147, 15, v2
	v_or3_b32 v148, v148, v145, v147
	v_ashrrev_i32_e32 v147, 31, v146
	v_lshl_add_u64 v[166:167], v[146:147], 2, s[38:39]
	global_load_dwordx4 v[162:165], v[166:167], off offset:16
	s_nop 0
	global_load_dwordx4 v[166:169], v[166:167], off
	v_lshlrev_b64 v[148:149], 4, v[148:149]
	s_waitcnt vmcnt(1)
	v_mul_f32_e32 v172, v138, v162
	s_waitcnt vmcnt(0)
	v_mul_f32_e32 v145, v136, v166
	v_mul_f32_e32 v147, v137, v167
	v_cvt_pk_bf16_f32 v170, v145, v147
	v_mul_f32_e32 v171, v153, v169
	v_lshlrev_b32_e32 v145, 16, v170
	v_fma_f32 v136, v136, v166, -v145
	v_and_b32_e32 v145, 0xffff0000, v170
	v_mul_f32_e32 v173, v139, v163
	v_fma_f32 v137, v137, v167, -v145
	v_mul_f32_e32 v161, v152, v168
	v_mul_f32_e32 v174, v150, v164
	v_mul_f32_e32 v175, v151, v165
	v_cvt_pk_bf16_f32 v171, v161, v171
	v_cvt_pk_bf16_f32 v172, v172, v173
	v_cvt_pk_bf16_f32 v173, v174, v175
	v_cvt_pk_bf16_f32 v136, v136, v137
	s_nop 0
	v_lshlrev_b32_e32 v137, 16, v171
	v_and_b32_e32 v145, 0xffff0000, v171
	v_fma_f32 v137, v152, v168, -v137
	v_fma_f32 v145, v153, v169, -v145
	v_cvt_pk_bf16_f32 v137, v137, v145
	v_lshlrev_b32_e32 v145, 16, v172
	v_fma_f32 v138, v138, v162, -v145
	v_and_b32_e32 v145, 0xffff0000, v172
	v_fma_f32 v139, v139, v163, -v145
	v_cvt_pk_bf16_f32 v138, v138, v139
	v_lshlrev_b32_e32 v139, 16, v173
	v_and_b32_e32 v145, 0xffff0000, v173
	v_fma_f32 v139, v150, v164, -v139
	v_fma_f32 v145, v151, v165, -v145
	v_lshl_add_u64 v[150:151], s[34:35], 0, v[148:149]
	v_cvt_pk_bf16_f32 v139, v139, v145
	global_store_dwordx4 v[150:151], v[170:173], off nt
	v_lshl_add_u64 v[148:149], s[36:37], 0, v[148:149]
	s_cbranch_execnz .LBB0_649

.LBB0_649:
	global_store_dwordx4 v[148:149], v[136:139], off nt
	ds_read2_b32 v[136:137], v155 offset0:8 offset1:41
	ds_read2_b32 v[152:153], v155 offset0:74 offset1:107
	ds_read2_b32 v[138:139], v155 offset0:140 offset1:173
	ds_read2_b32 v[150:151], v155 offset0:206 offset1:239
	v_cndmask_b32_e64 v2, 0, 1, s[40:41]
	v_cmp_ne_u32_e64 s[2:3], 1, v2
	s_andn2_b64 vcc, exec, s[40:41]
	v_add_u32_e32 v2, s75, v141
	s_waitcnt lgkmcnt(3)
	v_cvt_pk_bf16_f32 v132, v136, v137
	s_waitcnt lgkmcnt(2)
	v_cvt_pk_bf16_f32 v133, v152, v153
	s_waitcnt lgkmcnt(1)
	v_cvt_pk_bf16_f32 v134, v138, v139
	s_waitcnt lgkmcnt(0)
	v_cvt_pk_bf16_f32 v135, v150, v151
	s_cbranch_vccnz .LBB0_671
	v_lshlrev_b32_e32 v145, 2, v2
	v_and_b32_e32 v145, 0xffffffc0, v145
	v_ashrrev_i32_e32 v147, 5, v146
	v_add_u32_e32 v148, v145, v147
	v_ashrrev_i32_e32 v149, 31, v148
	v_lshlrev_b32_e32 v145, 1, v146
	v_lshlrev_b64 v[148:149], 6, v[148:149]
	v_and_b32_e32 v145, 48, v145
	v_and_b32_e32 v147, 15, v2
	v_or3_b32 v148, v148, v145, v147
	v_ashrrev_i32_e32 v147, 31, v146
	v_lshl_add_u64 v[166:167], v[146:147], 2, s[38:39]
	global_load_dwordx4 v[162:165], v[166:167], off offset:16
	s_nop 0
	global_load_dwordx4 v[166:169], v[166:167], off
	v_lshlrev_b64 v[148:149], 4, v[148:149]
	s_waitcnt vmcnt(1)
	v_mul_f32_e32 v172, v138, v162
	s_waitcnt vmcnt(0)
	v_mul_f32_e32 v145, v136, v166
	v_mul_f32_e32 v147, v137, v167
	v_cvt_pk_bf16_f32 v170, v145, v147
	v_mul_f32_e32 v171, v153, v169
	v_lshlrev_b32_e32 v145, 16, v170
	v_fma_f32 v136, v136, v166, -v145
	v_and_b32_e32 v145, 0xffff0000, v170
	v_mul_f32_e32 v173, v139, v163
	v_fma_f32 v137, v137, v167, -v145
	v_mul_f32_e32 v161, v152, v168
	v_mul_f32_e32 v174, v150, v164
	v_mul_f32_e32 v175, v151, v165
	v_cvt_pk_bf16_f32 v171, v161, v171
	v_cvt_pk_bf16_f32 v172, v172, v173
	v_cvt_pk_bf16_f32 v173, v174, v175
	v_cvt_pk_bf16_f32 v136, v136, v137
	s_nop 0
	v_lshlrev_b32_e32 v137, 16, v171
	v_and_b32_e32 v145, 0xffff0000, v171
	v_fma_f32 v137, v152, v168, -v137
	v_fma_f32 v145, v153, v169, -v145
	v_cvt_pk_bf16_f32 v137, v137, v145
	v_lshlrev_b32_e32 v145, 16, v172
	v_fma_f32 v138, v138, v162, -v145
	v_and_b32_e32 v145, 0xffff0000, v172
	v_fma_f32 v139, v139, v163, -v145
	v_cvt_pk_bf16_f32 v138, v138, v139
	v_lshlrev_b32_e32 v139, 16, v173
	v_and_b32_e32 v145, 0xffff0000, v173
	v_fma_f32 v139, v150, v164, -v139
	v_fma_f32 v145, v151, v165, -v145
	v_lshl_add_u64 v[150:151], s[34:35], 0, v[148:149]
	v_lshl_add_u64 v[148:149], s[36:37], 0, v[148:149]
	v_cvt_pk_bf16_f32 v139, v139, v145
	global_store_dwordx4 v[150:151], v[170:173], off nt
	s_cbranch_execnz .LBB0_652

.LBB0_652:
	global_store_dwordx4 v[148:149], v[136:139], off nt
	ds_read2_b32 v[136:137], v155 offset0:16 offset1:49
	ds_read2_b32 v[152:153], v155 offset0:82 offset1:115
	ds_read2_b32 v[138:139], v155 offset0:148 offset1:181
	ds_read2_b32 v[150:151], v155 offset0:214 offset1:247
	s_and_b64 vcc, exec, s[2:3]
	v_add_u32_e32 v2, s75, v143
	s_waitcnt lgkmcnt(3)
	v_cvt_pk_bf16_f32 v132, v136, v137
	s_waitcnt lgkmcnt(2)
	v_cvt_pk_bf16_f32 v133, v152, v153
	s_waitcnt lgkmcnt(1)
	v_cvt_pk_bf16_f32 v134, v138, v139
	s_waitcnt lgkmcnt(0)
	v_cvt_pk_bf16_f32 v135, v150, v151
	s_cbranch_vccnz .LBB0_672
	v_lshlrev_b32_e32 v145, 2, v2
	v_and_b32_e32 v145, 0xffffffc0, v145
	v_ashrrev_i32_e32 v147, 5, v146
	v_add_u32_e32 v148, v145, v147
	v_ashrrev_i32_e32 v149, 31, v148
	v_lshlrev_b32_e32 v145, 1, v146
	v_lshlrev_b64 v[148:149], 6, v[148:149]
	v_and_b32_e32 v145, 48, v145
	v_and_b32_e32 v147, 15, v2
	v_or3_b32 v148, v148, v145, v147
	v_ashrrev_i32_e32 v147, 31, v146
	v_lshl_add_u64 v[166:167], v[146:147], 2, s[38:39]
	global_load_dwordx4 v[162:165], v[166:167], off offset:16
	s_nop 0
	global_load_dwordx4 v[166:169], v[166:167], off
	v_lshlrev_b64 v[148:149], 4, v[148:149]
	s_waitcnt vmcnt(1)
	v_mul_f32_e32 v172, v138, v162
	s_waitcnt vmcnt(0)
	v_mul_f32_e32 v145, v136, v166
	v_mul_f32_e32 v147, v137, v167
	v_cvt_pk_bf16_f32 v170, v145, v147
	v_mul_f32_e32 v171, v153, v169
	v_lshlrev_b32_e32 v145, 16, v170
	v_fma_f32 v136, v136, v166, -v145
	v_and_b32_e32 v145, 0xffff0000, v170
	v_mul_f32_e32 v173, v139, v163
	v_fma_f32 v137, v137, v167, -v145
	v_mul_f32_e32 v161, v152, v168
	v_mul_f32_e32 v174, v150, v164
	v_mul_f32_e32 v175, v151, v165
	v_cvt_pk_bf16_f32 v171, v161, v171
	v_cvt_pk_bf16_f32 v172, v172, v173
	v_cvt_pk_bf16_f32 v173, v174, v175
	v_cvt_pk_bf16_f32 v136, v136, v137
	s_nop 0
	v_lshlrev_b32_e32 v137, 16, v171
	v_and_b32_e32 v145, 0xffff0000, v171
	v_fma_f32 v137, v152, v168, -v137
	v_fma_f32 v145, v153, v169, -v145
	v_cvt_pk_bf16_f32 v137, v137, v145
	v_lshlrev_b32_e32 v145, 16, v172
	v_fma_f32 v138, v138, v162, -v145
	v_and_b32_e32 v145, 0xffff0000, v172
	v_fma_f32 v139, v139, v163, -v145
	v_cvt_pk_bf16_f32 v138, v138, v139
	v_lshlrev_b32_e32 v139, 16, v173
	v_and_b32_e32 v145, 0xffff0000, v173
	v_fma_f32 v139, v150, v164, -v139
	v_fma_f32 v145, v151, v165, -v145
	v_lshl_add_u64 v[150:151], s[34:35], 0, v[148:149]
	v_lshl_add_u64 v[148:149], s[36:37], 0, v[148:149]
	v_cvt_pk_bf16_f32 v139, v139, v145
	global_store_dwordx4 v[150:151], v[170:173], off nt
	s_cbranch_execnz .LBB0_655

.LBB0_655:
	global_store_dwordx4 v[148:149], v[136:139], off nt
	ds_read2_b32 v[136:137], v155 offset0:24 offset1:57
	ds_read2_b32 v[152:153], v155 offset0:90 offset1:123
	ds_read2_b32 v[138:139], v155 offset0:156 offset1:189
	ds_read2_b32 v[150:151], v155 offset0:222 offset1:255
	s_and_b64 vcc, exec, s[2:3]
	v_add_u32_e32 v2, s75, v154
	s_waitcnt lgkmcnt(3)
	v_cvt_pk_bf16_f32 v132, v136, v137
	s_waitcnt lgkmcnt(2)
	v_cvt_pk_bf16_f32 v133, v152, v153
	s_waitcnt lgkmcnt(1)
	v_cvt_pk_bf16_f32 v134, v138, v139
	s_waitcnt lgkmcnt(0)
	v_cvt_pk_bf16_f32 v135, v150, v151
	s_cbranch_vccnz .LBB0_673
	v_lshlrev_b32_e32 v145, 2, v2
	v_and_b32_e32 v145, 0xffffffc0, v145
	v_ashrrev_i32_e32 v147, 5, v146
	v_add_u32_e32 v148, v145, v147
	v_ashrrev_i32_e32 v149, 31, v148
	v_lshlrev_b32_e32 v145, 1, v146
	v_lshlrev_b64 v[148:149], 6, v[148:149]
	v_and_b32_e32 v145, 48, v145
	v_and_b32_e32 v147, 15, v2
	v_or3_b32 v148, v148, v145, v147
	v_ashrrev_i32_e32 v147, 31, v146
	v_lshl_add_u64 v[146:147], v[146:147], 2, s[38:39]
	global_load_dwordx4 v[162:165], v[146:147], off offset:16
	global_load_dwordx4 v[166:169], v[146:147], off
	s_waitcnt vmcnt(1)
	v_mul_f32_e32 v172, v138, v162
	s_waitcnt vmcnt(0)
	v_mul_f32_e32 v145, v136, v166
	v_mul_f32_e32 v146, v137, v167
	v_cvt_pk_bf16_f32 v170, v145, v146
	v_mul_f32_e32 v173, v139, v163
	v_lshlrev_b32_e32 v145, 16, v170
	v_fma_f32 v136, v136, v166, -v145
	v_and_b32_e32 v145, 0xffff0000, v170
	v_fma_f32 v137, v137, v167, -v145
	v_mul_f32_e32 v147, v152, v168
	v_mul_f32_e32 v161, v153, v169
	v_mul_f32_e32 v174, v150, v164
	v_mul_f32_e32 v175, v151, v165
	v_cvt_pk_bf16_f32 v171, v147, v161
	v_cvt_pk_bf16_f32 v172, v172, v173
	v_cvt_pk_bf16_f32 v173, v174, v175
	v_cvt_pk_bf16_f32 v136, v136, v137
	v_lshlrev_b64 v[146:147], 4, v[148:149]
	v_lshlrev_b32_e32 v137, 16, v171
	v_and_b32_e32 v145, 0xffff0000, v171
	v_fma_f32 v137, v152, v168, -v137
	v_fma_f32 v145, v153, v169, -v145
	v_cvt_pk_bf16_f32 v137, v137, v145
	v_lshlrev_b32_e32 v145, 16, v172
	v_fma_f32 v138, v138, v162, -v145
	v_and_b32_e32 v145, 0xffff0000, v172
	v_fma_f32 v139, v139, v163, -v145
	v_cvt_pk_bf16_f32 v138, v138, v139
	v_lshlrev_b32_e32 v139, 16, v173
	v_fma_f32 v139, v150, v164, -v139
	v_and_b32_e32 v145, 0xffff0000, v173
	v_lshl_add_u64 v[148:149], s[34:35], 0, v[146:147]
	v_lshl_add_u64 v[146:147], s[36:37], 0, v[146:147]
	v_fma_f32 v145, v151, v165, -v145
	v_cvt_pk_bf16_f32 v139, v139, v145
	global_store_dwordx4 v[148:149], v[170:173], off nt
	s_cbranch_execnz .LBB0_658

.LBB0_658:
	v_readlane_b32 s2, v242, 51
	global_store_dwordx4 v[146:147], v[136:139], off nt
	s_add_i32 s2, s2, s73
	s_waitcnt lgkmcnt(0)
	s_add_i32 s2, s2, s72
	s_cmp_lt_i32 s2, s50
	s_cselect_b32 s81, s2, -1
	s_cmp_lt_i32 s81, 0
	s_cbranch_scc1 .LBB0_455
	s_mul_hi_u32 s2, s81, 0x9824d8ed
	s_lshr_b32 s2, s2, 15
	s_mul_i32 s3, s2, 0xd760
	s_sub_i32 s72, s81, s3
	s_cmpk_gt_u32 s72, 0xc2ff
	s_mov_b64 s[44:45], -1
	s_cbranch_scc0 .LBB0_697
	s_add_i32 s44, s2, 1
	s_add_i32 s3, s72, 0xffff3d00
	s_cmpk_lt_u32 s3, 0x1400
	s_cselect_b32 s3, s3, s72
	s_cmpk_gt_u32 s3, 0xbff
	s_mov_b64 s[48:49], -1
	s_cbranch_scc0 .LBB0_694
	s_cmpk_gt_u32 s3, 0x13ff
	s_cbranch_scc0 .LBB0_691
	s_cmpk_gt_u32 s3, 0x93ff
	s_cbranch_scc0 .LBB0_688
	s_cmpk_gt_u32 s3, 0xd3ff
	s_cbranch_scc0 .LBB0_685
	s_cmpk_gt_u32 s3, 0xd5ff
	s_cbranch_scc0 .LBB0_682
	s_cmpk_gt_u32 s3, 0xd6ff
	s_cbranch_scc0 .LBB0_679
	s_cmpk_gt_u32 s3, 0xd71f
	s_mov_b64 s[42:43], -1
	s_cbranch_scc0 .LBB0_668
	s_mov_b32 s45, s47
	v_readlane_b32 s48, v243, 40
	s_lshl_b64 s[34:35], s[44:45], 19
	v_readlane_b32 s54, v243, 46
	v_readlane_b32 s55, v243, 47
	s_add_u32 s40, s54, s34
	s_addc_u32 s41, s55, s35
	s_lshl_b64 s[36:37], s[44:45], 18
	v_readlane_b32 s24, v242, 42
	s_add_u32 s34, s24, s36
	v_readlane_b32 s24, v242, 43
	s_addc_u32 s35, s24, s37
	v_readlane_b32 s24, v242, 44
	s_add_u32 s36, s24, s36
	v_readlane_b32 s24, v242, 45
	v_readlane_b32 s50, v243, 42
	s_addc_u32 s37, s24, s37
	s_lshl_b32 s30, s44, 13
	v_readlane_b32 s51, v243, 43
	s_add_u32 s38, s50, s30
	s_addc_u32 s39, s51, 0
	s_lshl_b32 s42, s3, 5
	s_and_b32 s30, s42, 0x7fffffc0
	v_readlane_b32 s49, v243, 41
	v_readlane_b32 s52, v243, 44
	v_readlane_b32 s53, v243, 45
	v_readlane_b32 s56, v243, 48
	v_readlane_b32 s57, v243, 49
	v_readlane_b32 s58, v243, 50
	v_readlane_b32 s59, v243, 51
	v_readlane_b32 s60, v243, 52
	v_readlane_b32 s61, v243, 53
	v_readlane_b32 s62, v243, 54
	v_readlane_b32 s63, v243, 55
	s_mov_b32 s50, s79
	v_readlane_b32 s51, v242, 29
	s_add_i32 s30, s30, 0xffe51c00
	s_and_b32 s75, s42, 32
	s_mov_b64 s[42:43], 0

.LBB0_1142:
	v_add_u32_e32 v4, s4, v73
	v_ashrrev_i32_e32 v5, 31, v4
	v_mul_lo_u32 v6, s22, v5
	v_mul_lo_u32 v7, s23, v4
	v_mad_u64_u32 v[4:5], s[2:3], s22, v4, 0
	v_add3_u32 v5, v5, v6, v7
	v_add_u32_e32 v6, s4, v72
	s_ashr_i32 s25, s24, 31
	v_ashrrev_i32_e32 v7, 31, v6
	s_lshl_b64 s[2:3], s[24:25], 2
	v_mul_lo_u32 v8, s22, v7
	v_mul_lo_u32 v9, s23, v6
	v_mad_u64_u32 v[6:7], s[24:25], s22, v6, 0
	v_lshl_add_u64 v[4:5], v[4:5], 2, s[20:21]
	v_add3_u32 v7, v7, v8, v9
	v_lshl_add_u64 v[4:5], v[4:5], 0, s[2:3]
	v_lshl_add_u64 v[6:7], v[6:7], 2, s[20:21]
	v_lshl_add_u64 v[4:5], v[4:5], 0, v[2:3]
	v_lshl_add_u64 v[6:7], v[6:7], 0, s[2:3]
	v_lshl_add_u64 v[6:7], v[6:7], 0, v[2:3]
	global_load_dwordx4 v[32:35], v[4:5], off nt
	global_load_dwordx4 v[20:23], v[6:7], off nt
	v_add_u32_e32 v4, s4, v71
	v_ashrrev_i32_e32 v5, 31, v4
	v_mul_lo_u32 v6, s22, v5
	v_mul_lo_u32 v7, s23, v4
	v_mad_u64_u32 v[4:5], s[24:25], s22, v4, 0
	v_add3_u32 v5, v5, v6, v7
	v_add_u32_e32 v6, s4, v70
	v_ashrrev_i32_e32 v7, 31, v6
	v_mul_lo_u32 v8, s22, v7
	v_mul_lo_u32 v9, s23, v6
	v_mad_u64_u32 v[6:7], s[24:25], s22, v6, 0
	v_lshl_add_u64 v[4:5], v[4:5], 2, s[20:21]
	v_add3_u32 v7, v7, v8, v9
	v_lshl_add_u64 v[4:5], v[4:5], 0, s[2:3]
	v_lshl_add_u64 v[6:7], v[6:7], 2, s[20:21]
	v_lshl_add_u64 v[4:5], v[4:5], 0, v[2:3]
	v_lshl_add_u64 v[6:7], v[6:7], 0, s[2:3]
	v_lshl_add_u64 v[6:7], v[6:7], 0, v[2:3]
	global_load_dwordx4 v[28:31], v[4:5], off nt
	global_load_dwordx4 v[12:15], v[6:7], off nt
	v_add_u32_e32 v4, s4, v79
	v_ashrrev_i32_e32 v5, 31, v4
	v_mul_lo_u32 v6, s22, v5
	v_mul_lo_u32 v7, s23, v4
	v_mad_u64_u32 v[4:5], s[24:25], s22, v4, 0
	v_add3_u32 v5, v5, v6, v7
	v_add_u32_e32 v6, s4, v80
	v_ashrrev_i32_e32 v7, 31, v6
	v_mul_lo_u32 v8, s22, v7
	v_mul_lo_u32 v9, s23, v6
	v_mad_u64_u32 v[6:7], s[24:25], s22, v6, 0
	v_lshl_add_u64 v[4:5], v[4:5], 2, s[20:21]
	v_add3_u32 v7, v7, v8, v9
	v_lshl_add_u64 v[4:5], v[4:5], 0, s[2:3]
	v_lshl_add_u64 v[6:7], v[6:7], 2, s[20:21]
	v_lshl_add_u64 v[4:5], v[4:5], 0, v[2:3]
	v_lshl_add_u64 v[6:7], v[6:7], 0, s[2:3]
	v_lshl_add_u64 v[6:7], v[6:7], 0, v[2:3]
	global_load_dwordx4 v[24:27], v[4:5], off nt
	global_load_dwordx4 v[8:11], v[6:7], off nt
	v_add_u32_e32 v4, s4, v81
	v_ashrrev_i32_e32 v5, 31, v4
	v_mul_lo_u32 v6, s22, v5
	v_mul_lo_u32 v7, s23, v4
	v_mad_u64_u32 v[4:5], s[24:25], s22, v4, 0
	v_add3_u32 v5, v5, v6, v7
	v_add_u32_e32 v6, s4, v82
	v_ashrrev_i32_e32 v7, 31, v6
	v_mul_lo_u32 v16, s22, v7
	v_mul_lo_u32 v17, s23, v6
	v_mad_u64_u32 v[6:7], s[22:23], s22, v6, 0
	v_add3_u32 v7, v7, v16, v17
	v_lshl_add_u64 v[4:5], v[4:5], 2, s[20:21]
	v_lshl_add_u64 v[6:7], v[6:7], 2, s[20:21]
	v_lshl_add_u64 v[4:5], v[4:5], 0, s[2:3]
	v_lshl_add_u64 v[6:7], v[6:7], 0, s[2:3]
	v_lshl_add_u64 v[4:5], v[4:5], 0, v[2:3]
	v_lshl_add_u64 v[6:7], v[6:7], 0, v[2:3]
	global_load_dwordx4 v[16:19], v[4:5], off nt
	s_nop 0
	global_load_dwordx4 v[4:7], v[6:7], off nt
	s_waitcnt vmcnt(15)
	ds_write2_b32 v86, v36, v37 offset1:1
	ds_write2_b32 v86, v38, v39 offset0:2 offset1:3
	v_add_u32_e32 v36, 0x420, v86
	s_waitcnt vmcnt(14)
	ds_write2_b32 v36, v40, v41 offset1:1
	v_add_u32_e32 v36, 0x428, v86
	ds_write2_b32 v36, v42, v43 offset1:1
	v_add_u32_e32 v36, 0x840, v86
	s_waitcnt vmcnt(13)
	ds_write2_b32 v36, v44, v45 offset1:1
	v_add_u32_e32 v36, 0x848, v86
	ds_write2_b32 v36, v46, v47 offset1:1
	v_add_u32_e32 v36, 0xc60, v86
	s_waitcnt vmcnt(12)
	ds_write2_b32 v36, v48, v49 offset1:1
	v_add_u32_e32 v36, 0xc68, v86
	ds_write2_b32 v36, v50, v51 offset1:1
	v_add_u32_e32 v36, 0x1080, v86
	s_waitcnt vmcnt(11)
	ds_write2_b32 v36, v52, v53 offset1:1
	v_add_u32_e32 v36, 0x1088, v86
	ds_write2_b32 v36, v54, v55 offset1:1
	v_add_u32_e32 v36, 0x14a0, v86
	s_waitcnt vmcnt(10)
	ds_write2_b32 v36, v56, v57 offset1:1
	v_add_u32_e32 v36, 0x14a8, v86
	ds_write2_b32 v36, v58, v59 offset1:1
	v_add_u32_e32 v36, 0x18c0, v86
	s_waitcnt vmcnt(9)
	ds_write2_b32 v36, v60, v61 offset1:1
	v_add_u32_e32 v36, 0x18c8, v86
	ds_write2_b32 v36, v62, v63 offset1:1
	v_add_u32_e32 v36, 0x1ce0, v86
	s_waitcnt vmcnt(8)
	ds_write2_b32 v36, v64, v65 offset1:1
	v_add_u32_e32 v36, 0x1ce8, v86
	ds_write2_b32 v36, v66, v67 offset1:1
	s_waitcnt lgkmcnt(0)
	ds_read2_b32 v[40:41], v85 offset1:33
	ds_read2_b32 v[48:49], v85 offset0:66 offset1:99
	ds_read2_b32 v[42:43], v85 offset0:132 offset1:165
	ds_read2_b32 v[46:47], v85 offset0:198 offset1:231
	s_cmp_lg_u64 s[14:15], 0
	s_cselect_b64 s[20:21], -1, 0
	v_add_u32_e32 v44, s8, v68
	s_and_b64 vcc, exec, s[20:21]
	v_add_u32_e32 v50, s36, v73
	v_ashrrev_i32_e32 v53, 5, v44
	v_lshlrev_b32_e32 v52, 1, v44
	v_ashrrev_i32_e32 v45, 31, v44
	s_waitcnt lgkmcnt(3)
	v_cvt_pk_bf16_f32 v36, v40, v41
	s_waitcnt lgkmcnt(2)
	v_cvt_pk_bf16_f32 v37, v48, v49
	s_waitcnt lgkmcnt(1)
	v_cvt_pk_bf16_f32 v38, v42, v43
	s_waitcnt lgkmcnt(0)
	v_cvt_pk_bf16_f32 v39, v46, v47
	s_cbranch_vccz .LBB0_1156
	v_lshlrev_b32_e32 v51, 2, v50
	v_and_b32_e32 v51, 0xffffffc0, v51
	v_add_u32_e32 v54, v51, v53
	v_ashrrev_i32_e32 v55, 31, v54
	v_lshlrev_b64 v[66:67], 6, v[54:55]
	v_and_b32_e32 v51, 48, v52
	v_and_b32_e32 v54, 15, v50
	v_lshl_add_u64 v[58:59], v[44:45], 2, s[18:19]
	v_or3_b32 v66, v66, v51, v54
	global_load_dwordx4 v[54:57], v[58:59], off offset:16
	s_nop 0
	global_load_dwordx4 v[58:61], v[58:59], off
	s_waitcnt vmcnt(1)
	v_mul_f32_e32 v65, v42, v54
	s_waitcnt vmcnt(0)
	v_mul_f32_e32 v51, v40, v58
	v_mul_f32_e32 v62, v41, v59
	v_cvt_pk_bf16_f32 v62, v51, v62
	v_mul_f32_e32 v63, v48, v60
	v_lshlrev_b32_e32 v51, 16, v62
	v_fma_f32 v40, v40, v58, -v51
	v_and_b32_e32 v51, 0xffff0000, v62
	v_mul_f32_e32 v64, v49, v61
	v_fma_f32 v41, v41, v59, -v51
	v_mul_f32_e32 v87, v43, v55
	v_mul_f32_e32 v88, v46, v56
	v_mul_f32_e32 v89, v47, v57
	v_cvt_pk_bf16_f32 v63, v63, v64
	v_cvt_pk_bf16_f32 v64, v65, v87
	v_cvt_pk_bf16_f32 v65, v88, v89
	v_cvt_pk_bf16_f32 v40, v40, v41
	s_nop 0
	v_lshlrev_b32_e32 v41, 16, v63
	v_fma_f32 v41, v48, v60, -v41
	v_and_b32_e32 v48, 0xffff0000, v63
	v_fma_f32 v48, v49, v61, -v48
	v_cvt_pk_bf16_f32 v41, v41, v48
	v_lshlrev_b32_e32 v48, 16, v64
	v_fma_f32 v42, v42, v54, -v48
	v_and_b32_e32 v48, 0xffff0000, v64
	v_fma_f32 v43, v43, v55, -v48
	v_cvt_pk_bf16_f32 v42, v42, v43
	v_lshlrev_b32_e32 v43, 16, v65
	v_fma_f32 v43, v46, v56, -v43
	v_and_b32_e32 v46, 0xffff0000, v65
	v_fma_f32 v46, v47, v57, -v46
	v_cvt_pk_bf16_f32 v43, v43, v46
	v_lshlrev_b64 v[46:47], 4, v[66:67]
	v_lshl_add_u64 v[48:49], s[10:11], 0, v[46:47]
	global_store_dwordx4 v[48:49], v[62:65], off nt
	v_lshl_add_u64 v[48:49], s[14:15], 0, v[46:47]
	v_lshlrev_b32_e32 v46, 1, v68
	s_cbranch_execnz .LBB0_1145

.LBB0_1145:
	global_store_dwordx4 v[48:49], v[40:43], off
	ds_read2_b32 v[40:41], v85 offset0:8 offset1:41
	ds_read2_b32 v[50:51], v85 offset0:74 offset1:107
	ds_read2_b32 v[42:43], v85 offset0:140 offset1:173
	ds_read2_b32 v[48:49], v85 offset0:206 offset1:239
	v_cndmask_b32_e64 v47, 0, 1, s[20:21]
	v_cmp_ne_u32_e64 s[2:3], 1, v47
	s_andn2_b64 vcc, exec, s[20:21]
	v_add_u32_e32 v47, s36, v72
	s_waitcnt lgkmcnt(3)
	v_cvt_pk_bf16_f32 v36, v40, v41
	s_waitcnt lgkmcnt(2)
	v_cvt_pk_bf16_f32 v37, v50, v51
	s_waitcnt lgkmcnt(1)
	v_cvt_pk_bf16_f32 v38, v42, v43
	s_waitcnt lgkmcnt(0)
	v_cvt_pk_bf16_f32 v39, v48, v49
	s_cbranch_vccnz .LBB0_1157
	v_lshlrev_b32_e32 v54, 2, v47
	v_and_b32_e32 v54, 0xffffffc0, v54
	v_add_u32_e32 v54, v54, v53
	v_ashrrev_i32_e32 v55, 31, v54
	v_lshlrev_b64 v[66:67], 6, v[54:55]
	v_and_b32_e32 v54, 48, v52
	v_and_b32_e32 v55, 15, v47
	v_lshl_add_u64 v[58:59], v[44:45], 2, s[18:19]
	v_or3_b32 v66, v66, v54, v55
	global_load_dwordx4 v[54:57], v[58:59], off offset:16
	s_nop 0
	global_load_dwordx4 v[58:61], v[58:59], off
	s_waitcnt vmcnt(1)
	v_mul_f32_e32 v87, v42, v54
	s_waitcnt vmcnt(0)
	v_mul_f32_e32 v62, v40, v58
	v_mul_f32_e32 v63, v41, v59
	v_mul_f32_e32 v64, v50, v60
	v_mul_f32_e32 v65, v51, v61
	v_mul_f32_e32 v88, v43, v55
	v_cvt_pk_bf16_f32 v62, v62, v63
	v_cvt_pk_bf16_f32 v63, v64, v65
	v_cvt_pk_bf16_f32 v64, v87, v88
	v_mul_f32_e32 v89, v48, v56
	v_lshlrev_b32_e32 v87, 16, v62
	v_fma_f32 v40, v40, v58, -v87
	v_and_b32_e32 v58, 0xffff0000, v62
	v_fma_f32 v41, v41, v59, -v58
	v_mul_f32_e32 v90, v49, v57
	v_cvt_pk_bf16_f32 v65, v89, v90
	v_cvt_pk_bf16_f32 v40, v40, v41
	v_lshlrev_b32_e32 v41, 16, v63
	v_fma_f32 v41, v50, v60, -v41
	v_and_b32_e32 v50, 0xffff0000, v63
	v_fma_f32 v50, v51, v61, -v50
	v_cvt_pk_bf16_f32 v41, v41, v50
	v_lshlrev_b32_e32 v50, 16, v64
	v_fma_f32 v42, v42, v54, -v50
	v_and_b32_e32 v50, 0xffff0000, v64
	v_fma_f32 v43, v43, v55, -v50
	v_cvt_pk_bf16_f32 v42, v42, v43
	v_lshlrev_b32_e32 v43, 16, v65
	v_fma_f32 v43, v48, v56, -v43
	v_and_b32_e32 v48, 0xffff0000, v65
	v_fma_f32 v48, v49, v57, -v48
	v_cvt_pk_bf16_f32 v43, v43, v48
	v_lshlrev_b64 v[48:49], 4, v[66:67]
	v_lshl_add_u64 v[50:51], s[10:11], 0, v[48:49]
	v_lshl_add_u64 v[48:49], s[14:15], 0, v[48:49]
	global_store_dwordx4 v[50:51], v[62:65], off nt
	s_cbranch_execnz .LBB0_1148

.LBB0_1148:
	global_store_dwordx4 v[48:49], v[40:43], off nt
	ds_read2_b32 v[40:41], v85 offset0:16 offset1:49
	ds_read2_b32 v[50:51], v85 offset0:82 offset1:115
	ds_read2_b32 v[42:43], v85 offset0:148 offset1:181
	ds_read2_b32 v[48:49], v85 offset0:214 offset1:247
	s_and_b64 vcc, exec, s[2:3]
	v_add_u32_e32 v47, s36, v71
	s_waitcnt lgkmcnt(3)
	v_cvt_pk_bf16_f32 v36, v40, v41
	s_waitcnt lgkmcnt(2)
	v_cvt_pk_bf16_f32 v37, v50, v51
	s_waitcnt lgkmcnt(1)
	v_cvt_pk_bf16_f32 v38, v42, v43
	s_waitcnt lgkmcnt(0)
	v_cvt_pk_bf16_f32 v39, v48, v49
	s_cbranch_vccnz .LBB0_1158
	v_lshlrev_b32_e32 v54, 2, v47
	v_and_b32_e32 v54, 0xffffffc0, v54
	v_add_u32_e32 v54, v54, v53
	v_ashrrev_i32_e32 v55, 31, v54
	v_lshlrev_b64 v[66:67], 6, v[54:55]
	v_and_b32_e32 v54, 48, v52
	v_and_b32_e32 v55, 15, v47
	v_lshl_add_u64 v[58:59], v[44:45], 2, s[18:19]
	v_or3_b32 v66, v66, v54, v55
	global_load_dwordx4 v[54:57], v[58:59], off offset:16
	s_nop 0
	global_load_dwordx4 v[58:61], v[58:59], off
	s_waitcnt vmcnt(1)
	v_mul_f32_e32 v87, v42, v54
	s_waitcnt vmcnt(0)
	v_mul_f32_e32 v62, v40, v58
	v_mul_f32_e32 v63, v41, v59
	v_mul_f32_e32 v64, v50, v60
	v_mul_f32_e32 v65, v51, v61
	v_mul_f32_e32 v88, v43, v55
	v_cvt_pk_bf16_f32 v62, v62, v63
	v_cvt_pk_bf16_f32 v63, v64, v65
	v_cvt_pk_bf16_f32 v64, v87, v88
	v_mul_f32_e32 v89, v48, v56
	v_lshlrev_b32_e32 v87, 16, v62
	v_fma_f32 v40, v40, v58, -v87
	v_and_b32_e32 v58, 0xffff0000, v62
	v_fma_f32 v41, v41, v59, -v58
	v_mul_f32_e32 v90, v49, v57
	v_cvt_pk_bf16_f32 v65, v89, v90
	v_cvt_pk_bf16_f32 v40, v40, v41
	v_lshlrev_b32_e32 v41, 16, v63
	v_fma_f32 v41, v50, v60, -v41
	v_and_b32_e32 v50, 0xffff0000, v63
	v_fma_f32 v50, v51, v61, -v50
	v_cvt_pk_bf16_f32 v41, v41, v50
	v_lshlrev_b32_e32 v50, 16, v64
	v_fma_f32 v42, v42, v54, -v50
	v_and_b32_e32 v50, 0xffff0000, v64
	v_fma_f32 v43, v43, v55, -v50
	v_cvt_pk_bf16_f32 v42, v42, v43
	v_lshlrev_b32_e32 v43, 16, v65
	v_fma_f32 v43, v48, v56, -v43
	v_and_b32_e32 v48, 0xffff0000, v65
	v_fma_f32 v48, v49, v57, -v48
	v_cvt_pk_bf16_f32 v43, v43, v48
	v_lshlrev_b64 v[48:49], 4, v[66:67]
	v_lshl_add_u64 v[50:51], s[10:11], 0, v[48:49]
	v_lshl_add_u64 v[48:49], s[14:15], 0, v[48:49]
	global_store_dwordx4 v[50:51], v[62:65], off nt
	s_cbranch_execnz .LBB0_1151

.LBB0_1151:
	global_store_dwordx4 v[48:49], v[40:43], off nt
	ds_read2_b32 v[40:41], v85 offset0:24 offset1:57
	ds_read2_b32 v[50:51], v85 offset0:90 offset1:123
	ds_read2_b32 v[42:43], v85 offset0:156 offset1:189
	ds_read2_b32 v[48:49], v85 offset0:222 offset1:255
	s_and_b64 vcc, exec, s[2:3]
	v_add_u32_e32 v47, s36, v70
	s_waitcnt lgkmcnt(3)
	v_cvt_pk_bf16_f32 v36, v40, v41
	s_waitcnt lgkmcnt(2)
	v_cvt_pk_bf16_f32 v37, v50, v51
	s_waitcnt lgkmcnt(1)
	v_cvt_pk_bf16_f32 v38, v42, v43
	s_waitcnt lgkmcnt(0)
	v_cvt_pk_bf16_f32 v39, v48, v49
	s_cbranch_vccnz .LBB0_1159
	v_lshlrev_b32_e32 v54, 2, v47
	v_and_b32_e32 v54, 0xffffffc0, v54
	v_add_u32_e32 v54, v54, v53
	v_ashrrev_i32_e32 v55, 31, v54
	v_lshlrev_b64 v[64:65], 6, v[54:55]
	v_and_b32_e32 v52, 48, v52
	v_and_b32_e32 v53, 15, v47
	v_lshl_add_u64 v[44:45], v[44:45], 2, s[18:19]
	v_or3_b32 v64, v64, v52, v53
	global_load_dwordx4 v[52:55], v[44:45], off offset:16
	global_load_dwordx4 v[56:59], v[44:45], off
	s_waitcnt vmcnt(1)
	v_mul_f32_e32 v63, v42, v52
	s_waitcnt vmcnt(0)
	v_mul_f32_e32 v44, v40, v56
	v_mul_f32_e32 v45, v41, v57
	v_cvt_pk_bf16_f32 v60, v44, v45
	v_mul_f32_e32 v61, v50, v58
	v_lshlrev_b32_e32 v44, 16, v60
	v_fma_f32 v40, v40, v56, -v44
	v_and_b32_e32 v44, 0xffff0000, v60
	v_mul_f32_e32 v62, v51, v59
	v_fma_f32 v41, v41, v57, -v44
	v_mul_f32_e32 v66, v43, v53
	v_mul_f32_e32 v67, v48, v54
	v_mul_f32_e32 v87, v49, v55
	v_cvt_pk_bf16_f32 v61, v61, v62
	v_cvt_pk_bf16_f32 v62, v63, v66
	v_cvt_pk_bf16_f32 v63, v67, v87
	v_cvt_pk_bf16_f32 v40, v40, v41
	s_nop 0
	v_lshlrev_b32_e32 v41, 16, v61
	v_and_b32_e32 v44, 0xffff0000, v61
	v_fma_f32 v41, v50, v58, -v41
	v_fma_f32 v44, v51, v59, -v44
	v_cvt_pk_bf16_f32 v41, v41, v44
	v_lshlrev_b32_e32 v44, 16, v62
	v_fma_f32 v42, v42, v52, -v44
	v_and_b32_e32 v44, 0xffff0000, v62
	v_fma_f32 v43, v43, v53, -v44
	v_cvt_pk_bf16_f32 v42, v42, v43
	v_lshlrev_b32_e32 v43, 16, v63
	v_and_b32_e32 v44, 0xffff0000, v63
	v_fma_f32 v43, v48, v54, -v43
	v_fma_f32 v44, v49, v55, -v44
	v_cvt_pk_bf16_f32 v43, v43, v44
	v_lshlrev_b64 v[44:45], 4, v[64:65]
	v_lshl_add_u64 v[48:49], s[10:11], 0, v[44:45]
	v_lshl_add_u64 v[44:45], s[14:15], 0, v[44:45]
	global_store_dwordx4 v[48:49], v[60:63], off nt
	s_cbranch_execnz .LBB0_1154

.LBB0_1154:
	global_store_dwordx4 v[44:45], v[40:43], off nt
	s_waitcnt lgkmcnt(0)
	s_add_i32 s37, s37, s5
	s_add_i32 s57, s57, s58
	s_cmp_ge_i32 s37, s30
	s_cbranch_scc1 .LBB0_1163
	s_mov_b32 s36, s35
	s_mov_b32 s8, s4
	s_mov_b32 s34, s31
	s_mov_b64 s[18:19], s[16:17]
	s_mov_b64 s[14:15], s[12:13]
	s_mov_b64 s[10:11], s[6:7]
	s_waitcnt vmcnt(11)
	v_mov_b32_e32 v36, v32
	v_mov_b32_e32 v37, v33
	v_mov_b32_e32 v38, v34
	v_mov_b32_e32 v39, v35
	s_waitcnt vmcnt(10)
	v_mov_b32_e32 v40, v20
	v_mov_b32_e32 v41, v21
	v_mov_b32_e32 v42, v22
	v_mov_b32_e32 v43, v23
	s_waitcnt vmcnt(9)
	v_mov_b32_e32 v44, v28
	v_mov_b32_e32 v45, v29
	v_mov_b32_e32 v46, v30
	v_mov_b32_e32 v47, v31
	s_waitcnt vmcnt(8)
	v_mov_b32_e32 v48, v12
	v_mov_b32_e32 v49, v13
	v_mov_b32_e32 v50, v14
	v_mov_b32_e32 v51, v15
	s_waitcnt vmcnt(7)
	v_mov_b32_e32 v52, v24
	v_mov_b32_e32 v53, v25
	v_mov_b32_e32 v54, v26
	v_mov_b32_e32 v55, v27
	s_waitcnt vmcnt(6)
	v_mov_b32_e32 v56, v8
	v_mov_b32_e32 v57, v9
	v_mov_b32_e32 v58, v10
	v_mov_b32_e32 v59, v11
	s_waitcnt vmcnt(5)
	v_mov_b32_e32 v60, v16
	v_mov_b32_e32 v61, v17
	v_mov_b32_e32 v62, v18
	v_mov_b32_e32 v63, v19
	s_waitcnt vmcnt(4)
	v_mov_b32_e32 v64, v4
	v_mov_b32_e32 v65, v5
	v_mov_b32_e32 v66, v6
	v_mov_b32_e32 v67, v7
	s_branch .LBB0_1092

.LBB0_1163:
	v_add_u32_e32 v2, v84, v76
	s_waitcnt vmcnt(11)
	ds_write2_b32 v2, v32, v33 offset1:1
	ds_write2_b32 v2, v34, v35 offset0:2 offset1:3
	v_add_u32_e32 v32, v84, v77
	s_waitcnt vmcnt(10)
	ds_write2_b32 v32, v20, v21 offset1:1
	ds_write2_b32 v32, v22, v23 offset0:2 offset1:3
	v_add_u32_e32 v20, v84, v74
	s_waitcnt vmcnt(9)
	ds_write2_b32 v20, v28, v29 offset1:1
	ds_write2_b32 v20, v30, v31 offset0:2 offset1:3
	v_add_u32_e32 v20, v84, v75
	s_waitcnt vmcnt(8)
	ds_write2_b32 v20, v12, v13 offset1:1
	ds_write2_b32 v20, v14, v15 offset0:2 offset1:3
	v_add_u32_e32 v12, 0x1080, v2
	s_waitcnt vmcnt(7)
	ds_write2_b32 v12, v24, v25 offset1:1
	v_add_u32_e32 v12, 0x1088, v2
	ds_write2_b32 v12, v26, v27 offset1:1
	v_add_u32_e32 v12, 0x14a0, v2
	s_waitcnt vmcnt(6)
	ds_write2_b32 v12, v8, v9 offset1:1
	v_add_u32_e32 v8, 0x14a8, v2
	ds_write2_b32 v8, v10, v11 offset1:1
	v_add_u32_e32 v8, 0x18c0, v2
	s_waitcnt vmcnt(5)
	ds_write2_b32 v8, v16, v17 offset1:1
	v_add_u32_e32 v8, 0x18c8, v2
	ds_write2_b32 v8, v18, v19 offset1:1
	v_add_u32_e32 v8, 0x1ce0, v2
	v_add_u32_e32 v2, 0x1ce8, v2
	s_waitcnt vmcnt(4)
	ds_write2_b32 v8, v4, v5 offset1:1
	ds_write2_b32 v2, v6, v7 offset1:1
	s_waitcnt lgkmcnt(0)
	v_add3_u32 v18, s38, v78, v83
	ds_read2_b32 v[8:9], v18 offset1:33
	ds_read2_b32 v[16:17], v18 offset0:66 offset1:99
	ds_read2_b32 v[10:11], v18 offset0:132 offset1:165
	ds_read2_b32 v[14:15], v18 offset0:198 offset1:231
	s_cmp_lg_u64 s[12:13], 0
	s_cselect_b64 s[8:9], -1, 0
	v_add_u32_e32 v12, s4, v68
	s_and_b64 vcc, exec, s[8:9]
	v_add_u32_e32 v20, s35, v73
	v_ashrrev_i32_e32 v19, 5, v12
	v_lshlrev_b32_e32 v2, 1, v12
	v_ashrrev_i32_e32 v13, 31, v12
	s_waitcnt lgkmcnt(3)
	v_cvt_pk_bf16_f32 v4, v8, v9
	s_waitcnt lgkmcnt(2)
	v_cvt_pk_bf16_f32 v5, v16, v17
	s_waitcnt lgkmcnt(1)
	v_cvt_pk_bf16_f32 v6, v10, v11
	s_waitcnt lgkmcnt(0)
	v_cvt_pk_bf16_f32 v7, v14, v15
	s_cbranch_vccz .LBB0_1292
	v_lshlrev_b32_e32 v21, 2, v20
	v_and_b32_e32 v21, 0xffffffc0, v21
	v_add_u32_e32 v22, v21, v19
	v_ashrrev_i32_e32 v23, 31, v22
	v_lshlrev_b64 v[34:35], 6, v[22:23]
	v_and_b32_e32 v21, 48, v2
	v_and_b32_e32 v22, 15, v20
	v_lshl_add_u64 v[26:27], v[12:13], 2, s[16:17]
	v_or3_b32 v34, v34, v21, v22
	global_load_dwordx4 v[22:25], v[26:27], off offset:16
	s_nop 0
	global_load_dwordx4 v[26:29], v[26:27], off
	s_waitcnt vmcnt(1)
	v_mul_f32_e32 v33, v10, v22
	s_waitcnt vmcnt(0)
	v_mul_f32_e32 v21, v8, v26
	v_mul_f32_e32 v30, v9, v27
	v_cvt_pk_bf16_f32 v30, v21, v30
	v_mul_f32_e32 v31, v16, v28
	v_lshlrev_b32_e32 v21, 16, v30
	v_fma_f32 v8, v8, v26, -v21
	v_and_b32_e32 v21, 0xffff0000, v30
	v_mul_f32_e32 v32, v17, v29
	v_fma_f32 v9, v9, v27, -v21
	v_mul_f32_e32 v36, v11, v23
	v_mul_f32_e32 v37, v14, v24
	v_mul_f32_e32 v38, v15, v25
	v_cvt_pk_bf16_f32 v31, v31, v32
	v_cvt_pk_bf16_f32 v32, v33, v36
	v_cvt_pk_bf16_f32 v33, v37, v38
	v_cvt_pk_bf16_f32 v8, v8, v9
	s_nop 0
	v_lshlrev_b32_e32 v9, 16, v31
	v_fma_f32 v9, v16, v28, -v9
	v_and_b32_e32 v16, 0xffff0000, v31
	v_fma_f32 v16, v17, v29, -v16
	v_cvt_pk_bf16_f32 v9, v9, v16
	v_lshlrev_b32_e32 v16, 16, v32
	v_fma_f32 v10, v10, v22, -v16
	v_and_b32_e32 v16, 0xffff0000, v32
	v_fma_f32 v11, v11, v23, -v16
	v_cvt_pk_bf16_f32 v10, v10, v11
	v_lshlrev_b32_e32 v11, 16, v33
	v_fma_f32 v11, v14, v24, -v11
	v_and_b32_e32 v14, 0xffff0000, v33
	v_fma_f32 v14, v15, v25, -v14
	v_cvt_pk_bf16_f32 v11, v11, v14
	v_lshlrev_b64 v[14:15], 4, v[34:35]
	v_lshl_add_u64 v[16:17], s[6:7], 0, v[14:15]
	global_store_dwordx4 v[16:17], v[30:33], off nt
	v_lshl_add_u64 v[14:15], s[12:13], 0, v[14:15]
	s_cbranch_execnz .LBB0_1166

.LBB0_1166:
	global_store_dwordx4 v[14:15], v[8:11], off nt
	ds_read2_b32 v[8:9], v18 offset0:8 offset1:41
	ds_read2_b32 v[16:17], v18 offset0:74 offset1:107
	ds_read2_b32 v[10:11], v18 offset0:140 offset1:173
	ds_read2_b32 v[14:15], v18 offset0:206 offset1:239
	v_cndmask_b32_e64 v20, 0, 1, s[8:9]
	v_cmp_ne_u32_e64 s[2:3], 1, v20
	s_andn2_b64 vcc, exec, s[8:9]
	v_add_u32_e32 v20, s35, v72
	s_waitcnt lgkmcnt(3)
	v_cvt_pk_bf16_f32 v4, v8, v9
	s_waitcnt lgkmcnt(2)
	v_cvt_pk_bf16_f32 v5, v16, v17
	s_waitcnt lgkmcnt(1)
	v_cvt_pk_bf16_f32 v6, v10, v11
	s_waitcnt lgkmcnt(0)
	v_cvt_pk_bf16_f32 v7, v14, v15
	s_cbranch_vccnz .LBB0_1293
	v_lshlrev_b32_e32 v21, 2, v20
	v_and_b32_e32 v21, 0xffffffc0, v21
	v_add_u32_e32 v22, v21, v19
	v_ashrrev_i32_e32 v23, 31, v22
	v_lshlrev_b64 v[34:35], 6, v[22:23]
	v_and_b32_e32 v21, 48, v2
	v_and_b32_e32 v22, 15, v20
	v_lshl_add_u64 v[26:27], v[12:13], 2, s[16:17]
	v_or3_b32 v34, v34, v21, v22
	global_load_dwordx4 v[22:25], v[26:27], off offset:16
	s_nop 0
	global_load_dwordx4 v[26:29], v[26:27], off
	s_waitcnt vmcnt(1)
	v_mul_f32_e32 v33, v10, v22
	s_waitcnt vmcnt(0)
	v_mul_f32_e32 v21, v8, v26
	v_mul_f32_e32 v30, v9, v27
	v_cvt_pk_bf16_f32 v30, v21, v30
	v_mul_f32_e32 v31, v16, v28
	v_lshlrev_b32_e32 v21, 16, v30
	v_fma_f32 v8, v8, v26, -v21
	v_and_b32_e32 v21, 0xffff0000, v30
	v_mul_f32_e32 v32, v17, v29
	v_fma_f32 v9, v9, v27, -v21
	v_mul_f32_e32 v36, v11, v23
	v_mul_f32_e32 v37, v14, v24
	v_mul_f32_e32 v38, v15, v25
	v_cvt_pk_bf16_f32 v31, v31, v32
	v_cvt_pk_bf16_f32 v32, v33, v36
	v_cvt_pk_bf16_f32 v33, v37, v38
	v_cvt_pk_bf16_f32 v8, v8, v9
	s_nop 0
	v_lshlrev_b32_e32 v9, 16, v31
	v_fma_f32 v9, v16, v28, -v9
	v_and_b32_e32 v16, 0xffff0000, v31
	v_fma_f32 v16, v17, v29, -v16
	v_cvt_pk_bf16_f32 v9, v9, v16
	v_lshlrev_b32_e32 v16, 16, v32
	v_fma_f32 v10, v10, v22, -v16
	v_and_b32_e32 v16, 0xffff0000, v32
	v_fma_f32 v11, v11, v23, -v16
	v_cvt_pk_bf16_f32 v10, v10, v11
	v_lshlrev_b32_e32 v11, 16, v33
	v_fma_f32 v11, v14, v24, -v11
	v_and_b32_e32 v14, 0xffff0000, v33
	v_fma_f32 v14, v15, v25, -v14
	v_cvt_pk_bf16_f32 v11, v11, v14
	v_lshlrev_b64 v[14:15], 4, v[34:35]
	v_lshl_add_u64 v[16:17], s[6:7], 0, v[14:15]
	v_lshl_add_u64 v[14:15], s[12:13], 0, v[14:15]
	global_store_dwordx4 v[16:17], v[30:33], off nt
	s_cbranch_execnz .LBB0_1169

.LBB0_1169:
	global_store_dwordx4 v[14:15], v[8:11], off nt
	ds_read2_b32 v[8:9], v18 offset0:16 offset1:49
	ds_read2_b32 v[16:17], v18 offset0:82 offset1:115
	ds_read2_b32 v[10:11], v18 offset0:148 offset1:181
	ds_read2_b32 v[14:15], v18 offset0:214 offset1:247
	s_and_b64 vcc, exec, s[2:3]
	v_add_u32_e32 v20, s35, v71
	s_waitcnt lgkmcnt(3)
	v_cvt_pk_bf16_f32 v4, v8, v9
	s_waitcnt lgkmcnt(2)
	v_cvt_pk_bf16_f32 v5, v16, v17
	s_waitcnt lgkmcnt(1)
	v_cvt_pk_bf16_f32 v6, v10, v11
	s_waitcnt lgkmcnt(0)
	v_cvt_pk_bf16_f32 v7, v14, v15
	s_cbranch_vccnz .LBB0_1294
	v_lshlrev_b32_e32 v21, 2, v20
	v_and_b32_e32 v21, 0xffffffc0, v21
	v_add_u32_e32 v22, v21, v19
	v_ashrrev_i32_e32 v23, 31, v22
	v_lshlrev_b64 v[34:35], 6, v[22:23]
	v_and_b32_e32 v21, 48, v2
	v_and_b32_e32 v22, 15, v20
	v_lshl_add_u64 v[26:27], v[12:13], 2, s[16:17]
	v_or3_b32 v34, v34, v21, v22
	global_load_dwordx4 v[22:25], v[26:27], off offset:16
	s_nop 0
	global_load_dwordx4 v[26:29], v[26:27], off
	s_waitcnt vmcnt(1)
	v_mul_f32_e32 v33, v10, v22
	s_waitcnt vmcnt(0)
	v_mul_f32_e32 v21, v8, v26
	v_mul_f32_e32 v30, v9, v27
	v_cvt_pk_bf16_f32 v30, v21, v30
	v_mul_f32_e32 v31, v16, v28
	v_lshlrev_b32_e32 v21, 16, v30
	v_fma_f32 v8, v8, v26, -v21
	v_and_b32_e32 v21, 0xffff0000, v30
	v_mul_f32_e32 v32, v17, v29
	v_fma_f32 v9, v9, v27, -v21
	v_mul_f32_e32 v36, v11, v23
	v_mul_f32_e32 v37, v14, v24
	v_mul_f32_e32 v38, v15, v25
	v_cvt_pk_bf16_f32 v31, v31, v32
	v_cvt_pk_bf16_f32 v32, v33, v36
	v_cvt_pk_bf16_f32 v33, v37, v38
	v_cvt_pk_bf16_f32 v8, v8, v9
	s_nop 0
	v_lshlrev_b32_e32 v9, 16, v31
	v_fma_f32 v9, v16, v28, -v9
	v_and_b32_e32 v16, 0xffff0000, v31
	v_fma_f32 v16, v17, v29, -v16
	v_cvt_pk_bf16_f32 v9, v9, v16
	v_lshlrev_b32_e32 v16, 16, v32
	v_fma_f32 v10, v10, v22, -v16
	v_and_b32_e32 v16, 0xffff0000, v32
	v_fma_f32 v11, v11, v23, -v16
	v_cvt_pk_bf16_f32 v10, v10, v11
	v_lshlrev_b32_e32 v11, 16, v33
	v_fma_f32 v11, v14, v24, -v11
	v_and_b32_e32 v14, 0xffff0000, v33
	v_fma_f32 v14, v15, v25, -v14
	v_cvt_pk_bf16_f32 v11, v11, v14
	v_lshlrev_b64 v[14:15], 4, v[34:35]
	v_lshl_add_u64 v[16:17], s[6:7], 0, v[14:15]
	v_lshl_add_u64 v[14:15], s[12:13], 0, v[14:15]
	global_store_dwordx4 v[16:17], v[30:33], off nt
	s_cbranch_execnz .LBB0_1172

.LBB0_1172:
	global_store_dwordx4 v[14:15], v[8:11], off nt
	ds_read2_b32 v[8:9], v18 offset0:24 offset1:57
	ds_read2_b32 v[16:17], v18 offset0:90 offset1:123
	ds_read2_b32 v[10:11], v18 offset0:156 offset1:189
	ds_read2_b32 v[14:15], v18 offset0:222 offset1:255
	s_and_b64 vcc, exec, s[2:3]
	v_add_u32_e32 v18, s35, v70
	s_waitcnt lgkmcnt(3)
	v_cvt_pk_bf16_f32 v4, v8, v9
	s_waitcnt lgkmcnt(2)
	v_cvt_pk_bf16_f32 v5, v16, v17
	s_waitcnt lgkmcnt(1)
	v_cvt_pk_bf16_f32 v6, v10, v11
	s_waitcnt lgkmcnt(0)
	v_cvt_pk_bf16_f32 v7, v14, v15
	s_cbranch_vccnz .LBB0_1295
	v_lshlrev_b32_e32 v20, 2, v18
	v_and_b32_e32 v20, 0xffffffc0, v20
	v_add_u32_e32 v20, v20, v19
	v_ashrrev_i32_e32 v21, 31, v20
	v_lshl_add_u64 v[12:13], v[12:13], 2, s[16:17]
	v_lshlrev_b64 v[32:33], 6, v[20:21]
	global_load_dwordx4 v[20:23], v[12:13], off offset:16
	global_load_dwordx4 v[24:27], v[12:13], off
	v_and_b32_e32 v2, 48, v2
	v_and_b32_e32 v19, 15, v18
	v_or3_b32 v32, v32, v2, v19
	s_waitcnt vmcnt(1)
	v_mul_f32_e32 v30, v10, v20
	s_waitcnt vmcnt(0)
	v_mul_f32_e32 v2, v8, v24
	v_mul_f32_e32 v12, v9, v25
	v_cvt_pk_bf16_f32 v28, v2, v12
	v_mul_f32_e32 v31, v11, v21
	v_lshlrev_b32_e32 v2, 16, v28
	v_fma_f32 v2, v8, v24, -v2
	v_and_b32_e32 v8, 0xffff0000, v28
	v_fma_f32 v8, v9, v25, -v8
	v_mul_f32_e32 v13, v16, v26
	v_mul_f32_e32 v19, v17, v27
	v_mul_f32_e32 v34, v14, v22
	v_mul_f32_e32 v35, v15, v23
	v_cvt_pk_bf16_f32 v29, v13, v19
	v_cvt_pk_bf16_f32 v30, v30, v31
	v_cvt_pk_bf16_f32 v31, v34, v35
	v_cvt_pk_bf16_f32 v8, v2, v8
	v_lshlrev_b64 v[12:13], 4, v[32:33]
	v_lshlrev_b32_e32 v2, 16, v29
	v_and_b32_e32 v9, 0xffff0000, v29
	v_fma_f32 v2, v16, v26, -v2
	v_fma_f32 v9, v17, v27, -v9
	v_cvt_pk_bf16_f32 v9, v2, v9
	v_lshlrev_b32_e32 v2, 16, v30
	v_fma_f32 v2, v10, v20, -v2
	v_and_b32_e32 v10, 0xffff0000, v30
	v_fma_f32 v10, v11, v21, -v10
	v_cvt_pk_bf16_f32 v10, v2, v10
	v_lshlrev_b32_e32 v2, 16, v31
	v_and_b32_e32 v11, 0xffff0000, v31
	v_fma_f32 v2, v14, v22, -v2
	v_fma_f32 v11, v15, v23, -v11
	v_lshl_add_u64 v[14:15], s[6:7], 0, v[12:13]
	v_lshl_add_u64 v[12:13], s[12:13], 0, v[12:13]
	v_cvt_pk_bf16_f32 v11, v2, v11
	global_store_dwordx4 v[14:15], v[28:31], off nt
	s_cbranch_execnz .LBB0_1175

.LBB0_1175:
	global_store_dwordx4 v[12:13], v[8:11], off nt
	s_waitcnt lgkmcnt(0)

.LBB0_1394:
	v_add_u32_e32 v4, s4, v75
	v_ashrrev_i32_e32 v5, 31, v4
	v_mul_lo_u32 v6, s22, v5
	v_mul_lo_u32 v7, s23, v4
	v_mad_u64_u32 v[4:5], s[2:3], s22, v4, 0
	v_add3_u32 v5, v5, v6, v7
	v_add_u32_e32 v6, s4, v74
	s_ashr_i32 s25, s24, 31
	v_ashrrev_i32_e32 v7, 31, v6
	s_lshl_b64 s[2:3], s[24:25], 2
	v_mul_lo_u32 v8, s22, v7
	v_mul_lo_u32 v9, s23, v6
	v_mad_u64_u32 v[6:7], s[24:25], s22, v6, 0
	v_lshl_add_u64 v[4:5], v[4:5], 2, s[20:21]
	v_add3_u32 v7, v7, v8, v9
	v_lshl_add_u64 v[4:5], v[4:5], 0, s[2:3]
	v_lshl_add_u64 v[6:7], v[6:7], 2, s[20:21]
	v_lshl_add_u64 v[4:5], v[4:5], 0, v[2:3]
	v_lshl_add_u64 v[6:7], v[6:7], 0, s[2:3]
	v_lshl_add_u64 v[6:7], v[6:7], 0, v[2:3]
	global_load_dwordx4 v[32:35], v[4:5], off nt
	global_load_dwordx4 v[20:23], v[6:7], off nt
	v_add_u32_e32 v4, s4, v73
	v_ashrrev_i32_e32 v5, 31, v4
	v_mul_lo_u32 v6, s22, v5
	v_mul_lo_u32 v7, s23, v4
	v_mad_u64_u32 v[4:5], s[24:25], s22, v4, 0
	v_add3_u32 v5, v5, v6, v7
	v_add_u32_e32 v6, s4, v72
	v_ashrrev_i32_e32 v7, 31, v6
	v_mul_lo_u32 v8, s22, v7
	v_mul_lo_u32 v9, s23, v6
	v_mad_u64_u32 v[6:7], s[24:25], s22, v6, 0
	v_lshl_add_u64 v[4:5], v[4:5], 2, s[20:21]
	v_add3_u32 v7, v7, v8, v9
	v_lshl_add_u64 v[4:5], v[4:5], 0, s[2:3]
	v_lshl_add_u64 v[6:7], v[6:7], 2, s[20:21]
	v_lshl_add_u64 v[4:5], v[4:5], 0, v[2:3]
	v_lshl_add_u64 v[6:7], v[6:7], 0, s[2:3]
	v_lshl_add_u64 v[6:7], v[6:7], 0, v[2:3]
	global_load_dwordx4 v[28:31], v[4:5], off nt
	global_load_dwordx4 v[12:15], v[6:7], off nt
	v_add_u32_e32 v4, s4, v81
	v_ashrrev_i32_e32 v5, 31, v4
	v_mul_lo_u32 v6, s22, v5
	v_mul_lo_u32 v7, s23, v4
	v_mad_u64_u32 v[4:5], s[24:25], s22, v4, 0
	v_add3_u32 v5, v5, v6, v7
	v_add_u32_e32 v6, s4, v82
	v_ashrrev_i32_e32 v7, 31, v6
	v_mul_lo_u32 v8, s22, v7
	v_mul_lo_u32 v9, s23, v6
	v_mad_u64_u32 v[6:7], s[24:25], s22, v6, 0
	v_lshl_add_u64 v[4:5], v[4:5], 2, s[20:21]
	v_add3_u32 v7, v7, v8, v9
	v_lshl_add_u64 v[4:5], v[4:5], 0, s[2:3]
	v_lshl_add_u64 v[6:7], v[6:7], 2, s[20:21]
	v_lshl_add_u64 v[4:5], v[4:5], 0, v[2:3]
	v_lshl_add_u64 v[6:7], v[6:7], 0, s[2:3]
	v_lshl_add_u64 v[6:7], v[6:7], 0, v[2:3]
	global_load_dwordx4 v[24:27], v[4:5], off nt
	global_load_dwordx4 v[8:11], v[6:7], off nt
	v_add_u32_e32 v4, s4, v83
	v_ashrrev_i32_e32 v5, 31, v4
	v_mul_lo_u32 v6, s22, v5
	v_mul_lo_u32 v7, s23, v4
	v_mad_u64_u32 v[4:5], s[24:25], s22, v4, 0
	v_add3_u32 v5, v5, v6, v7
	v_add_u32_e32 v6, s4, v84
	v_ashrrev_i32_e32 v7, 31, v6
	v_mul_lo_u32 v16, s22, v7
	v_mul_lo_u32 v17, s23, v6
	v_mad_u64_u32 v[6:7], s[22:23], s22, v6, 0
	v_add3_u32 v7, v7, v16, v17
	v_lshl_add_u64 v[4:5], v[4:5], 2, s[20:21]
	v_lshl_add_u64 v[6:7], v[6:7], 2, s[20:21]
	v_lshl_add_u64 v[4:5], v[4:5], 0, s[2:3]
	v_lshl_add_u64 v[6:7], v[6:7], 0, s[2:3]
	v_lshl_add_u64 v[4:5], v[4:5], 0, v[2:3]
	v_lshl_add_u64 v[6:7], v[6:7], 0, v[2:3]
	global_load_dwordx4 v[16:19], v[4:5], off nt
	s_nop 0
	global_load_dwordx4 v[4:7], v[6:7], off nt
	s_waitcnt vmcnt(15)
	ds_write2_b32 v71, v36, v37 offset1:1
	ds_write2_b32 v71, v38, v39 offset0:2 offset1:3
	v_add_u32_e32 v36, 0x420, v71
	s_waitcnt vmcnt(14)
	ds_write2_b32 v36, v40, v41 offset1:1
	v_add_u32_e32 v36, 0x428, v71
	ds_write2_b32 v36, v42, v43 offset1:1
	v_add_u32_e32 v36, 0x840, v71
	s_waitcnt vmcnt(13)
	ds_write2_b32 v36, v44, v45 offset1:1
	v_add_u32_e32 v36, 0x848, v71
	ds_write2_b32 v36, v46, v47 offset1:1
	v_add_u32_e32 v36, 0xc60, v71
	s_waitcnt vmcnt(12)
	ds_write2_b32 v36, v48, v49 offset1:1
	v_add_u32_e32 v36, 0xc68, v71
	ds_write2_b32 v36, v50, v51 offset1:1
	v_add_u32_e32 v36, 0x1080, v71
	s_waitcnt vmcnt(11)
	ds_write2_b32 v36, v52, v53 offset1:1
	v_add_u32_e32 v36, 0x1088, v71
	ds_write2_b32 v36, v54, v55 offset1:1
	v_add_u32_e32 v36, 0x14a0, v71
	s_waitcnt vmcnt(10)
	ds_write2_b32 v36, v56, v57 offset1:1
	v_add_u32_e32 v36, 0x14a8, v71
	ds_write2_b32 v36, v58, v59 offset1:1
	v_add_u32_e32 v36, 0x18c0, v71
	s_waitcnt vmcnt(9)
	ds_write2_b32 v36, v60, v61 offset1:1
	v_add_u32_e32 v36, 0x18c8, v71
	ds_write2_b32 v36, v62, v63 offset1:1
	v_add_u32_e32 v36, 0x1ce0, v71
	s_waitcnt vmcnt(8)
	ds_write2_b32 v36, v64, v65 offset1:1
	v_add_u32_e32 v36, 0x1ce8, v71
	ds_write2_b32 v36, v66, v67 offset1:1
	s_waitcnt lgkmcnt(0)
	ds_read2_b32 v[40:41], v70 offset1:33
	ds_read2_b32 v[48:49], v70 offset0:66 offset1:99
	ds_read2_b32 v[42:43], v70 offset0:132 offset1:165
	ds_read2_b32 v[46:47], v70 offset0:198 offset1:231
	s_cmp_lg_u64 s[14:15], 0
	s_cselect_b64 s[20:21], -1, 0
	v_add_u32_e32 v44, s8, v68
	s_and_b64 vcc, exec, s[20:21]
	v_add_u32_e32 v50, s36, v75
	v_ashrrev_i32_e32 v53, 5, v44
	v_lshlrev_b32_e32 v52, 1, v44
	v_ashrrev_i32_e32 v45, 31, v44
	s_waitcnt lgkmcnt(3)
	v_cvt_pk_bf16_f32 v36, v40, v41
	s_waitcnt lgkmcnt(2)
	v_cvt_pk_bf16_f32 v37, v48, v49
	s_waitcnt lgkmcnt(1)
	v_cvt_pk_bf16_f32 v38, v42, v43
	s_waitcnt lgkmcnt(0)
	v_cvt_pk_bf16_f32 v39, v46, v47
	s_cbranch_vccz .LBB0_1408
	v_lshlrev_b32_e32 v51, 2, v50
	v_and_b32_e32 v51, 0xffffffc0, v51
	v_add_u32_e32 v54, v51, v53
	v_ashrrev_i32_e32 v55, 31, v54
	v_lshlrev_b64 v[66:67], 6, v[54:55]
	v_and_b32_e32 v51, 48, v52
	v_and_b32_e32 v54, 15, v50
	v_lshl_add_u64 v[58:59], v[44:45], 2, s[18:19]
	v_or3_b32 v66, v66, v51, v54
	global_load_dwordx4 v[54:57], v[58:59], off offset:16
	s_nop 0
	global_load_dwordx4 v[58:61], v[58:59], off
	s_waitcnt vmcnt(1)
	v_mul_f32_e32 v65, v42, v54
	s_waitcnt vmcnt(0)
	v_mul_f32_e32 v51, v40, v58
	v_mul_f32_e32 v62, v41, v59
	v_cvt_pk_bf16_f32 v62, v51, v62
	v_mul_f32_e32 v63, v48, v60
	v_lshlrev_b32_e32 v51, 16, v62
	v_fma_f32 v40, v40, v58, -v51
	v_and_b32_e32 v51, 0xffff0000, v62
	v_mul_f32_e32 v64, v49, v61
	v_fma_f32 v41, v41, v59, -v51
	v_mul_f32_e32 v87, v43, v55
	v_mul_f32_e32 v88, v46, v56
	v_mul_f32_e32 v89, v47, v57
	v_cvt_pk_bf16_f32 v63, v63, v64
	v_cvt_pk_bf16_f32 v64, v65, v87
	v_cvt_pk_bf16_f32 v65, v88, v89
	v_cvt_pk_bf16_f32 v40, v40, v41
	s_nop 0
	v_lshlrev_b32_e32 v41, 16, v63
	v_fma_f32 v41, v48, v60, -v41
	v_and_b32_e32 v48, 0xffff0000, v63
	v_fma_f32 v48, v49, v61, -v48
	v_cvt_pk_bf16_f32 v41, v41, v48
	v_lshlrev_b32_e32 v48, 16, v64
	v_fma_f32 v42, v42, v54, -v48
	v_and_b32_e32 v48, 0xffff0000, v64
	v_fma_f32 v43, v43, v55, -v48
	v_cvt_pk_bf16_f32 v42, v42, v43
	v_lshlrev_b32_e32 v43, 16, v65
	v_fma_f32 v43, v46, v56, -v43
	v_and_b32_e32 v46, 0xffff0000, v65
	v_fma_f32 v46, v47, v57, -v46
	v_cvt_pk_bf16_f32 v43, v43, v46
	v_lshlrev_b64 v[46:47], 4, v[66:67]
	v_lshl_add_u64 v[48:49], s[10:11], 0, v[46:47]
	global_store_dwordx4 v[48:49], v[62:65], off nt
	v_lshl_add_u64 v[48:49], s[14:15], 0, v[46:47]
	v_lshlrev_b32_e32 v46, 1, v68
	s_cbranch_execnz .LBB0_1397

.LBB0_1397:
	global_store_dwordx4 v[48:49], v[40:43], off
	ds_read2_b32 v[40:41], v70 offset0:8 offset1:41
	ds_read2_b32 v[50:51], v70 offset0:74 offset1:107
	ds_read2_b32 v[42:43], v70 offset0:140 offset1:173
	ds_read2_b32 v[48:49], v70 offset0:206 offset1:239
	v_cndmask_b32_e64 v47, 0, 1, s[20:21]
	v_cmp_ne_u32_e64 s[2:3], 1, v47
	s_andn2_b64 vcc, exec, s[20:21]
	v_add_u32_e32 v47, s36, v74
	s_waitcnt lgkmcnt(3)
	v_cvt_pk_bf16_f32 v36, v40, v41
	s_waitcnt lgkmcnt(2)
	v_cvt_pk_bf16_f32 v37, v50, v51
	s_waitcnt lgkmcnt(1)
	v_cvt_pk_bf16_f32 v38, v42, v43
	s_waitcnt lgkmcnt(0)
	v_cvt_pk_bf16_f32 v39, v48, v49
	s_cbranch_vccnz .LBB0_1409
	v_lshlrev_b32_e32 v54, 2, v47
	v_and_b32_e32 v54, 0xffffffc0, v54
	v_add_u32_e32 v54, v54, v53
	v_ashrrev_i32_e32 v55, 31, v54
	v_lshlrev_b64 v[66:67], 6, v[54:55]
	v_and_b32_e32 v54, 48, v52
	v_and_b32_e32 v55, 15, v47
	v_lshl_add_u64 v[58:59], v[44:45], 2, s[18:19]
	v_or3_b32 v66, v66, v54, v55
	global_load_dwordx4 v[54:57], v[58:59], off offset:16
	s_nop 0
	global_load_dwordx4 v[58:61], v[58:59], off
	s_waitcnt vmcnt(1)
	v_mul_f32_e32 v87, v42, v54
	s_waitcnt vmcnt(0)
	v_mul_f32_e32 v62, v40, v58
	v_mul_f32_e32 v63, v41, v59
	v_mul_f32_e32 v64, v50, v60
	v_mul_f32_e32 v65, v51, v61
	v_mul_f32_e32 v88, v43, v55
	v_cvt_pk_bf16_f32 v62, v62, v63
	v_cvt_pk_bf16_f32 v63, v64, v65
	v_cvt_pk_bf16_f32 v64, v87, v88
	v_mul_f32_e32 v89, v48, v56
	v_lshlrev_b32_e32 v87, 16, v62
	v_fma_f32 v40, v40, v58, -v87
	v_and_b32_e32 v58, 0xffff0000, v62
	v_fma_f32 v41, v41, v59, -v58
	v_mul_f32_e32 v90, v49, v57
	v_cvt_pk_bf16_f32 v65, v89, v90
	v_cvt_pk_bf16_f32 v40, v40, v41
	v_lshlrev_b32_e32 v41, 16, v63
	v_fma_f32 v41, v50, v60, -v41
	v_and_b32_e32 v50, 0xffff0000, v63
	v_fma_f32 v50, v51, v61, -v50
	v_cvt_pk_bf16_f32 v41, v41, v50
	v_lshlrev_b32_e32 v50, 16, v64
	v_fma_f32 v42, v42, v54, -v50
	v_and_b32_e32 v50, 0xffff0000, v64
	v_fma_f32 v43, v43, v55, -v50
	v_cvt_pk_bf16_f32 v42, v42, v43
	v_lshlrev_b32_e32 v43, 16, v65
	v_fma_f32 v43, v48, v56, -v43
	v_and_b32_e32 v48, 0xffff0000, v65
	v_fma_f32 v48, v49, v57, -v48
	v_cvt_pk_bf16_f32 v43, v43, v48
	v_lshlrev_b64 v[48:49], 4, v[66:67]
	v_lshl_add_u64 v[50:51], s[10:11], 0, v[48:49]
	v_lshl_add_u64 v[48:49], s[14:15], 0, v[48:49]
	global_store_dwordx4 v[50:51], v[62:65], off nt
	s_cbranch_execnz .LBB0_1400

.LBB0_1400:
	global_store_dwordx4 v[48:49], v[40:43], off nt
	ds_read2_b32 v[40:41], v70 offset0:16 offset1:49
	ds_read2_b32 v[50:51], v70 offset0:82 offset1:115
	ds_read2_b32 v[42:43], v70 offset0:148 offset1:181
	ds_read2_b32 v[48:49], v70 offset0:214 offset1:247
	s_and_b64 vcc, exec, s[2:3]
	v_add_u32_e32 v47, s36, v73
	s_waitcnt lgkmcnt(3)
	v_cvt_pk_bf16_f32 v36, v40, v41
	s_waitcnt lgkmcnt(2)
	v_cvt_pk_bf16_f32 v37, v50, v51
	s_waitcnt lgkmcnt(1)
	v_cvt_pk_bf16_f32 v38, v42, v43
	s_waitcnt lgkmcnt(0)
	v_cvt_pk_bf16_f32 v39, v48, v49
	s_cbranch_vccnz .LBB0_1410
	v_lshlrev_b32_e32 v54, 2, v47
	v_and_b32_e32 v54, 0xffffffc0, v54
	v_add_u32_e32 v54, v54, v53
	v_ashrrev_i32_e32 v55, 31, v54
	v_lshlrev_b64 v[66:67], 6, v[54:55]
	v_and_b32_e32 v54, 48, v52
	v_and_b32_e32 v55, 15, v47
	v_lshl_add_u64 v[58:59], v[44:45], 2, s[18:19]
	v_or3_b32 v66, v66, v54, v55
	global_load_dwordx4 v[54:57], v[58:59], off offset:16
	s_nop 0
	global_load_dwordx4 v[58:61], v[58:59], off
	s_waitcnt vmcnt(1)
	v_mul_f32_e32 v87, v42, v54
	s_waitcnt vmcnt(0)
	v_mul_f32_e32 v62, v40, v58
	v_mul_f32_e32 v63, v41, v59
	v_mul_f32_e32 v64, v50, v60
	v_mul_f32_e32 v65, v51, v61
	v_mul_f32_e32 v88, v43, v55
	v_cvt_pk_bf16_f32 v62, v62, v63
	v_cvt_pk_bf16_f32 v63, v64, v65
	v_cvt_pk_bf16_f32 v64, v87, v88
	v_mul_f32_e32 v89, v48, v56
	v_lshlrev_b32_e32 v87, 16, v62
	v_fma_f32 v40, v40, v58, -v87
	v_and_b32_e32 v58, 0xffff0000, v62
	v_fma_f32 v41, v41, v59, -v58
	v_mul_f32_e32 v90, v49, v57
	v_cvt_pk_bf16_f32 v65, v89, v90
	v_cvt_pk_bf16_f32 v40, v40, v41
	v_lshlrev_b32_e32 v41, 16, v63
	v_fma_f32 v41, v50, v60, -v41
	v_and_b32_e32 v50, 0xffff0000, v63
	v_fma_f32 v50, v51, v61, -v50
	v_cvt_pk_bf16_f32 v41, v41, v50
	v_lshlrev_b32_e32 v50, 16, v64
	v_fma_f32 v42, v42, v54, -v50
	v_and_b32_e32 v50, 0xffff0000, v64
	v_fma_f32 v43, v43, v55, -v50
	v_cvt_pk_bf16_f32 v42, v42, v43
	v_lshlrev_b32_e32 v43, 16, v65
	v_fma_f32 v43, v48, v56, -v43
	v_and_b32_e32 v48, 0xffff0000, v65
	v_fma_f32 v48, v49, v57, -v48
	v_cvt_pk_bf16_f32 v43, v43, v48
	v_lshlrev_b64 v[48:49], 4, v[66:67]
	v_lshl_add_u64 v[50:51], s[10:11], 0, v[48:49]
	v_lshl_add_u64 v[48:49], s[14:15], 0, v[48:49]
	global_store_dwordx4 v[50:51], v[62:65], off nt
	s_cbranch_execnz .LBB0_1403

.LBB0_1403:
	global_store_dwordx4 v[48:49], v[40:43], off nt
	ds_read2_b32 v[40:41], v70 offset0:24 offset1:57
	ds_read2_b32 v[50:51], v70 offset0:90 offset1:123
	ds_read2_b32 v[42:43], v70 offset0:156 offset1:189
	ds_read2_b32 v[48:49], v70 offset0:222 offset1:255
	s_and_b64 vcc, exec, s[2:3]
	v_add_u32_e32 v47, s36, v72
	s_waitcnt lgkmcnt(3)
	v_cvt_pk_bf16_f32 v36, v40, v41
	s_waitcnt lgkmcnt(2)
	v_cvt_pk_bf16_f32 v37, v50, v51
	s_waitcnt lgkmcnt(1)
	v_cvt_pk_bf16_f32 v38, v42, v43
	s_waitcnt lgkmcnt(0)
	v_cvt_pk_bf16_f32 v39, v48, v49
	s_cbranch_vccnz .LBB0_1411
	v_lshlrev_b32_e32 v54, 2, v47
	v_and_b32_e32 v54, 0xffffffc0, v54
	v_add_u32_e32 v54, v54, v53
	v_ashrrev_i32_e32 v55, 31, v54
	v_lshlrev_b64 v[64:65], 6, v[54:55]
	v_and_b32_e32 v52, 48, v52
	v_and_b32_e32 v53, 15, v47
	v_lshl_add_u64 v[44:45], v[44:45], 2, s[18:19]
	v_or3_b32 v64, v64, v52, v53
	global_load_dwordx4 v[52:55], v[44:45], off offset:16
	global_load_dwordx4 v[56:59], v[44:45], off
	s_waitcnt vmcnt(1)
	v_mul_f32_e32 v63, v42, v52
	s_waitcnt vmcnt(0)
	v_mul_f32_e32 v44, v40, v56
	v_mul_f32_e32 v45, v41, v57
	v_cvt_pk_bf16_f32 v60, v44, v45
	v_mul_f32_e32 v61, v50, v58
	v_lshlrev_b32_e32 v44, 16, v60
	v_fma_f32 v40, v40, v56, -v44
	v_and_b32_e32 v44, 0xffff0000, v60
	v_mul_f32_e32 v62, v51, v59
	v_fma_f32 v41, v41, v57, -v44
	v_mul_f32_e32 v66, v43, v53
	v_mul_f32_e32 v67, v48, v54
	v_mul_f32_e32 v87, v49, v55
	v_cvt_pk_bf16_f32 v61, v61, v62
	v_cvt_pk_bf16_f32 v62, v63, v66
	v_cvt_pk_bf16_f32 v63, v67, v87
	v_cvt_pk_bf16_f32 v40, v40, v41
	s_nop 0
	v_lshlrev_b32_e32 v41, 16, v61
	v_and_b32_e32 v44, 0xffff0000, v61
	v_fma_f32 v41, v50, v58, -v41
	v_fma_f32 v44, v51, v59, -v44
	v_cvt_pk_bf16_f32 v41, v41, v44
	v_lshlrev_b32_e32 v44, 16, v62
	v_fma_f32 v42, v42, v52, -v44
	v_and_b32_e32 v44, 0xffff0000, v62
	v_fma_f32 v43, v43, v53, -v44
	v_cvt_pk_bf16_f32 v42, v42, v43
	v_lshlrev_b32_e32 v43, 16, v63
	v_and_b32_e32 v44, 0xffff0000, v63
	v_fma_f32 v43, v48, v54, -v43
	v_fma_f32 v44, v49, v55, -v44
	v_cvt_pk_bf16_f32 v43, v43, v44
	v_lshlrev_b64 v[44:45], 4, v[64:65]
	v_lshl_add_u64 v[48:49], s[10:11], 0, v[44:45]
	v_lshl_add_u64 v[44:45], s[14:15], 0, v[44:45]
	global_store_dwordx4 v[48:49], v[60:63], off nt
	s_cbranch_execnz .LBB0_1406

.LBB0_1406:
	global_store_dwordx4 v[44:45], v[40:43], off nt
	s_waitcnt lgkmcnt(0)
	s_addk_i32 s5, 0x400
	s_add_i32 s56, s56, 0x8000
	s_cmp_ge_i32 s5, s30
	s_cbranch_scc1 .LBB0_1415
	s_mov_b32 s36, s35
	s_mov_b32 s8, s4
	s_mov_b32 s34, s31
	s_mov_b64 s[18:19], s[16:17]
	s_mov_b64 s[14:15], s[12:13]
	s_mov_b64 s[10:11], s[6:7]
	s_waitcnt vmcnt(11)
	v_mov_b32_e32 v36, v32
	v_mov_b32_e32 v37, v33
	v_mov_b32_e32 v38, v34
	v_mov_b32_e32 v39, v35
	s_waitcnt vmcnt(10)
	v_mov_b32_e32 v40, v20
	v_mov_b32_e32 v41, v21
	v_mov_b32_e32 v42, v22
	v_mov_b32_e32 v43, v23
	s_waitcnt vmcnt(9)
	v_mov_b32_e32 v44, v28
	v_mov_b32_e32 v45, v29
	v_mov_b32_e32 v46, v30
	v_mov_b32_e32 v47, v31
	s_waitcnt vmcnt(8)
	v_mov_b32_e32 v48, v12
	v_mov_b32_e32 v49, v13
	v_mov_b32_e32 v50, v14
	v_mov_b32_e32 v51, v15
	s_waitcnt vmcnt(7)
	v_mov_b32_e32 v52, v24
	v_mov_b32_e32 v53, v25
	v_mov_b32_e32 v54, v26
	v_mov_b32_e32 v55, v27
	s_waitcnt vmcnt(6)
	v_mov_b32_e32 v56, v8
	v_mov_b32_e32 v57, v9
	v_mov_b32_e32 v58, v10
	v_mov_b32_e32 v59, v11
	s_waitcnt vmcnt(5)
	v_mov_b32_e32 v60, v16
	v_mov_b32_e32 v61, v17
	v_mov_b32_e32 v62, v18
	v_mov_b32_e32 v63, v19
	s_waitcnt vmcnt(4)
	v_mov_b32_e32 v64, v4
	v_mov_b32_e32 v65, v5
	v_mov_b32_e32 v66, v6
	v_mov_b32_e32 v67, v7
	s_branch .LBB0_1344

.LBB0_1416:
	v_add_u32_e32 v2, v86, v79
	s_waitcnt vmcnt(11)
	ds_write2_b32 v2, v32, v33 offset1:1
	ds_write2_b32 v2, v34, v35 offset0:2 offset1:3
	v_add_u32_e32 v32, v86, v80
	s_waitcnt vmcnt(10)
	ds_write2_b32 v32, v20, v21 offset1:1
	ds_write2_b32 v32, v22, v23 offset0:2 offset1:3
	v_add_u32_e32 v20, v86, v76
	s_waitcnt vmcnt(9)
	ds_write2_b32 v20, v28, v29 offset1:1
	ds_write2_b32 v20, v30, v31 offset0:2 offset1:3
	v_add_u32_e32 v20, v86, v77
	s_waitcnt vmcnt(8)
	ds_write2_b32 v20, v12, v13 offset1:1
	ds_write2_b32 v20, v14, v15 offset0:2 offset1:3
	v_add_u32_e32 v12, 0x1080, v2
	s_waitcnt vmcnt(7)
	ds_write2_b32 v12, v24, v25 offset1:1
	v_add_u32_e32 v12, 0x1088, v2
	ds_write2_b32 v12, v26, v27 offset1:1
	v_add_u32_e32 v12, 0x14a0, v2
	s_waitcnt vmcnt(6)
	ds_write2_b32 v12, v8, v9 offset1:1
	v_add_u32_e32 v8, 0x14a8, v2
	ds_write2_b32 v8, v10, v11 offset1:1
	v_add_u32_e32 v8, 0x18c0, v2
	s_waitcnt vmcnt(5)
	ds_write2_b32 v8, v16, v17 offset1:1
	v_add_u32_e32 v8, 0x18c8, v2
	ds_write2_b32 v8, v18, v19 offset1:1
	v_add_u32_e32 v8, 0x1ce0, v2
	v_add_u32_e32 v2, 0x1ce8, v2
	s_waitcnt vmcnt(4)
	ds_write2_b32 v8, v4, v5 offset1:1
	ds_write2_b32 v2, v6, v7 offset1:1
	s_waitcnt lgkmcnt(0)
	v_add3_u32 v18, s37, v78, v85
	ds_read2_b32 v[8:9], v18 offset1:33
	ds_read2_b32 v[16:17], v18 offset0:66 offset1:99
	ds_read2_b32 v[10:11], v18 offset0:132 offset1:165
	ds_read2_b32 v[14:15], v18 offset0:198 offset1:231
	s_cmp_lg_u64 s[12:13], 0
	s_cselect_b64 s[8:9], -1, 0
	v_add_u32_e32 v12, s4, v68
	s_and_b64 vcc, exec, s[8:9]
	v_add_u32_e32 v20, s35, v75
	v_ashrrev_i32_e32 v19, 5, v12
	v_lshlrev_b32_e32 v2, 1, v12
	v_ashrrev_i32_e32 v13, 31, v12
	s_waitcnt lgkmcnt(3)
	v_cvt_pk_bf16_f32 v4, v8, v9
	s_waitcnt lgkmcnt(2)
	v_cvt_pk_bf16_f32 v5, v16, v17
	s_waitcnt lgkmcnt(1)
	v_cvt_pk_bf16_f32 v6, v10, v11
	s_waitcnt lgkmcnt(0)
	v_cvt_pk_bf16_f32 v7, v14, v15
	s_cbranch_vccz .LBB0_1418
	v_lshlrev_b32_e32 v21, 2, v20
	v_and_b32_e32 v21, 0xffffffc0, v21
	v_add_u32_e32 v22, v21, v19
	v_ashrrev_i32_e32 v23, 31, v22
	v_lshlrev_b64 v[34:35], 6, v[22:23]
	v_and_b32_e32 v21, 48, v2
	v_and_b32_e32 v22, 15, v20
	v_lshl_add_u64 v[26:27], v[12:13], 2, s[16:17]
	v_or3_b32 v34, v34, v21, v22
	global_load_dwordx4 v[22:25], v[26:27], off offset:16
	s_nop 0
	global_load_dwordx4 v[26:29], v[26:27], off
	s_mov_b64 s[2:3], 0
	s_waitcnt vmcnt(1)
	v_mul_f32_e32 v33, v10, v22
	s_waitcnt vmcnt(0)
	v_mul_f32_e32 v21, v8, v26
	v_mul_f32_e32 v30, v9, v27
	v_cvt_pk_bf16_f32 v30, v21, v30
	v_mul_f32_e32 v31, v16, v28
	v_lshlrev_b32_e32 v21, 16, v30
	v_fma_f32 v8, v8, v26, -v21
	v_and_b32_e32 v21, 0xffff0000, v30
	v_mul_f32_e32 v32, v17, v29
	v_fma_f32 v9, v9, v27, -v21
	v_mul_f32_e32 v36, v11, v23
	v_mul_f32_e32 v37, v14, v24
	v_mul_f32_e32 v38, v15, v25
	v_cvt_pk_bf16_f32 v31, v31, v32
	v_cvt_pk_bf16_f32 v32, v33, v36
	v_cvt_pk_bf16_f32 v33, v37, v38
	v_cvt_pk_bf16_f32 v8, v8, v9
	s_nop 0
	v_lshlrev_b32_e32 v9, 16, v31
	v_fma_f32 v9, v16, v28, -v9
	v_and_b32_e32 v16, 0xffff0000, v31
	v_fma_f32 v16, v17, v29, -v16
	v_cvt_pk_bf16_f32 v9, v9, v16
	v_lshlrev_b32_e32 v16, 16, v32
	v_fma_f32 v10, v10, v22, -v16
	v_and_b32_e32 v16, 0xffff0000, v32
	v_fma_f32 v11, v11, v23, -v16
	v_cvt_pk_bf16_f32 v10, v10, v11
	v_lshlrev_b32_e32 v11, 16, v33
	v_fma_f32 v11, v14, v24, -v11
	v_and_b32_e32 v14, 0xffff0000, v33
	v_fma_f32 v14, v15, v25, -v14
	v_cvt_pk_bf16_f32 v11, v11, v14
	v_lshlrev_b64 v[14:15], 4, v[34:35]
	v_lshl_add_u64 v[16:17], s[6:7], 0, v[14:15]
	global_store_dwordx4 v[16:17], v[30:33], off nt
	v_lshl_add_u64 v[14:15], s[12:13], 0, v[14:15]
	s_branch .LBB0_1419

.LBB0_1421:
	global_store_dwordx4 v[14:15], v[8:11], off
	ds_read2_b32 v[8:9], v18 offset0:8 offset1:41
	ds_read2_b32 v[16:17], v18 offset0:74 offset1:107
	ds_read2_b32 v[10:11], v18 offset0:140 offset1:173
	ds_read2_b32 v[14:15], v18 offset0:206 offset1:239
	v_cndmask_b32_e64 v20, 0, 1, s[8:9]
	v_cmp_ne_u32_e64 s[2:3], 1, v20
	s_andn2_b64 vcc, exec, s[8:9]
	v_add_u32_e32 v20, s35, v74
	s_waitcnt lgkmcnt(3)
	v_cvt_pk_bf16_f32 v4, v8, v9
	s_waitcnt lgkmcnt(2)
	v_cvt_pk_bf16_f32 v5, v16, v17
	s_waitcnt lgkmcnt(1)
	v_cvt_pk_bf16_f32 v6, v10, v11
	s_waitcnt lgkmcnt(0)
	v_cvt_pk_bf16_f32 v7, v14, v15
	s_cbranch_vccnz .LBB0_1614
	v_lshlrev_b32_e32 v21, 2, v20
	v_and_b32_e32 v21, 0xffffffc0, v21
	v_add_u32_e32 v22, v21, v19
	v_ashrrev_i32_e32 v23, 31, v22
	v_lshlrev_b64 v[34:35], 6, v[22:23]
	v_and_b32_e32 v21, 48, v2
	v_and_b32_e32 v22, 15, v20
	v_lshl_add_u64 v[26:27], v[12:13], 2, s[16:17]
	v_or3_b32 v34, v34, v21, v22
	global_load_dwordx4 v[22:25], v[26:27], off offset:16
	s_nop 0
	global_load_dwordx4 v[26:29], v[26:27], off
	s_waitcnt vmcnt(1)
	v_mul_f32_e32 v33, v10, v22
	s_waitcnt vmcnt(0)
	v_mul_f32_e32 v21, v8, v26
	v_mul_f32_e32 v30, v9, v27
	v_cvt_pk_bf16_f32 v30, v21, v30
	v_mul_f32_e32 v31, v16, v28
	v_lshlrev_b32_e32 v21, 16, v30
	v_fma_f32 v8, v8, v26, -v21
	v_and_b32_e32 v21, 0xffff0000, v30
	v_mul_f32_e32 v32, v17, v29
	v_fma_f32 v9, v9, v27, -v21
	v_mul_f32_e32 v36, v11, v23
	v_mul_f32_e32 v37, v14, v24
	v_mul_f32_e32 v38, v15, v25
	v_cvt_pk_bf16_f32 v31, v31, v32
	v_cvt_pk_bf16_f32 v32, v33, v36
	v_cvt_pk_bf16_f32 v33, v37, v38
	v_cvt_pk_bf16_f32 v8, v8, v9
	s_nop 0
	v_lshlrev_b32_e32 v9, 16, v31
	v_fma_f32 v9, v16, v28, -v9
	v_and_b32_e32 v16, 0xffff0000, v31
	v_fma_f32 v16, v17, v29, -v16
	v_cvt_pk_bf16_f32 v9, v9, v16
	v_lshlrev_b32_e32 v16, 16, v32
	v_fma_f32 v10, v10, v22, -v16
	v_and_b32_e32 v16, 0xffff0000, v32
	v_fma_f32 v11, v11, v23, -v16
	v_cvt_pk_bf16_f32 v10, v10, v11
	v_lshlrev_b32_e32 v11, 16, v33
	v_fma_f32 v11, v14, v24, -v11
	v_and_b32_e32 v14, 0xffff0000, v33
	v_fma_f32 v14, v15, v25, -v14
	v_cvt_pk_bf16_f32 v11, v11, v14
	v_lshlrev_b64 v[14:15], 4, v[34:35]
	v_lshl_add_u64 v[16:17], s[6:7], 0, v[14:15]
	v_lshl_add_u64 v[14:15], s[12:13], 0, v[14:15]
	global_store_dwordx4 v[16:17], v[30:33], off nt
	s_cbranch_execnz .LBB0_1424

.LBB0_1424:
	global_store_dwordx4 v[14:15], v[8:11], off nt
	ds_read2_b32 v[8:9], v18 offset0:16 offset1:49
	ds_read2_b32 v[16:17], v18 offset0:82 offset1:115
	ds_read2_b32 v[10:11], v18 offset0:148 offset1:181
	ds_read2_b32 v[14:15], v18 offset0:214 offset1:247
	s_and_b64 vcc, exec, s[2:3]
	v_add_u32_e32 v20, s35, v73
	s_waitcnt lgkmcnt(3)
	v_cvt_pk_bf16_f32 v4, v8, v9
	s_waitcnt lgkmcnt(2)
	v_cvt_pk_bf16_f32 v5, v16, v17
	s_waitcnt lgkmcnt(1)
	v_cvt_pk_bf16_f32 v6, v10, v11
	s_waitcnt lgkmcnt(0)
	v_cvt_pk_bf16_f32 v7, v14, v15
	s_cbranch_vccnz .LBB0_1615
	v_lshlrev_b32_e32 v21, 2, v20
	v_and_b32_e32 v21, 0xffffffc0, v21
	v_add_u32_e32 v22, v21, v19
	v_ashrrev_i32_e32 v23, 31, v22
	v_lshlrev_b64 v[34:35], 6, v[22:23]
	v_and_b32_e32 v21, 48, v2
	v_and_b32_e32 v22, 15, v20
	v_lshl_add_u64 v[26:27], v[12:13], 2, s[16:17]
	v_or3_b32 v34, v34, v21, v22
	global_load_dwordx4 v[22:25], v[26:27], off offset:16
	s_nop 0
	global_load_dwordx4 v[26:29], v[26:27], off
	s_waitcnt vmcnt(1)
	v_mul_f32_e32 v33, v10, v22
	s_waitcnt vmcnt(0)
	v_mul_f32_e32 v21, v8, v26
	v_mul_f32_e32 v30, v9, v27
	v_cvt_pk_bf16_f32 v30, v21, v30
	v_mul_f32_e32 v31, v16, v28
	v_lshlrev_b32_e32 v21, 16, v30
	v_fma_f32 v8, v8, v26, -v21
	v_and_b32_e32 v21, 0xffff0000, v30
	v_mul_f32_e32 v32, v17, v29
	v_fma_f32 v9, v9, v27, -v21
	v_mul_f32_e32 v36, v11, v23
	v_mul_f32_e32 v37, v14, v24
	v_mul_f32_e32 v38, v15, v25
	v_cvt_pk_bf16_f32 v31, v31, v32
	v_cvt_pk_bf16_f32 v32, v33, v36
	v_cvt_pk_bf16_f32 v33, v37, v38
	v_cvt_pk_bf16_f32 v8, v8, v9
	s_nop 0
	v_lshlrev_b32_e32 v9, 16, v31
	v_fma_f32 v9, v16, v28, -v9
	v_and_b32_e32 v16, 0xffff0000, v31
	v_fma_f32 v16, v17, v29, -v16
	v_cvt_pk_bf16_f32 v9, v9, v16
	v_lshlrev_b32_e32 v16, 16, v32
	v_fma_f32 v10, v10, v22, -v16
	v_and_b32_e32 v16, 0xffff0000, v32
	v_fma_f32 v11, v11, v23, -v16
	v_cvt_pk_bf16_f32 v10, v10, v11
	v_lshlrev_b32_e32 v11, 16, v33
	v_fma_f32 v11, v14, v24, -v11
	v_and_b32_e32 v14, 0xffff0000, v33
	v_fma_f32 v14, v15, v25, -v14
	v_cvt_pk_bf16_f32 v11, v11, v14
	v_lshlrev_b64 v[14:15], 4, v[34:35]
	v_lshl_add_u64 v[16:17], s[6:7], 0, v[14:15]
	v_lshl_add_u64 v[14:15], s[12:13], 0, v[14:15]
	global_store_dwordx4 v[16:17], v[30:33], off nt
	s_cbranch_execnz .LBB0_1427

.LBB0_1427:
	global_store_dwordx4 v[14:15], v[8:11], off nt
	ds_read2_b32 v[8:9], v18 offset0:24 offset1:57
	ds_read2_b32 v[16:17], v18 offset0:90 offset1:123
	ds_read2_b32 v[10:11], v18 offset0:156 offset1:189
	ds_read2_b32 v[14:15], v18 offset0:222 offset1:255
	s_and_b64 vcc, exec, s[2:3]
	v_add_u32_e32 v18, s35, v72
	s_waitcnt lgkmcnt(3)
	v_cvt_pk_bf16_f32 v4, v8, v9
	s_waitcnt lgkmcnt(2)
	v_cvt_pk_bf16_f32 v5, v16, v17
	s_waitcnt lgkmcnt(1)
	v_cvt_pk_bf16_f32 v6, v10, v11
	s_waitcnt lgkmcnt(0)
	v_cvt_pk_bf16_f32 v7, v14, v15
	s_cbranch_vccnz .LBB0_1616
	v_lshlrev_b32_e32 v20, 2, v18
	v_and_b32_e32 v20, 0xffffffc0, v20
	v_add_u32_e32 v20, v20, v19
	v_ashrrev_i32_e32 v21, 31, v20
	v_lshl_add_u64 v[12:13], v[12:13], 2, s[16:17]
	v_lshlrev_b64 v[32:33], 6, v[20:21]
	global_load_dwordx4 v[20:23], v[12:13], off offset:16
	global_load_dwordx4 v[24:27], v[12:13], off
	v_and_b32_e32 v2, 48, v2
	v_and_b32_e32 v19, 15, v18
	v_or3_b32 v32, v32, v2, v19
	s_waitcnt vmcnt(1)
	v_mul_f32_e32 v30, v10, v20
	s_waitcnt vmcnt(0)
	v_mul_f32_e32 v2, v8, v24
	v_mul_f32_e32 v12, v9, v25
	v_cvt_pk_bf16_f32 v28, v2, v12
	v_mul_f32_e32 v31, v11, v21
	v_lshlrev_b32_e32 v2, 16, v28
	v_fma_f32 v2, v8, v24, -v2
	v_and_b32_e32 v8, 0xffff0000, v28
	v_fma_f32 v8, v9, v25, -v8
	v_mul_f32_e32 v13, v16, v26
	v_mul_f32_e32 v19, v17, v27
	v_mul_f32_e32 v34, v14, v22
	v_mul_f32_e32 v35, v15, v23
	v_cvt_pk_bf16_f32 v29, v13, v19
	v_cvt_pk_bf16_f32 v30, v30, v31
	v_cvt_pk_bf16_f32 v31, v34, v35
	v_cvt_pk_bf16_f32 v8, v2, v8
	v_lshlrev_b64 v[12:13], 4, v[32:33]
	v_lshlrev_b32_e32 v2, 16, v29
	v_and_b32_e32 v9, 0xffff0000, v29
	v_fma_f32 v2, v16, v26, -v2
	v_fma_f32 v9, v17, v27, -v9
	v_cvt_pk_bf16_f32 v9, v2, v9
	v_lshlrev_b32_e32 v2, 16, v30
	v_fma_f32 v2, v10, v20, -v2
	v_and_b32_e32 v10, 0xffff0000, v30
	v_fma_f32 v10, v11, v21, -v10
	v_cvt_pk_bf16_f32 v10, v2, v10
	v_lshlrev_b32_e32 v2, 16, v31
	v_and_b32_e32 v11, 0xffff0000, v31
	v_fma_f32 v2, v14, v22, -v2
	v_fma_f32 v11, v15, v23, -v11
	v_lshl_add_u64 v[14:15], s[6:7], 0, v[12:13]
	v_lshl_add_u64 v[12:13], s[12:13], 0, v[12:13]
	v_cvt_pk_bf16_f32 v11, v2, v11
	global_store_dwordx4 v[14:15], v[28:31], off nt
	s_cbranch_execnz .LBB0_1430

.LBB0_1836:
	v_add_u32_e32 v163, 0x420, v162
	v_add_u32_e32 v164, 0x428, v162
	v_add_u32_e32 v165, 0x840, v162
	v_add_u32_e32 v166, 0x848, v162
	v_add_u32_e32 v167, 0xc60, v162
	v_add_u32_e32 v168, 0xc68, v162
	v_add_u32_e32 v169, 0x1080, v162
	v_add_u32_e32 v170, 0x1088, v162
	v_add_u32_e32 v171, 0x14a0, v162
	v_add_u32_e32 v172, 0x14a8, v162
	v_add_u32_e32 v173, 0x18c0, v162
	v_add_u32_e32 v174, 0x18c8, v162
	v_add_u32_e32 v175, 0x1ce0, v162
	v_add_u32_e32 v176, 0x1ce8, v162
	s_waitcnt vmcnt(7)
	ds_write2_b32 v162, v8, v9 offset1:1
	ds_write2_b32 v162, v10, v11 offset0:2 offset1:3
	s_waitcnt vmcnt(6)
	ds_write2_b32 v163, v4, v5 offset1:1
	ds_write2_b32 v164, v6, v7 offset1:1
	s_waitcnt vmcnt(5)
	ds_write2_b32 v165, v16, v17 offset1:1
	ds_write2_b32 v166, v18, v19 offset1:1
	s_waitcnt vmcnt(4)
	ds_write2_b32 v167, v12, v13 offset1:1
	ds_write2_b32 v168, v14, v15 offset1:1
	s_waitcnt vmcnt(3)
	ds_write2_b32 v169, v24, v25 offset1:1
	ds_write2_b32 v170, v26, v27 offset1:1
	s_waitcnt vmcnt(2)
	ds_write2_b32 v171, v20, v21 offset1:1
	ds_write2_b32 v172, v22, v23 offset1:1
	s_waitcnt vmcnt(1)
	ds_write2_b32 v173, v32, v33 offset1:1
	ds_write2_b32 v174, v34, v35 offset1:1
	s_waitcnt vmcnt(0)
	ds_write2_b32 v175, v28, v29 offset1:1
	ds_write2_b32 v176, v30, v31 offset1:1
	s_waitcnt lgkmcnt(0)
	ds_read2_b32 v[136:137], v157 offset1:33
	ds_read2_b32 v[150:151], v157 offset0:66 offset1:99
	ds_read2_b32 v[138:139], v157 offset0:132 offset1:165
	ds_read2_b32 v[148:149], v157 offset0:198 offset1:231
	s_cmp_lg_u64 s[12:13], 0
	s_cselect_b64 s[42:43], -1, 0
	s_and_b64 vcc, exec, s[42:43]
	v_add_u32_e32 v2, s89, v143
	v_add_u32_e32 v146, s8, v142
	s_waitcnt lgkmcnt(3)
	v_cvt_pk_bf16_f32 v132, v136, v137
	s_waitcnt lgkmcnt(2)
	v_cvt_pk_bf16_f32 v133, v150, v151
	s_waitcnt lgkmcnt(1)
	v_cvt_pk_bf16_f32 v134, v138, v139
	s_waitcnt lgkmcnt(0)
	v_cvt_pk_bf16_f32 v135, v148, v149
	s_cbranch_vccz .LBB0_2031
	v_lshlrev_b32_e32 v144, 2, v2
	v_and_b32_e32 v144, 0xffffffc0, v144
	v_ashrrev_i32_e32 v145, 5, v146
	v_add_u32_e32 v144, v145, v144
	v_ashrrev_i32_e32 v145, 31, v144
	v_lshlrev_b32_e32 v147, 1, v146
	v_lshlrev_b64 v[144:145], 6, v[144:145]
	v_and_b32_e32 v147, 48, v147
	v_and_b32_e32 v152, 15, v2
	v_or3_b32 v144, v144, v147, v152
	v_ashrrev_i32_e32 v147, 31, v146
	v_lshl_add_u64 v[152:153], v[146:147], 2, s[14:15]
	global_load_dwordx4 v[178:181], v[152:153], off offset:16
	global_load_dwordx4 v[182:185], v[152:153], off
	v_lshlrev_b64 v[144:145], 4, v[144:145]
	s_waitcnt vmcnt(1)
	v_mul_f32_e32 v188, v138, v178
	s_waitcnt vmcnt(0)
	v_mul_f32_e32 v147, v136, v182
	v_mul_f32_e32 v152, v137, v183
	v_cvt_pk_bf16_f32 v186, v147, v152
	v_mul_f32_e32 v189, v139, v179
	v_lshlrev_b32_e32 v147, 16, v186
	v_fma_f32 v136, v136, v182, -v147
	v_and_b32_e32 v147, 0xffff0000, v186
	v_fma_f32 v137, v137, v183, -v147
	v_mul_f32_e32 v153, v150, v184
	v_mul_f32_e32 v177, v151, v185
	v_mul_f32_e32 v190, v148, v180
	v_mul_f32_e32 v191, v149, v181
	v_cvt_pk_bf16_f32 v187, v153, v177
	v_cvt_pk_bf16_f32 v188, v188, v189
	v_cvt_pk_bf16_f32 v189, v190, v191
	v_cvt_pk_bf16_f32 v136, v136, v137
	s_nop 0
	v_lshlrev_b32_e32 v137, 16, v187
	v_and_b32_e32 v147, 0xffff0000, v187
	v_fma_f32 v137, v150, v184, -v137
	v_fma_f32 v147, v151, v185, -v147
	v_cvt_pk_bf16_f32 v137, v137, v147
	v_lshlrev_b32_e32 v147, 16, v188
	v_fma_f32 v138, v138, v178, -v147
	v_and_b32_e32 v147, 0xffff0000, v188
	v_fma_f32 v139, v139, v179, -v147
	v_cvt_pk_bf16_f32 v138, v138, v139
	v_lshlrev_b32_e32 v139, 16, v189
	v_and_b32_e32 v147, 0xffff0000, v189
	v_fma_f32 v139, v148, v180, -v139
	v_fma_f32 v147, v149, v181, -v147
	v_lshl_add_u64 v[148:149], s[10:11], 0, v[144:145]
	v_cvt_pk_bf16_f32 v139, v139, v147
	global_store_dwordx4 v[148:149], v[186:189], off nt
	v_lshl_add_u64 v[148:149], s[12:13], 0, v[144:145]
	v_lshlrev_b32_e32 v144, 1, v142
	s_cbranch_execnz .LBB0_1839

.LBB0_1839:
	global_store_dwordx4 v[148:149], v[136:139], off nt
	ds_read2_b32 v[136:137], v157 offset0:8 offset1:41
	ds_read2_b32 v[152:153], v157 offset0:74 offset1:107
	ds_read2_b32 v[138:139], v157 offset0:140 offset1:173
	ds_read2_b32 v[150:151], v157 offset0:206 offset1:239
	v_cndmask_b32_e64 v2, 0, 1, s[42:43]
	v_cmp_ne_u32_e64 s[2:3], 1, v2
	s_andn2_b64 vcc, exec, s[42:43]
	v_add_u32_e32 v2, s89, v154
	s_waitcnt lgkmcnt(3)
	v_cvt_pk_bf16_f32 v132, v136, v137
	s_waitcnt lgkmcnt(2)
	v_cvt_pk_bf16_f32 v133, v152, v153
	s_waitcnt lgkmcnt(1)
	v_cvt_pk_bf16_f32 v134, v138, v139
	s_waitcnt lgkmcnt(0)
	v_cvt_pk_bf16_f32 v135, v150, v151
	s_cbranch_vccnz .LBB0_2032
	v_lshlrev_b32_e32 v145, 2, v2
	v_and_b32_e32 v145, 0xffffffc0, v145
	v_ashrrev_i32_e32 v147, 5, v146
	v_add_u32_e32 v148, v147, v145
	v_ashrrev_i32_e32 v149, 31, v148
	v_lshlrev_b32_e32 v145, 1, v146
	v_lshlrev_b64 v[148:149], 6, v[148:149]
	v_and_b32_e32 v145, 48, v145
	v_and_b32_e32 v147, 15, v2
	v_or3_b32 v148, v148, v145, v147
	v_ashrrev_i32_e32 v147, 31, v146
	v_lshl_add_u64 v[182:183], v[146:147], 2, s[14:15]
	global_load_dwordx4 v[178:181], v[182:183], off offset:16
	s_nop 0
	global_load_dwordx4 v[182:185], v[182:183], off
	v_lshlrev_b64 v[148:149], 4, v[148:149]
	s_waitcnt vmcnt(1)
	v_mul_f32_e32 v188, v138, v178
	s_waitcnt vmcnt(0)
	v_mul_f32_e32 v145, v136, v182
	v_mul_f32_e32 v147, v137, v183
	v_cvt_pk_bf16_f32 v186, v145, v147
	v_mul_f32_e32 v187, v153, v185
	v_lshlrev_b32_e32 v145, 16, v186
	v_fma_f32 v136, v136, v182, -v145
	v_and_b32_e32 v145, 0xffff0000, v186
	v_mul_f32_e32 v189, v139, v179
	v_fma_f32 v137, v137, v183, -v145
	v_mul_f32_e32 v177, v152, v184
	v_mul_f32_e32 v190, v150, v180
	v_mul_f32_e32 v191, v151, v181
	v_cvt_pk_bf16_f32 v187, v177, v187
	v_cvt_pk_bf16_f32 v188, v188, v189
	v_cvt_pk_bf16_f32 v189, v190, v191
	v_cvt_pk_bf16_f32 v136, v136, v137
	s_nop 0
	v_lshlrev_b32_e32 v137, 16, v187
	v_and_b32_e32 v145, 0xffff0000, v187
	v_fma_f32 v137, v152, v184, -v137
	v_fma_f32 v145, v153, v185, -v145
	v_cvt_pk_bf16_f32 v137, v137, v145
	v_lshlrev_b32_e32 v145, 16, v188
	v_fma_f32 v138, v138, v178, -v145
	v_and_b32_e32 v145, 0xffff0000, v188
	v_fma_f32 v139, v139, v179, -v145
	v_cvt_pk_bf16_f32 v138, v138, v139
	v_lshlrev_b32_e32 v139, 16, v189
	v_and_b32_e32 v145, 0xffff0000, v189
	v_fma_f32 v139, v150, v180, -v139
	v_fma_f32 v145, v151, v181, -v145
	v_lshl_add_u64 v[150:151], s[10:11], 0, v[148:149]
	v_lshl_add_u64 v[148:149], s[12:13], 0, v[148:149]
	v_cvt_pk_bf16_f32 v139, v139, v145
	global_store_dwordx4 v[150:151], v[186:189], off nt
	s_cbranch_execnz .LBB0_1842

.LBB0_1842:
	global_store_dwordx4 v[148:149], v[136:139], off nt
	ds_read2_b32 v[136:137], v157 offset0:16 offset1:49
	ds_read2_b32 v[152:153], v157 offset0:82 offset1:115
	ds_read2_b32 v[138:139], v157 offset0:148 offset1:181
	ds_read2_b32 v[150:151], v157 offset0:214 offset1:247
	s_and_b64 vcc, exec, s[2:3]
	v_add_u32_e32 v2, s89, v155
	s_waitcnt lgkmcnt(3)
	v_cvt_pk_bf16_f32 v132, v136, v137
	s_waitcnt lgkmcnt(2)
	v_cvt_pk_bf16_f32 v133, v152, v153
	s_waitcnt lgkmcnt(1)
	v_cvt_pk_bf16_f32 v134, v138, v139
	s_waitcnt lgkmcnt(0)
	v_cvt_pk_bf16_f32 v135, v150, v151
	s_cbranch_vccnz .LBB0_2033
	v_lshlrev_b32_e32 v145, 2, v2
	v_and_b32_e32 v145, 0xffffffc0, v145
	v_ashrrev_i32_e32 v147, 5, v146
	v_add_u32_e32 v148, v147, v145
	v_ashrrev_i32_e32 v149, 31, v148
	v_lshlrev_b32_e32 v145, 1, v146
	v_lshlrev_b64 v[148:149], 6, v[148:149]
	v_and_b32_e32 v145, 48, v145
	v_and_b32_e32 v147, 15, v2
	v_or3_b32 v148, v148, v145, v147
	v_ashrrev_i32_e32 v147, 31, v146
	v_lshl_add_u64 v[182:183], v[146:147], 2, s[14:15]
	global_load_dwordx4 v[178:181], v[182:183], off offset:16
	s_nop 0
	global_load_dwordx4 v[182:185], v[182:183], off
	v_lshlrev_b64 v[148:149], 4, v[148:149]
	s_waitcnt vmcnt(1)
	v_mul_f32_e32 v188, v138, v178
	s_waitcnt vmcnt(0)
	v_mul_f32_e32 v145, v136, v182
	v_mul_f32_e32 v147, v137, v183
	v_cvt_pk_bf16_f32 v186, v145, v147
	v_mul_f32_e32 v187, v153, v185
	v_lshlrev_b32_e32 v145, 16, v186
	v_fma_f32 v136, v136, v182, -v145
	v_and_b32_e32 v145, 0xffff0000, v186
	v_mul_f32_e32 v189, v139, v179
	v_fma_f32 v137, v137, v183, -v145
	v_mul_f32_e32 v177, v152, v184
	v_mul_f32_e32 v190, v150, v180
	v_mul_f32_e32 v191, v151, v181
	v_cvt_pk_bf16_f32 v187, v177, v187
	v_cvt_pk_bf16_f32 v188, v188, v189
	v_cvt_pk_bf16_f32 v189, v190, v191
	v_cvt_pk_bf16_f32 v136, v136, v137
	s_nop 0
	v_lshlrev_b32_e32 v137, 16, v187
	v_and_b32_e32 v145, 0xffff0000, v187
	v_fma_f32 v137, v152, v184, -v137
	v_fma_f32 v145, v153, v185, -v145
	v_cvt_pk_bf16_f32 v137, v137, v145
	v_lshlrev_b32_e32 v145, 16, v188
	v_fma_f32 v138, v138, v178, -v145
	v_and_b32_e32 v145, 0xffff0000, v188
	v_fma_f32 v139, v139, v179, -v145
	v_cvt_pk_bf16_f32 v138, v138, v139
	v_lshlrev_b32_e32 v139, 16, v189
	v_and_b32_e32 v145, 0xffff0000, v189
	v_fma_f32 v139, v150, v180, -v139
	v_fma_f32 v145, v151, v181, -v145
	v_lshl_add_u64 v[150:151], s[10:11], 0, v[148:149]
	v_lshl_add_u64 v[148:149], s[12:13], 0, v[148:149]
	v_cvt_pk_bf16_f32 v139, v139, v145
	global_store_dwordx4 v[150:151], v[186:189], off nt
	s_cbranch_execnz .LBB0_1845

.LBB0_1845:
	global_store_dwordx4 v[148:149], v[136:139], off nt
	ds_read2_b32 v[136:137], v157 offset0:24 offset1:57
	ds_read2_b32 v[152:153], v157 offset0:90 offset1:123
	ds_read2_b32 v[138:139], v157 offset0:156 offset1:189
	ds_read2_b32 v[150:151], v157 offset0:222 offset1:255
	s_and_b64 vcc, exec, s[2:3]
	v_add_u32_e32 v2, s89, v156
	s_waitcnt lgkmcnt(3)
	v_cvt_pk_bf16_f32 v132, v136, v137
	s_waitcnt lgkmcnt(2)
	v_cvt_pk_bf16_f32 v133, v152, v153
	s_waitcnt lgkmcnt(1)
	v_cvt_pk_bf16_f32 v134, v138, v139
	s_waitcnt lgkmcnt(0)
	v_cvt_pk_bf16_f32 v135, v150, v151
	s_cbranch_vccnz .LBB0_2034
	v_lshlrev_b32_e32 v145, 2, v2
	v_and_b32_e32 v145, 0xffffffc0, v145
	v_ashrrev_i32_e32 v147, 5, v146
	v_add_u32_e32 v148, v147, v145
	v_ashrrev_i32_e32 v149, 31, v148
	v_lshlrev_b32_e32 v145, 1, v146
	v_lshlrev_b64 v[148:149], 6, v[148:149]
	v_and_b32_e32 v145, 48, v145
	v_and_b32_e32 v147, 15, v2
	v_or3_b32 v148, v148, v145, v147
	v_ashrrev_i32_e32 v147, 31, v146
	v_lshl_add_u64 v[146:147], v[146:147], 2, s[14:15]
	global_load_dwordx4 v[178:181], v[146:147], off offset:16
	global_load_dwordx4 v[182:185], v[146:147], off
	s_waitcnt vmcnt(1)
	v_mul_f32_e32 v188, v138, v178
	s_waitcnt vmcnt(0)
	v_mul_f32_e32 v145, v136, v182
	v_mul_f32_e32 v146, v137, v183
	v_cvt_pk_bf16_f32 v186, v145, v146
	v_mul_f32_e32 v189, v139, v179
	v_lshlrev_b32_e32 v145, 16, v186
	v_fma_f32 v136, v136, v182, -v145
	v_and_b32_e32 v145, 0xffff0000, v186
	v_fma_f32 v137, v137, v183, -v145
	v_mul_f32_e32 v147, v152, v184
	v_mul_f32_e32 v177, v153, v185
	v_mul_f32_e32 v190, v150, v180
	v_mul_f32_e32 v191, v151, v181
	v_cvt_pk_bf16_f32 v187, v147, v177
	v_cvt_pk_bf16_f32 v188, v188, v189
	v_cvt_pk_bf16_f32 v189, v190, v191
	v_cvt_pk_bf16_f32 v136, v136, v137
	v_lshlrev_b64 v[146:147], 4, v[148:149]
	v_lshlrev_b32_e32 v137, 16, v187
	v_and_b32_e32 v145, 0xffff0000, v187
	v_fma_f32 v137, v152, v184, -v137
	v_fma_f32 v145, v153, v185, -v145
	v_cvt_pk_bf16_f32 v137, v137, v145
	v_lshlrev_b32_e32 v145, 16, v188
	v_fma_f32 v138, v138, v178, -v145
	v_and_b32_e32 v145, 0xffff0000, v188
	v_fma_f32 v139, v139, v179, -v145
	v_cvt_pk_bf16_f32 v138, v138, v139
	v_lshlrev_b32_e32 v139, 16, v189
	v_fma_f32 v139, v150, v180, -v139
	v_and_b32_e32 v145, 0xffff0000, v189
	v_lshl_add_u64 v[148:149], s[10:11], 0, v[146:147]
	v_lshl_add_u64 v[146:147], s[12:13], 0, v[146:147]
	v_fma_f32 v145, v151, v181, -v145
	v_cvt_pk_bf16_f32 v139, v139, v145
	global_store_dwordx4 v[148:149], v[186:189], off nt
	s_cbranch_execnz .LBB0_1848

.LBB0_1848:
	s_lshr_b32 s2, s93, 3
	s_mul_i32 s2, s2, s82
	s_add_i32 s2, s2, s83
	s_and_b32 s73, s93, 4
	global_store_dwordx4 v[146:147], v[136:139], off nt
	s_lshl_b32 s72, s2, 6
	s_add_i32 s2, s54, s73
	s_waitcnt lgkmcnt(0)
	s_add_i32 s2, s2, s72
	s_cmp_lt_i32 s2, s50
	s_cselect_b32 s9, s2, -1
	s_cmp_lt_i32 s9, 0
	s_cbranch_scc1 .LBB0_1892
	s_mul_hi_u32 s2, s9, 0x9824d8ed
	s_lshr_b32 s2, s2, 15
	s_mul_i32 s3, s2, 0xd760
	s_sub_i32 s85, s9, s3
	s_cmpk_gt_u32 s85, 0xc2ff
	s_mov_b64 s[48:49], -1
	s_cbranch_scc0 .LBB0_1878
	s_add_i32 s48, s2, 1
	s_add_i32 s3, s85, 0xffff3d00
	s_cmpk_lt_u32 s3, 0x1400
	s_cselect_b32 s3, s3, s85
	s_cmpk_gt_u32 s3, 0xbff
	s_mov_b64 s[52:53], -1
	s_cbranch_scc0 .LBB0_1875
	s_cmpk_gt_u32 s3, 0x13ff
	s_cbranch_scc0 .LBB0_1872
	s_cmpk_gt_u32 s3, 0x93ff
	s_cbranch_scc0 .LBB0_1869
	s_cmpk_gt_u32 s3, 0xd3ff
	s_cbranch_scc0 .LBB0_1866
	s_cmpk_gt_u32 s3, 0xd5ff
	s_cbranch_scc0 .LBB0_1863
	s_cmpk_gt_u32 s3, 0xd6ff
	s_cbranch_scc0 .LBB0_1860
	s_cmpk_gt_u32 s3, 0xd71f
	s_mov_b64 s[44:45], -1
	s_cbranch_scc0 .LBB0_1858
	s_mov_b32 s49, s47
	v_readlane_b32 s56, v243, 40
	s_lshl_b64 s[10:11], s[48:49], 19
	v_readlane_b32 s62, v243, 46
	v_readlane_b32 s63, v243, 47
	s_add_u32 s42, s62, s10
	s_addc_u32 s43, s63, s11
	s_lshl_b64 s[12:13], s[48:49], 18
	v_readlane_b32 s8, v242, 33
	s_add_u32 s10, s8, s12
	v_readlane_b32 s8, v242, 52
	s_addc_u32 s11, s8, s13
	v_readlane_b32 s8, v242, 53
	s_add_u32 s12, s8, s12
	v_readlane_b32 s8, v242, 35
	v_readlane_b32 s58, v243, 42
	s_addc_u32 s13, s8, s13
	s_lshl_b32 s8, s48, 13
	v_readlane_b32 s59, v243, 43
	s_add_u32 s14, s58, s8
	s_addc_u32 s15, s59, 0
	s_lshl_b32 s44, s3, 5
	s_and_b32 s8, s44, 0x7fffffc0
	v_readlane_b32 s57, v243, 41
	v_readlane_b32 s60, v243, 44
	v_readlane_b32 s61, v243, 45
	v_readlane_b32 s64, v243, 48
	v_readlane_b32 s65, v243, 49
	v_readlane_b32 s66, v243, 50
	v_readlane_b32 s67, v243, 51
	v_readlane_b32 s68, v243, 52
	v_readlane_b32 s69, v243, 53
	v_readlane_b32 s70, v243, 54
	v_readlane_b32 s71, v243, 55
	s_add_i32 s8, s8, 0xffe51c00
	s_and_b32 s89, s44, 32
	s_mov_b64 s[44:45], 0

.LBB0_1892:
	s_cmp_lt_i32 s17, 0
	s_mov_b64 s[2:3], -1
	s_cbranch_scc1 .LBB0_1835
	ds_write2_b32 v162, v36, v37 offset1:1
	ds_write2_b32 v162, v38, v39 offset0:2 offset1:3
	ds_write2_b32 v163, v40, v41 offset1:1
	ds_write2_b32 v164, v42, v43 offset1:1
	ds_write2_b32 v165, v44, v45 offset1:1
	ds_write2_b32 v166, v46, v47 offset1:1
	ds_write2_b32 v167, v48, v49 offset1:1
	ds_write2_b32 v168, v50, v51 offset1:1
	ds_write2_b32 v169, v52, v53 offset1:1
	ds_write2_b32 v170, v54, v55 offset1:1
	ds_write2_b32 v171, v56, v57 offset1:1
	ds_write2_b32 v172, v58, v59 offset1:1
	ds_write2_b32 v173, v60, v61 offset1:1
	ds_write2_b32 v174, v62, v63 offset1:1
	ds_write2_b32 v175, v64, v65 offset1:1
	ds_write2_b32 v176, v66, v67 offset1:1
	s_waitcnt lgkmcnt(0)
	ds_read2_b32 v[136:137], v157 offset1:33
	ds_read2_b32 v[152:153], v157 offset0:66 offset1:99
	ds_read2_b32 v[138:139], v157 offset0:132 offset1:165
	ds_read2_b32 v[150:151], v157 offset0:198 offset1:231
	s_cmp_lg_u64 s[20:21], 0
	s_cselect_b64 s[42:43], -1, 0
	s_and_b64 vcc, exec, s[42:43]
	v_add_u32_e32 v2, s75, v143
	v_add_u32_e32 v146, s16, v142
	s_waitcnt lgkmcnt(3)
	v_cvt_pk_bf16_f32 v132, v136, v137
	s_waitcnt lgkmcnt(2)
	v_cvt_pk_bf16_f32 v133, v152, v153
	s_waitcnt lgkmcnt(1)
	v_cvt_pk_bf16_f32 v134, v138, v139
	s_waitcnt lgkmcnt(0)
	v_cvt_pk_bf16_f32 v135, v150, v151
	s_cbranch_vccz .LBB0_2035
	v_lshlrev_b32_e32 v145, 2, v2
	v_and_b32_e32 v145, 0xffffffc0, v145
	v_ashrrev_i32_e32 v147, 5, v146
	v_add_u32_e32 v148, v145, v147
	v_ashrrev_i32_e32 v149, 31, v148
	v_lshlrev_b32_e32 v145, 1, v146
	v_lshlrev_b64 v[148:149], 6, v[148:149]
	v_and_b32_e32 v145, 48, v145
	v_and_b32_e32 v147, 15, v2
	v_or3_b32 v148, v148, v145, v147
	v_ashrrev_i32_e32 v147, 31, v146
	v_lshl_add_u64 v[182:183], v[146:147], 2, s[22:23]
	global_load_dwordx4 v[178:181], v[182:183], off offset:16
	s_nop 0
	global_load_dwordx4 v[182:185], v[182:183], off
	v_lshlrev_b64 v[148:149], 4, v[148:149]
	s_waitcnt vmcnt(1)
	v_mul_f32_e32 v188, v138, v178
	s_waitcnt vmcnt(0)
	v_mul_f32_e32 v145, v136, v182
	v_mul_f32_e32 v147, v137, v183
	v_cvt_pk_bf16_f32 v186, v145, v147
	v_mul_f32_e32 v187, v153, v185
	v_lshlrev_b32_e32 v145, 16, v186
	v_fma_f32 v136, v136, v182, -v145
	v_and_b32_e32 v145, 0xffff0000, v186
	v_mul_f32_e32 v189, v139, v179
	v_fma_f32 v137, v137, v183, -v145
	v_mul_f32_e32 v177, v152, v184
	v_mul_f32_e32 v190, v150, v180
	v_mul_f32_e32 v191, v151, v181
	v_cvt_pk_bf16_f32 v187, v177, v187
	v_cvt_pk_bf16_f32 v188, v188, v189
	v_cvt_pk_bf16_f32 v189, v190, v191
	v_cvt_pk_bf16_f32 v136, v136, v137
	s_nop 0
	v_lshlrev_b32_e32 v137, 16, v187
	v_and_b32_e32 v145, 0xffff0000, v187
	v_fma_f32 v137, v152, v184, -v137
	v_fma_f32 v145, v153, v185, -v145
	v_cvt_pk_bf16_f32 v137, v137, v145
	v_lshlrev_b32_e32 v145, 16, v188
	v_fma_f32 v138, v138, v178, -v145
	v_and_b32_e32 v145, 0xffff0000, v188
	v_fma_f32 v139, v139, v179, -v145
	v_cvt_pk_bf16_f32 v138, v138, v139
	v_lshlrev_b32_e32 v139, 16, v189
	v_and_b32_e32 v145, 0xffff0000, v189
	v_fma_f32 v139, v150, v180, -v139
	v_fma_f32 v145, v151, v181, -v145
	v_lshl_add_u64 v[150:151], s[18:19], 0, v[148:149]
	v_cvt_pk_bf16_f32 v139, v139, v145
	global_store_dwordx4 v[150:151], v[186:189], off nt
	v_lshl_add_u64 v[148:149], s[20:21], 0, v[148:149]
	s_cbranch_execnz .LBB0_1896

.LBB0_1896:
	global_store_dwordx4 v[148:149], v[136:139], off nt
	ds_read2_b32 v[136:137], v157 offset0:8 offset1:41
	ds_read2_b32 v[152:153], v157 offset0:74 offset1:107
	ds_read2_b32 v[138:139], v157 offset0:140 offset1:173
	ds_read2_b32 v[150:151], v157 offset0:206 offset1:239
	v_cndmask_b32_e64 v2, 0, 1, s[42:43]
	v_cmp_ne_u32_e64 s[2:3], 1, v2
	s_andn2_b64 vcc, exec, s[42:43]
	v_add_u32_e32 v2, s75, v154
	s_waitcnt lgkmcnt(3)
	v_cvt_pk_bf16_f32 v132, v136, v137
	s_waitcnt lgkmcnt(2)
	v_cvt_pk_bf16_f32 v133, v152, v153
	s_waitcnt lgkmcnt(1)
	v_cvt_pk_bf16_f32 v134, v138, v139
	s_waitcnt lgkmcnt(0)
	v_cvt_pk_bf16_f32 v135, v150, v151
	s_cbranch_vccnz .LBB0_2036
	v_lshlrev_b32_e32 v145, 2, v2
	v_and_b32_e32 v145, 0xffffffc0, v145
	v_ashrrev_i32_e32 v147, 5, v146
	v_add_u32_e32 v148, v145, v147
	v_ashrrev_i32_e32 v149, 31, v148
	v_lshlrev_b32_e32 v145, 1, v146
	v_lshlrev_b64 v[148:149], 6, v[148:149]
	v_and_b32_e32 v145, 48, v145
	v_and_b32_e32 v147, 15, v2
	v_or3_b32 v148, v148, v145, v147
	v_ashrrev_i32_e32 v147, 31, v146
	v_lshl_add_u64 v[182:183], v[146:147], 2, s[22:23]
	global_load_dwordx4 v[178:181], v[182:183], off offset:16
	s_nop 0
	global_load_dwordx4 v[182:185], v[182:183], off
	v_lshlrev_b64 v[148:149], 4, v[148:149]
	s_waitcnt vmcnt(1)
	v_mul_f32_e32 v188, v138, v178
	s_waitcnt vmcnt(0)
	v_mul_f32_e32 v145, v136, v182
	v_mul_f32_e32 v147, v137, v183
	v_cvt_pk_bf16_f32 v186, v145, v147
	v_mul_f32_e32 v187, v153, v185
	v_lshlrev_b32_e32 v145, 16, v186
	v_fma_f32 v136, v136, v182, -v145
	v_and_b32_e32 v145, 0xffff0000, v186
	v_mul_f32_e32 v189, v139, v179
	v_fma_f32 v137, v137, v183, -v145
	v_mul_f32_e32 v177, v152, v184
	v_mul_f32_e32 v190, v150, v180
	v_mul_f32_e32 v191, v151, v181
	v_cvt_pk_bf16_f32 v187, v177, v187
	v_cvt_pk_bf16_f32 v188, v188, v189
	v_cvt_pk_bf16_f32 v189, v190, v191
	v_cvt_pk_bf16_f32 v136, v136, v137
	s_nop 0
	v_lshlrev_b32_e32 v137, 16, v187
	v_and_b32_e32 v145, 0xffff0000, v187
	v_fma_f32 v137, v152, v184, -v137
	v_fma_f32 v145, v153, v185, -v145
	v_cvt_pk_bf16_f32 v137, v137, v145
	v_lshlrev_b32_e32 v145, 16, v188
	v_fma_f32 v138, v138, v178, -v145
	v_and_b32_e32 v145, 0xffff0000, v188
	v_fma_f32 v139, v139, v179, -v145
	v_cvt_pk_bf16_f32 v138, v138, v139
	v_lshlrev_b32_e32 v139, 16, v189
	v_and_b32_e32 v145, 0xffff0000, v189
	v_fma_f32 v139, v150, v180, -v139
	v_fma_f32 v145, v151, v181, -v145
	v_lshl_add_u64 v[150:151], s[18:19], 0, v[148:149]
	v_lshl_add_u64 v[148:149], s[20:21], 0, v[148:149]
	v_cvt_pk_bf16_f32 v139, v139, v145
	global_store_dwordx4 v[150:151], v[186:189], off nt
	s_cbranch_execnz .LBB0_1899

.LBB0_1899:
	global_store_dwordx4 v[148:149], v[136:139], off nt
	ds_read2_b32 v[136:137], v157 offset0:16 offset1:49
	ds_read2_b32 v[152:153], v157 offset0:82 offset1:115
	ds_read2_b32 v[138:139], v157 offset0:148 offset1:181
	ds_read2_b32 v[150:151], v157 offset0:214 offset1:247
	s_and_b64 vcc, exec, s[2:3]
	v_add_u32_e32 v2, s75, v155
	s_waitcnt lgkmcnt(3)
	v_cvt_pk_bf16_f32 v132, v136, v137
	s_waitcnt lgkmcnt(2)
	v_cvt_pk_bf16_f32 v133, v152, v153
	s_waitcnt lgkmcnt(1)
	v_cvt_pk_bf16_f32 v134, v138, v139
	s_waitcnt lgkmcnt(0)
	v_cvt_pk_bf16_f32 v135, v150, v151
	s_cbranch_vccnz .LBB0_2037
	v_lshlrev_b32_e32 v145, 2, v2
	v_and_b32_e32 v145, 0xffffffc0, v145
	v_ashrrev_i32_e32 v147, 5, v146
	v_add_u32_e32 v148, v145, v147
	v_ashrrev_i32_e32 v149, 31, v148
	v_lshlrev_b32_e32 v145, 1, v146
	v_lshlrev_b64 v[148:149], 6, v[148:149]
	v_and_b32_e32 v145, 48, v145
	v_and_b32_e32 v147, 15, v2
	v_or3_b32 v148, v148, v145, v147
	v_ashrrev_i32_e32 v147, 31, v146
	v_lshl_add_u64 v[182:183], v[146:147], 2, s[22:23]
	global_load_dwordx4 v[178:181], v[182:183], off offset:16
	s_nop 0
	global_load_dwordx4 v[182:185], v[182:183], off
	v_lshlrev_b64 v[148:149], 4, v[148:149]
	s_waitcnt vmcnt(1)
	v_mul_f32_e32 v188, v138, v178
	s_waitcnt vmcnt(0)
	v_mul_f32_e32 v145, v136, v182
	v_mul_f32_e32 v147, v137, v183
	v_cvt_pk_bf16_f32 v186, v145, v147
	v_mul_f32_e32 v187, v153, v185
	v_lshlrev_b32_e32 v145, 16, v186
	v_fma_f32 v136, v136, v182, -v145
	v_and_b32_e32 v145, 0xffff0000, v186
	v_mul_f32_e32 v189, v139, v179
	v_fma_f32 v137, v137, v183, -v145
	v_mul_f32_e32 v177, v152, v184
	v_mul_f32_e32 v190, v150, v180
	v_mul_f32_e32 v191, v151, v181
	v_cvt_pk_bf16_f32 v187, v177, v187
	v_cvt_pk_bf16_f32 v188, v188, v189
	v_cvt_pk_bf16_f32 v189, v190, v191
	v_cvt_pk_bf16_f32 v136, v136, v137
	s_nop 0
	v_lshlrev_b32_e32 v137, 16, v187
	v_and_b32_e32 v145, 0xffff0000, v187
	v_fma_f32 v137, v152, v184, -v137
	v_fma_f32 v145, v153, v185, -v145
	v_cvt_pk_bf16_f32 v137, v137, v145
	v_lshlrev_b32_e32 v145, 16, v188
	v_fma_f32 v138, v138, v178, -v145
	v_and_b32_e32 v145, 0xffff0000, v188
	v_fma_f32 v139, v139, v179, -v145
	v_cvt_pk_bf16_f32 v138, v138, v139
	v_lshlrev_b32_e32 v139, 16, v189
	v_and_b32_e32 v145, 0xffff0000, v189
	v_fma_f32 v139, v150, v180, -v139
	v_fma_f32 v145, v151, v181, -v145
	v_lshl_add_u64 v[150:151], s[18:19], 0, v[148:149]
	v_lshl_add_u64 v[148:149], s[20:21], 0, v[148:149]
	v_cvt_pk_bf16_f32 v139, v139, v145
	global_store_dwordx4 v[150:151], v[186:189], off nt
	s_cbranch_execnz .LBB0_1902

.LBB0_1902:
	global_store_dwordx4 v[148:149], v[136:139], off nt
	ds_read2_b32 v[136:137], v157 offset0:24 offset1:57
	ds_read2_b32 v[152:153], v157 offset0:90 offset1:123
	ds_read2_b32 v[138:139], v157 offset0:156 offset1:189
	ds_read2_b32 v[150:151], v157 offset0:222 offset1:255
	s_and_b64 vcc, exec, s[2:3]
	v_add_u32_e32 v2, s75, v156
	s_waitcnt lgkmcnt(3)
	v_cvt_pk_bf16_f32 v132, v136, v137
	s_waitcnt lgkmcnt(2)
	v_cvt_pk_bf16_f32 v133, v152, v153
	s_waitcnt lgkmcnt(1)
	v_cvt_pk_bf16_f32 v134, v138, v139
	s_waitcnt lgkmcnt(0)
	v_cvt_pk_bf16_f32 v135, v150, v151
	s_cbranch_vccnz .LBB0_2038
	v_lshlrev_b32_e32 v145, 2, v2
	v_and_b32_e32 v145, 0xffffffc0, v145
	v_ashrrev_i32_e32 v147, 5, v146
	v_add_u32_e32 v148, v145, v147
	v_ashrrev_i32_e32 v149, 31, v148
	v_lshlrev_b32_e32 v145, 1, v146
	v_lshlrev_b64 v[148:149], 6, v[148:149]
	v_and_b32_e32 v145, 48, v145
	v_and_b32_e32 v147, 15, v2
	v_or3_b32 v148, v148, v145, v147
	v_ashrrev_i32_e32 v147, 31, v146
	v_lshl_add_u64 v[146:147], v[146:147], 2, s[22:23]
	global_load_dwordx4 v[178:181], v[146:147], off offset:16
	global_load_dwordx4 v[182:185], v[146:147], off
	s_waitcnt vmcnt(1)
	v_mul_f32_e32 v188, v138, v178
	s_waitcnt vmcnt(0)
	v_mul_f32_e32 v145, v136, v182
	v_mul_f32_e32 v146, v137, v183
	v_cvt_pk_bf16_f32 v186, v145, v146
	v_mul_f32_e32 v189, v139, v179
	v_lshlrev_b32_e32 v145, 16, v186
	v_fma_f32 v136, v136, v182, -v145
	v_and_b32_e32 v145, 0xffff0000, v186
	v_fma_f32 v137, v137, v183, -v145
	v_mul_f32_e32 v147, v152, v184
	v_mul_f32_e32 v177, v153, v185
	v_mul_f32_e32 v190, v150, v180
	v_mul_f32_e32 v191, v151, v181
	v_cvt_pk_bf16_f32 v187, v147, v177
	v_cvt_pk_bf16_f32 v188, v188, v189
	v_cvt_pk_bf16_f32 v189, v190, v191
	v_cvt_pk_bf16_f32 v136, v136, v137
	v_lshlrev_b64 v[146:147], 4, v[148:149]
	v_lshlrev_b32_e32 v137, 16, v187
	v_and_b32_e32 v145, 0xffff0000, v187
	v_fma_f32 v137, v152, v184, -v137
	v_fma_f32 v145, v153, v185, -v145
	v_cvt_pk_bf16_f32 v137, v137, v145
	v_lshlrev_b32_e32 v145, 16, v188
	v_fma_f32 v138, v138, v178, -v145
	v_and_b32_e32 v145, 0xffff0000, v188
	v_fma_f32 v139, v139, v179, -v145
	v_cvt_pk_bf16_f32 v138, v138, v139
	v_lshlrev_b32_e32 v139, 16, v189
	v_fma_f32 v139, v150, v180, -v139
	v_and_b32_e32 v145, 0xffff0000, v189
	v_lshl_add_u64 v[148:149], s[18:19], 0, v[146:147]
	v_lshl_add_u64 v[146:147], s[20:21], 0, v[146:147]
	v_fma_f32 v145, v151, v181, -v145
	v_cvt_pk_bf16_f32 v139, v139, v145
	global_store_dwordx4 v[148:149], v[186:189], off nt
	s_cbranch_execnz .LBB0_1905

.LBB0_1905:
	global_store_dwordx4 v[146:147], v[136:139], off nt
	s_add_i32 s2, s86, s73
	s_waitcnt lgkmcnt(0)
	s_add_i32 s2, s2, s72
	s_cmp_lt_i32 s2, s50
	s_cselect_b32 s17, s2, -1
	s_cmp_lt_i32 s17, 0
	s_cbranch_scc1 .LBB0_1949
	s_mul_hi_u32 s2, s17, 0x9824d8ed
	s_lshr_b32 s2, s2, 15
	s_mul_i32 s3, s2, 0xd760
	s_sub_i32 s85, s17, s3
	s_cmpk_gt_u32 s85, 0xc2ff
	s_mov_b64 s[48:49], -1
	s_cbranch_scc0 .LBB0_1935
	s_add_i32 s48, s2, 1
	s_add_i32 s3, s85, 0xffff3d00
	s_cmpk_lt_u32 s3, 0x1400
	s_cselect_b32 s3, s3, s85
	s_cmpk_gt_u32 s3, 0xbff
	s_mov_b64 s[52:53], -1
	s_cbranch_scc0 .LBB0_1932
	s_cmpk_gt_u32 s3, 0x13ff
	s_cbranch_scc0 .LBB0_1929
	s_cmpk_gt_u32 s3, 0x93ff
	s_cbranch_scc0 .LBB0_1926
	s_cmpk_gt_u32 s3, 0xd3ff
	s_cbranch_scc0 .LBB0_1923
	s_cmpk_gt_u32 s3, 0xd5ff
	s_cbranch_scc0 .LBB0_1920
	s_cmpk_gt_u32 s3, 0xd6ff
	s_cbranch_scc0 .LBB0_1917
	s_cmpk_gt_u32 s3, 0xd71f
	s_mov_b64 s[44:45], -1
	s_cbranch_scc0 .LBB0_1915
	s_mov_b32 s49, s47
	v_readlane_b32 s56, v243, 40
	s_lshl_b64 s[18:19], s[48:49], 19
	v_readlane_b32 s62, v243, 46
	v_readlane_b32 s63, v243, 47
	s_add_u32 s42, s62, s18
	s_addc_u32 s43, s63, s19
	s_lshl_b64 s[20:21], s[48:49], 18
	v_readlane_b32 s16, v242, 33
	s_add_u32 s18, s16, s20
	v_readlane_b32 s16, v242, 52
	s_addc_u32 s19, s16, s21
	v_readlane_b32 s16, v242, 53
	s_add_u32 s20, s16, s20
	v_readlane_b32 s16, v242, 35
	v_readlane_b32 s58, v243, 42
	s_addc_u32 s21, s16, s21
	s_lshl_b32 s16, s48, 13
	v_readlane_b32 s59, v243, 43
	s_add_u32 s22, s58, s16
	s_addc_u32 s23, s59, 0
	s_lshl_b32 s44, s3, 5
	s_and_b32 s16, s44, 0x7fffffc0
	v_readlane_b32 s57, v243, 41
	v_readlane_b32 s60, v243, 44
	v_readlane_b32 s61, v243, 45
	v_readlane_b32 s64, v243, 48
	v_readlane_b32 s65, v243, 49
	v_readlane_b32 s66, v243, 50
	v_readlane_b32 s67, v243, 51
	v_readlane_b32 s68, v243, 52
	v_readlane_b32 s69, v243, 53
	v_readlane_b32 s70, v243, 54
	v_readlane_b32 s71, v243, 55
	s_add_i32 s16, s16, 0xffe51c00
	s_and_b32 s75, s44, 32
	s_mov_b64 s[44:45], 0

.LBB0_1949:
	s_cmp_lt_i32 s25, 0
	s_mov_b64 s[2:3], -1
	s_cbranch_scc1 .LBB0_1835
	ds_write2_b32 v162, v68, v69 offset1:1
	ds_write2_b32 v162, v70, v71 offset0:2 offset1:3
	ds_write2_b32 v163, v72, v73 offset1:1
	ds_write2_b32 v164, v74, v75 offset1:1
	ds_write2_b32 v165, v76, v77 offset1:1
	ds_write2_b32 v166, v78, v79 offset1:1
	ds_write2_b32 v167, v80, v81 offset1:1
	ds_write2_b32 v168, v82, v83 offset1:1
	ds_write2_b32 v169, v84, v85 offset1:1
	ds_write2_b32 v170, v86, v87 offset1:1
	ds_write2_b32 v171, v88, v89 offset1:1
	ds_write2_b32 v172, v90, v91 offset1:1
	ds_write2_b32 v173, v92, v93 offset1:1
	ds_write2_b32 v174, v94, v95 offset1:1
	ds_write2_b32 v175, v96, v97 offset1:1
	ds_write2_b32 v176, v98, v99 offset1:1
	s_waitcnt lgkmcnt(0)
	ds_read2_b32 v[136:137], v157 offset1:33
	ds_read2_b32 v[152:153], v157 offset0:66 offset1:99
	ds_read2_b32 v[138:139], v157 offset0:132 offset1:165
	ds_read2_b32 v[150:151], v157 offset0:198 offset1:231
	s_cmp_lg_u64 s[28:29], 0
	s_cselect_b64 s[42:43], -1, 0
	s_and_b64 vcc, exec, s[42:43]
	v_add_u32_e32 v2, s87, v143
	v_add_u32_e32 v146, s24, v142
	s_waitcnt lgkmcnt(3)
	v_cvt_pk_bf16_f32 v132, v136, v137
	s_waitcnt lgkmcnt(2)
	v_cvt_pk_bf16_f32 v133, v152, v153
	s_waitcnt lgkmcnt(1)
	v_cvt_pk_bf16_f32 v134, v138, v139
	s_waitcnt lgkmcnt(0)
	v_cvt_pk_bf16_f32 v135, v150, v151
	s_cbranch_vccz .LBB0_2039
	v_lshlrev_b32_e32 v145, 2, v2
	v_and_b32_e32 v145, 0xffffffc0, v145
	v_ashrrev_i32_e32 v147, 5, v146
	v_add_u32_e32 v148, v145, v147
	v_ashrrev_i32_e32 v149, 31, v148
	v_lshlrev_b32_e32 v145, 1, v146
	v_lshlrev_b64 v[148:149], 6, v[148:149]
	v_and_b32_e32 v145, 48, v145
	v_and_b32_e32 v147, 15, v2
	v_or3_b32 v148, v148, v145, v147
	v_ashrrev_i32_e32 v147, 31, v146
	v_lshl_add_u64 v[182:183], v[146:147], 2, s[30:31]
	global_load_dwordx4 v[178:181], v[182:183], off offset:16
	s_nop 0
	global_load_dwordx4 v[182:185], v[182:183], off
	v_lshlrev_b64 v[148:149], 4, v[148:149]
	s_waitcnt vmcnt(1)
	v_mul_f32_e32 v188, v138, v178
	s_waitcnt vmcnt(0)
	v_mul_f32_e32 v145, v136, v182
	v_mul_f32_e32 v147, v137, v183
	v_cvt_pk_bf16_f32 v186, v145, v147
	v_mul_f32_e32 v187, v153, v185
	v_lshlrev_b32_e32 v145, 16, v186
	v_fma_f32 v136, v136, v182, -v145
	v_and_b32_e32 v145, 0xffff0000, v186
	v_mul_f32_e32 v189, v139, v179
	v_fma_f32 v137, v137, v183, -v145
	v_mul_f32_e32 v177, v152, v184
	v_mul_f32_e32 v190, v150, v180
	v_mul_f32_e32 v191, v151, v181
	v_cvt_pk_bf16_f32 v187, v177, v187
	v_cvt_pk_bf16_f32 v188, v188, v189
	v_cvt_pk_bf16_f32 v189, v190, v191
	v_cvt_pk_bf16_f32 v136, v136, v137
	s_nop 0
	v_lshlrev_b32_e32 v137, 16, v187
	v_and_b32_e32 v145, 0xffff0000, v187
	v_fma_f32 v137, v152, v184, -v137
	v_fma_f32 v145, v153, v185, -v145
	v_cvt_pk_bf16_f32 v137, v137, v145
	v_lshlrev_b32_e32 v145, 16, v188
	v_fma_f32 v138, v138, v178, -v145
	v_and_b32_e32 v145, 0xffff0000, v188
	v_fma_f32 v139, v139, v179, -v145
	v_cvt_pk_bf16_f32 v138, v138, v139
	v_lshlrev_b32_e32 v139, 16, v189
	v_and_b32_e32 v145, 0xffff0000, v189
	v_fma_f32 v139, v150, v180, -v139
	v_fma_f32 v145, v151, v181, -v145
	v_lshl_add_u64 v[150:151], s[26:27], 0, v[148:149]
	v_cvt_pk_bf16_f32 v139, v139, v145
	global_store_dwordx4 v[150:151], v[186:189], off nt
	v_lshl_add_u64 v[148:149], s[28:29], 0, v[148:149]
	s_cbranch_execnz .LBB0_1953

.LBB0_1953:
	global_store_dwordx4 v[148:149], v[136:139], off nt
	ds_read2_b32 v[136:137], v157 offset0:8 offset1:41
	ds_read2_b32 v[152:153], v157 offset0:74 offset1:107
	ds_read2_b32 v[138:139], v157 offset0:140 offset1:173
	ds_read2_b32 v[150:151], v157 offset0:206 offset1:239
	v_cndmask_b32_e64 v2, 0, 1, s[42:43]
	v_cmp_ne_u32_e64 s[2:3], 1, v2
	s_andn2_b64 vcc, exec, s[42:43]
	v_add_u32_e32 v2, s87, v154
	s_waitcnt lgkmcnt(3)
	v_cvt_pk_bf16_f32 v132, v136, v137
	s_waitcnt lgkmcnt(2)
	v_cvt_pk_bf16_f32 v133, v152, v153
	s_waitcnt lgkmcnt(1)
	v_cvt_pk_bf16_f32 v134, v138, v139
	s_waitcnt lgkmcnt(0)
	v_cvt_pk_bf16_f32 v135, v150, v151
	s_cbranch_vccnz .LBB0_2040
	v_lshlrev_b32_e32 v145, 2, v2
	v_and_b32_e32 v145, 0xffffffc0, v145
	v_ashrrev_i32_e32 v147, 5, v146
	v_add_u32_e32 v148, v145, v147
	v_ashrrev_i32_e32 v149, 31, v148
	v_lshlrev_b32_e32 v145, 1, v146
	v_lshlrev_b64 v[148:149], 6, v[148:149]
	v_and_b32_e32 v145, 48, v145
	v_and_b32_e32 v147, 15, v2
	v_or3_b32 v148, v148, v145, v147
	v_ashrrev_i32_e32 v147, 31, v146
	v_lshl_add_u64 v[182:183], v[146:147], 2, s[30:31]
	global_load_dwordx4 v[178:181], v[182:183], off offset:16
	s_nop 0
	global_load_dwordx4 v[182:185], v[182:183], off
	v_lshlrev_b64 v[148:149], 4, v[148:149]
	s_waitcnt vmcnt(1)
	v_mul_f32_e32 v188, v138, v178
	s_waitcnt vmcnt(0)
	v_mul_f32_e32 v145, v136, v182
	v_mul_f32_e32 v147, v137, v183
	v_cvt_pk_bf16_f32 v186, v145, v147
	v_mul_f32_e32 v187, v153, v185
	v_lshlrev_b32_e32 v145, 16, v186
	v_fma_f32 v136, v136, v182, -v145
	v_and_b32_e32 v145, 0xffff0000, v186
	v_mul_f32_e32 v189, v139, v179
	v_fma_f32 v137, v137, v183, -v145
	v_mul_f32_e32 v177, v152, v184
	v_mul_f32_e32 v190, v150, v180
	v_mul_f32_e32 v191, v151, v181
	v_cvt_pk_bf16_f32 v187, v177, v187
	v_cvt_pk_bf16_f32 v188, v188, v189
	v_cvt_pk_bf16_f32 v189, v190, v191
	v_cvt_pk_bf16_f32 v136, v136, v137
	s_nop 0
	v_lshlrev_b32_e32 v137, 16, v187
	v_and_b32_e32 v145, 0xffff0000, v187
	v_fma_f32 v137, v152, v184, -v137
	v_fma_f32 v145, v153, v185, -v145
	v_cvt_pk_bf16_f32 v137, v137, v145
	v_lshlrev_b32_e32 v145, 16, v188
	v_fma_f32 v138, v138, v178, -v145
	v_and_b32_e32 v145, 0xffff0000, v188
	v_fma_f32 v139, v139, v179, -v145
	v_cvt_pk_bf16_f32 v138, v138, v139
	v_lshlrev_b32_e32 v139, 16, v189
	v_and_b32_e32 v145, 0xffff0000, v189
	v_fma_f32 v139, v150, v180, -v139
	v_fma_f32 v145, v151, v181, -v145
	v_lshl_add_u64 v[150:151], s[26:27], 0, v[148:149]
	v_lshl_add_u64 v[148:149], s[28:29], 0, v[148:149]
	v_cvt_pk_bf16_f32 v139, v139, v145
	global_store_dwordx4 v[150:151], v[186:189], off nt
	s_cbranch_execnz .LBB0_1956

.LBB0_1956:
	global_store_dwordx4 v[148:149], v[136:139], off nt
	ds_read2_b32 v[136:137], v157 offset0:16 offset1:49
	ds_read2_b32 v[152:153], v157 offset0:82 offset1:115
	ds_read2_b32 v[138:139], v157 offset0:148 offset1:181
	ds_read2_b32 v[150:151], v157 offset0:214 offset1:247
	s_and_b64 vcc, exec, s[2:3]
	v_add_u32_e32 v2, s87, v155
	s_waitcnt lgkmcnt(3)
	v_cvt_pk_bf16_f32 v132, v136, v137
	s_waitcnt lgkmcnt(2)
	v_cvt_pk_bf16_f32 v133, v152, v153
	s_waitcnt lgkmcnt(1)
	v_cvt_pk_bf16_f32 v134, v138, v139
	s_waitcnt lgkmcnt(0)
	v_cvt_pk_bf16_f32 v135, v150, v151
	s_cbranch_vccnz .LBB0_2041
	v_lshlrev_b32_e32 v145, 2, v2
	v_and_b32_e32 v145, 0xffffffc0, v145
	v_ashrrev_i32_e32 v147, 5, v146
	v_add_u32_e32 v148, v145, v147
	v_ashrrev_i32_e32 v149, 31, v148
	v_lshlrev_b32_e32 v145, 1, v146
	v_lshlrev_b64 v[148:149], 6, v[148:149]
	v_and_b32_e32 v145, 48, v145
	v_and_b32_e32 v147, 15, v2
	v_or3_b32 v148, v148, v145, v147
	v_ashrrev_i32_e32 v147, 31, v146
	v_lshl_add_u64 v[182:183], v[146:147], 2, s[30:31]
	global_load_dwordx4 v[178:181], v[182:183], off offset:16
	s_nop 0
	global_load_dwordx4 v[182:185], v[182:183], off
	v_lshlrev_b64 v[148:149], 4, v[148:149]
	s_waitcnt vmcnt(1)
	v_mul_f32_e32 v188, v138, v178
	s_waitcnt vmcnt(0)
	v_mul_f32_e32 v145, v136, v182
	v_mul_f32_e32 v147, v137, v183
	v_cvt_pk_bf16_f32 v186, v145, v147
	v_mul_f32_e32 v187, v153, v185
	v_lshlrev_b32_e32 v145, 16, v186
	v_fma_f32 v136, v136, v182, -v145
	v_and_b32_e32 v145, 0xffff0000, v186
	v_mul_f32_e32 v189, v139, v179
	v_fma_f32 v137, v137, v183, -v145
	v_mul_f32_e32 v177, v152, v184
	v_mul_f32_e32 v190, v150, v180
	v_mul_f32_e32 v191, v151, v181
	v_cvt_pk_bf16_f32 v187, v177, v187
	v_cvt_pk_bf16_f32 v188, v188, v189
	v_cvt_pk_bf16_f32 v189, v190, v191
	v_cvt_pk_bf16_f32 v136, v136, v137
	s_nop 0
	v_lshlrev_b32_e32 v137, 16, v187
	v_and_b32_e32 v145, 0xffff0000, v187
	v_fma_f32 v137, v152, v184, -v137
	v_fma_f32 v145, v153, v185, -v145
	v_cvt_pk_bf16_f32 v137, v137, v145
	v_lshlrev_b32_e32 v145, 16, v188
	v_fma_f32 v138, v138, v178, -v145
	v_and_b32_e32 v145, 0xffff0000, v188
	v_fma_f32 v139, v139, v179, -v145
	v_cvt_pk_bf16_f32 v138, v138, v139
	v_lshlrev_b32_e32 v139, 16, v189
	v_and_b32_e32 v145, 0xffff0000, v189
	v_fma_f32 v139, v150, v180, -v139
	v_fma_f32 v145, v151, v181, -v145
	v_lshl_add_u64 v[150:151], s[26:27], 0, v[148:149]
	v_lshl_add_u64 v[148:149], s[28:29], 0, v[148:149]
	v_cvt_pk_bf16_f32 v139, v139, v145
	global_store_dwordx4 v[150:151], v[186:189], off nt
	s_cbranch_execnz .LBB0_1959

.LBB0_1959:
	global_store_dwordx4 v[148:149], v[136:139], off nt
	ds_read2_b32 v[136:137], v157 offset0:24 offset1:57
	ds_read2_b32 v[152:153], v157 offset0:90 offset1:123
	ds_read2_b32 v[138:139], v157 offset0:156 offset1:189
	ds_read2_b32 v[150:151], v157 offset0:222 offset1:255
	s_and_b64 vcc, exec, s[2:3]
	v_add_u32_e32 v2, s87, v156
	s_waitcnt lgkmcnt(3)
	v_cvt_pk_bf16_f32 v132, v136, v137
	s_waitcnt lgkmcnt(2)
	v_cvt_pk_bf16_f32 v133, v152, v153
	s_waitcnt lgkmcnt(1)
	v_cvt_pk_bf16_f32 v134, v138, v139
	s_waitcnt lgkmcnt(0)
	v_cvt_pk_bf16_f32 v135, v150, v151
	s_cbranch_vccnz .LBB0_2042
	v_lshlrev_b32_e32 v145, 2, v2
	v_and_b32_e32 v145, 0xffffffc0, v145
	v_ashrrev_i32_e32 v147, 5, v146
	v_add_u32_e32 v148, v145, v147
	v_ashrrev_i32_e32 v149, 31, v148
	v_lshlrev_b32_e32 v145, 1, v146
	v_lshlrev_b64 v[148:149], 6, v[148:149]
	v_and_b32_e32 v145, 48, v145
	v_and_b32_e32 v147, 15, v2
	v_or3_b32 v148, v148, v145, v147
	v_ashrrev_i32_e32 v147, 31, v146
	v_lshl_add_u64 v[146:147], v[146:147], 2, s[30:31]
	global_load_dwordx4 v[178:181], v[146:147], off offset:16
	global_load_dwordx4 v[182:185], v[146:147], off
	s_waitcnt vmcnt(1)
	v_mul_f32_e32 v188, v138, v178
	s_waitcnt vmcnt(0)
	v_mul_f32_e32 v145, v136, v182
	v_mul_f32_e32 v146, v137, v183
	v_cvt_pk_bf16_f32 v186, v145, v146
	v_mul_f32_e32 v189, v139, v179
	v_lshlrev_b32_e32 v145, 16, v186
	v_fma_f32 v136, v136, v182, -v145
	v_and_b32_e32 v145, 0xffff0000, v186
	v_fma_f32 v137, v137, v183, -v145
	v_mul_f32_e32 v147, v152, v184
	v_mul_f32_e32 v177, v153, v185
	v_mul_f32_e32 v190, v150, v180
	v_mul_f32_e32 v191, v151, v181
	v_cvt_pk_bf16_f32 v187, v147, v177
	v_cvt_pk_bf16_f32 v188, v188, v189
	v_cvt_pk_bf16_f32 v189, v190, v191
	v_cvt_pk_bf16_f32 v136, v136, v137
	v_lshlrev_b64 v[146:147], 4, v[148:149]
	v_lshlrev_b32_e32 v137, 16, v187
	v_and_b32_e32 v145, 0xffff0000, v187
	v_fma_f32 v137, v152, v184, -v137
	v_fma_f32 v145, v153, v185, -v145
	v_cvt_pk_bf16_f32 v137, v137, v145
	v_lshlrev_b32_e32 v145, 16, v188
	v_fma_f32 v138, v138, v178, -v145
	v_and_b32_e32 v145, 0xffff0000, v188
	v_fma_f32 v139, v139, v179, -v145
	v_cvt_pk_bf16_f32 v138, v138, v139
	v_lshlrev_b32_e32 v139, 16, v189
	v_fma_f32 v139, v150, v180, -v139
	v_and_b32_e32 v145, 0xffff0000, v189
	v_lshl_add_u64 v[148:149], s[26:27], 0, v[146:147]
	v_lshl_add_u64 v[146:147], s[28:29], 0, v[146:147]
	v_fma_f32 v145, v151, v181, -v145
	v_cvt_pk_bf16_f32 v139, v139, v145
	global_store_dwordx4 v[148:149], v[186:189], off nt
	s_cbranch_execnz .LBB0_1962

.LBB0_1962:
	global_store_dwordx4 v[146:147], v[136:139], off nt
	s_add_i32 s2, s4, s73
	s_waitcnt lgkmcnt(0)
	s_add_i32 s2, s2, s72
	s_cmp_lt_i32 s2, s50
	s_cselect_b32 s25, s2, -1
	s_cmp_lt_i32 s25, 0
	s_cbranch_scc1 .LBB0_2006
	s_mul_hi_u32 s2, s25, 0x9824d8ed
	s_lshr_b32 s2, s2, 15
	s_mul_i32 s3, s2, 0xd760
	s_sub_i32 s85, s25, s3
	s_cmpk_gt_u32 s85, 0xc2ff
	s_mov_b64 s[48:49], -1
	s_cbranch_scc0 .LBB0_1992
	s_add_i32 s48, s2, 1
	s_add_i32 s3, s85, 0xffff3d00
	s_cmpk_lt_u32 s3, 0x1400
	s_cselect_b32 s3, s3, s85
	s_cmpk_gt_u32 s3, 0xbff
	s_mov_b64 s[52:53], -1
	s_cbranch_scc0 .LBB0_1989
	s_cmpk_gt_u32 s3, 0x13ff
	s_cbranch_scc0 .LBB0_1986
	s_cmpk_gt_u32 s3, 0x93ff
	s_cbranch_scc0 .LBB0_1983
	s_cmpk_gt_u32 s3, 0xd3ff
	s_cbranch_scc0 .LBB0_1980
	s_cmpk_gt_u32 s3, 0xd5ff
	s_cbranch_scc0 .LBB0_1977
	s_cmpk_gt_u32 s3, 0xd6ff
	s_cbranch_scc0 .LBB0_1974
	s_cmpk_gt_u32 s3, 0xd71f
	s_mov_b64 s[44:45], -1
	s_cbranch_scc0 .LBB0_1972
	s_mov_b32 s49, s47
	v_readlane_b32 s56, v243, 40
	s_lshl_b64 s[26:27], s[48:49], 19
	v_readlane_b32 s62, v243, 46
	v_readlane_b32 s63, v243, 47
	s_add_u32 s42, s62, s26
	s_addc_u32 s43, s63, s27
	s_lshl_b64 s[28:29], s[48:49], 18
	v_readlane_b32 s24, v242, 33
	s_add_u32 s26, s24, s28
	v_readlane_b32 s24, v242, 52
	s_addc_u32 s27, s24, s29
	v_readlane_b32 s24, v242, 53
	s_add_u32 s28, s24, s28
	v_readlane_b32 s24, v242, 35
	v_readlane_b32 s58, v243, 42
	s_addc_u32 s29, s24, s29
	s_lshl_b32 s24, s48, 13
	v_readlane_b32 s59, v243, 43
	s_add_u32 s30, s58, s24
	s_addc_u32 s31, s59, 0
	s_lshl_b32 s44, s3, 5
	s_and_b32 s24, s44, 0x7fffffc0
	v_readlane_b32 s57, v243, 41
	v_readlane_b32 s60, v243, 44
	v_readlane_b32 s61, v243, 45
	v_readlane_b32 s64, v243, 48
	v_readlane_b32 s65, v243, 49
	v_readlane_b32 s66, v243, 50
	v_readlane_b32 s67, v243, 51
	v_readlane_b32 s68, v243, 52
	v_readlane_b32 s69, v243, 53
	v_readlane_b32 s70, v243, 54
	v_readlane_b32 s71, v243, 55
	s_add_i32 s24, s24, 0xffe51c00
	s_and_b32 s87, s44, 32
	s_mov_b64 s[44:45], 0

.LBB0_2006:
	s_cmp_lt_i32 s35, 0
	s_mov_b64 s[2:3], -1
	s_cbranch_scc1 .LBB0_1835
	ds_write2_b32 v162, v100, v101 offset1:1
	ds_write2_b32 v162, v102, v103 offset0:2 offset1:3
	ds_write2_b32 v163, v104, v105 offset1:1
	ds_write2_b32 v164, v106, v107 offset1:1
	ds_write2_b32 v165, v108, v109 offset1:1
	ds_write2_b32 v166, v110, v111 offset1:1
	ds_write2_b32 v167, v112, v113 offset1:1
	ds_write2_b32 v168, v114, v115 offset1:1
	ds_write2_b32 v169, v116, v117 offset1:1
	ds_write2_b32 v170, v118, v119 offset1:1
	ds_write2_b32 v171, v120, v121 offset1:1
	ds_write2_b32 v172, v122, v123 offset1:1
	ds_write2_b32 v173, v124, v125 offset1:1
	ds_write2_b32 v174, v126, v127 offset1:1
	ds_write2_b32 v175, v128, v129 offset1:1
	ds_write2_b32 v176, v130, v131 offset1:1
	s_waitcnt lgkmcnt(0)
	ds_read2_b32 v[136:137], v157 offset1:33
	ds_read2_b32 v[152:153], v157 offset0:66 offset1:99
	ds_read2_b32 v[138:139], v157 offset0:132 offset1:165
	ds_read2_b32 v[150:151], v157 offset0:198 offset1:231
	s_cmp_lg_u64 s[38:39], 0
	s_cselect_b64 s[42:43], -1, 0
	s_and_b64 vcc, exec, s[42:43]
	v_add_u32_e32 v2, s0, v143
	v_add_u32_e32 v146, s34, v142
	s_waitcnt lgkmcnt(3)
	v_cvt_pk_bf16_f32 v132, v136, v137
	s_waitcnt lgkmcnt(2)
	v_cvt_pk_bf16_f32 v133, v152, v153
	s_waitcnt lgkmcnt(1)
	v_cvt_pk_bf16_f32 v134, v138, v139
	s_waitcnt lgkmcnt(0)
	v_cvt_pk_bf16_f32 v135, v150, v151
	s_cbranch_vccz .LBB0_2043
	v_lshlrev_b32_e32 v145, 2, v2
	v_and_b32_e32 v145, 0xffffffc0, v145
	v_ashrrev_i32_e32 v147, 5, v146
	v_add_u32_e32 v148, v145, v147
	v_ashrrev_i32_e32 v149, 31, v148
	v_lshlrev_b32_e32 v145, 1, v146
	v_lshlrev_b64 v[148:149], 6, v[148:149]
	v_and_b32_e32 v145, 48, v145
	v_and_b32_e32 v147, 15, v2
	v_or3_b32 v148, v148, v145, v147
	v_ashrrev_i32_e32 v147, 31, v146
	v_lshl_add_u64 v[168:169], v[146:147], 2, s[40:41]
	global_load_dwordx4 v[164:167], v[168:169], off offset:16
	s_nop 0
	global_load_dwordx4 v[168:171], v[168:169], off
	v_lshlrev_b64 v[148:149], 4, v[148:149]
	s_waitcnt vmcnt(1)
	v_mul_f32_e32 v174, v138, v164
	s_waitcnt vmcnt(0)
	v_mul_f32_e32 v145, v136, v168
	v_mul_f32_e32 v147, v137, v169
	v_cvt_pk_bf16_f32 v172, v145, v147
	v_mul_f32_e32 v173, v153, v171
	v_lshlrev_b32_e32 v145, 16, v172
	v_fma_f32 v136, v136, v168, -v145
	v_and_b32_e32 v145, 0xffff0000, v172
	v_mul_f32_e32 v175, v139, v165
	v_fma_f32 v137, v137, v169, -v145
	v_mul_f32_e32 v163, v152, v170
	v_mul_f32_e32 v176, v150, v166
	v_mul_f32_e32 v177, v151, v167
	v_cvt_pk_bf16_f32 v173, v163, v173
	v_cvt_pk_bf16_f32 v174, v174, v175
	v_cvt_pk_bf16_f32 v175, v176, v177
	v_cvt_pk_bf16_f32 v136, v136, v137
	s_nop 0
	v_lshlrev_b32_e32 v137, 16, v173
	v_and_b32_e32 v145, 0xffff0000, v173
	v_fma_f32 v137, v152, v170, -v137
	v_fma_f32 v145, v153, v171, -v145
	v_cvt_pk_bf16_f32 v137, v137, v145
	v_lshlrev_b32_e32 v145, 16, v174
	v_fma_f32 v138, v138, v164, -v145
	v_and_b32_e32 v145, 0xffff0000, v174
	v_fma_f32 v139, v139, v165, -v145
	v_cvt_pk_bf16_f32 v138, v138, v139
	v_lshlrev_b32_e32 v139, 16, v175
	v_and_b32_e32 v145, 0xffff0000, v175
	v_fma_f32 v139, v150, v166, -v139
	v_fma_f32 v145, v151, v167, -v145
	v_lshl_add_u64 v[150:151], s[36:37], 0, v[148:149]
	v_cvt_pk_bf16_f32 v139, v139, v145
	global_store_dwordx4 v[150:151], v[172:175], off nt
	v_lshl_add_u64 v[148:149], s[38:39], 0, v[148:149]
	s_cbranch_execnz .LBB0_2010

.LBB0_2010:
	global_store_dwordx4 v[148:149], v[136:139], off nt
	ds_read2_b32 v[136:137], v157 offset0:8 offset1:41
	ds_read2_b32 v[152:153], v157 offset0:74 offset1:107
	ds_read2_b32 v[138:139], v157 offset0:140 offset1:173
	ds_read2_b32 v[150:151], v157 offset0:206 offset1:239
	v_cndmask_b32_e64 v2, 0, 1, s[42:43]
	v_cmp_ne_u32_e64 s[2:3], 1, v2
	s_andn2_b64 vcc, exec, s[42:43]
	v_add_u32_e32 v2, s0, v154
	s_waitcnt lgkmcnt(3)
	v_cvt_pk_bf16_f32 v132, v136, v137
	s_waitcnt lgkmcnt(2)
	v_cvt_pk_bf16_f32 v133, v152, v153
	s_waitcnt lgkmcnt(1)
	v_cvt_pk_bf16_f32 v134, v138, v139
	s_waitcnt lgkmcnt(0)
	v_cvt_pk_bf16_f32 v135, v150, v151
	s_cbranch_vccnz .LBB0_2044
	v_lshlrev_b32_e32 v145, 2, v2
	v_and_b32_e32 v145, 0xffffffc0, v145
	v_ashrrev_i32_e32 v147, 5, v146
	v_add_u32_e32 v148, v145, v147
	v_ashrrev_i32_e32 v149, 31, v148
	v_lshlrev_b32_e32 v145, 1, v146
	v_lshlrev_b64 v[148:149], 6, v[148:149]
	v_and_b32_e32 v145, 48, v145
	v_and_b32_e32 v147, 15, v2
	v_or3_b32 v148, v148, v145, v147
	v_ashrrev_i32_e32 v147, 31, v146
	v_lshl_add_u64 v[168:169], v[146:147], 2, s[40:41]
	global_load_dwordx4 v[164:167], v[168:169], off offset:16
	s_nop 0
	global_load_dwordx4 v[168:171], v[168:169], off
	v_lshlrev_b64 v[148:149], 4, v[148:149]
	s_waitcnt vmcnt(1)
	v_mul_f32_e32 v174, v138, v164
	s_waitcnt vmcnt(0)
	v_mul_f32_e32 v145, v136, v168
	v_mul_f32_e32 v147, v137, v169
	v_cvt_pk_bf16_f32 v172, v145, v147
	v_mul_f32_e32 v173, v153, v171
	v_lshlrev_b32_e32 v145, 16, v172
	v_fma_f32 v136, v136, v168, -v145
	v_and_b32_e32 v145, 0xffff0000, v172
	v_mul_f32_e32 v175, v139, v165
	v_fma_f32 v137, v137, v169, -v145
	v_mul_f32_e32 v163, v152, v170
	v_mul_f32_e32 v176, v150, v166
	v_mul_f32_e32 v177, v151, v167
	v_cvt_pk_bf16_f32 v173, v163, v173
	v_cvt_pk_bf16_f32 v174, v174, v175
	v_cvt_pk_bf16_f32 v175, v176, v177
	v_cvt_pk_bf16_f32 v136, v136, v137
	s_nop 0
	v_lshlrev_b32_e32 v137, 16, v173
	v_and_b32_e32 v145, 0xffff0000, v173
	v_fma_f32 v137, v152, v170, -v137
	v_fma_f32 v145, v153, v171, -v145
	v_cvt_pk_bf16_f32 v137, v137, v145
	v_lshlrev_b32_e32 v145, 16, v174
	v_fma_f32 v138, v138, v164, -v145
	v_and_b32_e32 v145, 0xffff0000, v174
	v_fma_f32 v139, v139, v165, -v145
	v_cvt_pk_bf16_f32 v138, v138, v139
	v_lshlrev_b32_e32 v139, 16, v175
	v_and_b32_e32 v145, 0xffff0000, v175
	v_fma_f32 v139, v150, v166, -v139
	v_fma_f32 v145, v151, v167, -v145
	v_lshl_add_u64 v[150:151], s[36:37], 0, v[148:149]
	v_lshl_add_u64 v[148:149], s[38:39], 0, v[148:149]
	v_cvt_pk_bf16_f32 v139, v139, v145
	global_store_dwordx4 v[150:151], v[172:175], off nt
	s_cbranch_execnz .LBB0_2013

.LBB0_2013:
	global_store_dwordx4 v[148:149], v[136:139], off nt
	ds_read2_b32 v[136:137], v157 offset0:16 offset1:49
	ds_read2_b32 v[152:153], v157 offset0:82 offset1:115
	ds_read2_b32 v[138:139], v157 offset0:148 offset1:181
	ds_read2_b32 v[150:151], v157 offset0:214 offset1:247
	s_and_b64 vcc, exec, s[2:3]
	v_add_u32_e32 v2, s0, v155
	s_waitcnt lgkmcnt(3)
	v_cvt_pk_bf16_f32 v132, v136, v137
	s_waitcnt lgkmcnt(2)
	v_cvt_pk_bf16_f32 v133, v152, v153
	s_waitcnt lgkmcnt(1)
	v_cvt_pk_bf16_f32 v134, v138, v139
	s_waitcnt lgkmcnt(0)
	v_cvt_pk_bf16_f32 v135, v150, v151
	s_cbranch_vccnz .LBB0_2045
	v_lshlrev_b32_e32 v145, 2, v2
	v_and_b32_e32 v145, 0xffffffc0, v145
	v_ashrrev_i32_e32 v147, 5, v146
	v_add_u32_e32 v148, v145, v147
	v_ashrrev_i32_e32 v149, 31, v148
	v_lshlrev_b32_e32 v145, 1, v146
	v_lshlrev_b64 v[148:149], 6, v[148:149]
	v_and_b32_e32 v145, 48, v145
	v_and_b32_e32 v147, 15, v2
	v_or3_b32 v148, v148, v145, v147
	v_ashrrev_i32_e32 v147, 31, v146
	v_lshl_add_u64 v[168:169], v[146:147], 2, s[40:41]
	global_load_dwordx4 v[164:167], v[168:169], off offset:16
	s_nop 0
	global_load_dwordx4 v[168:171], v[168:169], off
	v_lshlrev_b64 v[148:149], 4, v[148:149]
	s_waitcnt vmcnt(1)
	v_mul_f32_e32 v174, v138, v164
	s_waitcnt vmcnt(0)
	v_mul_f32_e32 v145, v136, v168
	v_mul_f32_e32 v147, v137, v169
	v_cvt_pk_bf16_f32 v172, v145, v147
	v_mul_f32_e32 v173, v153, v171
	v_lshlrev_b32_e32 v145, 16, v172
	v_fma_f32 v136, v136, v168, -v145
	v_and_b32_e32 v145, 0xffff0000, v172
	v_mul_f32_e32 v175, v139, v165
	v_fma_f32 v137, v137, v169, -v145
	v_mul_f32_e32 v163, v152, v170
	v_mul_f32_e32 v176, v150, v166
	v_mul_f32_e32 v177, v151, v167
	v_cvt_pk_bf16_f32 v173, v163, v173
	v_cvt_pk_bf16_f32 v174, v174, v175
	v_cvt_pk_bf16_f32 v175, v176, v177
	v_cvt_pk_bf16_f32 v136, v136, v137
	s_nop 0
	v_lshlrev_b32_e32 v137, 16, v173
	v_and_b32_e32 v145, 0xffff0000, v173
	v_fma_f32 v137, v152, v170, -v137
	v_fma_f32 v145, v153, v171, -v145
	v_cvt_pk_bf16_f32 v137, v137, v145
	v_lshlrev_b32_e32 v145, 16, v174
	v_fma_f32 v138, v138, v164, -v145
	v_and_b32_e32 v145, 0xffff0000, v174
	v_fma_f32 v139, v139, v165, -v145
	v_cvt_pk_bf16_f32 v138, v138, v139
	v_lshlrev_b32_e32 v139, 16, v175
	v_and_b32_e32 v145, 0xffff0000, v175
	v_fma_f32 v139, v150, v166, -v139
	v_fma_f32 v145, v151, v167, -v145
	v_lshl_add_u64 v[150:151], s[36:37], 0, v[148:149]
	v_lshl_add_u64 v[148:149], s[38:39], 0, v[148:149]
	v_cvt_pk_bf16_f32 v139, v139, v145
	global_store_dwordx4 v[150:151], v[172:175], off nt
	s_cbranch_execnz .LBB0_2016

.LBB0_2016:
	global_store_dwordx4 v[148:149], v[136:139], off nt
	ds_read2_b32 v[136:137], v157 offset0:24 offset1:57
	ds_read2_b32 v[152:153], v157 offset0:90 offset1:123
	ds_read2_b32 v[138:139], v157 offset0:156 offset1:189
	ds_read2_b32 v[150:151], v157 offset0:222 offset1:255
	s_and_b64 vcc, exec, s[2:3]
	v_add_u32_e32 v2, s0, v156
	s_waitcnt lgkmcnt(3)
	v_cvt_pk_bf16_f32 v132, v136, v137
	s_waitcnt lgkmcnt(2)
	v_cvt_pk_bf16_f32 v133, v152, v153
	s_waitcnt lgkmcnt(1)
	v_cvt_pk_bf16_f32 v134, v138, v139
	s_waitcnt lgkmcnt(0)
	v_cvt_pk_bf16_f32 v135, v150, v151
	s_cbranch_vccnz .LBB0_2046
	v_lshlrev_b32_e32 v145, 2, v2
	v_and_b32_e32 v145, 0xffffffc0, v145
	v_ashrrev_i32_e32 v147, 5, v146
	v_add_u32_e32 v148, v145, v147
	v_ashrrev_i32_e32 v149, 31, v148
	v_lshlrev_b32_e32 v145, 1, v146
	v_lshlrev_b64 v[148:149], 6, v[148:149]
	v_and_b32_e32 v145, 48, v145
	v_and_b32_e32 v147, 15, v2
	v_or3_b32 v148, v148, v145, v147
	v_ashrrev_i32_e32 v147, 31, v146
	v_lshl_add_u64 v[146:147], v[146:147], 2, s[40:41]
	global_load_dwordx4 v[164:167], v[146:147], off offset:16
	global_load_dwordx4 v[168:171], v[146:147], off
	s_waitcnt vmcnt(1)
	v_mul_f32_e32 v174, v138, v164
	s_waitcnt vmcnt(0)
	v_mul_f32_e32 v145, v136, v168
	v_mul_f32_e32 v146, v137, v169
	v_cvt_pk_bf16_f32 v172, v145, v146
	v_mul_f32_e32 v175, v139, v165
	v_lshlrev_b32_e32 v145, 16, v172
	v_fma_f32 v136, v136, v168, -v145
	v_and_b32_e32 v145, 0xffff0000, v172
	v_fma_f32 v137, v137, v169, -v145
	v_mul_f32_e32 v147, v152, v170
	v_mul_f32_e32 v163, v153, v171
	v_mul_f32_e32 v176, v150, v166
	v_mul_f32_e32 v177, v151, v167
	v_cvt_pk_bf16_f32 v173, v147, v163
	v_cvt_pk_bf16_f32 v174, v174, v175
	v_cvt_pk_bf16_f32 v175, v176, v177
	v_cvt_pk_bf16_f32 v136, v136, v137
	v_lshlrev_b64 v[146:147], 4, v[148:149]
	v_lshlrev_b32_e32 v137, 16, v173
	v_and_b32_e32 v145, 0xffff0000, v173
	v_fma_f32 v137, v152, v170, -v137
	v_fma_f32 v145, v153, v171, -v145
	v_cvt_pk_bf16_f32 v137, v137, v145
	v_lshlrev_b32_e32 v145, 16, v174
	v_fma_f32 v138, v138, v164, -v145
	v_and_b32_e32 v145, 0xffff0000, v174
	v_fma_f32 v139, v139, v165, -v145
	v_cvt_pk_bf16_f32 v138, v138, v139
	v_lshlrev_b32_e32 v139, 16, v175
	v_fma_f32 v139, v150, v166, -v139
	v_and_b32_e32 v145, 0xffff0000, v175
	v_lshl_add_u64 v[148:149], s[36:37], 0, v[146:147]
	v_lshl_add_u64 v[146:147], s[38:39], 0, v[146:147]
	v_fma_f32 v145, v151, v167, -v145
	v_cvt_pk_bf16_f32 v139, v139, v145
	global_store_dwordx4 v[148:149], v[172:175], off nt
	s_cbranch_execnz .LBB0_2019

.LBB0_2019:
	v_readlane_b32 s2, v242, 48
	global_store_dwordx4 v[146:147], v[136:139], off nt
	s_add_i32 s2, s2, s73
	s_waitcnt lgkmcnt(0)
	s_add_i32 s2, s2, s72
	s_cmp_lt_i32 s2, s50
	s_cselect_b32 s35, s2, -1
	s_cmp_lt_i32 s35, 0
	s_cbranch_scc1 .LBB0_1834
	s_mul_hi_u32 s2, s35, 0x9824d8ed
	s_lshr_b32 s2, s2, 15
	s_mul_i32 s3, s2, 0xd760
	s_sub_i32 s72, s35, s3
	s_cmpk_gt_u32 s72, 0xc2ff
	s_mov_b64 s[48:49], -1
	s_cbranch_scc0 .LBB0_2073
	s_add_i32 s48, s2, 1
	s_add_i32 s3, s72, 0xffff3d00
	s_cmpk_lt_u32 s3, 0x1400
	s_cselect_b32 s3, s3, s72
	s_cmpk_gt_u32 s3, 0xbff
	s_mov_b64 s[52:53], -1
	s_cbranch_scc0 .LBB0_2070
	s_cmpk_gt_u32 s3, 0x13ff
	s_cbranch_scc0 .LBB0_2067
	s_cmpk_gt_u32 s3, 0x93ff
	s_cbranch_scc0 .LBB0_2064
	s_cmpk_gt_u32 s3, 0xd3ff
	s_cbranch_scc0 .LBB0_2061
	s_cmpk_gt_u32 s3, 0xd5ff
	s_cbranch_scc0 .LBB0_2058
	s_cmpk_gt_u32 s3, 0xd6ff
	s_cbranch_scc0 .LBB0_2055
	s_cmpk_gt_u32 s3, 0xd71f
	s_mov_b64 s[44:45], -1
	s_cbranch_scc0 .LBB0_2029
	s_mov_b32 s49, s47
	v_readlane_b32 s56, v243, 40
	s_lshl_b64 s[36:37], s[48:49], 19
	v_readlane_b32 s62, v243, 46
	v_readlane_b32 s63, v243, 47
	s_add_u32 s42, s62, s36
	s_addc_u32 s43, s63, s37
	s_lshl_b64 s[38:39], s[48:49], 18
	v_readlane_b32 s0, v242, 33
	s_add_u32 s36, s0, s38
	v_readlane_b32 s0, v242, 52
	s_addc_u32 s37, s0, s39
	v_readlane_b32 s0, v242, 53
	s_add_u32 s38, s0, s38
	v_readlane_b32 s0, v242, 35
	v_readlane_b32 s58, v243, 42
	s_addc_u32 s39, s0, s39
	s_lshl_b32 s34, s48, 13
	v_readlane_b32 s59, v243, 43
	s_add_u32 s40, s58, s34
	s_addc_u32 s41, s59, 0
	s_lshl_b32 s44, s3, 5
	s_and_b32 s34, s44, 0x7fffffc0
	v_readlane_b32 s57, v243, 41
	v_readlane_b32 s60, v243, 44
	v_readlane_b32 s61, v243, 45
	v_readlane_b32 s64, v243, 48
	v_readlane_b32 s65, v243, 49
	v_readlane_b32 s66, v243, 50
	v_readlane_b32 s67, v243, 51
	v_readlane_b32 s68, v243, 52
	v_readlane_b32 s69, v243, 53
	v_readlane_b32 s70, v243, 54
	v_readlane_b32 s71, v243, 55
	s_add_i32 s34, s34, 0xffe51c00
	s_and_b32 s0, s44, 32
	s_mov_b64 s[44:45], 0

.LBB0_2399:
	v_add_u32_e32 v163, 0x420, v162
	v_add_u32_e32 v164, 0x428, v162
	v_add_u32_e32 v165, 0x840, v162
	v_add_u32_e32 v166, 0x848, v162
	v_add_u32_e32 v167, 0xc60, v162
	v_add_u32_e32 v168, 0xc68, v162
	v_add_u32_e32 v169, 0x1080, v162
	v_add_u32_e32 v170, 0x1088, v162
	v_add_u32_e32 v171, 0x14a0, v162
	v_add_u32_e32 v172, 0x14a8, v162
	v_add_u32_e32 v173, 0x18c0, v162
	v_add_u32_e32 v174, 0x18c8, v162
	v_add_u32_e32 v175, 0x1ce0, v162
	v_add_u32_e32 v176, 0x1ce8, v162
	s_waitcnt vmcnt(7)
	ds_write2_b32 v162, v8, v9 offset1:1
	ds_write2_b32 v162, v10, v11 offset0:2 offset1:3
	s_waitcnt vmcnt(6)
	ds_write2_b32 v163, v4, v5 offset1:1
	ds_write2_b32 v164, v6, v7 offset1:1
	s_waitcnt vmcnt(5)
	ds_write2_b32 v165, v16, v17 offset1:1
	ds_write2_b32 v166, v18, v19 offset1:1
	s_waitcnt vmcnt(4)
	ds_write2_b32 v167, v12, v13 offset1:1
	ds_write2_b32 v168, v14, v15 offset1:1
	s_waitcnt vmcnt(3)
	ds_write2_b32 v169, v24, v25 offset1:1
	ds_write2_b32 v170, v26, v27 offset1:1
	s_waitcnt vmcnt(2)
	ds_write2_b32 v171, v20, v21 offset1:1
	ds_write2_b32 v172, v22, v23 offset1:1
	s_waitcnt vmcnt(1)
	ds_write2_b32 v173, v32, v33 offset1:1
	ds_write2_b32 v174, v34, v35 offset1:1
	s_waitcnt vmcnt(0)
	ds_write2_b32 v175, v28, v29 offset1:1
	ds_write2_b32 v176, v30, v31 offset1:1
	s_waitcnt lgkmcnt(0)
	ds_read2_b32 v[136:137], v157 offset1:33
	ds_read2_b32 v[150:151], v157 offset0:66 offset1:99
	ds_read2_b32 v[138:139], v157 offset0:132 offset1:165
	ds_read2_b32 v[148:149], v157 offset0:198 offset1:231
	s_cmp_lg_u64 s[10:11], 0
	s_cselect_b64 s[40:41], -1, 0
	s_and_b64 vcc, exec, s[40:41]
	v_add_u32_e32 v2, s4, v143
	v_add_u32_e32 v146, s6, v142
	s_waitcnt lgkmcnt(3)
	v_cvt_pk_bf16_f32 v132, v136, v137
	s_waitcnt lgkmcnt(2)
	v_cvt_pk_bf16_f32 v133, v150, v151
	s_waitcnt lgkmcnt(1)
	v_cvt_pk_bf16_f32 v134, v138, v139
	s_waitcnt lgkmcnt(0)
	v_cvt_pk_bf16_f32 v135, v148, v149
	s_cbranch_vccz .LBB0_2448
	v_lshlrev_b32_e32 v144, 2, v2
	v_and_b32_e32 v144, 0xffffffc0, v144
	v_ashrrev_i32_e32 v145, 5, v146
	v_add_u32_e32 v144, v145, v144
	v_ashrrev_i32_e32 v145, 31, v144
	v_lshlrev_b32_e32 v147, 1, v146
	v_lshlrev_b64 v[144:145], 6, v[144:145]
	v_and_b32_e32 v147, 48, v147
	v_and_b32_e32 v152, 15, v2
	v_or3_b32 v144, v144, v147, v152
	v_ashrrev_i32_e32 v147, 31, v146
	v_lshl_add_u64 v[152:153], v[146:147], 2, s[12:13]
	global_load_dwordx4 v[178:181], v[152:153], off offset:16
	global_load_dwordx4 v[182:185], v[152:153], off
	v_lshlrev_b64 v[144:145], 4, v[144:145]
	s_waitcnt vmcnt(1)
	v_mul_f32_e32 v188, v138, v178
	s_waitcnt vmcnt(0)
	v_mul_f32_e32 v147, v136, v182
	v_mul_f32_e32 v152, v137, v183
	v_cvt_pk_bf16_f32 v186, v147, v152
	v_mul_f32_e32 v189, v139, v179
	v_lshlrev_b32_e32 v147, 16, v186
	v_fma_f32 v136, v136, v182, -v147
	v_and_b32_e32 v147, 0xffff0000, v186
	v_fma_f32 v137, v137, v183, -v147
	v_mul_f32_e32 v153, v150, v184
	v_mul_f32_e32 v177, v151, v185
	v_mul_f32_e32 v190, v148, v180
	v_mul_f32_e32 v191, v149, v181
	v_cvt_pk_bf16_f32 v187, v153, v177
	v_cvt_pk_bf16_f32 v188, v188, v189
	v_cvt_pk_bf16_f32 v189, v190, v191
	v_cvt_pk_bf16_f32 v136, v136, v137
	s_nop 0
	v_lshlrev_b32_e32 v137, 16, v187
	v_and_b32_e32 v147, 0xffff0000, v187
	v_fma_f32 v137, v150, v184, -v137
	v_fma_f32 v147, v151, v185, -v147
	v_cvt_pk_bf16_f32 v137, v137, v147
	v_lshlrev_b32_e32 v147, 16, v188
	v_fma_f32 v138, v138, v178, -v147
	v_and_b32_e32 v147, 0xffff0000, v188
	v_fma_f32 v139, v139, v179, -v147
	v_cvt_pk_bf16_f32 v138, v138, v139
	v_lshlrev_b32_e32 v139, 16, v189
	v_and_b32_e32 v147, 0xffff0000, v189
	v_fma_f32 v139, v148, v180, -v139
	v_fma_f32 v147, v149, v181, -v147
	v_lshl_add_u64 v[148:149], s[8:9], 0, v[144:145]
	v_cvt_pk_bf16_f32 v139, v139, v147
	global_store_dwordx4 v[148:149], v[186:189], off nt
	v_lshl_add_u64 v[148:149], s[10:11], 0, v[144:145]
	v_lshlrev_b32_e32 v144, 1, v142
	s_cbranch_execnz .LBB0_2402

.LBB0_2402:
	global_store_dwordx4 v[148:149], v[136:139], off nt
	ds_read2_b32 v[136:137], v157 offset0:8 offset1:41
	ds_read2_b32 v[152:153], v157 offset0:74 offset1:107
	ds_read2_b32 v[138:139], v157 offset0:140 offset1:173
	ds_read2_b32 v[150:151], v157 offset0:206 offset1:239
	v_cndmask_b32_e64 v2, 0, 1, s[40:41]
	v_cmp_ne_u32_e64 s[2:3], 1, v2
	s_andn2_b64 vcc, exec, s[40:41]
	v_add_u32_e32 v2, s4, v154
	s_waitcnt lgkmcnt(3)
	v_cvt_pk_bf16_f32 v132, v136, v137
	s_waitcnt lgkmcnt(2)
	v_cvt_pk_bf16_f32 v133, v152, v153
	s_waitcnt lgkmcnt(1)
	v_cvt_pk_bf16_f32 v134, v138, v139
	s_waitcnt lgkmcnt(0)
	v_cvt_pk_bf16_f32 v135, v150, v151
	s_cbranch_vccnz .LBB0_2449
	v_lshlrev_b32_e32 v145, 2, v2
	v_and_b32_e32 v145, 0xffffffc0, v145
	v_ashrrev_i32_e32 v147, 5, v146
	v_add_u32_e32 v148, v147, v145
	v_ashrrev_i32_e32 v149, 31, v148
	v_lshlrev_b32_e32 v145, 1, v146
	v_lshlrev_b64 v[148:149], 6, v[148:149]
	v_and_b32_e32 v145, 48, v145
	v_and_b32_e32 v147, 15, v2
	v_or3_b32 v148, v148, v145, v147
	v_ashrrev_i32_e32 v147, 31, v146
	v_lshl_add_u64 v[182:183], v[146:147], 2, s[12:13]
	global_load_dwordx4 v[178:181], v[182:183], off offset:16
	s_nop 0
	global_load_dwordx4 v[182:185], v[182:183], off
	v_lshlrev_b64 v[148:149], 4, v[148:149]
	s_waitcnt vmcnt(1)
	v_mul_f32_e32 v188, v138, v178
	s_waitcnt vmcnt(0)
	v_mul_f32_e32 v145, v136, v182
	v_mul_f32_e32 v147, v137, v183
	v_cvt_pk_bf16_f32 v186, v145, v147
	v_mul_f32_e32 v187, v153, v185
	v_lshlrev_b32_e32 v145, 16, v186
	v_fma_f32 v136, v136, v182, -v145
	v_and_b32_e32 v145, 0xffff0000, v186
	v_mul_f32_e32 v189, v139, v179
	v_fma_f32 v137, v137, v183, -v145
	v_mul_f32_e32 v177, v152, v184
	v_mul_f32_e32 v190, v150, v180
	v_mul_f32_e32 v191, v151, v181
	v_cvt_pk_bf16_f32 v187, v177, v187
	v_cvt_pk_bf16_f32 v188, v188, v189
	v_cvt_pk_bf16_f32 v189, v190, v191
	v_cvt_pk_bf16_f32 v136, v136, v137
	s_nop 0
	v_lshlrev_b32_e32 v137, 16, v187
	v_and_b32_e32 v145, 0xffff0000, v187
	v_fma_f32 v137, v152, v184, -v137
	v_fma_f32 v145, v153, v185, -v145
	v_cvt_pk_bf16_f32 v137, v137, v145
	v_lshlrev_b32_e32 v145, 16, v188
	v_fma_f32 v138, v138, v178, -v145
	v_and_b32_e32 v145, 0xffff0000, v188
	v_fma_f32 v139, v139, v179, -v145
	v_cvt_pk_bf16_f32 v138, v138, v139
	v_lshlrev_b32_e32 v139, 16, v189
	v_and_b32_e32 v145, 0xffff0000, v189
	v_fma_f32 v139, v150, v180, -v139
	v_fma_f32 v145, v151, v181, -v145
	v_lshl_add_u64 v[150:151], s[8:9], 0, v[148:149]
	v_lshl_add_u64 v[148:149], s[10:11], 0, v[148:149]
	v_cvt_pk_bf16_f32 v139, v139, v145
	global_store_dwordx4 v[150:151], v[186:189], off nt
	s_cbranch_execnz .LBB0_2405

.LBB0_2405:
	global_store_dwordx4 v[148:149], v[136:139], off nt
	ds_read2_b32 v[136:137], v157 offset0:16 offset1:49
	ds_read2_b32 v[152:153], v157 offset0:82 offset1:115
	ds_read2_b32 v[138:139], v157 offset0:148 offset1:181
	ds_read2_b32 v[150:151], v157 offset0:214 offset1:247
	s_and_b64 vcc, exec, s[2:3]
	v_add_u32_e32 v2, s4, v155
	s_waitcnt lgkmcnt(3)
	v_cvt_pk_bf16_f32 v132, v136, v137
	s_waitcnt lgkmcnt(2)
	v_cvt_pk_bf16_f32 v133, v152, v153
	s_waitcnt lgkmcnt(1)
	v_cvt_pk_bf16_f32 v134, v138, v139
	s_waitcnt lgkmcnt(0)
	v_cvt_pk_bf16_f32 v135, v150, v151
	s_cbranch_vccnz .LBB0_2450
	v_lshlrev_b32_e32 v145, 2, v2
	v_and_b32_e32 v145, 0xffffffc0, v145
	v_ashrrev_i32_e32 v147, 5, v146
	v_add_u32_e32 v148, v147, v145
	v_ashrrev_i32_e32 v149, 31, v148
	v_lshlrev_b32_e32 v145, 1, v146
	v_lshlrev_b64 v[148:149], 6, v[148:149]
	v_and_b32_e32 v145, 48, v145
	v_and_b32_e32 v147, 15, v2
	v_or3_b32 v148, v148, v145, v147
	v_ashrrev_i32_e32 v147, 31, v146
	v_lshl_add_u64 v[182:183], v[146:147], 2, s[12:13]
	global_load_dwordx4 v[178:181], v[182:183], off offset:16
	s_nop 0
	global_load_dwordx4 v[182:185], v[182:183], off
	v_lshlrev_b64 v[148:149], 4, v[148:149]
	s_waitcnt vmcnt(1)
	v_mul_f32_e32 v188, v138, v178
	s_waitcnt vmcnt(0)
	v_mul_f32_e32 v145, v136, v182
	v_mul_f32_e32 v147, v137, v183
	v_cvt_pk_bf16_f32 v186, v145, v147
	v_mul_f32_e32 v187, v153, v185
	v_lshlrev_b32_e32 v145, 16, v186
	v_fma_f32 v136, v136, v182, -v145
	v_and_b32_e32 v145, 0xffff0000, v186
	v_mul_f32_e32 v189, v139, v179
	v_fma_f32 v137, v137, v183, -v145
	v_mul_f32_e32 v177, v152, v184
	v_mul_f32_e32 v190, v150, v180
	v_mul_f32_e32 v191, v151, v181
	v_cvt_pk_bf16_f32 v187, v177, v187
	v_cvt_pk_bf16_f32 v188, v188, v189
	v_cvt_pk_bf16_f32 v189, v190, v191
	v_cvt_pk_bf16_f32 v136, v136, v137
	s_nop 0
	v_lshlrev_b32_e32 v137, 16, v187
	v_and_b32_e32 v145, 0xffff0000, v187
	v_fma_f32 v137, v152, v184, -v137
	v_fma_f32 v145, v153, v185, -v145
	v_cvt_pk_bf16_f32 v137, v137, v145
	v_lshlrev_b32_e32 v145, 16, v188
	v_fma_f32 v138, v138, v178, -v145
	v_and_b32_e32 v145, 0xffff0000, v188
	v_fma_f32 v139, v139, v179, -v145
	v_cvt_pk_bf16_f32 v138, v138, v139
	v_lshlrev_b32_e32 v139, 16, v189
	v_and_b32_e32 v145, 0xffff0000, v189
	v_fma_f32 v139, v150, v180, -v139
	v_fma_f32 v145, v151, v181, -v145
	v_lshl_add_u64 v[150:151], s[8:9], 0, v[148:149]
	v_lshl_add_u64 v[148:149], s[10:11], 0, v[148:149]
	v_cvt_pk_bf16_f32 v139, v139, v145
	global_store_dwordx4 v[150:151], v[186:189], off nt
	s_cbranch_execnz .LBB0_2408

.LBB0_2408:
	global_store_dwordx4 v[148:149], v[136:139], off nt
	ds_read2_b32 v[136:137], v157 offset0:24 offset1:57
	ds_read2_b32 v[152:153], v157 offset0:90 offset1:123
	ds_read2_b32 v[138:139], v157 offset0:156 offset1:189
	ds_read2_b32 v[150:151], v157 offset0:222 offset1:255
	s_and_b64 vcc, exec, s[2:3]
	v_add_u32_e32 v2, s4, v156
	s_waitcnt lgkmcnt(3)
	v_cvt_pk_bf16_f32 v132, v136, v137
	s_waitcnt lgkmcnt(2)
	v_cvt_pk_bf16_f32 v133, v152, v153
	s_waitcnt lgkmcnt(1)
	v_cvt_pk_bf16_f32 v134, v138, v139
	s_waitcnt lgkmcnt(0)
	v_cvt_pk_bf16_f32 v135, v150, v151
	s_cbranch_vccnz .LBB0_2451
	v_lshlrev_b32_e32 v145, 2, v2
	v_and_b32_e32 v145, 0xffffffc0, v145
	v_ashrrev_i32_e32 v147, 5, v146
	v_add_u32_e32 v148, v147, v145
	v_ashrrev_i32_e32 v149, 31, v148
	v_lshlrev_b32_e32 v145, 1, v146
	v_lshlrev_b64 v[148:149], 6, v[148:149]
	v_and_b32_e32 v145, 48, v145
	v_and_b32_e32 v147, 15, v2
	v_or3_b32 v148, v148, v145, v147
	v_ashrrev_i32_e32 v147, 31, v146
	v_lshl_add_u64 v[146:147], v[146:147], 2, s[12:13]
	global_load_dwordx4 v[178:181], v[146:147], off offset:16
	global_load_dwordx4 v[182:185], v[146:147], off
	s_waitcnt vmcnt(1)
	v_mul_f32_e32 v188, v138, v178
	s_waitcnt vmcnt(0)
	v_mul_f32_e32 v145, v136, v182
	v_mul_f32_e32 v146, v137, v183
	v_cvt_pk_bf16_f32 v186, v145, v146
	v_mul_f32_e32 v189, v139, v179
	v_lshlrev_b32_e32 v145, 16, v186
	v_fma_f32 v136, v136, v182, -v145
	v_and_b32_e32 v145, 0xffff0000, v186
	v_fma_f32 v137, v137, v183, -v145
	v_mul_f32_e32 v147, v152, v184
	v_mul_f32_e32 v177, v153, v185
	v_mul_f32_e32 v190, v150, v180
	v_mul_f32_e32 v191, v151, v181
	v_cvt_pk_bf16_f32 v187, v147, v177
	v_cvt_pk_bf16_f32 v188, v188, v189
	v_cvt_pk_bf16_f32 v189, v190, v191
	v_cvt_pk_bf16_f32 v136, v136, v137
	v_lshlrev_b64 v[146:147], 4, v[148:149]
	v_lshlrev_b32_e32 v137, 16, v187
	v_and_b32_e32 v145, 0xffff0000, v187
	v_fma_f32 v137, v152, v184, -v137
	v_fma_f32 v145, v153, v185, -v145
	v_cvt_pk_bf16_f32 v137, v137, v145
	v_lshlrev_b32_e32 v145, 16, v188
	v_fma_f32 v138, v138, v178, -v145
	v_and_b32_e32 v145, 0xffff0000, v188
	v_fma_f32 v139, v139, v179, -v145
	v_cvt_pk_bf16_f32 v138, v138, v139
	v_lshlrev_b32_e32 v139, 16, v189
	v_fma_f32 v139, v150, v180, -v139
	v_and_b32_e32 v145, 0xffff0000, v189
	v_lshl_add_u64 v[148:149], s[8:9], 0, v[146:147]
	v_lshl_add_u64 v[146:147], s[10:11], 0, v[146:147]
	v_fma_f32 v145, v151, v181, -v145
	v_cvt_pk_bf16_f32 v139, v139, v145
	global_store_dwordx4 v[148:149], v[186:189], off nt
	s_cbranch_execnz .LBB0_2411

.LBB0_2411:
	s_lshr_b32 s2, s93, 3
	s_mul_i32 s2, s2, s89
	s_add_i32 s2, s2, s86
	s_and_b32 s73, s93, 4
	global_store_dwordx4 v[146:147], v[136:139], off nt
	s_lshl_b32 s72, s2, 6
	s_add_i32 s2, s92, s73
	s_waitcnt lgkmcnt(0)
	s_add_i32 s2, s2, s72
	s_cmp_lt_i32 s2, s50
	s_cselect_b32 s7, s2, -1
	s_cmp_lt_i32 s7, 0
	s_cbranch_scc1 .LBB0_2461
	s_mul_hi_u32 s2, s7, 0x9824d8ed
	s_lshr_b32 s2, s2, 15
	s_mul_i32 s3, s2, 0xd760
	s_sub_i32 s85, s7, s3
	s_cmpk_gt_u32 s85, 0xc2ff
	s_mov_b64 s[44:45], -1
	s_cbranch_scc0 .LBB0_2441
	s_add_i32 s44, s2, 1
	s_add_i32 s3, s85, 0xffff3d00
	s_cmpk_lt_u32 s3, 0x1400
	s_cselect_b32 s3, s3, s85
	s_cmpk_gt_u32 s3, 0xbff
	s_mov_b64 s[48:49], -1
	s_cbranch_scc0 .LBB0_2438
	s_cmpk_gt_u32 s3, 0x13ff
	s_cbranch_scc0 .LBB0_2435
	s_cmpk_gt_u32 s3, 0x93ff
	s_cbranch_scc0 .LBB0_2432
	s_cmpk_gt_u32 s3, 0xd3ff
	s_cbranch_scc0 .LBB0_2429
	s_cmpk_gt_u32 s3, 0xd5ff
	s_cbranch_scc0 .LBB0_2426
	s_cmpk_gt_u32 s3, 0xd6ff
	s_cbranch_scc0 .LBB0_2423
	s_cmpk_gt_u32 s3, 0xd71f
	s_mov_b64 s[42:43], -1
	s_cbranch_scc0 .LBB0_2421
	s_mov_b32 s45, s47
	v_readlane_b32 s48, v243, 40
	s_lshl_b64 s[8:9], s[44:45], 19
	v_readlane_b32 s54, v243, 46
	v_readlane_b32 s55, v243, 47
	s_add_u32 s40, s54, s8
	s_addc_u32 s41, s55, s9
	s_lshl_b64 s[10:11], s[44:45], 18
	v_readlane_b32 s4, v242, 42
	s_add_u32 s8, s4, s10
	v_readlane_b32 s4, v242, 43
	s_addc_u32 s9, s4, s11
	v_readlane_b32 s4, v242, 44
	s_add_u32 s10, s4, s10
	v_readlane_b32 s4, v242, 45
	v_readlane_b32 s50, v243, 42
	s_addc_u32 s11, s4, s11
	s_lshl_b32 s6, s44, 13
	v_readlane_b32 s51, v243, 43
	s_add_u32 s12, s50, s6
	s_addc_u32 s13, s51, 0
	s_lshl_b32 s42, s3, 5
	s_and_b32 s6, s42, 0x7fffffc0
	v_readlane_b32 s49, v243, 41
	v_readlane_b32 s52, v243, 44
	v_readlane_b32 s53, v243, 45
	v_readlane_b32 s56, v243, 48
	v_readlane_b32 s57, v243, 49
	v_readlane_b32 s58, v243, 50
	v_readlane_b32 s59, v243, 51
	v_readlane_b32 s60, v243, 52
	v_readlane_b32 s61, v243, 53
	v_readlane_b32 s62, v243, 54
	v_readlane_b32 s63, v243, 55
	s_mov_b32 s50, s91
	v_readlane_b32 s51, v242, 29
	s_add_i32 s6, s6, 0xffe51c00
	s_and_b32 s4, s42, 32
	s_mov_b64 s[42:43], 0

.LBB0_2461:
	s_cmp_lt_i32 s15, 0
	s_mov_b64 s[2:3], -1
	s_cbranch_scc1 .LBB0_2398
	ds_write2_b32 v162, v36, v37 offset1:1
	ds_write2_b32 v162, v38, v39 offset0:2 offset1:3
	ds_write2_b32 v163, v40, v41 offset1:1
	ds_write2_b32 v164, v42, v43 offset1:1
	ds_write2_b32 v165, v44, v45 offset1:1
	ds_write2_b32 v166, v46, v47 offset1:1
	ds_write2_b32 v167, v48, v49 offset1:1
	ds_write2_b32 v168, v50, v51 offset1:1
	ds_write2_b32 v169, v52, v53 offset1:1
	ds_write2_b32 v170, v54, v55 offset1:1
	ds_write2_b32 v171, v56, v57 offset1:1
	ds_write2_b32 v172, v58, v59 offset1:1
	ds_write2_b32 v173, v60, v61 offset1:1
	ds_write2_b32 v174, v62, v63 offset1:1
	ds_write2_b32 v175, v64, v65 offset1:1
	ds_write2_b32 v176, v66, v67 offset1:1
	s_waitcnt lgkmcnt(0)
	ds_read2_b32 v[136:137], v157 offset1:33
	ds_read2_b32 v[152:153], v157 offset0:66 offset1:99
	ds_read2_b32 v[138:139], v157 offset0:132 offset1:165
	ds_read2_b32 v[150:151], v157 offset0:198 offset1:231
	s_cmp_lg_u64 s[18:19], 0
	s_cselect_b64 s[40:41], -1, 0
	s_and_b64 vcc, exec, s[40:41]
	v_add_u32_e32 v2, s0, v143
	v_add_u32_e32 v146, s14, v142
	s_waitcnt lgkmcnt(3)
	v_cvt_pk_bf16_f32 v132, v136, v137
	s_waitcnt lgkmcnt(2)
	v_cvt_pk_bf16_f32 v133, v152, v153
	s_waitcnt lgkmcnt(1)
	v_cvt_pk_bf16_f32 v134, v138, v139
	s_waitcnt lgkmcnt(0)
	v_cvt_pk_bf16_f32 v135, v150, v151
	s_cbranch_vccz .LBB0_2511
	v_lshlrev_b32_e32 v145, 2, v2
	v_and_b32_e32 v145, 0xffffffc0, v145
	v_ashrrev_i32_e32 v147, 5, v146
	v_add_u32_e32 v148, v145, v147
	v_ashrrev_i32_e32 v149, 31, v148
	v_lshlrev_b32_e32 v145, 1, v146
	v_lshlrev_b64 v[148:149], 6, v[148:149]
	v_and_b32_e32 v145, 48, v145
	v_and_b32_e32 v147, 15, v2
	v_or3_b32 v148, v148, v145, v147
	v_ashrrev_i32_e32 v147, 31, v146
	v_lshl_add_u64 v[182:183], v[146:147], 2, s[20:21]
	global_load_dwordx4 v[178:181], v[182:183], off offset:16
	s_nop 0
	global_load_dwordx4 v[182:185], v[182:183], off
	v_lshlrev_b64 v[148:149], 4, v[148:149]
	s_waitcnt vmcnt(1)
	v_mul_f32_e32 v188, v138, v178
	s_waitcnt vmcnt(0)
	v_mul_f32_e32 v145, v136, v182
	v_mul_f32_e32 v147, v137, v183
	v_cvt_pk_bf16_f32 v186, v145, v147
	v_mul_f32_e32 v187, v153, v185
	v_lshlrev_b32_e32 v145, 16, v186
	v_fma_f32 v136, v136, v182, -v145
	v_and_b32_e32 v145, 0xffff0000, v186
	v_mul_f32_e32 v189, v139, v179
	v_fma_f32 v137, v137, v183, -v145
	v_mul_f32_e32 v177, v152, v184
	v_mul_f32_e32 v190, v150, v180
	v_mul_f32_e32 v191, v151, v181
	v_cvt_pk_bf16_f32 v187, v177, v187
	v_cvt_pk_bf16_f32 v188, v188, v189
	v_cvt_pk_bf16_f32 v189, v190, v191
	v_cvt_pk_bf16_f32 v136, v136, v137
	s_nop 0
	v_lshlrev_b32_e32 v137, 16, v187
	v_and_b32_e32 v145, 0xffff0000, v187
	v_fma_f32 v137, v152, v184, -v137
	v_fma_f32 v145, v153, v185, -v145
	v_cvt_pk_bf16_f32 v137, v137, v145
	v_lshlrev_b32_e32 v145, 16, v188
	v_fma_f32 v138, v138, v178, -v145
	v_and_b32_e32 v145, 0xffff0000, v188
	v_fma_f32 v139, v139, v179, -v145
	v_cvt_pk_bf16_f32 v138, v138, v139
	v_lshlrev_b32_e32 v139, 16, v189
	v_and_b32_e32 v145, 0xffff0000, v189
	v_fma_f32 v139, v150, v180, -v139
	v_fma_f32 v145, v151, v181, -v145
	v_lshl_add_u64 v[150:151], s[16:17], 0, v[148:149]
	v_cvt_pk_bf16_f32 v139, v139, v145
	global_store_dwordx4 v[150:151], v[186:189], off nt
	v_lshl_add_u64 v[148:149], s[18:19], 0, v[148:149]
	s_cbranch_execnz .LBB0_2465

.LBB0_2465:
	global_store_dwordx4 v[148:149], v[136:139], off nt
	ds_read2_b32 v[136:137], v157 offset0:8 offset1:41
	ds_read2_b32 v[152:153], v157 offset0:74 offset1:107
	ds_read2_b32 v[138:139], v157 offset0:140 offset1:173
	ds_read2_b32 v[150:151], v157 offset0:206 offset1:239
	v_cndmask_b32_e64 v2, 0, 1, s[40:41]
	v_cmp_ne_u32_e64 s[2:3], 1, v2
	s_andn2_b64 vcc, exec, s[40:41]
	v_add_u32_e32 v2, s0, v154
	s_waitcnt lgkmcnt(3)
	v_cvt_pk_bf16_f32 v132, v136, v137
	s_waitcnt lgkmcnt(2)
	v_cvt_pk_bf16_f32 v133, v152, v153
	s_waitcnt lgkmcnt(1)
	v_cvt_pk_bf16_f32 v134, v138, v139
	s_waitcnt lgkmcnt(0)
	v_cvt_pk_bf16_f32 v135, v150, v151
	s_cbranch_vccnz .LBB0_2512
	v_lshlrev_b32_e32 v145, 2, v2
	v_and_b32_e32 v145, 0xffffffc0, v145
	v_ashrrev_i32_e32 v147, 5, v146
	v_add_u32_e32 v148, v145, v147
	v_ashrrev_i32_e32 v149, 31, v148
	v_lshlrev_b32_e32 v145, 1, v146
	v_lshlrev_b64 v[148:149], 6, v[148:149]
	v_and_b32_e32 v145, 48, v145
	v_and_b32_e32 v147, 15, v2
	v_or3_b32 v148, v148, v145, v147
	v_ashrrev_i32_e32 v147, 31, v146
	v_lshl_add_u64 v[182:183], v[146:147], 2, s[20:21]
	global_load_dwordx4 v[178:181], v[182:183], off offset:16
	s_nop 0
	global_load_dwordx4 v[182:185], v[182:183], off
	v_lshlrev_b64 v[148:149], 4, v[148:149]
	s_waitcnt vmcnt(1)
	v_mul_f32_e32 v188, v138, v178
	s_waitcnt vmcnt(0)
	v_mul_f32_e32 v145, v136, v182
	v_mul_f32_e32 v147, v137, v183
	v_cvt_pk_bf16_f32 v186, v145, v147
	v_mul_f32_e32 v187, v153, v185
	v_lshlrev_b32_e32 v145, 16, v186
	v_fma_f32 v136, v136, v182, -v145
	v_and_b32_e32 v145, 0xffff0000, v186
	v_mul_f32_e32 v189, v139, v179
	v_fma_f32 v137, v137, v183, -v145
	v_mul_f32_e32 v177, v152, v184
	v_mul_f32_e32 v190, v150, v180
	v_mul_f32_e32 v191, v151, v181
	v_cvt_pk_bf16_f32 v187, v177, v187
	v_cvt_pk_bf16_f32 v188, v188, v189
	v_cvt_pk_bf16_f32 v189, v190, v191
	v_cvt_pk_bf16_f32 v136, v136, v137
	s_nop 0
	v_lshlrev_b32_e32 v137, 16, v187
	v_and_b32_e32 v145, 0xffff0000, v187
	v_fma_f32 v137, v152, v184, -v137
	v_fma_f32 v145, v153, v185, -v145
	v_cvt_pk_bf16_f32 v137, v137, v145
	v_lshlrev_b32_e32 v145, 16, v188
	v_fma_f32 v138, v138, v178, -v145
	v_and_b32_e32 v145, 0xffff0000, v188
	v_fma_f32 v139, v139, v179, -v145
	v_cvt_pk_bf16_f32 v138, v138, v139
	v_lshlrev_b32_e32 v139, 16, v189
	v_and_b32_e32 v145, 0xffff0000, v189
	v_fma_f32 v139, v150, v180, -v139
	v_fma_f32 v145, v151, v181, -v145
	v_lshl_add_u64 v[150:151], s[16:17], 0, v[148:149]
	v_lshl_add_u64 v[148:149], s[18:19], 0, v[148:149]
	v_cvt_pk_bf16_f32 v139, v139, v145
	global_store_dwordx4 v[150:151], v[186:189], off nt
	s_cbranch_execnz .LBB0_2468

.LBB0_2468:
	global_store_dwordx4 v[148:149], v[136:139], off nt
	ds_read2_b32 v[136:137], v157 offset0:16 offset1:49
	ds_read2_b32 v[152:153], v157 offset0:82 offset1:115
	ds_read2_b32 v[138:139], v157 offset0:148 offset1:181
	ds_read2_b32 v[150:151], v157 offset0:214 offset1:247
	s_and_b64 vcc, exec, s[2:3]
	v_add_u32_e32 v2, s0, v155
	s_waitcnt lgkmcnt(3)
	v_cvt_pk_bf16_f32 v132, v136, v137
	s_waitcnt lgkmcnt(2)
	v_cvt_pk_bf16_f32 v133, v152, v153
	s_waitcnt lgkmcnt(1)
	v_cvt_pk_bf16_f32 v134, v138, v139
	s_waitcnt lgkmcnt(0)
	v_cvt_pk_bf16_f32 v135, v150, v151
	s_cbranch_vccnz .LBB0_2513
	v_lshlrev_b32_e32 v145, 2, v2
	v_and_b32_e32 v145, 0xffffffc0, v145
	v_ashrrev_i32_e32 v147, 5, v146
	v_add_u32_e32 v148, v145, v147
	v_ashrrev_i32_e32 v149, 31, v148
	v_lshlrev_b32_e32 v145, 1, v146
	v_lshlrev_b64 v[148:149], 6, v[148:149]
	v_and_b32_e32 v145, 48, v145
	v_and_b32_e32 v147, 15, v2
	v_or3_b32 v148, v148, v145, v147
	v_ashrrev_i32_e32 v147, 31, v146
	v_lshl_add_u64 v[182:183], v[146:147], 2, s[20:21]
	global_load_dwordx4 v[178:181], v[182:183], off offset:16
	s_nop 0
	global_load_dwordx4 v[182:185], v[182:183], off
	v_lshlrev_b64 v[148:149], 4, v[148:149]
	s_waitcnt vmcnt(1)
	v_mul_f32_e32 v188, v138, v178
	s_waitcnt vmcnt(0)
	v_mul_f32_e32 v145, v136, v182
	v_mul_f32_e32 v147, v137, v183
	v_cvt_pk_bf16_f32 v186, v145, v147
	v_mul_f32_e32 v187, v153, v185
	v_lshlrev_b32_e32 v145, 16, v186
	v_fma_f32 v136, v136, v182, -v145
	v_and_b32_e32 v145, 0xffff0000, v186
	v_mul_f32_e32 v189, v139, v179
	v_fma_f32 v137, v137, v183, -v145
	v_mul_f32_e32 v177, v152, v184
	v_mul_f32_e32 v190, v150, v180
	v_mul_f32_e32 v191, v151, v181
	v_cvt_pk_bf16_f32 v187, v177, v187
	v_cvt_pk_bf16_f32 v188, v188, v189
	v_cvt_pk_bf16_f32 v189, v190, v191
	v_cvt_pk_bf16_f32 v136, v136, v137
	s_nop 0
	v_lshlrev_b32_e32 v137, 16, v187
	v_and_b32_e32 v145, 0xffff0000, v187
	v_fma_f32 v137, v152, v184, -v137
	v_fma_f32 v145, v153, v185, -v145
	v_cvt_pk_bf16_f32 v137, v137, v145
	v_lshlrev_b32_e32 v145, 16, v188
	v_fma_f32 v138, v138, v178, -v145
	v_and_b32_e32 v145, 0xffff0000, v188
	v_fma_f32 v139, v139, v179, -v145
	v_cvt_pk_bf16_f32 v138, v138, v139
	v_lshlrev_b32_e32 v139, 16, v189
	v_and_b32_e32 v145, 0xffff0000, v189
	v_fma_f32 v139, v150, v180, -v139
	v_fma_f32 v145, v151, v181, -v145
	v_lshl_add_u64 v[150:151], s[16:17], 0, v[148:149]
	v_lshl_add_u64 v[148:149], s[18:19], 0, v[148:149]
	v_cvt_pk_bf16_f32 v139, v139, v145
	global_store_dwordx4 v[150:151], v[186:189], off nt
	s_cbranch_execnz .LBB0_2471

.LBB0_2471:
	global_store_dwordx4 v[148:149], v[136:139], off nt
	ds_read2_b32 v[136:137], v157 offset0:24 offset1:57
	ds_read2_b32 v[152:153], v157 offset0:90 offset1:123
	ds_read2_b32 v[138:139], v157 offset0:156 offset1:189
	ds_read2_b32 v[150:151], v157 offset0:222 offset1:255
	s_and_b64 vcc, exec, s[2:3]
	v_add_u32_e32 v2, s0, v156
	s_waitcnt lgkmcnt(3)
	v_cvt_pk_bf16_f32 v132, v136, v137
	s_waitcnt lgkmcnt(2)
	v_cvt_pk_bf16_f32 v133, v152, v153
	s_waitcnt lgkmcnt(1)
	v_cvt_pk_bf16_f32 v134, v138, v139
	s_waitcnt lgkmcnt(0)
	v_cvt_pk_bf16_f32 v135, v150, v151
	s_cbranch_vccnz .LBB0_2514
	v_lshlrev_b32_e32 v145, 2, v2
	v_and_b32_e32 v145, 0xffffffc0, v145
	v_ashrrev_i32_e32 v147, 5, v146
	v_add_u32_e32 v148, v145, v147
	v_ashrrev_i32_e32 v149, 31, v148
	v_lshlrev_b32_e32 v145, 1, v146
	v_lshlrev_b64 v[148:149], 6, v[148:149]
	v_and_b32_e32 v145, 48, v145
	v_and_b32_e32 v147, 15, v2
	v_or3_b32 v148, v148, v145, v147
	v_ashrrev_i32_e32 v147, 31, v146
	v_lshl_add_u64 v[146:147], v[146:147], 2, s[20:21]
	global_load_dwordx4 v[178:181], v[146:147], off offset:16
	global_load_dwordx4 v[182:185], v[146:147], off
	s_waitcnt vmcnt(1)
	v_mul_f32_e32 v188, v138, v178
	s_waitcnt vmcnt(0)
	v_mul_f32_e32 v145, v136, v182
	v_mul_f32_e32 v146, v137, v183
	v_cvt_pk_bf16_f32 v186, v145, v146
	v_mul_f32_e32 v189, v139, v179
	v_lshlrev_b32_e32 v145, 16, v186
	v_fma_f32 v136, v136, v182, -v145
	v_and_b32_e32 v145, 0xffff0000, v186
	v_fma_f32 v137, v137, v183, -v145
	v_mul_f32_e32 v147, v152, v184
	v_mul_f32_e32 v177, v153, v185
	v_mul_f32_e32 v190, v150, v180
	v_mul_f32_e32 v191, v151, v181
	v_cvt_pk_bf16_f32 v187, v147, v177
	v_cvt_pk_bf16_f32 v188, v188, v189
	v_cvt_pk_bf16_f32 v189, v190, v191
	v_cvt_pk_bf16_f32 v136, v136, v137
	v_lshlrev_b64 v[146:147], 4, v[148:149]
	v_lshlrev_b32_e32 v137, 16, v187
	v_and_b32_e32 v145, 0xffff0000, v187
	v_fma_f32 v137, v152, v184, -v137
	v_fma_f32 v145, v153, v185, -v145
	v_cvt_pk_bf16_f32 v137, v137, v145
	v_lshlrev_b32_e32 v145, 16, v188
	v_fma_f32 v138, v138, v178, -v145
	v_and_b32_e32 v145, 0xffff0000, v188
	v_fma_f32 v139, v139, v179, -v145
	v_cvt_pk_bf16_f32 v138, v138, v139
	v_lshlrev_b32_e32 v139, 16, v189
	v_fma_f32 v139, v150, v180, -v139
	v_and_b32_e32 v145, 0xffff0000, v189
	v_lshl_add_u64 v[148:149], s[16:17], 0, v[146:147]
	v_lshl_add_u64 v[146:147], s[18:19], 0, v[146:147]
	v_fma_f32 v145, v151, v181, -v145
	v_cvt_pk_bf16_f32 v139, v139, v145
	global_store_dwordx4 v[148:149], v[186:189], off nt
	s_cbranch_execnz .LBB0_2474

.LBB0_2474:
	global_store_dwordx4 v[146:147], v[136:139], off nt
	s_add_i32 s2, s74, s73
	s_waitcnt lgkmcnt(0)
	s_add_i32 s2, s2, s72
	s_cmp_lt_i32 s2, s50
	s_cselect_b32 s15, s2, -1
	s_cmp_lt_i32 s15, 0
	s_cbranch_scc1 .LBB0_2524
	s_mul_hi_u32 s2, s15, 0x9824d8ed
	s_lshr_b32 s2, s2, 15
	s_mul_i32 s3, s2, 0xd760
	s_sub_i32 s85, s15, s3
	s_cmpk_gt_u32 s85, 0xc2ff
	s_mov_b64 s[44:45], -1
	s_cbranch_scc0 .LBB0_2504
	s_add_i32 s44, s2, 1
	s_add_i32 s3, s85, 0xffff3d00
	s_cmpk_lt_u32 s3, 0x1400
	s_cselect_b32 s3, s3, s85
	s_cmpk_gt_u32 s3, 0xbff
	s_mov_b64 s[48:49], -1
	s_cbranch_scc0 .LBB0_2501
	s_cmpk_gt_u32 s3, 0x13ff
	s_cbranch_scc0 .LBB0_2498
	s_cmpk_gt_u32 s3, 0x93ff
	s_cbranch_scc0 .LBB0_2495
	s_cmpk_gt_u32 s3, 0xd3ff
	s_cbranch_scc0 .LBB0_2492
	s_cmpk_gt_u32 s3, 0xd5ff
	s_cbranch_scc0 .LBB0_2489
	s_cmpk_gt_u32 s3, 0xd6ff
	s_cbranch_scc0 .LBB0_2486
	s_cmpk_gt_u32 s3, 0xd71f
	s_mov_b64 s[42:43], -1
	s_cbranch_scc0 .LBB0_2484
	s_mov_b32 s45, s47
	v_readlane_b32 s48, v243, 40
	s_lshl_b64 s[16:17], s[44:45], 19
	v_readlane_b32 s54, v243, 46
	v_readlane_b32 s55, v243, 47
	s_add_u32 s40, s54, s16
	s_addc_u32 s41, s55, s17
	s_lshl_b64 s[18:19], s[44:45], 18
	v_readlane_b32 s0, v242, 42
	s_add_u32 s16, s0, s18
	v_readlane_b32 s0, v242, 43
	s_addc_u32 s17, s0, s19
	v_readlane_b32 s0, v242, 44
	s_add_u32 s18, s0, s18
	v_readlane_b32 s0, v242, 45
	v_readlane_b32 s50, v243, 42
	s_addc_u32 s19, s0, s19
	s_lshl_b32 s14, s44, 13
	v_readlane_b32 s51, v243, 43
	s_add_u32 s20, s50, s14
	s_addc_u32 s21, s51, 0
	s_lshl_b32 s42, s3, 5
	s_and_b32 s14, s42, 0x7fffffc0
	v_readlane_b32 s49, v243, 41
	v_readlane_b32 s52, v243, 44
	v_readlane_b32 s53, v243, 45
	v_readlane_b32 s56, v243, 48
	v_readlane_b32 s57, v243, 49
	v_readlane_b32 s58, v243, 50
	v_readlane_b32 s59, v243, 51
	v_readlane_b32 s60, v243, 52
	v_readlane_b32 s61, v243, 53
	v_readlane_b32 s62, v243, 54
	v_readlane_b32 s63, v243, 55
	s_mov_b32 s50, s91
	v_readlane_b32 s51, v242, 29
	s_add_i32 s14, s14, 0xffe51c00
	s_and_b32 s0, s42, 32
	s_mov_b64 s[42:43], 0

.LBB0_2524:
	s_cmp_lt_i32 s23, 0
	s_mov_b64 s[2:3], -1
	s_cbranch_scc1 .LBB0_2398
	ds_write2_b32 v162, v68, v69 offset1:1
	ds_write2_b32 v162, v70, v71 offset0:2 offset1:3
	ds_write2_b32 v163, v72, v73 offset1:1
	ds_write2_b32 v164, v74, v75 offset1:1
	ds_write2_b32 v165, v76, v77 offset1:1
	ds_write2_b32 v166, v78, v79 offset1:1
	ds_write2_b32 v167, v80, v81 offset1:1
	ds_write2_b32 v168, v82, v83 offset1:1
	ds_write2_b32 v169, v84, v85 offset1:1
	ds_write2_b32 v170, v86, v87 offset1:1
	ds_write2_b32 v171, v88, v89 offset1:1
	ds_write2_b32 v172, v90, v91 offset1:1
	ds_write2_b32 v173, v92, v93 offset1:1
	ds_write2_b32 v174, v94, v95 offset1:1
	ds_write2_b32 v175, v96, v97 offset1:1
	ds_write2_b32 v176, v98, v99 offset1:1
	s_waitcnt lgkmcnt(0)
	ds_read2_b32 v[136:137], v157 offset1:33
	ds_read2_b32 v[152:153], v157 offset0:66 offset1:99
	ds_read2_b32 v[138:139], v157 offset0:132 offset1:165
	ds_read2_b32 v[150:151], v157 offset0:198 offset1:231
	s_cmp_lg_u64 s[76:77], 0
	s_cselect_b64 s[40:41], -1, 0
	s_and_b64 vcc, exec, s[40:41]
	v_add_u32_e32 v2, s81, v143
	v_add_u32_e32 v146, s22, v142
	s_waitcnt lgkmcnt(3)
	v_cvt_pk_bf16_f32 v132, v136, v137
	s_waitcnt lgkmcnt(2)
	v_cvt_pk_bf16_f32 v133, v152, v153
	s_waitcnt lgkmcnt(1)
	v_cvt_pk_bf16_f32 v134, v138, v139
	s_waitcnt lgkmcnt(0)
	v_cvt_pk_bf16_f32 v135, v150, v151
	s_cbranch_vccz .LBB0_2574
	v_lshlrev_b32_e32 v145, 2, v2
	v_and_b32_e32 v145, 0xffffffc0, v145
	v_ashrrev_i32_e32 v147, 5, v146
	v_add_u32_e32 v148, v145, v147
	v_ashrrev_i32_e32 v149, 31, v148
	v_lshlrev_b32_e32 v145, 1, v146
	v_lshlrev_b64 v[148:149], 6, v[148:149]
	v_and_b32_e32 v145, 48, v145
	v_and_b32_e32 v147, 15, v2
	v_or3_b32 v148, v148, v145, v147
	v_ashrrev_i32_e32 v147, 31, v146
	v_lshl_add_u64 v[182:183], v[146:147], 2, s[26:27]
	global_load_dwordx4 v[178:181], v[182:183], off offset:16
	s_nop 0
	global_load_dwordx4 v[182:185], v[182:183], off
	v_lshlrev_b64 v[148:149], 4, v[148:149]
	s_waitcnt vmcnt(1)
	v_mul_f32_e32 v188, v138, v178
	s_waitcnt vmcnt(0)
	v_mul_f32_e32 v145, v136, v182
	v_mul_f32_e32 v147, v137, v183
	v_cvt_pk_bf16_f32 v186, v145, v147
	v_mul_f32_e32 v187, v153, v185
	v_lshlrev_b32_e32 v145, 16, v186
	v_fma_f32 v136, v136, v182, -v145
	v_and_b32_e32 v145, 0xffff0000, v186
	v_mul_f32_e32 v189, v139, v179
	v_fma_f32 v137, v137, v183, -v145
	v_mul_f32_e32 v177, v152, v184
	v_mul_f32_e32 v190, v150, v180
	v_mul_f32_e32 v191, v151, v181
	v_cvt_pk_bf16_f32 v187, v177, v187
	v_cvt_pk_bf16_f32 v188, v188, v189
	v_cvt_pk_bf16_f32 v189, v190, v191
	v_cvt_pk_bf16_f32 v136, v136, v137
	s_nop 0
	v_lshlrev_b32_e32 v137, 16, v187
	v_and_b32_e32 v145, 0xffff0000, v187
	v_fma_f32 v137, v152, v184, -v137
	v_fma_f32 v145, v153, v185, -v145
	v_cvt_pk_bf16_f32 v137, v137, v145
	v_lshlrev_b32_e32 v145, 16, v188
	v_fma_f32 v138, v138, v178, -v145
	v_and_b32_e32 v145, 0xffff0000, v188
	v_fma_f32 v139, v139, v179, -v145
	v_cvt_pk_bf16_f32 v138, v138, v139
	v_lshlrev_b32_e32 v139, 16, v189
	v_and_b32_e32 v145, 0xffff0000, v189
	v_fma_f32 v139, v150, v180, -v139
	v_fma_f32 v145, v151, v181, -v145
	v_lshl_add_u64 v[150:151], s[82:83], 0, v[148:149]
	v_cvt_pk_bf16_f32 v139, v139, v145
	global_store_dwordx4 v[150:151], v[186:189], off nt
	v_lshl_add_u64 v[148:149], s[76:77], 0, v[148:149]
	s_cbranch_execnz .LBB0_2528

.LBB0_2528:
	global_store_dwordx4 v[148:149], v[136:139], off nt
	ds_read2_b32 v[136:137], v157 offset0:8 offset1:41
	ds_read2_b32 v[152:153], v157 offset0:74 offset1:107
	ds_read2_b32 v[138:139], v157 offset0:140 offset1:173
	ds_read2_b32 v[150:151], v157 offset0:206 offset1:239
	v_cndmask_b32_e64 v2, 0, 1, s[40:41]
	v_cmp_ne_u32_e64 s[2:3], 1, v2
	s_andn2_b64 vcc, exec, s[40:41]
	v_add_u32_e32 v2, s81, v154
	s_waitcnt lgkmcnt(3)
	v_cvt_pk_bf16_f32 v132, v136, v137
	s_waitcnt lgkmcnt(2)
	v_cvt_pk_bf16_f32 v133, v152, v153
	s_waitcnt lgkmcnt(1)
	v_cvt_pk_bf16_f32 v134, v138, v139
	s_waitcnt lgkmcnt(0)
	v_cvt_pk_bf16_f32 v135, v150, v151
	s_cbranch_vccnz .LBB0_2575
	v_lshlrev_b32_e32 v145, 2, v2
	v_and_b32_e32 v145, 0xffffffc0, v145
	v_ashrrev_i32_e32 v147, 5, v146
	v_add_u32_e32 v148, v145, v147
	v_ashrrev_i32_e32 v149, 31, v148
	v_lshlrev_b32_e32 v145, 1, v146
	v_lshlrev_b64 v[148:149], 6, v[148:149]
	v_and_b32_e32 v145, 48, v145
	v_and_b32_e32 v147, 15, v2
	v_or3_b32 v148, v148, v145, v147
	v_ashrrev_i32_e32 v147, 31, v146
	v_lshl_add_u64 v[182:183], v[146:147], 2, s[26:27]
	global_load_dwordx4 v[178:181], v[182:183], off offset:16
	s_nop 0
	global_load_dwordx4 v[182:185], v[182:183], off
	v_lshlrev_b64 v[148:149], 4, v[148:149]
	s_waitcnt vmcnt(1)
	v_mul_f32_e32 v188, v138, v178
	s_waitcnt vmcnt(0)
	v_mul_f32_e32 v145, v136, v182
	v_mul_f32_e32 v147, v137, v183
	v_cvt_pk_bf16_f32 v186, v145, v147
	v_mul_f32_e32 v187, v153, v185
	v_lshlrev_b32_e32 v145, 16, v186
	v_fma_f32 v136, v136, v182, -v145
	v_and_b32_e32 v145, 0xffff0000, v186
	v_mul_f32_e32 v189, v139, v179
	v_fma_f32 v137, v137, v183, -v145
	v_mul_f32_e32 v177, v152, v184
	v_mul_f32_e32 v190, v150, v180
	v_mul_f32_e32 v191, v151, v181
	v_cvt_pk_bf16_f32 v187, v177, v187
	v_cvt_pk_bf16_f32 v188, v188, v189
	v_cvt_pk_bf16_f32 v189, v190, v191
	v_cvt_pk_bf16_f32 v136, v136, v137
	s_nop 0
	v_lshlrev_b32_e32 v137, 16, v187
	v_and_b32_e32 v145, 0xffff0000, v187
	v_fma_f32 v137, v152, v184, -v137
	v_fma_f32 v145, v153, v185, -v145
	v_cvt_pk_bf16_f32 v137, v137, v145
	v_lshlrev_b32_e32 v145, 16, v188
	v_fma_f32 v138, v138, v178, -v145
	v_and_b32_e32 v145, 0xffff0000, v188
	v_fma_f32 v139, v139, v179, -v145
	v_cvt_pk_bf16_f32 v138, v138, v139
	v_lshlrev_b32_e32 v139, 16, v189
	v_and_b32_e32 v145, 0xffff0000, v189
	v_fma_f32 v139, v150, v180, -v139
	v_fma_f32 v145, v151, v181, -v145
	v_lshl_add_u64 v[150:151], s[82:83], 0, v[148:149]
	v_lshl_add_u64 v[148:149], s[76:77], 0, v[148:149]
	v_cvt_pk_bf16_f32 v139, v139, v145
	global_store_dwordx4 v[150:151], v[186:189], off nt
	s_cbranch_execnz .LBB0_2531

.LBB0_2531:
	global_store_dwordx4 v[148:149], v[136:139], off nt
	ds_read2_b32 v[136:137], v157 offset0:16 offset1:49
	ds_read2_b32 v[152:153], v157 offset0:82 offset1:115
	ds_read2_b32 v[138:139], v157 offset0:148 offset1:181
	ds_read2_b32 v[150:151], v157 offset0:214 offset1:247
	s_and_b64 vcc, exec, s[2:3]
	v_add_u32_e32 v2, s81, v155
	s_waitcnt lgkmcnt(3)
	v_cvt_pk_bf16_f32 v132, v136, v137
	s_waitcnt lgkmcnt(2)
	v_cvt_pk_bf16_f32 v133, v152, v153
	s_waitcnt lgkmcnt(1)
	v_cvt_pk_bf16_f32 v134, v138, v139
	s_waitcnt lgkmcnt(0)
	v_cvt_pk_bf16_f32 v135, v150, v151
	s_cbranch_vccnz .LBB0_2576
	v_lshlrev_b32_e32 v145, 2, v2
	v_and_b32_e32 v145, 0xffffffc0, v145
	v_ashrrev_i32_e32 v147, 5, v146
	v_add_u32_e32 v148, v145, v147
	v_ashrrev_i32_e32 v149, 31, v148
	v_lshlrev_b32_e32 v145, 1, v146
	v_lshlrev_b64 v[148:149], 6, v[148:149]
	v_and_b32_e32 v145, 48, v145
	v_and_b32_e32 v147, 15, v2
	v_or3_b32 v148, v148, v145, v147
	v_ashrrev_i32_e32 v147, 31, v146
	v_lshl_add_u64 v[182:183], v[146:147], 2, s[26:27]
	global_load_dwordx4 v[178:181], v[182:183], off offset:16
	s_nop 0
	global_load_dwordx4 v[182:185], v[182:183], off
	v_lshlrev_b64 v[148:149], 4, v[148:149]
	s_waitcnt vmcnt(1)
	v_mul_f32_e32 v188, v138, v178
	s_waitcnt vmcnt(0)
	v_mul_f32_e32 v145, v136, v182
	v_mul_f32_e32 v147, v137, v183
	v_cvt_pk_bf16_f32 v186, v145, v147
	v_mul_f32_e32 v187, v153, v185
	v_lshlrev_b32_e32 v145, 16, v186
	v_fma_f32 v136, v136, v182, -v145
	v_and_b32_e32 v145, 0xffff0000, v186
	v_mul_f32_e32 v189, v139, v179
	v_fma_f32 v137, v137, v183, -v145
	v_mul_f32_e32 v177, v152, v184
	v_mul_f32_e32 v190, v150, v180
	v_mul_f32_e32 v191, v151, v181
	v_cvt_pk_bf16_f32 v187, v177, v187
	v_cvt_pk_bf16_f32 v188, v188, v189
	v_cvt_pk_bf16_f32 v189, v190, v191
	v_cvt_pk_bf16_f32 v136, v136, v137
	s_nop 0
	v_lshlrev_b32_e32 v137, 16, v187
	v_and_b32_e32 v145, 0xffff0000, v187
	v_fma_f32 v137, v152, v184, -v137
	v_fma_f32 v145, v153, v185, -v145
	v_cvt_pk_bf16_f32 v137, v137, v145
	v_lshlrev_b32_e32 v145, 16, v188
	v_fma_f32 v138, v138, v178, -v145
	v_and_b32_e32 v145, 0xffff0000, v188
	v_fma_f32 v139, v139, v179, -v145
	v_cvt_pk_bf16_f32 v138, v138, v139
	v_lshlrev_b32_e32 v139, 16, v189
	v_and_b32_e32 v145, 0xffff0000, v189
	v_fma_f32 v139, v150, v180, -v139
	v_fma_f32 v145, v151, v181, -v145
	v_lshl_add_u64 v[150:151], s[82:83], 0, v[148:149]
	v_lshl_add_u64 v[148:149], s[76:77], 0, v[148:149]
	v_cvt_pk_bf16_f32 v139, v139, v145
	global_store_dwordx4 v[150:151], v[186:189], off nt
	s_cbranch_execnz .LBB0_2534

.LBB0_2534:
	global_store_dwordx4 v[148:149], v[136:139], off nt
	ds_read2_b32 v[136:137], v157 offset0:24 offset1:57
	ds_read2_b32 v[152:153], v157 offset0:90 offset1:123
	ds_read2_b32 v[138:139], v157 offset0:156 offset1:189
	ds_read2_b32 v[150:151], v157 offset0:222 offset1:255
	s_and_b64 vcc, exec, s[2:3]
	v_add_u32_e32 v2, s81, v156
	s_waitcnt lgkmcnt(3)
	v_cvt_pk_bf16_f32 v132, v136, v137
	s_waitcnt lgkmcnt(2)
	v_cvt_pk_bf16_f32 v133, v152, v153
	s_waitcnt lgkmcnt(1)
	v_cvt_pk_bf16_f32 v134, v138, v139
	s_waitcnt lgkmcnt(0)
	v_cvt_pk_bf16_f32 v135, v150, v151
	s_cbranch_vccnz .LBB0_2577
	v_lshlrev_b32_e32 v145, 2, v2
	v_and_b32_e32 v145, 0xffffffc0, v145
	v_ashrrev_i32_e32 v147, 5, v146
	v_add_u32_e32 v148, v145, v147
	v_ashrrev_i32_e32 v149, 31, v148
	v_lshlrev_b32_e32 v145, 1, v146
	v_lshlrev_b64 v[148:149], 6, v[148:149]
	v_and_b32_e32 v145, 48, v145
	v_and_b32_e32 v147, 15, v2
	v_or3_b32 v148, v148, v145, v147
	v_ashrrev_i32_e32 v147, 31, v146
	v_lshl_add_u64 v[146:147], v[146:147], 2, s[26:27]
	global_load_dwordx4 v[178:181], v[146:147], off offset:16
	global_load_dwordx4 v[182:185], v[146:147], off
	s_waitcnt vmcnt(1)
	v_mul_f32_e32 v188, v138, v178
	s_waitcnt vmcnt(0)
	v_mul_f32_e32 v145, v136, v182
	v_mul_f32_e32 v146, v137, v183
	v_cvt_pk_bf16_f32 v186, v145, v146
	v_mul_f32_e32 v189, v139, v179
	v_lshlrev_b32_e32 v145, 16, v186
	v_fma_f32 v136, v136, v182, -v145
	v_and_b32_e32 v145, 0xffff0000, v186
	v_fma_f32 v137, v137, v183, -v145
	v_mul_f32_e32 v147, v152, v184
	v_mul_f32_e32 v177, v153, v185
	v_mul_f32_e32 v190, v150, v180
	v_mul_f32_e32 v191, v151, v181
	v_cvt_pk_bf16_f32 v187, v147, v177
	v_cvt_pk_bf16_f32 v188, v188, v189
	v_cvt_pk_bf16_f32 v189, v190, v191
	v_cvt_pk_bf16_f32 v136, v136, v137
	v_lshlrev_b64 v[146:147], 4, v[148:149]
	v_lshlrev_b32_e32 v137, 16, v187
	v_and_b32_e32 v145, 0xffff0000, v187
	v_fma_f32 v137, v152, v184, -v137
	v_fma_f32 v145, v153, v185, -v145
	v_cvt_pk_bf16_f32 v137, v137, v145
	v_lshlrev_b32_e32 v145, 16, v188
	v_fma_f32 v138, v138, v178, -v145
	v_and_b32_e32 v145, 0xffff0000, v188
	v_fma_f32 v139, v139, v179, -v145
	v_cvt_pk_bf16_f32 v138, v138, v139
	v_lshlrev_b32_e32 v139, 16, v189
	v_fma_f32 v139, v150, v180, -v139
	v_and_b32_e32 v145, 0xffff0000, v189
	v_lshl_add_u64 v[148:149], s[82:83], 0, v[146:147]
	v_lshl_add_u64 v[146:147], s[76:77], 0, v[146:147]
	v_fma_f32 v145, v151, v181, -v145
	v_cvt_pk_bf16_f32 v139, v139, v145
	global_store_dwordx4 v[148:149], v[186:189], off nt
	s_cbranch_execnz .LBB0_2537

.LBB0_2537:
	v_readlane_b32 s2, v242, 39
	global_store_dwordx4 v[146:147], v[136:139], off nt
	s_add_i32 s2, s2, s73
	s_waitcnt lgkmcnt(0)
	s_add_i32 s2, s2, s72
	s_cmp_lt_i32 s2, s50
	s_cselect_b32 s23, s2, -1
	s_cmp_lt_i32 s23, 0
	s_cbranch_scc1 .LBB0_2587
	s_mul_hi_u32 s2, s23, 0x9824d8ed
	s_lshr_b32 s2, s2, 15
	s_mul_i32 s3, s2, 0xd760
	s_sub_i32 s85, s23, s3
	s_cmpk_gt_u32 s85, 0xc2ff
	s_mov_b64 s[44:45], -1
	s_cbranch_scc0 .LBB0_2567
	s_add_i32 s44, s2, 1
	s_add_i32 s3, s85, 0xffff3d00
	s_cmpk_lt_u32 s3, 0x1400
	s_cselect_b32 s3, s3, s85
	s_cmpk_gt_u32 s3, 0xbff
	s_mov_b64 s[48:49], -1
	s_cbranch_scc0 .LBB0_2564
	s_cmpk_gt_u32 s3, 0x13ff
	s_cbranch_scc0 .LBB0_2561
	s_cmpk_gt_u32 s3, 0x93ff
	s_cbranch_scc0 .LBB0_2558
	s_cmpk_gt_u32 s3, 0xd3ff
	s_cbranch_scc0 .LBB0_2555
	s_cmpk_gt_u32 s3, 0xd5ff
	s_cbranch_scc0 .LBB0_2552
	s_cmpk_gt_u32 s3, 0xd6ff
	s_cbranch_scc0 .LBB0_2549
	s_cmpk_gt_u32 s3, 0xd71f
	s_mov_b64 s[42:43], -1
	s_cbranch_scc0 .LBB0_2547
	s_mov_b32 s45, s47
	v_readlane_b32 s48, v243, 40
	s_lshl_b64 s[24:25], s[44:45], 19
	v_readlane_b32 s54, v243, 46
	v_readlane_b32 s55, v243, 47
	s_add_u32 s40, s54, s24
	s_addc_u32 s41, s55, s25
	s_lshl_b64 s[26:27], s[44:45], 18
	v_readlane_b32 s22, v242, 42
	s_add_u32 s82, s22, s26
	v_readlane_b32 s22, v242, 43
	s_addc_u32 s83, s22, s27
	v_readlane_b32 s22, v242, 44
	s_add_u32 s76, s22, s26
	v_readlane_b32 s22, v242, 45
	v_readlane_b32 s50, v243, 42
	s_addc_u32 s77, s22, s27
	s_lshl_b32 s22, s44, 13
	v_readlane_b32 s51, v243, 43
	s_add_u32 s26, s50, s22
	s_addc_u32 s27, s51, 0
	s_lshl_b32 s42, s3, 5
	s_and_b32 s22, s42, 0x7fffffc0
	v_readlane_b32 s49, v243, 41
	v_readlane_b32 s52, v243, 44
	v_readlane_b32 s53, v243, 45
	v_readlane_b32 s56, v243, 48
	v_readlane_b32 s57, v243, 49
	v_readlane_b32 s58, v243, 50
	v_readlane_b32 s59, v243, 51
	v_readlane_b32 s60, v243, 52
	v_readlane_b32 s61, v243, 53
	v_readlane_b32 s62, v243, 54
	v_readlane_b32 s63, v243, 55
	s_mov_b32 s50, s91
	v_readlane_b32 s51, v242, 29
	s_add_i32 s22, s22, 0xffe51c00
	s_and_b32 s81, s42, 32
	s_mov_b64 s[42:43], 0

.LBB0_2587:
	s_cmp_lt_i32 s80, 0
	s_mov_b64 s[2:3], -1
	s_cbranch_scc1 .LBB0_2398
	ds_write2_b32 v162, v100, v101 offset1:1
	ds_write2_b32 v162, v102, v103 offset0:2 offset1:3
	ds_write2_b32 v163, v104, v105 offset1:1
	ds_write2_b32 v164, v106, v107 offset1:1
	ds_write2_b32 v165, v108, v109 offset1:1
	ds_write2_b32 v166, v110, v111 offset1:1
	ds_write2_b32 v167, v112, v113 offset1:1
	ds_write2_b32 v168, v114, v115 offset1:1
	ds_write2_b32 v169, v116, v117 offset1:1
	ds_write2_b32 v170, v118, v119 offset1:1
	ds_write2_b32 v171, v120, v121 offset1:1
	ds_write2_b32 v172, v122, v123 offset1:1
	ds_write2_b32 v173, v124, v125 offset1:1
	ds_write2_b32 v174, v126, v127 offset1:1
	ds_write2_b32 v175, v128, v129 offset1:1
	ds_write2_b32 v176, v130, v131 offset1:1
	s_waitcnt lgkmcnt(0)
	ds_read2_b32 v[136:137], v157 offset1:33
	ds_read2_b32 v[152:153], v157 offset0:66 offset1:99
	ds_read2_b32 v[138:139], v157 offset0:132 offset1:165
	ds_read2_b32 v[150:151], v157 offset0:198 offset1:231
	s_cmp_lg_u64 s[36:37], 0
	s_cselect_b64 s[40:41], -1, 0
	s_and_b64 vcc, exec, s[40:41]
	v_add_u32_e32 v2, s75, v143
	v_add_u32_e32 v146, s30, v142
	s_waitcnt lgkmcnt(3)
	v_cvt_pk_bf16_f32 v132, v136, v137
	s_waitcnt lgkmcnt(2)
	v_cvt_pk_bf16_f32 v133, v152, v153
	s_waitcnt lgkmcnt(1)
	v_cvt_pk_bf16_f32 v134, v138, v139
	s_waitcnt lgkmcnt(0)
	v_cvt_pk_bf16_f32 v135, v150, v151
	s_cbranch_vccz .LBB0_2612
	v_lshlrev_b32_e32 v145, 2, v2
	v_and_b32_e32 v145, 0xffffffc0, v145
	v_ashrrev_i32_e32 v147, 5, v146
	v_add_u32_e32 v148, v145, v147
	v_ashrrev_i32_e32 v149, 31, v148
	v_lshlrev_b32_e32 v145, 1, v146
	v_lshlrev_b64 v[148:149], 6, v[148:149]
	v_and_b32_e32 v145, 48, v145
	v_and_b32_e32 v147, 15, v2
	v_or3_b32 v148, v148, v145, v147
	v_ashrrev_i32_e32 v147, 31, v146
	v_lshl_add_u64 v[168:169], v[146:147], 2, s[38:39]
	global_load_dwordx4 v[164:167], v[168:169], off offset:16
	s_nop 0
	global_load_dwordx4 v[168:171], v[168:169], off
	v_lshlrev_b64 v[148:149], 4, v[148:149]
	s_waitcnt vmcnt(1)
	v_mul_f32_e32 v174, v138, v164
	s_waitcnt vmcnt(0)
	v_mul_f32_e32 v145, v136, v168
	v_mul_f32_e32 v147, v137, v169
	v_cvt_pk_bf16_f32 v172, v145, v147
	v_mul_f32_e32 v173, v153, v171
	v_lshlrev_b32_e32 v145, 16, v172
	v_fma_f32 v136, v136, v168, -v145
	v_and_b32_e32 v145, 0xffff0000, v172
	v_mul_f32_e32 v175, v139, v165
	v_fma_f32 v137, v137, v169, -v145
	v_mul_f32_e32 v163, v152, v170
	v_mul_f32_e32 v176, v150, v166
	v_mul_f32_e32 v177, v151, v167
	v_cvt_pk_bf16_f32 v173, v163, v173
	v_cvt_pk_bf16_f32 v174, v174, v175
	v_cvt_pk_bf16_f32 v175, v176, v177
	v_cvt_pk_bf16_f32 v136, v136, v137
	s_nop 0
	v_lshlrev_b32_e32 v137, 16, v173
	v_and_b32_e32 v145, 0xffff0000, v173
	v_fma_f32 v137, v152, v170, -v137
	v_fma_f32 v145, v153, v171, -v145
	v_cvt_pk_bf16_f32 v137, v137, v145
	v_lshlrev_b32_e32 v145, 16, v174
	v_fma_f32 v138, v138, v164, -v145
	v_and_b32_e32 v145, 0xffff0000, v174
	v_fma_f32 v139, v139, v165, -v145
	v_cvt_pk_bf16_f32 v138, v138, v139
	v_lshlrev_b32_e32 v139, 16, v175
	v_and_b32_e32 v145, 0xffff0000, v175
	v_fma_f32 v139, v150, v166, -v139
	v_fma_f32 v145, v151, v167, -v145
	v_lshl_add_u64 v[150:151], s[34:35], 0, v[148:149]
	v_cvt_pk_bf16_f32 v139, v139, v145
	global_store_dwordx4 v[150:151], v[172:175], off nt
	v_lshl_add_u64 v[148:149], s[36:37], 0, v[148:149]
	s_cbranch_execnz .LBB0_2591

.LBB0_2591:
	global_store_dwordx4 v[148:149], v[136:139], off nt
	ds_read2_b32 v[136:137], v157 offset0:8 offset1:41
	ds_read2_b32 v[152:153], v157 offset0:74 offset1:107
	ds_read2_b32 v[138:139], v157 offset0:140 offset1:173
	ds_read2_b32 v[150:151], v157 offset0:206 offset1:239
	v_cndmask_b32_e64 v2, 0, 1, s[40:41]
	v_cmp_ne_u32_e64 s[2:3], 1, v2
	s_andn2_b64 vcc, exec, s[40:41]
	v_add_u32_e32 v2, s75, v154
	s_waitcnt lgkmcnt(3)
	v_cvt_pk_bf16_f32 v132, v136, v137
	s_waitcnt lgkmcnt(2)
	v_cvt_pk_bf16_f32 v133, v152, v153
	s_waitcnt lgkmcnt(1)
	v_cvt_pk_bf16_f32 v134, v138, v139
	s_waitcnt lgkmcnt(0)
	v_cvt_pk_bf16_f32 v135, v150, v151
	s_cbranch_vccnz .LBB0_2613
	v_lshlrev_b32_e32 v145, 2, v2
	v_and_b32_e32 v145, 0xffffffc0, v145
	v_ashrrev_i32_e32 v147, 5, v146
	v_add_u32_e32 v148, v145, v147
	v_ashrrev_i32_e32 v149, 31, v148
	v_lshlrev_b32_e32 v145, 1, v146
	v_lshlrev_b64 v[148:149], 6, v[148:149]
	v_and_b32_e32 v145, 48, v145
	v_and_b32_e32 v147, 15, v2
	v_or3_b32 v148, v148, v145, v147
	v_ashrrev_i32_e32 v147, 31, v146
	v_lshl_add_u64 v[168:169], v[146:147], 2, s[38:39]
	global_load_dwordx4 v[164:167], v[168:169], off offset:16
	s_nop 0
	global_load_dwordx4 v[168:171], v[168:169], off
	v_lshlrev_b64 v[148:149], 4, v[148:149]
	s_waitcnt vmcnt(1)
	v_mul_f32_e32 v174, v138, v164
	s_waitcnt vmcnt(0)
	v_mul_f32_e32 v145, v136, v168
	v_mul_f32_e32 v147, v137, v169
	v_cvt_pk_bf16_f32 v172, v145, v147
	v_mul_f32_e32 v173, v153, v171
	v_lshlrev_b32_e32 v145, 16, v172
	v_fma_f32 v136, v136, v168, -v145
	v_and_b32_e32 v145, 0xffff0000, v172
	v_mul_f32_e32 v175, v139, v165
	v_fma_f32 v137, v137, v169, -v145
	v_mul_f32_e32 v163, v152, v170
	v_mul_f32_e32 v176, v150, v166
	v_mul_f32_e32 v177, v151, v167
	v_cvt_pk_bf16_f32 v173, v163, v173
	v_cvt_pk_bf16_f32 v174, v174, v175
	v_cvt_pk_bf16_f32 v175, v176, v177
	v_cvt_pk_bf16_f32 v136, v136, v137
	s_nop 0
	v_lshlrev_b32_e32 v137, 16, v173
	v_and_b32_e32 v145, 0xffff0000, v173
	v_fma_f32 v137, v152, v170, -v137
	v_fma_f32 v145, v153, v171, -v145
	v_cvt_pk_bf16_f32 v137, v137, v145
	v_lshlrev_b32_e32 v145, 16, v174
	v_fma_f32 v138, v138, v164, -v145
	v_and_b32_e32 v145, 0xffff0000, v174
	v_fma_f32 v139, v139, v165, -v145
	v_cvt_pk_bf16_f32 v138, v138, v139
	v_lshlrev_b32_e32 v139, 16, v175
	v_and_b32_e32 v145, 0xffff0000, v175
	v_fma_f32 v139, v150, v166, -v139
	v_fma_f32 v145, v151, v167, -v145
	v_lshl_add_u64 v[150:151], s[34:35], 0, v[148:149]
	v_lshl_add_u64 v[148:149], s[36:37], 0, v[148:149]
	v_cvt_pk_bf16_f32 v139, v139, v145
	global_store_dwordx4 v[150:151], v[172:175], off nt
	s_cbranch_execnz .LBB0_2594

.LBB0_2594:
	global_store_dwordx4 v[148:149], v[136:139], off nt
	ds_read2_b32 v[136:137], v157 offset0:16 offset1:49
	ds_read2_b32 v[152:153], v157 offset0:82 offset1:115
	ds_read2_b32 v[138:139], v157 offset0:148 offset1:181
	ds_read2_b32 v[150:151], v157 offset0:214 offset1:247
	s_and_b64 vcc, exec, s[2:3]
	v_add_u32_e32 v2, s75, v155
	s_waitcnt lgkmcnt(3)
	v_cvt_pk_bf16_f32 v132, v136, v137
	s_waitcnt lgkmcnt(2)
	v_cvt_pk_bf16_f32 v133, v152, v153
	s_waitcnt lgkmcnt(1)
	v_cvt_pk_bf16_f32 v134, v138, v139
	s_waitcnt lgkmcnt(0)
	v_cvt_pk_bf16_f32 v135, v150, v151
	s_cbranch_vccnz .LBB0_2614
	v_lshlrev_b32_e32 v145, 2, v2
	v_and_b32_e32 v145, 0xffffffc0, v145
	v_ashrrev_i32_e32 v147, 5, v146
	v_add_u32_e32 v148, v145, v147
	v_ashrrev_i32_e32 v149, 31, v148
	v_lshlrev_b32_e32 v145, 1, v146
	v_lshlrev_b64 v[148:149], 6, v[148:149]
	v_and_b32_e32 v145, 48, v145
	v_and_b32_e32 v147, 15, v2
	v_or3_b32 v148, v148, v145, v147
	v_ashrrev_i32_e32 v147, 31, v146
	v_lshl_add_u64 v[168:169], v[146:147], 2, s[38:39]
	global_load_dwordx4 v[164:167], v[168:169], off offset:16
	s_nop 0
	global_load_dwordx4 v[168:171], v[168:169], off
	v_lshlrev_b64 v[148:149], 4, v[148:149]
	s_waitcnt vmcnt(1)
	v_mul_f32_e32 v174, v138, v164
	s_waitcnt vmcnt(0)
	v_mul_f32_e32 v145, v136, v168
	v_mul_f32_e32 v147, v137, v169
	v_cvt_pk_bf16_f32 v172, v145, v147
	v_mul_f32_e32 v173, v153, v171
	v_lshlrev_b32_e32 v145, 16, v172
	v_fma_f32 v136, v136, v168, -v145
	v_and_b32_e32 v145, 0xffff0000, v172
	v_mul_f32_e32 v175, v139, v165
	v_fma_f32 v137, v137, v169, -v145
	v_mul_f32_e32 v163, v152, v170
	v_mul_f32_e32 v176, v150, v166
	v_mul_f32_e32 v177, v151, v167
	v_cvt_pk_bf16_f32 v173, v163, v173
	v_cvt_pk_bf16_f32 v174, v174, v175
	v_cvt_pk_bf16_f32 v175, v176, v177
	v_cvt_pk_bf16_f32 v136, v136, v137
	s_nop 0
	v_lshlrev_b32_e32 v137, 16, v173
	v_and_b32_e32 v145, 0xffff0000, v173
	v_fma_f32 v137, v152, v170, -v137
	v_fma_f32 v145, v153, v171, -v145
	v_cvt_pk_bf16_f32 v137, v137, v145
	v_lshlrev_b32_e32 v145, 16, v174
	v_fma_f32 v138, v138, v164, -v145
	v_and_b32_e32 v145, 0xffff0000, v174
	v_fma_f32 v139, v139, v165, -v145
	v_cvt_pk_bf16_f32 v138, v138, v139
	v_lshlrev_b32_e32 v139, 16, v175
	v_and_b32_e32 v145, 0xffff0000, v175
	v_fma_f32 v139, v150, v166, -v139
	v_fma_f32 v145, v151, v167, -v145
	v_lshl_add_u64 v[150:151], s[34:35], 0, v[148:149]
	v_lshl_add_u64 v[148:149], s[36:37], 0, v[148:149]
	v_cvt_pk_bf16_f32 v139, v139, v145
	global_store_dwordx4 v[150:151], v[172:175], off nt
	s_cbranch_execnz .LBB0_2597

.LBB0_2597:
	global_store_dwordx4 v[148:149], v[136:139], off nt
	ds_read2_b32 v[136:137], v157 offset0:24 offset1:57
	ds_read2_b32 v[152:153], v157 offset0:90 offset1:123
	ds_read2_b32 v[138:139], v157 offset0:156 offset1:189
	ds_read2_b32 v[150:151], v157 offset0:222 offset1:255
	s_and_b64 vcc, exec, s[2:3]
	v_add_u32_e32 v2, s75, v156
	s_waitcnt lgkmcnt(3)
	v_cvt_pk_bf16_f32 v132, v136, v137
	s_waitcnt lgkmcnt(2)
	v_cvt_pk_bf16_f32 v133, v152, v153
	s_waitcnt lgkmcnt(1)
	v_cvt_pk_bf16_f32 v134, v138, v139
	s_waitcnt lgkmcnt(0)
	v_cvt_pk_bf16_f32 v135, v150, v151
	s_cbranch_vccnz .LBB0_2615
	v_lshlrev_b32_e32 v145, 2, v2
	v_and_b32_e32 v145, 0xffffffc0, v145
	v_ashrrev_i32_e32 v147, 5, v146
	v_add_u32_e32 v148, v145, v147
	v_ashrrev_i32_e32 v149, 31, v148
	v_lshlrev_b32_e32 v145, 1, v146
	v_lshlrev_b64 v[148:149], 6, v[148:149]
	v_and_b32_e32 v145, 48, v145
	v_and_b32_e32 v147, 15, v2
	v_or3_b32 v148, v148, v145, v147
	v_ashrrev_i32_e32 v147, 31, v146
	v_lshl_add_u64 v[146:147], v[146:147], 2, s[38:39]
	global_load_dwordx4 v[164:167], v[146:147], off offset:16
	global_load_dwordx4 v[168:171], v[146:147], off
	s_waitcnt vmcnt(1)
	v_mul_f32_e32 v174, v138, v164
	s_waitcnt vmcnt(0)
	v_mul_f32_e32 v145, v136, v168
	v_mul_f32_e32 v146, v137, v169
	v_cvt_pk_bf16_f32 v172, v145, v146
	v_mul_f32_e32 v175, v139, v165
	v_lshlrev_b32_e32 v145, 16, v172
	v_fma_f32 v136, v136, v168, -v145
	v_and_b32_e32 v145, 0xffff0000, v172
	v_fma_f32 v137, v137, v169, -v145
	v_mul_f32_e32 v147, v152, v170
	v_mul_f32_e32 v163, v153, v171
	v_mul_f32_e32 v176, v150, v166
	v_mul_f32_e32 v177, v151, v167
	v_cvt_pk_bf16_f32 v173, v147, v163
	v_cvt_pk_bf16_f32 v174, v174, v175
	v_cvt_pk_bf16_f32 v175, v176, v177
	v_cvt_pk_bf16_f32 v136, v136, v137
	v_lshlrev_b64 v[146:147], 4, v[148:149]
	v_lshlrev_b32_e32 v137, 16, v173
	v_and_b32_e32 v145, 0xffff0000, v173
	v_fma_f32 v137, v152, v170, -v137
	v_fma_f32 v145, v153, v171, -v145
	v_cvt_pk_bf16_f32 v137, v137, v145
	v_lshlrev_b32_e32 v145, 16, v174
	v_fma_f32 v138, v138, v164, -v145
	v_and_b32_e32 v145, 0xffff0000, v174
	v_fma_f32 v139, v139, v165, -v145
	v_cvt_pk_bf16_f32 v138, v138, v139
	v_lshlrev_b32_e32 v139, 16, v175
	v_fma_f32 v139, v150, v166, -v139
	v_and_b32_e32 v145, 0xffff0000, v175
	v_lshl_add_u64 v[148:149], s[34:35], 0, v[146:147]
	v_lshl_add_u64 v[146:147], s[36:37], 0, v[146:147]
	v_fma_f32 v145, v151, v167, -v145
	v_cvt_pk_bf16_f32 v139, v139, v145
	global_store_dwordx4 v[148:149], v[172:175], off nt
	s_cbranch_execnz .LBB0_2600

.LBB0_2600:
	v_readlane_b32 s2, v242, 36
	global_store_dwordx4 v[146:147], v[136:139], off nt
	s_add_i32 s2, s2, s73
	s_waitcnt lgkmcnt(0)
	s_add_i32 s2, s2, s72
	s_cmp_lt_i32 s2, s50
	s_cselect_b32 s80, s2, -1
	s_cmp_lt_i32 s80, 0
	s_cbranch_scc1 .LBB0_2397
	s_mul_hi_u32 s2, s80, 0x9824d8ed
	s_lshr_b32 s2, s2, 15
	s_mul_i32 s3, s2, 0xd760
	s_sub_i32 s72, s80, s3
	s_cmpk_gt_u32 s72, 0xc2ff
	s_mov_b64 s[44:45], -1
	s_cbranch_scc0 .LBB0_2639
	s_add_i32 s44, s2, 1
	s_add_i32 s3, s72, 0xffff3d00
	s_cmpk_lt_u32 s3, 0x1400
	s_cselect_b32 s3, s3, s72
	s_cmpk_gt_u32 s3, 0xbff
	s_mov_b64 s[48:49], -1
	s_cbranch_scc0 .LBB0_2636
	s_cmpk_gt_u32 s3, 0x13ff
	s_cbranch_scc0 .LBB0_2633
	s_cmpk_gt_u32 s3, 0x93ff
	s_cbranch_scc0 .LBB0_2630
	s_cmpk_gt_u32 s3, 0xd3ff
	s_cbranch_scc0 .LBB0_2627
	s_cmpk_gt_u32 s3, 0xd5ff
	s_cbranch_scc0 .LBB0_2624
	s_cmpk_gt_u32 s3, 0xd6ff
	s_cbranch_scc0 .LBB0_2621
	s_cmpk_gt_u32 s3, 0xd71f
	s_mov_b64 s[42:43], -1
	s_cbranch_scc0 .LBB0_2610
	s_mov_b32 s45, s47
	v_readlane_b32 s48, v243, 40
	s_lshl_b64 s[34:35], s[44:45], 19
	v_readlane_b32 s54, v243, 46
	v_readlane_b32 s55, v243, 47
	s_add_u32 s40, s54, s34
	s_addc_u32 s41, s55, s35
	s_lshl_b64 s[36:37], s[44:45], 18
	v_readlane_b32 s24, v242, 42
	s_add_u32 s34, s24, s36
	v_readlane_b32 s24, v242, 43
	s_addc_u32 s35, s24, s37
	v_readlane_b32 s24, v242, 44
	s_add_u32 s36, s24, s36
	v_readlane_b32 s24, v242, 45
	v_readlane_b32 s50, v243, 42
	s_addc_u32 s37, s24, s37
	s_lshl_b32 s30, s44, 13
	v_readlane_b32 s51, v243, 43
	s_add_u32 s38, s50, s30
	s_addc_u32 s39, s51, 0
	s_lshl_b32 s42, s3, 5
	s_and_b32 s30, s42, 0x7fffffc0
	v_readlane_b32 s49, v243, 41
	v_readlane_b32 s52, v243, 44
	v_readlane_b32 s53, v243, 45
	v_readlane_b32 s56, v243, 48
	v_readlane_b32 s57, v243, 49
	v_readlane_b32 s58, v243, 50
	v_readlane_b32 s59, v243, 51
	v_readlane_b32 s60, v243, 52
	v_readlane_b32 s61, v243, 53
	v_readlane_b32 s62, v243, 54
	v_readlane_b32 s63, v243, 55
	s_mov_b32 s50, s91
	v_readlane_b32 s51, v242, 29
	s_add_i32 s30, s30, 0xffe51c00
	s_and_b32 s75, s42, 32
	s_mov_b64 s[42:43], 0

.LBB0_2866:
	v_add_u32_e32 v4, s8, v72
	v_ashrrev_i32_e32 v5, 31, v4
	v_mul_lo_u32 v6, s26, v5
	v_mul_lo_u32 v7, s27, v4
	v_mad_u64_u32 v[4:5], s[2:3], s26, v4, 0
	v_add3_u32 v5, v5, v6, v7
	v_add_u32_e32 v6, s8, v71
	s_ashr_i32 s29, s28, 31
	v_ashrrev_i32_e32 v7, 31, v6
	s_lshl_b64 s[2:3], s[28:29], 2
	v_mul_lo_u32 v8, s26, v7
	v_mul_lo_u32 v9, s27, v6
	v_mad_u64_u32 v[6:7], s[28:29], s26, v6, 0
	v_lshl_add_u64 v[4:5], v[4:5], 2, s[24:25]
	v_add3_u32 v7, v7, v8, v9
	v_lshl_add_u64 v[4:5], v[4:5], 0, s[2:3]
	v_lshl_add_u64 v[6:7], v[6:7], 2, s[24:25]
	v_lshl_add_u64 v[4:5], v[4:5], 0, v[2:3]
	v_lshl_add_u64 v[6:7], v[6:7], 0, s[2:3]
	v_lshl_add_u64 v[6:7], v[6:7], 0, v[2:3]
	global_load_dwordx4 v[32:35], v[4:5], off nt
	global_load_dwordx4 v[20:23], v[6:7], off nt
	v_add_u32_e32 v4, s8, v70
	v_ashrrev_i32_e32 v5, 31, v4
	v_mul_lo_u32 v6, s26, v5
	v_mul_lo_u32 v7, s27, v4
	v_mad_u64_u32 v[4:5], s[28:29], s26, v4, 0
	v_add3_u32 v5, v5, v6, v7
	v_add_u32_e32 v6, s8, v1
	v_ashrrev_i32_e32 v7, 31, v6
	v_mul_lo_u32 v8, s26, v7
	v_mul_lo_u32 v9, s27, v6
	v_mad_u64_u32 v[6:7], s[28:29], s26, v6, 0
	v_lshl_add_u64 v[4:5], v[4:5], 2, s[24:25]
	v_add3_u32 v7, v7, v8, v9
	v_lshl_add_u64 v[4:5], v[4:5], 0, s[2:3]
	v_lshl_add_u64 v[6:7], v[6:7], 2, s[24:25]
	v_lshl_add_u64 v[4:5], v[4:5], 0, v[2:3]
	v_lshl_add_u64 v[6:7], v[6:7], 0, s[2:3]
	v_lshl_add_u64 v[6:7], v[6:7], 0, v[2:3]
	global_load_dwordx4 v[28:31], v[4:5], off nt
	global_load_dwordx4 v[12:15], v[6:7], off nt
	v_add_u32_e32 v4, s8, v78
	v_ashrrev_i32_e32 v5, 31, v4
	v_mul_lo_u32 v6, s26, v5
	v_mul_lo_u32 v7, s27, v4
	v_mad_u64_u32 v[4:5], s[28:29], s26, v4, 0
	v_add3_u32 v5, v5, v6, v7
	v_add_u32_e32 v6, s8, v79
	v_ashrrev_i32_e32 v7, 31, v6
	v_mul_lo_u32 v8, s26, v7
	v_mul_lo_u32 v9, s27, v6
	v_mad_u64_u32 v[6:7], s[28:29], s26, v6, 0
	v_lshl_add_u64 v[4:5], v[4:5], 2, s[24:25]
	v_add3_u32 v7, v7, v8, v9
	v_lshl_add_u64 v[4:5], v[4:5], 0, s[2:3]
	v_lshl_add_u64 v[6:7], v[6:7], 2, s[24:25]
	v_lshl_add_u64 v[4:5], v[4:5], 0, v[2:3]
	v_lshl_add_u64 v[6:7], v[6:7], 0, s[2:3]
	v_lshl_add_u64 v[6:7], v[6:7], 0, v[2:3]
	global_load_dwordx4 v[24:27], v[4:5], off nt
	global_load_dwordx4 v[8:11], v[6:7], off nt
	v_add_u32_e32 v4, s8, v80
	v_ashrrev_i32_e32 v5, 31, v4
	v_mul_lo_u32 v6, s26, v5
	v_mul_lo_u32 v7, s27, v4
	v_mad_u64_u32 v[4:5], s[28:29], s26, v4, 0
	v_add3_u32 v5, v5, v6, v7
	v_add_u32_e32 v6, s8, v81
	v_ashrrev_i32_e32 v7, 31, v6
	v_mul_lo_u32 v16, s26, v7
	v_mul_lo_u32 v17, s27, v6
	v_mad_u64_u32 v[6:7], s[26:27], s26, v6, 0
	v_add3_u32 v7, v7, v16, v17
	v_lshl_add_u64 v[4:5], v[4:5], 2, s[24:25]
	v_lshl_add_u64 v[6:7], v[6:7], 2, s[24:25]
	v_lshl_add_u64 v[4:5], v[4:5], 0, s[2:3]
	v_lshl_add_u64 v[6:7], v[6:7], 0, s[2:3]
	v_lshl_add_u64 v[4:5], v[4:5], 0, v[2:3]
	v_lshl_add_u64 v[6:7], v[6:7], 0, v[2:3]
	global_load_dwordx4 v[16:19], v[4:5], off nt
	s_nop 0
	global_load_dwordx4 v[4:7], v[6:7], off nt
	s_waitcnt vmcnt(15)
	ds_write2_b32 v85, v36, v37 offset1:1
	ds_write2_b32 v85, v38, v39 offset0:2 offset1:3
	v_add_u32_e32 v36, 0x420, v85
	s_waitcnt vmcnt(14)
	ds_write2_b32 v36, v40, v41 offset1:1
	v_add_u32_e32 v36, 0x428, v85
	ds_write2_b32 v36, v42, v43 offset1:1
	v_add_u32_e32 v36, 0x840, v85
	s_waitcnt vmcnt(13)
	ds_write2_b32 v36, v44, v45 offset1:1
	v_add_u32_e32 v36, 0x848, v85
	ds_write2_b32 v36, v46, v47 offset1:1
	v_add_u32_e32 v36, 0xc60, v85
	s_waitcnt vmcnt(12)
	ds_write2_b32 v36, v48, v49 offset1:1
	v_add_u32_e32 v36, 0xc68, v85
	ds_write2_b32 v36, v50, v51 offset1:1
	v_add_u32_e32 v36, 0x1080, v85
	s_waitcnt vmcnt(11)
	ds_write2_b32 v36, v52, v53 offset1:1
	v_add_u32_e32 v36, 0x1088, v85
	ds_write2_b32 v36, v54, v55 offset1:1
	v_add_u32_e32 v36, 0x14a0, v85
	s_waitcnt vmcnt(10)
	ds_write2_b32 v36, v56, v57 offset1:1
	v_add_u32_e32 v36, 0x14a8, v85
	ds_write2_b32 v36, v58, v59 offset1:1
	v_add_u32_e32 v36, 0x18c0, v85
	s_waitcnt vmcnt(9)
	ds_write2_b32 v36, v60, v61 offset1:1
	v_add_u32_e32 v36, 0x18c8, v85
	ds_write2_b32 v36, v62, v63 offset1:1
	v_add_u32_e32 v36, 0x1ce0, v85
	s_waitcnt vmcnt(8)
	ds_write2_b32 v36, v64, v65 offset1:1
	v_add_u32_e32 v36, 0x1ce8, v85
	ds_write2_b32 v36, v66, v67 offset1:1
	s_waitcnt lgkmcnt(0)
	ds_read2_b32 v[40:41], v84 offset1:33
	ds_read2_b32 v[48:49], v84 offset0:66 offset1:99
	ds_read2_b32 v[42:43], v84 offset0:132 offset1:165
	ds_read2_b32 v[46:47], v84 offset0:198 offset1:231
	s_cmp_lg_u64 s[18:19], 0
	s_cselect_b64 s[24:25], -1, 0
	v_add_u32_e32 v44, s12, v68
	s_and_b64 vcc, exec, s[24:25]
	v_add_u32_e32 v50, s42, v72
	v_ashrrev_i32_e32 v53, 5, v44
	v_lshlrev_b32_e32 v52, 1, v44
	v_ashrrev_i32_e32 v45, 31, v44
	s_waitcnt lgkmcnt(3)
	v_cvt_pk_bf16_f32 v36, v40, v41
	s_waitcnt lgkmcnt(2)
	v_cvt_pk_bf16_f32 v37, v48, v49
	s_waitcnt lgkmcnt(1)
	v_cvt_pk_bf16_f32 v38, v42, v43
	s_waitcnt lgkmcnt(0)
	v_cvt_pk_bf16_f32 v39, v46, v47
	s_cbranch_vccz .LBB0_2880
	v_lshlrev_b32_e32 v51, 2, v50
	v_and_b32_e32 v51, 0xffffffc0, v51
	v_add_u32_e32 v54, v51, v53
	v_ashrrev_i32_e32 v55, 31, v54
	v_lshlrev_b64 v[66:67], 6, v[54:55]
	v_and_b32_e32 v51, 48, v52
	v_and_b32_e32 v54, 15, v50
	v_lshl_add_u64 v[58:59], v[44:45], 2, s[22:23]
	v_or3_b32 v66, v66, v51, v54
	global_load_dwordx4 v[54:57], v[58:59], off offset:16
	s_nop 0
	global_load_dwordx4 v[58:61], v[58:59], off
	s_waitcnt vmcnt(1)
	v_mul_f32_e32 v65, v42, v54
	s_waitcnt vmcnt(0)
	v_mul_f32_e32 v51, v40, v58
	v_mul_f32_e32 v62, v41, v59
	v_cvt_pk_bf16_f32 v62, v51, v62
	v_mul_f32_e32 v63, v48, v60
	v_lshlrev_b32_e32 v51, 16, v62
	v_fma_f32 v40, v40, v58, -v51
	v_and_b32_e32 v51, 0xffff0000, v62
	v_mul_f32_e32 v64, v49, v61
	v_fma_f32 v41, v41, v59, -v51
	v_mul_f32_e32 v86, v43, v55
	v_mul_f32_e32 v87, v46, v56
	v_mul_f32_e32 v88, v47, v57
	v_cvt_pk_bf16_f32 v63, v63, v64
	v_cvt_pk_bf16_f32 v64, v65, v86
	v_cvt_pk_bf16_f32 v65, v87, v88
	v_cvt_pk_bf16_f32 v40, v40, v41
	s_nop 0
	v_lshlrev_b32_e32 v41, 16, v63
	v_fma_f32 v41, v48, v60, -v41
	v_and_b32_e32 v48, 0xffff0000, v63
	v_fma_f32 v48, v49, v61, -v48
	v_cvt_pk_bf16_f32 v41, v41, v48
	v_lshlrev_b32_e32 v48, 16, v64
	v_fma_f32 v42, v42, v54, -v48
	v_and_b32_e32 v48, 0xffff0000, v64
	v_fma_f32 v43, v43, v55, -v48
	v_cvt_pk_bf16_f32 v42, v42, v43
	v_lshlrev_b32_e32 v43, 16, v65
	v_fma_f32 v43, v46, v56, -v43
	v_and_b32_e32 v46, 0xffff0000, v65
	v_fma_f32 v46, v47, v57, -v46
	v_cvt_pk_bf16_f32 v43, v43, v46
	v_lshlrev_b64 v[46:47], 4, v[66:67]
	v_lshl_add_u64 v[48:49], s[14:15], 0, v[46:47]
	global_store_dwordx4 v[48:49], v[62:65], off nt
	v_lshl_add_u64 v[48:49], s[18:19], 0, v[46:47]
	v_lshlrev_b32_e32 v46, 1, v68
	s_cbranch_execnz .LBB0_2869

.LBB0_2869:
	global_store_dwordx4 v[48:49], v[40:43], off
	ds_read2_b32 v[40:41], v84 offset0:8 offset1:41
	ds_read2_b32 v[50:51], v84 offset0:74 offset1:107
	ds_read2_b32 v[42:43], v84 offset0:140 offset1:173
	ds_read2_b32 v[48:49], v84 offset0:206 offset1:239
	v_cndmask_b32_e64 v47, 0, 1, s[24:25]
	v_cmp_ne_u32_e64 s[2:3], 1, v47
	s_andn2_b64 vcc, exec, s[24:25]
	v_add_u32_e32 v47, s42, v71
	s_waitcnt lgkmcnt(3)
	v_cvt_pk_bf16_f32 v36, v40, v41
	s_waitcnt lgkmcnt(2)
	v_cvt_pk_bf16_f32 v37, v50, v51
	s_waitcnt lgkmcnt(1)
	v_cvt_pk_bf16_f32 v38, v42, v43
	s_waitcnt lgkmcnt(0)
	v_cvt_pk_bf16_f32 v39, v48, v49
	s_cbranch_vccnz .LBB0_2881
	v_lshlrev_b32_e32 v54, 2, v47
	v_and_b32_e32 v54, 0xffffffc0, v54
	v_add_u32_e32 v54, v54, v53
	v_ashrrev_i32_e32 v55, 31, v54
	v_lshlrev_b64 v[66:67], 6, v[54:55]
	v_and_b32_e32 v54, 48, v52
	v_and_b32_e32 v55, 15, v47
	v_lshl_add_u64 v[58:59], v[44:45], 2, s[22:23]
	v_or3_b32 v66, v66, v54, v55
	global_load_dwordx4 v[54:57], v[58:59], off offset:16
	s_nop 0
	global_load_dwordx4 v[58:61], v[58:59], off
	s_waitcnt vmcnt(1)
	v_mul_f32_e32 v86, v42, v54
	s_waitcnt vmcnt(0)
	v_mul_f32_e32 v62, v40, v58
	v_mul_f32_e32 v63, v41, v59
	v_mul_f32_e32 v64, v50, v60
	v_mul_f32_e32 v65, v51, v61
	v_mul_f32_e32 v87, v43, v55
	v_cvt_pk_bf16_f32 v62, v62, v63
	v_cvt_pk_bf16_f32 v63, v64, v65
	v_cvt_pk_bf16_f32 v64, v86, v87
	v_mul_f32_e32 v88, v48, v56
	v_lshlrev_b32_e32 v86, 16, v62
	v_fma_f32 v40, v40, v58, -v86
	v_and_b32_e32 v58, 0xffff0000, v62
	v_fma_f32 v41, v41, v59, -v58
	v_mul_f32_e32 v89, v49, v57
	v_cvt_pk_bf16_f32 v65, v88, v89
	v_cvt_pk_bf16_f32 v40, v40, v41
	v_lshlrev_b32_e32 v41, 16, v63
	v_fma_f32 v41, v50, v60, -v41
	v_and_b32_e32 v50, 0xffff0000, v63
	v_fma_f32 v50, v51, v61, -v50
	v_cvt_pk_bf16_f32 v41, v41, v50
	v_lshlrev_b32_e32 v50, 16, v64
	v_fma_f32 v42, v42, v54, -v50
	v_and_b32_e32 v50, 0xffff0000, v64
	v_fma_f32 v43, v43, v55, -v50
	v_cvt_pk_bf16_f32 v42, v42, v43
	v_lshlrev_b32_e32 v43, 16, v65
	v_fma_f32 v43, v48, v56, -v43
	v_and_b32_e32 v48, 0xffff0000, v65
	v_fma_f32 v48, v49, v57, -v48
	v_cvt_pk_bf16_f32 v43, v43, v48
	v_lshlrev_b64 v[48:49], 4, v[66:67]
	v_lshl_add_u64 v[50:51], s[14:15], 0, v[48:49]
	v_lshl_add_u64 v[48:49], s[18:19], 0, v[48:49]
	global_store_dwordx4 v[50:51], v[62:65], off nt
	s_cbranch_execnz .LBB0_2872

.LBB0_2872:
	global_store_dwordx4 v[48:49], v[40:43], off nt
	ds_read2_b32 v[40:41], v84 offset0:16 offset1:49
	ds_read2_b32 v[50:51], v84 offset0:82 offset1:115
	ds_read2_b32 v[42:43], v84 offset0:148 offset1:181
	ds_read2_b32 v[48:49], v84 offset0:214 offset1:247
	s_and_b64 vcc, exec, s[2:3]
	v_add_u32_e32 v47, s42, v70
	s_waitcnt lgkmcnt(3)
	v_cvt_pk_bf16_f32 v36, v40, v41
	s_waitcnt lgkmcnt(2)
	v_cvt_pk_bf16_f32 v37, v50, v51
	s_waitcnt lgkmcnt(1)
	v_cvt_pk_bf16_f32 v38, v42, v43
	s_waitcnt lgkmcnt(0)
	v_cvt_pk_bf16_f32 v39, v48, v49
	s_cbranch_vccnz .LBB0_2882
	v_lshlrev_b32_e32 v54, 2, v47
	v_and_b32_e32 v54, 0xffffffc0, v54
	v_add_u32_e32 v54, v54, v53
	v_ashrrev_i32_e32 v55, 31, v54
	v_lshlrev_b64 v[66:67], 6, v[54:55]
	v_and_b32_e32 v54, 48, v52
	v_and_b32_e32 v55, 15, v47
	v_lshl_add_u64 v[58:59], v[44:45], 2, s[22:23]
	v_or3_b32 v66, v66, v54, v55
	global_load_dwordx4 v[54:57], v[58:59], off offset:16
	s_nop 0
	global_load_dwordx4 v[58:61], v[58:59], off
	s_waitcnt vmcnt(1)
	v_mul_f32_e32 v86, v42, v54
	s_waitcnt vmcnt(0)
	v_mul_f32_e32 v62, v40, v58
	v_mul_f32_e32 v63, v41, v59
	v_mul_f32_e32 v64, v50, v60
	v_mul_f32_e32 v65, v51, v61
	v_mul_f32_e32 v87, v43, v55
	v_cvt_pk_bf16_f32 v62, v62, v63
	v_cvt_pk_bf16_f32 v63, v64, v65
	v_cvt_pk_bf16_f32 v64, v86, v87
	v_mul_f32_e32 v88, v48, v56
	v_lshlrev_b32_e32 v86, 16, v62
	v_fma_f32 v40, v40, v58, -v86
	v_and_b32_e32 v58, 0xffff0000, v62
	v_fma_f32 v41, v41, v59, -v58
	v_mul_f32_e32 v89, v49, v57
	v_cvt_pk_bf16_f32 v65, v88, v89
	v_cvt_pk_bf16_f32 v40, v40, v41
	v_lshlrev_b32_e32 v41, 16, v63
	v_fma_f32 v41, v50, v60, -v41
	v_and_b32_e32 v50, 0xffff0000, v63
	v_fma_f32 v50, v51, v61, -v50
	v_cvt_pk_bf16_f32 v41, v41, v50
	v_lshlrev_b32_e32 v50, 16, v64
	v_fma_f32 v42, v42, v54, -v50
	v_and_b32_e32 v50, 0xffff0000, v64
	v_fma_f32 v43, v43, v55, -v50
	v_cvt_pk_bf16_f32 v42, v42, v43
	v_lshlrev_b32_e32 v43, 16, v65
	v_fma_f32 v43, v48, v56, -v43
	v_and_b32_e32 v48, 0xffff0000, v65
	v_fma_f32 v48, v49, v57, -v48
	v_cvt_pk_bf16_f32 v43, v43, v48
	v_lshlrev_b64 v[48:49], 4, v[66:67]
	v_lshl_add_u64 v[50:51], s[14:15], 0, v[48:49]
	v_lshl_add_u64 v[48:49], s[18:19], 0, v[48:49]
	global_store_dwordx4 v[50:51], v[62:65], off nt
	s_cbranch_execnz .LBB0_2875

.LBB0_2875:
	global_store_dwordx4 v[48:49], v[40:43], off nt
	ds_read2_b32 v[40:41], v84 offset0:24 offset1:57
	ds_read2_b32 v[50:51], v84 offset0:90 offset1:123
	ds_read2_b32 v[42:43], v84 offset0:156 offset1:189
	ds_read2_b32 v[48:49], v84 offset0:222 offset1:255
	s_and_b64 vcc, exec, s[2:3]
	v_add_u32_e32 v47, s42, v1
	s_waitcnt lgkmcnt(3)
	v_cvt_pk_bf16_f32 v36, v40, v41
	s_waitcnt lgkmcnt(2)
	v_cvt_pk_bf16_f32 v37, v50, v51
	s_waitcnt lgkmcnt(1)
	v_cvt_pk_bf16_f32 v38, v42, v43
	s_waitcnt lgkmcnt(0)
	v_cvt_pk_bf16_f32 v39, v48, v49
	s_cbranch_vccnz .LBB0_2883
	v_lshlrev_b32_e32 v54, 2, v47
	v_and_b32_e32 v54, 0xffffffc0, v54
	v_add_u32_e32 v54, v54, v53
	v_ashrrev_i32_e32 v55, 31, v54
	v_lshlrev_b64 v[64:65], 6, v[54:55]
	v_and_b32_e32 v52, 48, v52
	v_and_b32_e32 v53, 15, v47
	v_lshl_add_u64 v[44:45], v[44:45], 2, s[22:23]
	v_or3_b32 v64, v64, v52, v53
	global_load_dwordx4 v[52:55], v[44:45], off offset:16
	global_load_dwordx4 v[56:59], v[44:45], off
	s_waitcnt vmcnt(1)
	v_mul_f32_e32 v63, v42, v52
	s_waitcnt vmcnt(0)
	v_mul_f32_e32 v44, v40, v56
	v_mul_f32_e32 v45, v41, v57
	v_cvt_pk_bf16_f32 v60, v44, v45
	v_mul_f32_e32 v61, v50, v58
	v_lshlrev_b32_e32 v44, 16, v60
	v_fma_f32 v40, v40, v56, -v44
	v_and_b32_e32 v44, 0xffff0000, v60
	v_mul_f32_e32 v62, v51, v59
	v_fma_f32 v41, v41, v57, -v44
	v_mul_f32_e32 v66, v43, v53
	v_mul_f32_e32 v67, v48, v54
	v_mul_f32_e32 v86, v49, v55
	v_cvt_pk_bf16_f32 v61, v61, v62
	v_cvt_pk_bf16_f32 v62, v63, v66
	v_cvt_pk_bf16_f32 v63, v67, v86
	v_cvt_pk_bf16_f32 v40, v40, v41
	s_nop 0
	v_lshlrev_b32_e32 v41, 16, v61
	v_and_b32_e32 v44, 0xffff0000, v61
	v_fma_f32 v41, v50, v58, -v41
	v_fma_f32 v44, v51, v59, -v44
	v_cvt_pk_bf16_f32 v41, v41, v44
	v_lshlrev_b32_e32 v44, 16, v62
	v_fma_f32 v42, v42, v52, -v44
	v_and_b32_e32 v44, 0xffff0000, v62
	v_fma_f32 v43, v43, v53, -v44
	v_cvt_pk_bf16_f32 v42, v42, v43
	v_lshlrev_b32_e32 v43, 16, v63
	v_and_b32_e32 v44, 0xffff0000, v63
	v_fma_f32 v43, v48, v54, -v43
	v_fma_f32 v44, v49, v55, -v44
	v_cvt_pk_bf16_f32 v43, v43, v44
	v_lshlrev_b64 v[44:45], 4, v[64:65]
	v_lshl_add_u64 v[48:49], s[14:15], 0, v[44:45]
	v_lshl_add_u64 v[44:45], s[18:19], 0, v[44:45]
	global_store_dwordx4 v[48:49], v[60:63], off nt
	s_cbranch_execnz .LBB0_2878

.LBB0_2878:
	global_store_dwordx4 v[44:45], v[40:43], off nt
	s_waitcnt lgkmcnt(0)
	s_add_i32 s43, s43, s9
	s_add_i32 s62, s62, s63
	s_cmp_ge_i32 s43, s38
	s_cbranch_scc1 .LBB0_2886
	s_mov_b32 s42, s41
	s_mov_b32 s12, s8
	s_mov_b32 s40, s39
	s_mov_b64 s[22:23], s[20:21]
	s_mov_b64 s[18:19], s[16:17]
	s_mov_b64 s[14:15], s[10:11]
	s_waitcnt vmcnt(11)
	v_mov_b32_e32 v36, v32
	v_mov_b32_e32 v37, v33
	v_mov_b32_e32 v38, v34
	v_mov_b32_e32 v39, v35
	s_waitcnt vmcnt(10)
	v_mov_b32_e32 v40, v20
	v_mov_b32_e32 v41, v21
	v_mov_b32_e32 v42, v22
	v_mov_b32_e32 v43, v23
	s_waitcnt vmcnt(9)
	v_mov_b32_e32 v44, v28
	v_mov_b32_e32 v45, v29
	v_mov_b32_e32 v46, v30
	v_mov_b32_e32 v47, v31
	s_waitcnt vmcnt(8)
	v_mov_b32_e32 v48, v12
	v_mov_b32_e32 v49, v13
	v_mov_b32_e32 v50, v14
	v_mov_b32_e32 v51, v15
	s_waitcnt vmcnt(7)
	v_mov_b32_e32 v52, v24
	v_mov_b32_e32 v53, v25
	v_mov_b32_e32 v54, v26
	v_mov_b32_e32 v55, v27
	s_waitcnt vmcnt(6)
	v_mov_b32_e32 v56, v8
	v_mov_b32_e32 v57, v9
	v_mov_b32_e32 v58, v10
	v_mov_b32_e32 v59, v11
	s_waitcnt vmcnt(5)
	v_mov_b32_e32 v60, v16
	v_mov_b32_e32 v61, v17
	v_mov_b32_e32 v62, v18
	v_mov_b32_e32 v63, v19
	s_waitcnt vmcnt(4)
	v_mov_b32_e32 v64, v4
	v_mov_b32_e32 v65, v5
	v_mov_b32_e32 v66, v6
	v_mov_b32_e32 v67, v7
	s_branch .LBB0_2814

.LBB0_2887:
	v_add_u32_e32 v2, v83, v75
	s_waitcnt vmcnt(11)
	ds_write2_b32 v2, v32, v33 offset1:1
	ds_write2_b32 v2, v34, v35 offset0:2 offset1:3
	v_add_u32_e32 v32, v83, v76
	s_waitcnt vmcnt(10)
	ds_write2_b32 v32, v20, v21 offset1:1
	ds_write2_b32 v32, v22, v23 offset0:2 offset1:3
	v_add_u32_e32 v20, v83, v73
	s_waitcnt vmcnt(9)
	ds_write2_b32 v20, v28, v29 offset1:1
	ds_write2_b32 v20, v30, v31 offset0:2 offset1:3
	v_add_u32_e32 v20, v83, v74
	s_waitcnt vmcnt(8)
	ds_write2_b32 v20, v12, v13 offset1:1
	ds_write2_b32 v20, v14, v15 offset0:2 offset1:3
	v_add_u32_e32 v12, 0x1080, v2
	s_waitcnt vmcnt(7)
	ds_write2_b32 v12, v24, v25 offset1:1
	v_add_u32_e32 v12, 0x1088, v2
	ds_write2_b32 v12, v26, v27 offset1:1
	v_add_u32_e32 v12, 0x14a0, v2
	s_waitcnt vmcnt(6)
	ds_write2_b32 v12, v8, v9 offset1:1
	v_add_u32_e32 v8, 0x14a8, v2
	ds_write2_b32 v8, v10, v11 offset1:1
	v_add_u32_e32 v8, 0x18c0, v2
	s_waitcnt vmcnt(5)
	ds_write2_b32 v8, v16, v17 offset1:1
	v_add_u32_e32 v8, 0x18c8, v2
	ds_write2_b32 v8, v18, v19 offset1:1
	v_add_u32_e32 v8, 0x1ce0, v2
	v_add_u32_e32 v2, 0x1ce8, v2
	s_waitcnt vmcnt(4)
	ds_write2_b32 v8, v4, v5 offset1:1
	ds_write2_b32 v2, v6, v7 offset1:1
	s_waitcnt lgkmcnt(0)
	v_add3_u32 v18, s44, v77, v82
	ds_read2_b32 v[8:9], v18 offset1:33
	ds_read2_b32 v[16:17], v18 offset0:66 offset1:99
	ds_read2_b32 v[10:11], v18 offset0:132 offset1:165
	ds_read2_b32 v[14:15], v18 offset0:198 offset1:231
	s_cmp_lg_u64 s[16:17], 0
	s_cselect_b64 s[12:13], -1, 0
	v_add_u32_e32 v12, s8, v68
	s_and_b64 vcc, exec, s[12:13]
	v_add_u32_e32 v20, s41, v72
	v_ashrrev_i32_e32 v19, 5, v12
	v_lshlrev_b32_e32 v2, 1, v12
	v_ashrrev_i32_e32 v13, 31, v12
	s_waitcnt lgkmcnt(3)
	v_cvt_pk_bf16_f32 v4, v8, v9
	s_waitcnt lgkmcnt(2)
	v_cvt_pk_bf16_f32 v5, v16, v17
	s_waitcnt lgkmcnt(1)
	v_cvt_pk_bf16_f32 v6, v10, v11
	s_waitcnt lgkmcnt(0)
	v_cvt_pk_bf16_f32 v7, v14, v15
	s_cbranch_vccz .LBB0_2929
	v_lshlrev_b32_e32 v21, 2, v20
	v_and_b32_e32 v21, 0xffffffc0, v21
	v_add_u32_e32 v22, v21, v19
	v_ashrrev_i32_e32 v23, 31, v22
	v_lshlrev_b64 v[34:35], 6, v[22:23]
	v_and_b32_e32 v21, 48, v2
	v_and_b32_e32 v22, 15, v20
	v_lshl_add_u64 v[26:27], v[12:13], 2, s[20:21]
	v_or3_b32 v34, v34, v21, v22
	global_load_dwordx4 v[22:25], v[26:27], off offset:16
	s_nop 0
	global_load_dwordx4 v[26:29], v[26:27], off
	s_waitcnt vmcnt(1)
	v_mul_f32_e32 v33, v10, v22
	s_waitcnt vmcnt(0)
	v_mul_f32_e32 v21, v8, v26
	v_mul_f32_e32 v30, v9, v27
	v_cvt_pk_bf16_f32 v30, v21, v30
	v_mul_f32_e32 v31, v16, v28
	v_lshlrev_b32_e32 v21, 16, v30
	v_fma_f32 v8, v8, v26, -v21
	v_and_b32_e32 v21, 0xffff0000, v30
	v_mul_f32_e32 v32, v17, v29
	v_fma_f32 v9, v9, v27, -v21
	v_mul_f32_e32 v36, v11, v23
	v_mul_f32_e32 v37, v14, v24
	v_mul_f32_e32 v38, v15, v25
	v_cvt_pk_bf16_f32 v31, v31, v32
	v_cvt_pk_bf16_f32 v32, v33, v36
	v_cvt_pk_bf16_f32 v33, v37, v38
	v_cvt_pk_bf16_f32 v8, v8, v9
	s_nop 0
	v_lshlrev_b32_e32 v9, 16, v31
	v_fma_f32 v9, v16, v28, -v9
	v_and_b32_e32 v16, 0xffff0000, v31
	v_fma_f32 v16, v17, v29, -v16
	v_cvt_pk_bf16_f32 v9, v9, v16
	v_lshlrev_b32_e32 v16, 16, v32
	v_fma_f32 v10, v10, v22, -v16
	v_and_b32_e32 v16, 0xffff0000, v32
	v_fma_f32 v11, v11, v23, -v16
	v_cvt_pk_bf16_f32 v10, v10, v11
	v_lshlrev_b32_e32 v11, 16, v33
	v_fma_f32 v11, v14, v24, -v11
	v_and_b32_e32 v14, 0xffff0000, v33
	v_fma_f32 v14, v15, v25, -v14
	v_cvt_pk_bf16_f32 v11, v11, v14
	v_lshlrev_b64 v[14:15], 4, v[34:35]
	v_lshl_add_u64 v[16:17], s[10:11], 0, v[14:15]
	global_store_dwordx4 v[16:17], v[30:33], off nt
	v_lshl_add_u64 v[14:15], s[16:17], 0, v[14:15]
	s_cbranch_execnz .LBB0_2890

.LBB0_2890:
	global_store_dwordx4 v[14:15], v[8:11], off nt
	ds_read2_b32 v[8:9], v18 offset0:8 offset1:41
	ds_read2_b32 v[16:17], v18 offset0:74 offset1:107
	ds_read2_b32 v[10:11], v18 offset0:140 offset1:173
	ds_read2_b32 v[14:15], v18 offset0:206 offset1:239
	v_cndmask_b32_e64 v20, 0, 1, s[12:13]
	v_cmp_ne_u32_e64 s[2:3], 1, v20
	s_andn2_b64 vcc, exec, s[12:13]
	v_add_u32_e32 v20, s41, v71
	s_waitcnt lgkmcnt(3)
	v_cvt_pk_bf16_f32 v4, v8, v9
	s_waitcnt lgkmcnt(2)
	v_cvt_pk_bf16_f32 v5, v16, v17
	s_waitcnt lgkmcnt(1)
	v_cvt_pk_bf16_f32 v6, v10, v11
	s_waitcnt lgkmcnt(0)
	v_cvt_pk_bf16_f32 v7, v14, v15
	s_cbranch_vccnz .LBB0_2930
	v_lshlrev_b32_e32 v21, 2, v20
	v_and_b32_e32 v21, 0xffffffc0, v21
	v_add_u32_e32 v22, v21, v19
	v_ashrrev_i32_e32 v23, 31, v22
	v_lshlrev_b64 v[34:35], 6, v[22:23]
	v_and_b32_e32 v21, 48, v2
	v_and_b32_e32 v22, 15, v20
	v_lshl_add_u64 v[26:27], v[12:13], 2, s[20:21]
	v_or3_b32 v34, v34, v21, v22
	global_load_dwordx4 v[22:25], v[26:27], off offset:16
	s_nop 0
	global_load_dwordx4 v[26:29], v[26:27], off
	s_waitcnt vmcnt(1)
	v_mul_f32_e32 v33, v10, v22
	s_waitcnt vmcnt(0)
	v_mul_f32_e32 v21, v8, v26
	v_mul_f32_e32 v30, v9, v27
	v_cvt_pk_bf16_f32 v30, v21, v30
	v_mul_f32_e32 v31, v16, v28
	v_lshlrev_b32_e32 v21, 16, v30
	v_fma_f32 v8, v8, v26, -v21
	v_and_b32_e32 v21, 0xffff0000, v30
	v_mul_f32_e32 v32, v17, v29
	v_fma_f32 v9, v9, v27, -v21
	v_mul_f32_e32 v36, v11, v23
	v_mul_f32_e32 v37, v14, v24
	v_mul_f32_e32 v38, v15, v25
	v_cvt_pk_bf16_f32 v31, v31, v32
	v_cvt_pk_bf16_f32 v32, v33, v36
	v_cvt_pk_bf16_f32 v33, v37, v38
	v_cvt_pk_bf16_f32 v8, v8, v9
	s_nop 0
	v_lshlrev_b32_e32 v9, 16, v31
	v_fma_f32 v9, v16, v28, -v9
	v_and_b32_e32 v16, 0xffff0000, v31
	v_fma_f32 v16, v17, v29, -v16
	v_cvt_pk_bf16_f32 v9, v9, v16
	v_lshlrev_b32_e32 v16, 16, v32
	v_fma_f32 v10, v10, v22, -v16
	v_and_b32_e32 v16, 0xffff0000, v32
	v_fma_f32 v11, v11, v23, -v16
	v_cvt_pk_bf16_f32 v10, v10, v11
	v_lshlrev_b32_e32 v11, 16, v33
	v_fma_f32 v11, v14, v24, -v11
	v_and_b32_e32 v14, 0xffff0000, v33
	v_fma_f32 v14, v15, v25, -v14
	v_cvt_pk_bf16_f32 v11, v11, v14
	v_lshlrev_b64 v[14:15], 4, v[34:35]
	v_lshl_add_u64 v[16:17], s[10:11], 0, v[14:15]
	v_lshl_add_u64 v[14:15], s[16:17], 0, v[14:15]
	global_store_dwordx4 v[16:17], v[30:33], off nt
	s_cbranch_execnz .LBB0_2893

.LBB0_2893:
	global_store_dwordx4 v[14:15], v[8:11], off nt
	ds_read2_b32 v[8:9], v18 offset0:16 offset1:49
	ds_read2_b32 v[16:17], v18 offset0:82 offset1:115
	ds_read2_b32 v[10:11], v18 offset0:148 offset1:181
	ds_read2_b32 v[14:15], v18 offset0:214 offset1:247
	s_and_b64 vcc, exec, s[2:3]
	v_add_u32_e32 v20, s41, v70
	s_waitcnt lgkmcnt(3)
	v_cvt_pk_bf16_f32 v4, v8, v9
	s_waitcnt lgkmcnt(2)
	v_cvt_pk_bf16_f32 v5, v16, v17
	s_waitcnt lgkmcnt(1)
	v_cvt_pk_bf16_f32 v6, v10, v11
	s_waitcnt lgkmcnt(0)
	v_cvt_pk_bf16_f32 v7, v14, v15
	s_cbranch_vccnz .LBB0_2931
	v_lshlrev_b32_e32 v21, 2, v20
	v_and_b32_e32 v21, 0xffffffc0, v21
	v_add_u32_e32 v22, v21, v19
	v_ashrrev_i32_e32 v23, 31, v22
	v_lshlrev_b64 v[34:35], 6, v[22:23]
	v_and_b32_e32 v21, 48, v2
	v_and_b32_e32 v22, 15, v20
	v_lshl_add_u64 v[26:27], v[12:13], 2, s[20:21]
	v_or3_b32 v34, v34, v21, v22
	global_load_dwordx4 v[22:25], v[26:27], off offset:16
	s_nop 0
	global_load_dwordx4 v[26:29], v[26:27], off
	s_waitcnt vmcnt(1)
	v_mul_f32_e32 v33, v10, v22
	s_waitcnt vmcnt(0)
	v_mul_f32_e32 v21, v8, v26
	v_mul_f32_e32 v30, v9, v27
	v_cvt_pk_bf16_f32 v30, v21, v30
	v_mul_f32_e32 v31, v16, v28
	v_lshlrev_b32_e32 v21, 16, v30
	v_fma_f32 v8, v8, v26, -v21
	v_and_b32_e32 v21, 0xffff0000, v30
	v_mul_f32_e32 v32, v17, v29
	v_fma_f32 v9, v9, v27, -v21
	v_mul_f32_e32 v36, v11, v23
	v_mul_f32_e32 v37, v14, v24
	v_mul_f32_e32 v38, v15, v25
	v_cvt_pk_bf16_f32 v31, v31, v32
	v_cvt_pk_bf16_f32 v32, v33, v36
	v_cvt_pk_bf16_f32 v33, v37, v38
	v_cvt_pk_bf16_f32 v8, v8, v9
	s_nop 0
	v_lshlrev_b32_e32 v9, 16, v31
	v_fma_f32 v9, v16, v28, -v9
	v_and_b32_e32 v16, 0xffff0000, v31
	v_fma_f32 v16, v17, v29, -v16
	v_cvt_pk_bf16_f32 v9, v9, v16
	v_lshlrev_b32_e32 v16, 16, v32
	v_fma_f32 v10, v10, v22, -v16
	v_and_b32_e32 v16, 0xffff0000, v32
	v_fma_f32 v11, v11, v23, -v16
	v_cvt_pk_bf16_f32 v10, v10, v11
	v_lshlrev_b32_e32 v11, 16, v33
	v_fma_f32 v11, v14, v24, -v11
	v_and_b32_e32 v14, 0xffff0000, v33
	v_fma_f32 v14, v15, v25, -v14
	v_cvt_pk_bf16_f32 v11, v11, v14
	v_lshlrev_b64 v[14:15], 4, v[34:35]
	v_lshl_add_u64 v[16:17], s[10:11], 0, v[14:15]
	v_lshl_add_u64 v[14:15], s[16:17], 0, v[14:15]
	global_store_dwordx4 v[16:17], v[30:33], off nt
	s_cbranch_execnz .LBB0_2896

.LBB0_2896:
	global_store_dwordx4 v[14:15], v[8:11], off nt
	ds_read2_b32 v[8:9], v18 offset0:24 offset1:57
	ds_read2_b32 v[16:17], v18 offset0:90 offset1:123
	ds_read2_b32 v[10:11], v18 offset0:156 offset1:189
	ds_read2_b32 v[14:15], v18 offset0:222 offset1:255
	s_and_b64 vcc, exec, s[2:3]
	v_add_u32_e32 v1, s41, v1
	s_waitcnt lgkmcnt(3)
	v_cvt_pk_bf16_f32 v4, v8, v9
	s_waitcnt lgkmcnt(2)
	v_cvt_pk_bf16_f32 v5, v16, v17
	s_waitcnt lgkmcnt(1)
	v_cvt_pk_bf16_f32 v6, v10, v11
	s_waitcnt lgkmcnt(0)
	v_cvt_pk_bf16_f32 v7, v14, v15
	s_cbranch_vccnz .LBB0_2932
	v_lshlrev_b32_e32 v18, 2, v1
	v_and_b32_e32 v18, 0xffffffc0, v18
	v_add_u32_e32 v18, v18, v19
	v_ashrrev_i32_e32 v19, 31, v18
	v_lshlrev_b64 v[30:31], 6, v[18:19]
	v_and_b32_e32 v2, 48, v2
	v_and_b32_e32 v18, 15, v1
	v_lshl_add_u64 v[12:13], v[12:13], 2, s[20:21]
	v_or3_b32 v30, v30, v2, v18
	global_load_dwordx4 v[18:21], v[12:13], off offset:16
	global_load_dwordx4 v[22:25], v[12:13], off
	s_waitcnt vmcnt(1)
	v_mul_f32_e32 v28, v10, v18
	s_waitcnt vmcnt(0)
	v_mul_f32_e32 v2, v8, v22
	v_mul_f32_e32 v12, v9, v23
	v_cvt_pk_bf16_f32 v26, v2, v12
	v_mul_f32_e32 v27, v17, v25
	v_lshlrev_b32_e32 v2, 16, v26
	v_fma_f32 v2, v8, v22, -v2
	v_and_b32_e32 v8, 0xffff0000, v26
	v_mul_f32_e32 v29, v11, v19
	v_fma_f32 v8, v9, v23, -v8
	v_mul_f32_e32 v13, v16, v24
	v_mul_f32_e32 v32, v14, v20
	v_mul_f32_e32 v33, v15, v21
	v_cvt_pk_bf16_f32 v27, v13, v27
	v_cvt_pk_bf16_f32 v28, v28, v29
	v_cvt_pk_bf16_f32 v29, v32, v33
	v_cvt_pk_bf16_f32 v8, v2, v8
	v_lshlrev_b64 v[12:13], 4, v[30:31]
	v_lshlrev_b32_e32 v2, 16, v27
	v_and_b32_e32 v9, 0xffff0000, v27
	v_fma_f32 v2, v16, v24, -v2
	v_fma_f32 v9, v17, v25, -v9
	v_cvt_pk_bf16_f32 v9, v2, v9
	v_lshlrev_b32_e32 v2, 16, v28
	v_fma_f32 v2, v10, v18, -v2
	v_and_b32_e32 v10, 0xffff0000, v28
	v_fma_f32 v10, v11, v19, -v10
	v_cvt_pk_bf16_f32 v10, v2, v10
	v_lshlrev_b32_e32 v2, 16, v29
	v_and_b32_e32 v11, 0xffff0000, v29
	v_fma_f32 v2, v14, v20, -v2
	v_fma_f32 v11, v15, v21, -v11
	v_lshl_add_u64 v[14:15], s[10:11], 0, v[12:13]
	v_lshl_add_u64 v[12:13], s[16:17], 0, v[12:13]
	v_cvt_pk_bf16_f32 v11, v2, v11
	global_store_dwordx4 v[14:15], v[26:29], off nt
	s_cbranch_execnz .LBB0_2899
